# router on f32 MFMA with pitch-65 transposed tile (2-way instead of 8-way LDS write conflicts)
# speedup vs baseline: 1.0203x; 1.0031x over previous
.LBB0_651:
	s_waitcnt vmcnt(0)
	s_barrier
	s_waitcnt vmcnt(0)
	buffer_inv sc1
	s_waitcnt vmcnt(0)
	v_readlane_b32 s98, v253, 20
	v_mbcnt_lo_u32_b32 v216, -1, 0
	v_mbcnt_hi_u32_b32 v216, -1, v216
	s_lshr_b32 s99, s98, 1
	s_and_b32 s100, s98, 1
	v_lshrrev_b32_e32 v217, 5, v216
	v_and_b32_e32 v216, 31, v216
	s_lshl_b32 s101, s99, 4
	v_add_u32_e32 v218, s101, v217
	v_lshlrev_b32_e32 v219, 7, v218
	v_lshl_add_u32 v219, v216, 2, v219
	v_add_u32_e32 v219, 0xa400, v219
	v_mul_u32_u24_e32 v218, 0x104, v218
	s_lshl_b32 s101, s100, 7
	v_add_u32_e32 v218, s101, v218
	v_lshl_add_u32 v218, v216, 2, v218
	v_add_u32_e32 v218, 0x6000, v218
	v_mov_b32_e32 v221, s98
	v_mbcnt_lo_u32_b32 v220, -1, 0
	v_mbcnt_hi_u32_b32 v220, -1, v220
	v_lshl_add_u32 v220, v221, 6, v220
	v_and_b32_e32 v221, 7, v220
	v_lshrrev_b32_e32 v220, 3, v220
	v_mul_u32_u24_e32 v221, 0x820, v221
	v_lshl_add_u32 v220, v220, 2, v221
	v_add_u32_e32 v220, 0x6000, v220
	v_add_u32_e32 v221, 0x410, v220
	s_lshl_b32 s101, s99, 13
	s_lshl_b32 s100, s100, 12
	s_add_i32 s101, s101, s100
	v_lshlrev_b32_e32 v217, 9, v217
	v_add_u32_e32 v217, s101, v217
	v_lshl_add_u32 v217, v216, 2, v217
	s_and_saveexec_b64 s[16:17], s[4:5]
	ds_write_b32 v103, v45 offset:58624
	s_or_b64 exec, exec, s[16:17]
	v_add_u32_e32 v0, s62, v42
	v_ashrrev_i32_e32 v1, 31, v0
	v_lshlrev_b64 v[0:1], 11, v[0:1]
	v_lshl_add_u64 v[94:95], v[46:47], 0, v[0:1]
	global_load_dwordx4 v[30:33], v[94:95], off
	global_load_dwordx4 v[34:37], v[48:49], off
	global_load_dwordx4 v[20:23], v[52:53], off
	global_load_dwordx4 v[24:27], v[94:95], off offset:128
	ds_read_b64 v[38:39], v115 offset:20480
	ds_read_b128 v[98:101], v43 offset:12288
	ds_read_b128 v[122:125], v43 offset:12304
	ds_read_b128 v[126:129], v43 offset:16384
	ds_read_b128 v[130:133], v43 offset:16400
	v_add_u32_e32 v96, 0x6000, v105
	v_mov_b32_e32 v4, 0
	s_waitcnt lgkmcnt(4)
	v_mov_b32_e32 v0, v38
	v_mov_b32_e32 v1, v38
	v_mov_b32_e32 v2, v38
	v_mov_b32_e32 v3, v38
	v_mov_b32_e32 v90, v39
	v_mov_b32_e32 v91, v39
	v_mov_b32_e32 v92, v39
	v_mov_b32_e32 v93, v39
	v_add_u32_e32 v44, 0x6400, v105
	s_mov_b32 s16, 0
	v_mov_b32_e32 v28, v112
	v_mov_b32_e32 v5, v4
	v_mov_b32_e32 v6, v4
	v_mov_b32_e32 v7, v4
	v_mov_b32_e32 v8, v4
	v_mov_b32_e32 v9, v4
	v_mov_b32_e32 v10, v4
	v_mov_b32_e32 v11, v4
	v_mov_b32_e32 v12, v4
	v_mov_b32_e32 v13, v4
	v_mov_b32_e32 v14, v4
	v_mov_b32_e32 v15, v4
	v_mov_b32_e32 v16, v4
	v_mov_b32_e32 v17, v4
	v_mov_b32_e32 v18, v4
	s_waitcnt vmcnt(3)
	v_cvt_f32_f16_sdwa v19, v31 dst_sel:DWORD dst_unused:UNUSED_PAD src0_sel:WORD_1
	v_cvt_f32_f16_e32 v29, v31
	v_cvt_f32_f16_sdwa v31, v30 dst_sel:DWORD dst_unused:UNUSED_PAD src0_sel:WORD_1
	v_cvt_f32_f16_e32 v30, v30
	v_cvt_f32_f16_sdwa v97, v33 dst_sel:DWORD dst_unused:UNUSED_PAD src0_sel:WORD_1
	v_cvt_f32_f16_e32 v136, v33
	v_cvt_f32_f16_sdwa v135, v32 dst_sel:DWORD dst_unused:UNUSED_PAD src0_sel:WORD_1
	v_cvt_f32_f16_e32 v134, v32
	v_sub_f32_e32 v30, v30, v38
	v_sub_f32_e32 v31, v31, v38
	v_sub_f32_e32 v32, v29, v38
	v_sub_f32_e32 v33, v19, v38
	v_sub_f32_e32 v134, v134, v38
	v_sub_f32_e32 v135, v135, v38
	v_sub_f32_e32 v136, v136, v38
	v_sub_f32_e32 v137, v97, v38
	v_pk_mul_f32 v[30:31], v[38:39], v[30:31] op_sel:[1,0]
	v_pk_mul_f32 v[32:33], v[38:39], v[32:33] op_sel:[1,0]
	v_pk_mul_f32 v[136:137], v[38:39], v[136:137] op_sel:[1,0]
	v_pk_mul_f32 v[38:39], v[38:39], v[134:135] op_sel:[1,0]
	s_waitcnt lgkmcnt(1)
	v_fma_f32 v19, v98, v30, v126
	v_fma_f32 v30, v99, v31, v127
	s_waitcnt lgkmcnt(0)
	v_fma_f32 v29, v122, v38, v130
	v_fma_f32 v31, v123, v39, v131
	v_fma_f32 v32, v100, v32, v128
	v_fma_f32 v38, v124, v136, v132
	v_fmac_f32_e32 v129, v101, v33
	v_fmac_f32_e32 v133, v125, v137
	ds_write2_b32 v220, v19, v30 offset1:65
	ds_write2_b32 v221, v29, v31 offset1:65
	ds_write2_b32 v220, v32, v129 offset0:130 offset1:195
	ds_write2_b32 v221, v38, v133 offset0:130 offset1:195
	s_waitcnt vmcnt(2)
	ds_write_b128 v104, v[34:37] offset:41984
	v_mov_b32_e32 v19, v4
	s_waitcnt lgkmcnt(0)
	s_barrier
	ds_read_b32 v200, v218
	ds_read_b32 v208, v219
	ds_read_b32 v201, v218 offset:520
	ds_read_b32 v209, v219 offset:256
	ds_read_b32 v202, v218 offset:1040
	ds_read_b32 v210, v219 offset:512
	ds_read_b32 v203, v218 offset:1560
	ds_read_b32 v211, v219 offset:768
	ds_read_b32 v204, v218 offset:2080
	ds_read_b32 v212, v219 offset:1024
	ds_read_b32 v205, v218 offset:2600
	ds_read_b32 v213, v219 offset:1280
	ds_read_b32 v206, v218 offset:3120
	ds_read_b32 v214, v219 offset:1536
	s_waitcnt lgkmcnt(12)
	v_mfma_f32_32x32x2_f32 v[4:19], v200, v208, v[4:19]
	ds_read_b32 v207, v218 offset:3640
	ds_read_b32 v215, v219 offset:1792
	s_waitcnt lgkmcnt(12)
	v_mfma_f32_32x32x2_f32 v[4:19], v201, v209, v[4:19]
	s_waitcnt lgkmcnt(10)
	v_mfma_f32_32x32x2_f32 v[4:19], v202, v210, v[4:19]
	s_waitcnt lgkmcnt(8)
	v_mfma_f32_32x32x2_f32 v[4:19], v203, v211, v[4:19]
	s_waitcnt lgkmcnt(6)
	v_mfma_f32_32x32x2_f32 v[4:19], v204, v212, v[4:19]
	s_waitcnt lgkmcnt(4)
	v_mfma_f32_32x32x2_f32 v[4:19], v205, v213, v[4:19]
	s_waitcnt lgkmcnt(2)
	v_mfma_f32_32x32x2_f32 v[4:19], v206, v214, v[4:19]
	s_waitcnt lgkmcnt(0)
	v_mfma_f32_32x32x2_f32 v[4:19], v207, v215, v[4:19]
	s_barrier
	global_load_dwordx4 v[32:35], v[94:95], off offset:256
	global_load_dwordx4 v[28:31], v[54:55], off
	s_waitcnt vmcnt(2)
	v_cvt_f32_f16_sdwa v130, v24 dst_sel:DWORD dst_unused:UNUSED_PAD src0_sel:WORD_1
	v_cvt_f32_f16_e32 v24, v24
	v_cvt_f32_f16_e32 v131, v25
	v_cvt_f32_f16_sdwa v132, v26 dst_sel:DWORD dst_unused:UNUSED_PAD src0_sel:WORD_1
	v_cvt_f32_f16_e32 v135, v26
	ds_read_b128 v[36:39], v43 offset:12544
	ds_read_b128 v[98:101], v43 offset:12560
	ds_read_b128 v[122:125], v43 offset:16640
	ds_read_b128 v[126:129], v43 offset:16656
	v_cvt_f32_f16_sdwa v97, v25 dst_sel:DWORD dst_unused:UNUSED_PAD src0_sel:WORD_1
	v_cvt_f32_f16_sdwa v133, v27 dst_sel:DWORD dst_unused:UNUSED_PAD src0_sel:WORD_1
	v_cvt_f32_f16_e32 v134, v27
	v_sub_f32_e32 v24, v24, v0
	v_sub_f32_e32 v25, v130, v1
	v_sub_f32_e32 v26, v131, v2
	v_pk_mul_f32 v[24:25], v[90:91], v[24:25]
	v_sub_f32_e32 v130, v135, v0
	v_sub_f32_e32 v131, v132, v1
	v_sub_f32_e32 v27, v97, v3
	v_sub_f32_e32 v132, v134, v2
	v_sub_f32_e32 v133, v133, v3
	v_pk_mul_f32 v[130:131], v[90:91], v[130:131]
	s_waitcnt lgkmcnt(1)
	v_fma_f32 v24, v36, v24, v122
	v_fma_f32 v25, v37, v25, v123
	v_pk_mul_f32 v[26:27], v[92:93], v[26:27]
	v_pk_mul_f32 v[132:133], v[92:93], v[132:133]
	s_waitcnt lgkmcnt(0)
	v_fma_f32 v36, v98, v130, v126
	ds_write2_b32 v220, v24, v25 offset1:65
	v_fma_f32 v24, v99, v131, v127
	ds_write2_b32 v221, v36, v24 offset1:65
	v_fma_f32 v24, v38, v26, v124
	v_fma_f32 v25, v100, v132, v128
	v_fmac_f32_e32 v125, v39, v27
	v_fmac_f32_e32 v129, v101, v133
	ds_write2_b32 v220, v24, v125 offset0:130 offset1:195
	ds_write2_b32 v221, v25, v129 offset0:130 offset1:195
	ds_write_b128 v104, v[20:23] offset:41984
	s_mov_b32 s16, 0
	v_mov_b32_e32 v20, v112
	s_waitcnt lgkmcnt(0)
	s_barrier
	ds_read_b32 v200, v218
	ds_read_b32 v208, v219
	ds_read_b32 v201, v218 offset:520
	ds_read_b32 v209, v219 offset:256
	ds_read_b32 v202, v218 offset:1040
	ds_read_b32 v210, v219 offset:512
	ds_read_b32 v203, v218 offset:1560
	ds_read_b32 v211, v219 offset:768
	ds_read_b32 v204, v218 offset:2080
	ds_read_b32 v212, v219 offset:1024
	ds_read_b32 v205, v218 offset:2600
	ds_read_b32 v213, v219 offset:1280
	ds_read_b32 v206, v218 offset:3120
	ds_read_b32 v214, v219 offset:1536
	s_waitcnt lgkmcnt(12)
	v_mfma_f32_32x32x2_f32 v[4:19], v200, v208, v[4:19]
	ds_read_b32 v207, v218 offset:3640
	ds_read_b32 v215, v219 offset:1792
	s_waitcnt lgkmcnt(12)
	v_mfma_f32_32x32x2_f32 v[4:19], v201, v209, v[4:19]
	s_waitcnt lgkmcnt(10)
	v_mfma_f32_32x32x2_f32 v[4:19], v202, v210, v[4:19]
	s_waitcnt lgkmcnt(8)
	v_mfma_f32_32x32x2_f32 v[4:19], v203, v211, v[4:19]
	s_waitcnt lgkmcnt(6)
	v_mfma_f32_32x32x2_f32 v[4:19], v204, v212, v[4:19]
	s_waitcnt lgkmcnt(4)
	v_mfma_f32_32x32x2_f32 v[4:19], v205, v213, v[4:19]
	s_waitcnt lgkmcnt(2)
	v_mfma_f32_32x32x2_f32 v[4:19], v206, v214, v[4:19]
	s_waitcnt lgkmcnt(0)
	v_mfma_f32_32x32x2_f32 v[4:19], v207, v215, v[4:19]
	s_barrier
	global_load_dwordx4 v[36:39], v[94:95], off offset:384
	global_load_dwordx4 v[20:23], v[56:57], off
	s_waitcnt vmcnt(3)
	v_cvt_f32_f16_sdwa v130, v32 dst_sel:DWORD dst_unused:UNUSED_PAD src0_sel:WORD_1
	v_cvt_f32_f16_e32 v32, v32
	v_cvt_f32_f16_e32 v131, v33
	v_cvt_f32_f16_sdwa v132, v34 dst_sel:DWORD dst_unused:UNUSED_PAD src0_sel:WORD_1
	v_cvt_f32_f16_e32 v135, v34
	ds_read_b128 v[24:27], v43 offset:12800
	ds_read_b128 v[98:101], v43 offset:12816
	ds_read_b128 v[122:125], v43 offset:16896
	ds_read_b128 v[126:129], v43 offset:16912
	v_cvt_f32_f16_sdwa v97, v33 dst_sel:DWORD dst_unused:UNUSED_PAD src0_sel:WORD_1
	v_cvt_f32_f16_sdwa v133, v35 dst_sel:DWORD dst_unused:UNUSED_PAD src0_sel:WORD_1
	v_cvt_f32_f16_e32 v134, v35
	v_sub_f32_e32 v32, v32, v0
	v_sub_f32_e32 v33, v130, v1
	v_sub_f32_e32 v34, v131, v2
	v_pk_mul_f32 v[32:33], v[90:91], v[32:33]
	v_sub_f32_e32 v130, v135, v0
	v_sub_f32_e32 v131, v132, v1
	v_sub_f32_e32 v35, v97, v3
	v_pk_mul_f32 v[130:131], v[90:91], v[130:131]
	s_waitcnt lgkmcnt(1)
	v_fma_f32 v24, v24, v32, v122
	v_fma_f32 v25, v25, v33, v123
	v_pk_mul_f32 v[34:35], v[92:93], v[34:35]
	v_sub_f32_e32 v132, v134, v2
	v_sub_f32_e32 v133, v133, v3
	s_waitcnt lgkmcnt(0)
	v_fma_f32 v32, v98, v130, v126
	ds_write2_b32 v220, v24, v25 offset1:65
	v_fma_f32 v24, v99, v131, v127
	v_pk_mul_f32 v[132:133], v[92:93], v[132:133]
	ds_write2_b32 v221, v32, v24 offset1:65
	v_fma_f32 v24, v26, v34, v124
	v_fmac_f32_e32 v125, v27, v35
	v_fma_f32 v25, v100, v132, v128
	ds_write2_b32 v220, v24, v125 offset0:130 offset1:195
	v_fmac_f32_e32 v129, v101, v133
	s_mov_b32 s16, 0
	v_mov_b32_e32 v24, v112
	ds_write2_b32 v221, v25, v129 offset0:130 offset1:195
	s_waitcnt vmcnt(2)
	ds_write_b128 v104, v[28:31] offset:41984
	s_waitcnt lgkmcnt(0)
	s_barrier
	ds_read_b32 v200, v218
	ds_read_b32 v208, v219
	ds_read_b32 v201, v218 offset:520
	ds_read_b32 v209, v219 offset:256
	ds_read_b32 v202, v218 offset:1040
	ds_read_b32 v210, v219 offset:512
	ds_read_b32 v203, v218 offset:1560
	ds_read_b32 v211, v219 offset:768
	ds_read_b32 v204, v218 offset:2080
	ds_read_b32 v212, v219 offset:1024
	ds_read_b32 v205, v218 offset:2600
	ds_read_b32 v213, v219 offset:1280
	ds_read_b32 v206, v218 offset:3120
	ds_read_b32 v214, v219 offset:1536
	s_waitcnt lgkmcnt(12)
	v_mfma_f32_32x32x2_f32 v[4:19], v200, v208, v[4:19]
	ds_read_b32 v207, v218 offset:3640
	ds_read_b32 v215, v219 offset:1792
	s_waitcnt lgkmcnt(12)
	v_mfma_f32_32x32x2_f32 v[4:19], v201, v209, v[4:19]
	s_waitcnt lgkmcnt(10)
	v_mfma_f32_32x32x2_f32 v[4:19], v202, v210, v[4:19]
	s_waitcnt lgkmcnt(8)
	v_mfma_f32_32x32x2_f32 v[4:19], v203, v211, v[4:19]
	s_waitcnt lgkmcnt(6)
	v_mfma_f32_32x32x2_f32 v[4:19], v204, v212, v[4:19]
	s_waitcnt lgkmcnt(4)
	v_mfma_f32_32x32x2_f32 v[4:19], v205, v213, v[4:19]
	s_waitcnt lgkmcnt(2)
	v_mfma_f32_32x32x2_f32 v[4:19], v206, v214, v[4:19]
	s_waitcnt lgkmcnt(0)
	v_mfma_f32_32x32x2_f32 v[4:19], v207, v215, v[4:19]
	s_barrier
	global_load_dwordx4 v[28:31], v[94:95], off offset:512
	global_load_dwordx4 v[24:27], v[58:59], off
	s_waitcnt vmcnt(3)
	v_cvt_f32_f16_sdwa v130, v36 dst_sel:DWORD dst_unused:UNUSED_PAD src0_sel:WORD_1
	v_cvt_f32_f16_e32 v36, v36
	v_cvt_f32_f16_e32 v131, v37
	v_cvt_f32_f16_sdwa v132, v38 dst_sel:DWORD dst_unused:UNUSED_PAD src0_sel:WORD_1
	v_cvt_f32_f16_e32 v135, v38
	ds_read_b128 v[32:35], v43 offset:13056
	ds_read_b128 v[98:101], v43 offset:13072
	ds_read_b128 v[122:125], v43 offset:17152
	ds_read_b128 v[126:129], v43 offset:17168
	v_cvt_f32_f16_sdwa v97, v37 dst_sel:DWORD dst_unused:UNUSED_PAD src0_sel:WORD_1
	v_cvt_f32_f16_sdwa v133, v39 dst_sel:DWORD dst_unused:UNUSED_PAD src0_sel:WORD_1
	v_cvt_f32_f16_e32 v134, v39
	v_sub_f32_e32 v36, v36, v0
	v_sub_f32_e32 v37, v130, v1
	v_sub_f32_e32 v38, v131, v2
	v_pk_mul_f32 v[36:37], v[90:91], v[36:37]
	v_sub_f32_e32 v130, v135, v0
	v_sub_f32_e32 v131, v132, v1
	v_sub_f32_e32 v39, v97, v3
	v_sub_f32_e32 v132, v134, v2
	v_sub_f32_e32 v133, v133, v3
	v_pk_mul_f32 v[130:131], v[90:91], v[130:131]
	s_waitcnt lgkmcnt(1)
	v_fma_f32 v32, v32, v36, v122
	v_fma_f32 v33, v33, v37, v123
	v_pk_mul_f32 v[38:39], v[92:93], v[38:39]
	v_pk_mul_f32 v[132:133], v[92:93], v[132:133]
	s_waitcnt lgkmcnt(0)
	v_fma_f32 v36, v98, v130, v126
	ds_write2_b32 v220, v32, v33 offset1:65
	v_fma_f32 v32, v99, v131, v127
	ds_write2_b32 v221, v36, v32 offset1:65
	v_fma_f32 v32, v34, v38, v124
	v_fma_f32 v33, v100, v132, v128
	v_fmac_f32_e32 v125, v35, v39
	v_fmac_f32_e32 v129, v101, v133
	ds_write2_b32 v220, v32, v125 offset0:130 offset1:195
	ds_write2_b32 v221, v33, v129 offset0:130 offset1:195
	s_waitcnt vmcnt(2)
	ds_write_b128 v104, v[20:23] offset:41984
	s_mov_b32 s16, 0
	v_mov_b32_e32 v20, v112
	s_waitcnt lgkmcnt(0)
	s_barrier
	ds_read_b32 v200, v218
	ds_read_b32 v208, v219
	ds_read_b32 v201, v218 offset:520
	ds_read_b32 v209, v219 offset:256
	ds_read_b32 v202, v218 offset:1040
	ds_read_b32 v210, v219 offset:512
	ds_read_b32 v203, v218 offset:1560
	ds_read_b32 v211, v219 offset:768
	ds_read_b32 v204, v218 offset:2080
	ds_read_b32 v212, v219 offset:1024
	ds_read_b32 v205, v218 offset:2600
	ds_read_b32 v213, v219 offset:1280
	ds_read_b32 v206, v218 offset:3120
	ds_read_b32 v214, v219 offset:1536
	s_waitcnt lgkmcnt(12)
	v_mfma_f32_32x32x2_f32 v[4:19], v200, v208, v[4:19]
	ds_read_b32 v207, v218 offset:3640
	ds_read_b32 v215, v219 offset:1792
	s_waitcnt lgkmcnt(12)
	v_mfma_f32_32x32x2_f32 v[4:19], v201, v209, v[4:19]
	s_waitcnt lgkmcnt(10)
	v_mfma_f32_32x32x2_f32 v[4:19], v202, v210, v[4:19]
	s_waitcnt lgkmcnt(8)
	v_mfma_f32_32x32x2_f32 v[4:19], v203, v211, v[4:19]
	s_waitcnt lgkmcnt(6)
	v_mfma_f32_32x32x2_f32 v[4:19], v204, v212, v[4:19]
	s_waitcnt lgkmcnt(4)
	v_mfma_f32_32x32x2_f32 v[4:19], v205, v213, v[4:19]
	s_waitcnt lgkmcnt(2)
	v_mfma_f32_32x32x2_f32 v[4:19], v206, v214, v[4:19]
	s_waitcnt lgkmcnt(0)
	v_mfma_f32_32x32x2_f32 v[4:19], v207, v215, v[4:19]
	s_barrier
	global_load_dwordx4 v[32:35], v[94:95], off offset:640
	global_load_dwordx4 v[20:23], v[60:61], off
	s_waitcnt vmcnt(3)
	v_cvt_f32_f16_sdwa v130, v28 dst_sel:DWORD dst_unused:UNUSED_PAD src0_sel:WORD_1
	v_cvt_f32_f16_e32 v28, v28
	v_cvt_f32_f16_e32 v131, v29
	v_cvt_f32_f16_sdwa v132, v30 dst_sel:DWORD dst_unused:UNUSED_PAD src0_sel:WORD_1
	v_cvt_f32_f16_e32 v135, v30
	ds_read_b128 v[36:39], v43 offset:13312
	ds_read_b128 v[98:101], v43 offset:13328
	ds_read_b128 v[122:125], v43 offset:17408
	ds_read_b128 v[126:129], v43 offset:17424
	v_cvt_f32_f16_sdwa v97, v29 dst_sel:DWORD dst_unused:UNUSED_PAD src0_sel:WORD_1
	v_cvt_f32_f16_sdwa v133, v31 dst_sel:DWORD dst_unused:UNUSED_PAD src0_sel:WORD_1
	v_cvt_f32_f16_e32 v134, v31
	v_sub_f32_e32 v28, v28, v0
	v_sub_f32_e32 v29, v130, v1
	v_sub_f32_e32 v30, v131, v2
	v_pk_mul_f32 v[28:29], v[90:91], v[28:29]
	v_sub_f32_e32 v130, v135, v0
	v_sub_f32_e32 v131, v132, v1
	v_sub_f32_e32 v31, v97, v3
	v_sub_f32_e32 v132, v134, v2
	v_sub_f32_e32 v133, v133, v3
	v_pk_mul_f32 v[130:131], v[90:91], v[130:131]
	s_waitcnt lgkmcnt(1)
	v_fma_f32 v28, v36, v28, v122
	v_fma_f32 v29, v37, v29, v123
	v_pk_mul_f32 v[30:31], v[92:93], v[30:31]
	v_pk_mul_f32 v[132:133], v[92:93], v[132:133]
	s_waitcnt lgkmcnt(0)
	v_fma_f32 v36, v98, v130, v126
	ds_write2_b32 v220, v28, v29 offset1:65
	v_fma_f32 v28, v99, v131, v127
	ds_write2_b32 v221, v36, v28 offset1:65
	v_fma_f32 v28, v38, v30, v124
	v_fma_f32 v29, v100, v132, v128
	v_fmac_f32_e32 v125, v39, v31
	v_fmac_f32_e32 v129, v101, v133
	ds_write2_b32 v220, v28, v125 offset0:130 offset1:195
	ds_write2_b32 v221, v29, v129 offset0:130 offset1:195
	s_waitcnt vmcnt(2)
	ds_write_b128 v104, v[24:27] offset:41984
	s_mov_b32 s16, 0
	v_mov_b32_e32 v24, v112
	s_waitcnt lgkmcnt(0)
	s_barrier
	ds_read_b32 v200, v218
	ds_read_b32 v208, v219
	ds_read_b32 v201, v218 offset:520
	ds_read_b32 v209, v219 offset:256
	ds_read_b32 v202, v218 offset:1040
	ds_read_b32 v210, v219 offset:512
	ds_read_b32 v203, v218 offset:1560
	ds_read_b32 v211, v219 offset:768
	ds_read_b32 v204, v218 offset:2080
	ds_read_b32 v212, v219 offset:1024
	ds_read_b32 v205, v218 offset:2600
	ds_read_b32 v213, v219 offset:1280
	ds_read_b32 v206, v218 offset:3120
	ds_read_b32 v214, v219 offset:1536
	s_waitcnt lgkmcnt(12)
	v_mfma_f32_32x32x2_f32 v[4:19], v200, v208, v[4:19]
	ds_read_b32 v207, v218 offset:3640
	ds_read_b32 v215, v219 offset:1792
	s_waitcnt lgkmcnt(12)
	v_mfma_f32_32x32x2_f32 v[4:19], v201, v209, v[4:19]
	s_waitcnt lgkmcnt(10)
	v_mfma_f32_32x32x2_f32 v[4:19], v202, v210, v[4:19]
	s_waitcnt lgkmcnt(8)
	v_mfma_f32_32x32x2_f32 v[4:19], v203, v211, v[4:19]
	s_waitcnt lgkmcnt(6)
	v_mfma_f32_32x32x2_f32 v[4:19], v204, v212, v[4:19]
	s_waitcnt lgkmcnt(4)
	v_mfma_f32_32x32x2_f32 v[4:19], v205, v213, v[4:19]
	s_waitcnt lgkmcnt(2)
	v_mfma_f32_32x32x2_f32 v[4:19], v206, v214, v[4:19]
	s_waitcnt lgkmcnt(0)
	v_mfma_f32_32x32x2_f32 v[4:19], v207, v215, v[4:19]
	s_barrier
	global_load_dwordx4 v[28:31], v[94:95], off offset:768
	global_load_dwordx4 v[24:27], v[62:63], off
	s_waitcnt vmcnt(3)
	v_cvt_f32_f16_sdwa v130, v32 dst_sel:DWORD dst_unused:UNUSED_PAD src0_sel:WORD_1
	v_cvt_f32_f16_e32 v32, v32
	v_cvt_f32_f16_e32 v131, v33
	v_cvt_f32_f16_sdwa v132, v34 dst_sel:DWORD dst_unused:UNUSED_PAD src0_sel:WORD_1
	v_cvt_f32_f16_e32 v135, v34
	ds_read_b128 v[36:39], v43 offset:13568
	ds_read_b128 v[98:101], v43 offset:13584
	ds_read_b128 v[122:125], v43 offset:17664
	ds_read_b128 v[126:129], v43 offset:17680
	v_cvt_f32_f16_sdwa v97, v33 dst_sel:DWORD dst_unused:UNUSED_PAD src0_sel:WORD_1
	v_cvt_f32_f16_sdwa v133, v35 dst_sel:DWORD dst_unused:UNUSED_PAD src0_sel:WORD_1
	v_cvt_f32_f16_e32 v134, v35
	v_sub_f32_e32 v32, v32, v0
	v_sub_f32_e32 v33, v130, v1
	v_sub_f32_e32 v34, v131, v2
	v_pk_mul_f32 v[32:33], v[90:91], v[32:33]
	v_sub_f32_e32 v130, v135, v0
	v_sub_f32_e32 v131, v132, v1
	v_sub_f32_e32 v35, v97, v3
	v_sub_f32_e32 v132, v134, v2
	v_sub_f32_e32 v133, v133, v3
	v_pk_mul_f32 v[130:131], v[90:91], v[130:131]
	s_waitcnt lgkmcnt(1)
	v_fma_f32 v32, v36, v32, v122
	v_fma_f32 v33, v37, v33, v123
	v_pk_mul_f32 v[34:35], v[92:93], v[34:35]
	v_pk_mul_f32 v[132:133], v[92:93], v[132:133]
	s_waitcnt lgkmcnt(0)
	v_fma_f32 v36, v98, v130, v126
	ds_write2_b32 v220, v32, v33 offset1:65
	v_fma_f32 v32, v99, v131, v127
	ds_write2_b32 v221, v36, v32 offset1:65
	v_fma_f32 v32, v38, v34, v124
	v_fma_f32 v33, v100, v132, v128
	v_fmac_f32_e32 v125, v39, v35
	v_fmac_f32_e32 v129, v101, v133
	ds_write2_b32 v220, v32, v125 offset0:130 offset1:195
	ds_write2_b32 v221, v33, v129 offset0:130 offset1:195
	s_waitcnt vmcnt(2)
	ds_write_b128 v104, v[20:23] offset:41984
	s_mov_b32 s16, 0
	v_mov_b32_e32 v20, v112
	s_waitcnt lgkmcnt(0)
	s_barrier
	ds_read_b32 v200, v218
	ds_read_b32 v208, v219
	ds_read_b32 v201, v218 offset:520
	ds_read_b32 v209, v219 offset:256
	ds_read_b32 v202, v218 offset:1040
	ds_read_b32 v210, v219 offset:512
	ds_read_b32 v203, v218 offset:1560
	ds_read_b32 v211, v219 offset:768
	ds_read_b32 v204, v218 offset:2080
	ds_read_b32 v212, v219 offset:1024
	ds_read_b32 v205, v218 offset:2600
	ds_read_b32 v213, v219 offset:1280
	ds_read_b32 v206, v218 offset:3120
	ds_read_b32 v214, v219 offset:1536
	s_waitcnt lgkmcnt(12)
	v_mfma_f32_32x32x2_f32 v[4:19], v200, v208, v[4:19]
	ds_read_b32 v207, v218 offset:3640
	ds_read_b32 v215, v219 offset:1792
	s_waitcnt lgkmcnt(12)
	v_mfma_f32_32x32x2_f32 v[4:19], v201, v209, v[4:19]
	s_waitcnt lgkmcnt(10)
	v_mfma_f32_32x32x2_f32 v[4:19], v202, v210, v[4:19]
	s_waitcnt lgkmcnt(8)
	v_mfma_f32_32x32x2_f32 v[4:19], v203, v211, v[4:19]
	s_waitcnt lgkmcnt(6)
	v_mfma_f32_32x32x2_f32 v[4:19], v204, v212, v[4:19]
	s_waitcnt lgkmcnt(4)
	v_mfma_f32_32x32x2_f32 v[4:19], v205, v213, v[4:19]
	s_waitcnt lgkmcnt(2)
	v_mfma_f32_32x32x2_f32 v[4:19], v206, v214, v[4:19]
	s_waitcnt lgkmcnt(0)
	v_mfma_f32_32x32x2_f32 v[4:19], v207, v215, v[4:19]
	s_barrier
	global_load_dwordx4 v[32:35], v[94:95], off offset:896
	global_load_dwordx4 v[20:23], v[64:65], off
	s_waitcnt vmcnt(3)
	v_cvt_f32_f16_sdwa v130, v28 dst_sel:DWORD dst_unused:UNUSED_PAD src0_sel:WORD_1
	v_cvt_f32_f16_e32 v28, v28
	v_cvt_f32_f16_e32 v131, v29
	v_cvt_f32_f16_sdwa v132, v30 dst_sel:DWORD dst_unused:UNUSED_PAD src0_sel:WORD_1
	v_cvt_f32_f16_e32 v135, v30
	ds_read_b128 v[36:39], v43 offset:13824
	ds_read_b128 v[98:101], v43 offset:13840
	ds_read_b128 v[122:125], v43 offset:17920
	ds_read_b128 v[126:129], v43 offset:17936
	v_cvt_f32_f16_sdwa v97, v29 dst_sel:DWORD dst_unused:UNUSED_PAD src0_sel:WORD_1
	v_cvt_f32_f16_sdwa v133, v31 dst_sel:DWORD dst_unused:UNUSED_PAD src0_sel:WORD_1
	v_cvt_f32_f16_e32 v134, v31
	v_sub_f32_e32 v28, v28, v0
	v_sub_f32_e32 v29, v130, v1
	v_sub_f32_e32 v30, v131, v2
	v_pk_mul_f32 v[28:29], v[90:91], v[28:29]
	v_sub_f32_e32 v130, v135, v0
	v_sub_f32_e32 v131, v132, v1
	v_sub_f32_e32 v31, v97, v3
	v_sub_f32_e32 v132, v134, v2
	v_sub_f32_e32 v133, v133, v3
	v_pk_mul_f32 v[130:131], v[90:91], v[130:131]
	s_waitcnt lgkmcnt(1)
	v_fma_f32 v28, v36, v28, v122
	v_fma_f32 v29, v37, v29, v123
	v_pk_mul_f32 v[30:31], v[92:93], v[30:31]
	v_pk_mul_f32 v[132:133], v[92:93], v[132:133]
	s_waitcnt lgkmcnt(0)
	v_fma_f32 v36, v98, v130, v126
	ds_write2_b32 v220, v28, v29 offset1:65
	v_fma_f32 v28, v99, v131, v127
	ds_write2_b32 v221, v36, v28 offset1:65
	v_fma_f32 v28, v38, v30, v124
	v_fma_f32 v29, v100, v132, v128
	v_fmac_f32_e32 v125, v39, v31
	v_fmac_f32_e32 v129, v101, v133
	ds_write2_b32 v220, v28, v125 offset0:130 offset1:195
	ds_write2_b32 v221, v29, v129 offset0:130 offset1:195
	s_waitcnt vmcnt(2)
	ds_write_b128 v104, v[24:27] offset:41984
	s_mov_b32 s16, 0
	v_mov_b32_e32 v24, v112
	s_waitcnt lgkmcnt(0)
	s_barrier
	ds_read_b32 v200, v218
	ds_read_b32 v208, v219
	ds_read_b32 v201, v218 offset:520
	ds_read_b32 v209, v219 offset:256
	ds_read_b32 v202, v218 offset:1040
	ds_read_b32 v210, v219 offset:512
	ds_read_b32 v203, v218 offset:1560
	ds_read_b32 v211, v219 offset:768
	ds_read_b32 v204, v218 offset:2080
	ds_read_b32 v212, v219 offset:1024
	ds_read_b32 v205, v218 offset:2600
	ds_read_b32 v213, v219 offset:1280
	ds_read_b32 v206, v218 offset:3120
	ds_read_b32 v214, v219 offset:1536
	s_waitcnt lgkmcnt(12)
	v_mfma_f32_32x32x2_f32 v[4:19], v200, v208, v[4:19]
	ds_read_b32 v207, v218 offset:3640
	ds_read_b32 v215, v219 offset:1792
	s_waitcnt lgkmcnt(12)
	v_mfma_f32_32x32x2_f32 v[4:19], v201, v209, v[4:19]
	s_waitcnt lgkmcnt(10)
	v_mfma_f32_32x32x2_f32 v[4:19], v202, v210, v[4:19]
	s_waitcnt lgkmcnt(8)
	v_mfma_f32_32x32x2_f32 v[4:19], v203, v211, v[4:19]
	s_waitcnt lgkmcnt(6)
	v_mfma_f32_32x32x2_f32 v[4:19], v204, v212, v[4:19]
	s_waitcnt lgkmcnt(4)
	v_mfma_f32_32x32x2_f32 v[4:19], v205, v213, v[4:19]
	s_waitcnt lgkmcnt(2)
	v_mfma_f32_32x32x2_f32 v[4:19], v206, v214, v[4:19]
	s_waitcnt lgkmcnt(0)
	v_mfma_f32_32x32x2_f32 v[4:19], v207, v215, v[4:19]
	s_barrier
	global_load_dwordx4 v[28:31], v[94:95], off offset:1024
	global_load_dwordx4 v[24:27], v[66:67], off
	s_waitcnt vmcnt(3)
	v_cvt_f32_f16_sdwa v130, v32 dst_sel:DWORD dst_unused:UNUSED_PAD src0_sel:WORD_1
	v_cvt_f32_f16_e32 v32, v32
	v_cvt_f32_f16_e32 v131, v33
	v_cvt_f32_f16_sdwa v132, v34 dst_sel:DWORD dst_unused:UNUSED_PAD src0_sel:WORD_1
	v_cvt_f32_f16_e32 v135, v34
	ds_read_b128 v[36:39], v43 offset:14080
	ds_read_b128 v[98:101], v43 offset:14096
	ds_read_b128 v[122:125], v43 offset:18176
	ds_read_b128 v[126:129], v43 offset:18192
	v_cvt_f32_f16_sdwa v97, v33 dst_sel:DWORD dst_unused:UNUSED_PAD src0_sel:WORD_1
	v_cvt_f32_f16_sdwa v133, v35 dst_sel:DWORD dst_unused:UNUSED_PAD src0_sel:WORD_1
	v_cvt_f32_f16_e32 v134, v35
	v_sub_f32_e32 v32, v32, v0
	v_sub_f32_e32 v33, v130, v1
	v_sub_f32_e32 v34, v131, v2
	v_pk_mul_f32 v[32:33], v[90:91], v[32:33]
	v_sub_f32_e32 v130, v135, v0
	v_sub_f32_e32 v131, v132, v1
	v_sub_f32_e32 v35, v97, v3
	v_sub_f32_e32 v132, v134, v2
	v_sub_f32_e32 v133, v133, v3
	v_pk_mul_f32 v[130:131], v[90:91], v[130:131]
	s_waitcnt lgkmcnt(1)
	v_fma_f32 v32, v36, v32, v122
	v_fma_f32 v33, v37, v33, v123
	v_pk_mul_f32 v[34:35], v[92:93], v[34:35]
	v_pk_mul_f32 v[132:133], v[92:93], v[132:133]
	s_waitcnt lgkmcnt(0)
	v_fma_f32 v36, v98, v130, v126
	ds_write2_b32 v220, v32, v33 offset1:65
	v_fma_f32 v32, v99, v131, v127
	ds_write2_b32 v221, v36, v32 offset1:65
	v_fma_f32 v32, v38, v34, v124
	v_fma_f32 v33, v100, v132, v128
	v_fmac_f32_e32 v125, v39, v35
	v_fmac_f32_e32 v129, v101, v133
	ds_write2_b32 v220, v32, v125 offset0:130 offset1:195
	ds_write2_b32 v221, v33, v129 offset0:130 offset1:195
	s_waitcnt vmcnt(2)
	ds_write_b128 v104, v[20:23] offset:41984
	s_mov_b32 s16, 0
	v_mov_b32_e32 v20, v112
	s_waitcnt lgkmcnt(0)
	s_barrier
	ds_read_b32 v200, v218
	ds_read_b32 v208, v219
	ds_read_b32 v201, v218 offset:520
	ds_read_b32 v209, v219 offset:256
	ds_read_b32 v202, v218 offset:1040
	ds_read_b32 v210, v219 offset:512
	ds_read_b32 v203, v218 offset:1560
	ds_read_b32 v211, v219 offset:768
	ds_read_b32 v204, v218 offset:2080
	ds_read_b32 v212, v219 offset:1024
	ds_read_b32 v205, v218 offset:2600
	ds_read_b32 v213, v219 offset:1280
	ds_read_b32 v206, v218 offset:3120
	ds_read_b32 v214, v219 offset:1536
	s_waitcnt lgkmcnt(12)
	v_mfma_f32_32x32x2_f32 v[4:19], v200, v208, v[4:19]
	ds_read_b32 v207, v218 offset:3640
	ds_read_b32 v215, v219 offset:1792
	s_waitcnt lgkmcnt(12)
	v_mfma_f32_32x32x2_f32 v[4:19], v201, v209, v[4:19]
	s_waitcnt lgkmcnt(10)
	v_mfma_f32_32x32x2_f32 v[4:19], v202, v210, v[4:19]
	s_waitcnt lgkmcnt(8)
	v_mfma_f32_32x32x2_f32 v[4:19], v203, v211, v[4:19]
	s_waitcnt lgkmcnt(6)
	v_mfma_f32_32x32x2_f32 v[4:19], v204, v212, v[4:19]
	s_waitcnt lgkmcnt(4)
	v_mfma_f32_32x32x2_f32 v[4:19], v205, v213, v[4:19]
	s_waitcnt lgkmcnt(2)
	v_mfma_f32_32x32x2_f32 v[4:19], v206, v214, v[4:19]
	s_waitcnt lgkmcnt(0)
	v_mfma_f32_32x32x2_f32 v[4:19], v207, v215, v[4:19]
	s_barrier
	global_load_dwordx4 v[32:35], v[94:95], off offset:1152
	global_load_dwordx4 v[20:23], v[68:69], off
	s_waitcnt vmcnt(3)
	v_cvt_f32_f16_sdwa v130, v28 dst_sel:DWORD dst_unused:UNUSED_PAD src0_sel:WORD_1
	v_cvt_f32_f16_e32 v28, v28
	v_cvt_f32_f16_e32 v131, v29
	v_cvt_f32_f16_sdwa v132, v30 dst_sel:DWORD dst_unused:UNUSED_PAD src0_sel:WORD_1
	v_cvt_f32_f16_e32 v135, v30
	ds_read_b128 v[36:39], v43 offset:14336
	ds_read_b128 v[98:101], v43 offset:14352
	ds_read_b128 v[122:125], v43 offset:18432
	ds_read_b128 v[126:129], v43 offset:18448
	v_cvt_f32_f16_sdwa v97, v29 dst_sel:DWORD dst_unused:UNUSED_PAD src0_sel:WORD_1
	v_cvt_f32_f16_sdwa v133, v31 dst_sel:DWORD dst_unused:UNUSED_PAD src0_sel:WORD_1
	v_cvt_f32_f16_e32 v134, v31
	v_sub_f32_e32 v28, v28, v0
	v_sub_f32_e32 v29, v130, v1
	v_sub_f32_e32 v30, v131, v2
	v_pk_mul_f32 v[28:29], v[90:91], v[28:29]
	v_sub_f32_e32 v130, v135, v0
	v_sub_f32_e32 v131, v132, v1
	v_sub_f32_e32 v31, v97, v3
	v_sub_f32_e32 v132, v134, v2
	v_sub_f32_e32 v133, v133, v3
	v_pk_mul_f32 v[130:131], v[90:91], v[130:131]
	s_waitcnt lgkmcnt(1)
	v_fma_f32 v28, v36, v28, v122
	v_fma_f32 v29, v37, v29, v123
	v_pk_mul_f32 v[30:31], v[92:93], v[30:31]
	v_pk_mul_f32 v[132:133], v[92:93], v[132:133]
	s_waitcnt lgkmcnt(0)
	v_fma_f32 v36, v98, v130, v126
	ds_write2_b32 v220, v28, v29 offset1:65
	v_fma_f32 v28, v99, v131, v127
	ds_write2_b32 v221, v36, v28 offset1:65
	v_fma_f32 v28, v38, v30, v124
	v_fma_f32 v29, v100, v132, v128
	v_fmac_f32_e32 v125, v39, v31
	v_fmac_f32_e32 v129, v101, v133
	ds_write2_b32 v220, v28, v125 offset0:130 offset1:195
	ds_write2_b32 v221, v29, v129 offset0:130 offset1:195
	s_waitcnt vmcnt(2)
	ds_write_b128 v104, v[24:27] offset:41984
	s_mov_b32 s16, 0
	v_mov_b32_e32 v24, v112
	s_waitcnt lgkmcnt(0)
	s_barrier
	ds_read_b32 v200, v218
	ds_read_b32 v208, v219
	ds_read_b32 v201, v218 offset:520
	ds_read_b32 v209, v219 offset:256
	ds_read_b32 v202, v218 offset:1040
	ds_read_b32 v210, v219 offset:512
	ds_read_b32 v203, v218 offset:1560
	ds_read_b32 v211, v219 offset:768
	ds_read_b32 v204, v218 offset:2080
	ds_read_b32 v212, v219 offset:1024
	ds_read_b32 v205, v218 offset:2600
	ds_read_b32 v213, v219 offset:1280
	ds_read_b32 v206, v218 offset:3120
	ds_read_b32 v214, v219 offset:1536
	s_waitcnt lgkmcnt(12)
	v_mfma_f32_32x32x2_f32 v[4:19], v200, v208, v[4:19]
	ds_read_b32 v207, v218 offset:3640
	ds_read_b32 v215, v219 offset:1792
	s_waitcnt lgkmcnt(12)
	v_mfma_f32_32x32x2_f32 v[4:19], v201, v209, v[4:19]
	s_waitcnt lgkmcnt(10)
	v_mfma_f32_32x32x2_f32 v[4:19], v202, v210, v[4:19]
	s_waitcnt lgkmcnt(8)
	v_mfma_f32_32x32x2_f32 v[4:19], v203, v211, v[4:19]
	s_waitcnt lgkmcnt(6)
	v_mfma_f32_32x32x2_f32 v[4:19], v204, v212, v[4:19]
	s_waitcnt lgkmcnt(4)
	v_mfma_f32_32x32x2_f32 v[4:19], v205, v213, v[4:19]
	s_waitcnt lgkmcnt(2)
	v_mfma_f32_32x32x2_f32 v[4:19], v206, v214, v[4:19]
	s_waitcnt lgkmcnt(0)
	v_mfma_f32_32x32x2_f32 v[4:19], v207, v215, v[4:19]
	s_barrier
	global_load_dwordx4 v[28:31], v[94:95], off offset:1280
	global_load_dwordx4 v[24:27], v[70:71], off
	s_waitcnt vmcnt(3)
	v_cvt_f32_f16_sdwa v130, v32 dst_sel:DWORD dst_unused:UNUSED_PAD src0_sel:WORD_1
	v_cvt_f32_f16_e32 v32, v32
	v_cvt_f32_f16_e32 v131, v33
	v_cvt_f32_f16_sdwa v132, v34 dst_sel:DWORD dst_unused:UNUSED_PAD src0_sel:WORD_1
	v_cvt_f32_f16_e32 v135, v34
	ds_read_b128 v[36:39], v43 offset:14592
	ds_read_b128 v[98:101], v43 offset:14608
	ds_read_b128 v[122:125], v43 offset:18688
	ds_read_b128 v[126:129], v43 offset:18704
	v_cvt_f32_f16_sdwa v97, v33 dst_sel:DWORD dst_unused:UNUSED_PAD src0_sel:WORD_1
	v_cvt_f32_f16_sdwa v133, v35 dst_sel:DWORD dst_unused:UNUSED_PAD src0_sel:WORD_1
	v_cvt_f32_f16_e32 v134, v35
	v_sub_f32_e32 v32, v32, v0
	v_sub_f32_e32 v33, v130, v1
	v_sub_f32_e32 v34, v131, v2
	v_pk_mul_f32 v[32:33], v[90:91], v[32:33]
	v_sub_f32_e32 v130, v135, v0
	v_sub_f32_e32 v131, v132, v1
	v_sub_f32_e32 v35, v97, v3
	v_sub_f32_e32 v132, v134, v2
	v_sub_f32_e32 v133, v133, v3
	v_pk_mul_f32 v[130:131], v[90:91], v[130:131]
	s_waitcnt lgkmcnt(1)
	v_fma_f32 v32, v36, v32, v122
	v_fma_f32 v33, v37, v33, v123
	v_pk_mul_f32 v[34:35], v[92:93], v[34:35]
	v_pk_mul_f32 v[132:133], v[92:93], v[132:133]
	s_waitcnt lgkmcnt(0)
	v_fma_f32 v36, v98, v130, v126
	ds_write2_b32 v220, v32, v33 offset1:65
	v_fma_f32 v32, v99, v131, v127
	ds_write2_b32 v221, v36, v32 offset1:65
	v_fma_f32 v32, v38, v34, v124
	v_fma_f32 v33, v100, v132, v128
	v_fmac_f32_e32 v125, v39, v35
	v_fmac_f32_e32 v129, v101, v133
	ds_write2_b32 v220, v32, v125 offset0:130 offset1:195
	ds_write2_b32 v221, v33, v129 offset0:130 offset1:195
	s_waitcnt vmcnt(2)
	ds_write_b128 v104, v[20:23] offset:41984
	s_mov_b32 s16, 0
	v_mov_b32_e32 v20, v112
	s_waitcnt lgkmcnt(0)
	s_barrier
	ds_read_b32 v200, v218
	ds_read_b32 v208, v219
	ds_read_b32 v201, v218 offset:520
	ds_read_b32 v209, v219 offset:256
	ds_read_b32 v202, v218 offset:1040
	ds_read_b32 v210, v219 offset:512
	ds_read_b32 v203, v218 offset:1560
	ds_read_b32 v211, v219 offset:768
	ds_read_b32 v204, v218 offset:2080
	ds_read_b32 v212, v219 offset:1024
	ds_read_b32 v205, v218 offset:2600
	ds_read_b32 v213, v219 offset:1280
	ds_read_b32 v206, v218 offset:3120
	ds_read_b32 v214, v219 offset:1536
	s_waitcnt lgkmcnt(12)
	v_mfma_f32_32x32x2_f32 v[4:19], v200, v208, v[4:19]
	ds_read_b32 v207, v218 offset:3640
	ds_read_b32 v215, v219 offset:1792
	s_waitcnt lgkmcnt(12)
	v_mfma_f32_32x32x2_f32 v[4:19], v201, v209, v[4:19]
	s_waitcnt lgkmcnt(10)
	v_mfma_f32_32x32x2_f32 v[4:19], v202, v210, v[4:19]
	s_waitcnt lgkmcnt(8)
	v_mfma_f32_32x32x2_f32 v[4:19], v203, v211, v[4:19]
	s_waitcnt lgkmcnt(6)
	v_mfma_f32_32x32x2_f32 v[4:19], v204, v212, v[4:19]
	s_waitcnt lgkmcnt(4)
	v_mfma_f32_32x32x2_f32 v[4:19], v205, v213, v[4:19]
	s_waitcnt lgkmcnt(2)
	v_mfma_f32_32x32x2_f32 v[4:19], v206, v214, v[4:19]
	s_waitcnt lgkmcnt(0)
	v_mfma_f32_32x32x2_f32 v[4:19], v207, v215, v[4:19]
	s_barrier
	global_load_dwordx4 v[32:35], v[94:95], off offset:1408
	global_load_dwordx4 v[20:23], v[72:73], off
	s_waitcnt vmcnt(3)
	v_cvt_f32_f16_sdwa v130, v28 dst_sel:DWORD dst_unused:UNUSED_PAD src0_sel:WORD_1
	v_cvt_f32_f16_e32 v28, v28
	v_cvt_f32_f16_e32 v131, v29
	v_cvt_f32_f16_sdwa v132, v30 dst_sel:DWORD dst_unused:UNUSED_PAD src0_sel:WORD_1
	v_cvt_f32_f16_e32 v135, v30
	ds_read_b128 v[36:39], v43 offset:14848
	ds_read_b128 v[98:101], v43 offset:14864
	ds_read_b128 v[122:125], v43 offset:18944
	ds_read_b128 v[126:129], v43 offset:18960
	v_cvt_f32_f16_sdwa v97, v29 dst_sel:DWORD dst_unused:UNUSED_PAD src0_sel:WORD_1
	v_cvt_f32_f16_sdwa v133, v31 dst_sel:DWORD dst_unused:UNUSED_PAD src0_sel:WORD_1
	v_cvt_f32_f16_e32 v134, v31
	v_sub_f32_e32 v28, v28, v0
	v_sub_f32_e32 v29, v130, v1
	v_sub_f32_e32 v30, v131, v2
	v_pk_mul_f32 v[28:29], v[90:91], v[28:29]
	v_sub_f32_e32 v130, v135, v0
	v_sub_f32_e32 v131, v132, v1
	v_sub_f32_e32 v31, v97, v3
	v_sub_f32_e32 v132, v134, v2
	v_sub_f32_e32 v133, v133, v3
	v_pk_mul_f32 v[130:131], v[90:91], v[130:131]
	s_waitcnt lgkmcnt(1)
	v_fma_f32 v28, v36, v28, v122
	v_fma_f32 v29, v37, v29, v123
	v_pk_mul_f32 v[30:31], v[92:93], v[30:31]
	v_pk_mul_f32 v[132:133], v[92:93], v[132:133]
	s_waitcnt lgkmcnt(0)
	v_fma_f32 v36, v98, v130, v126
	ds_write2_b32 v220, v28, v29 offset1:65
	v_fma_f32 v28, v99, v131, v127
	ds_write2_b32 v221, v36, v28 offset1:65
	v_fma_f32 v28, v38, v30, v124
	v_fma_f32 v29, v100, v132, v128
	v_fmac_f32_e32 v125, v39, v31
	v_fmac_f32_e32 v129, v101, v133
	ds_write2_b32 v220, v28, v125 offset0:130 offset1:195
	ds_write2_b32 v221, v29, v129 offset0:130 offset1:195
	s_waitcnt vmcnt(2)
	ds_write_b128 v104, v[24:27] offset:41984
	s_mov_b32 s16, 0
	v_mov_b32_e32 v24, v112
	s_waitcnt lgkmcnt(0)
	s_barrier
	ds_read_b32 v200, v218
	ds_read_b32 v208, v219
	ds_read_b32 v201, v218 offset:520
	ds_read_b32 v209, v219 offset:256
	ds_read_b32 v202, v218 offset:1040
	ds_read_b32 v210, v219 offset:512
	ds_read_b32 v203, v218 offset:1560
	ds_read_b32 v211, v219 offset:768
	ds_read_b32 v204, v218 offset:2080
	ds_read_b32 v212, v219 offset:1024
	ds_read_b32 v205, v218 offset:2600
	ds_read_b32 v213, v219 offset:1280
	ds_read_b32 v206, v218 offset:3120
	ds_read_b32 v214, v219 offset:1536
	s_waitcnt lgkmcnt(12)
	v_mfma_f32_32x32x2_f32 v[4:19], v200, v208, v[4:19]
	ds_read_b32 v207, v218 offset:3640
	ds_read_b32 v215, v219 offset:1792
	s_waitcnt lgkmcnt(12)
	v_mfma_f32_32x32x2_f32 v[4:19], v201, v209, v[4:19]
	s_waitcnt lgkmcnt(10)
	v_mfma_f32_32x32x2_f32 v[4:19], v202, v210, v[4:19]
	s_waitcnt lgkmcnt(8)
	v_mfma_f32_32x32x2_f32 v[4:19], v203, v211, v[4:19]
	s_waitcnt lgkmcnt(6)
	v_mfma_f32_32x32x2_f32 v[4:19], v204, v212, v[4:19]
	s_waitcnt lgkmcnt(4)
	v_mfma_f32_32x32x2_f32 v[4:19], v205, v213, v[4:19]
	s_waitcnt lgkmcnt(2)
	v_mfma_f32_32x32x2_f32 v[4:19], v206, v214, v[4:19]
	s_waitcnt lgkmcnt(0)
	v_mfma_f32_32x32x2_f32 v[4:19], v207, v215, v[4:19]
	s_barrier
	global_load_dwordx4 v[28:31], v[94:95], off offset:1536
	global_load_dwordx4 v[24:27], v[74:75], off
	s_waitcnt vmcnt(3)
	v_cvt_f32_f16_sdwa v130, v32 dst_sel:DWORD dst_unused:UNUSED_PAD src0_sel:WORD_1
	v_cvt_f32_f16_e32 v32, v32
	v_cvt_f32_f16_e32 v131, v33
	v_cvt_f32_f16_sdwa v132, v34 dst_sel:DWORD dst_unused:UNUSED_PAD src0_sel:WORD_1
	v_cvt_f32_f16_e32 v135, v34
	ds_read_b128 v[36:39], v43 offset:15104
	ds_read_b128 v[98:101], v43 offset:15120
	ds_read_b128 v[122:125], v43 offset:19200
	ds_read_b128 v[126:129], v43 offset:19216
	v_cvt_f32_f16_sdwa v97, v33 dst_sel:DWORD dst_unused:UNUSED_PAD src0_sel:WORD_1
	v_cvt_f32_f16_sdwa v133, v35 dst_sel:DWORD dst_unused:UNUSED_PAD src0_sel:WORD_1
	v_cvt_f32_f16_e32 v134, v35
	v_sub_f32_e32 v32, v32, v0
	v_sub_f32_e32 v33, v130, v1
	v_sub_f32_e32 v34, v131, v2
	v_pk_mul_f32 v[32:33], v[90:91], v[32:33]
	v_sub_f32_e32 v130, v135, v0
	v_sub_f32_e32 v131, v132, v1
	v_sub_f32_e32 v35, v97, v3
	v_sub_f32_e32 v132, v134, v2
	v_sub_f32_e32 v133, v133, v3
	v_pk_mul_f32 v[130:131], v[90:91], v[130:131]
	s_waitcnt lgkmcnt(1)
	v_fma_f32 v32, v36, v32, v122
	v_fma_f32 v33, v37, v33, v123
	v_pk_mul_f32 v[34:35], v[92:93], v[34:35]
	v_pk_mul_f32 v[132:133], v[92:93], v[132:133]
	s_waitcnt lgkmcnt(0)
	v_fma_f32 v36, v98, v130, v126
	ds_write2_b32 v220, v32, v33 offset1:65
	v_fma_f32 v32, v99, v131, v127
	ds_write2_b32 v221, v36, v32 offset1:65
	v_fma_f32 v32, v38, v34, v124
	v_fma_f32 v33, v100, v132, v128
	v_fmac_f32_e32 v125, v39, v35
	v_fmac_f32_e32 v129, v101, v133
	ds_write2_b32 v220, v32, v125 offset0:130 offset1:195
	ds_write2_b32 v221, v33, v129 offset0:130 offset1:195
	s_waitcnt vmcnt(2)
	ds_write_b128 v104, v[20:23] offset:41984
	s_mov_b32 s16, 0
	v_mov_b32_e32 v20, v112
	s_waitcnt lgkmcnt(0)
	s_barrier
	ds_read_b32 v200, v218
	ds_read_b32 v208, v219
	ds_read_b32 v201, v218 offset:520
	ds_read_b32 v209, v219 offset:256
	ds_read_b32 v202, v218 offset:1040
	ds_read_b32 v210, v219 offset:512
	ds_read_b32 v203, v218 offset:1560
	ds_read_b32 v211, v219 offset:768
	ds_read_b32 v204, v218 offset:2080
	ds_read_b32 v212, v219 offset:1024
	ds_read_b32 v205, v218 offset:2600
	ds_read_b32 v213, v219 offset:1280
	ds_read_b32 v206, v218 offset:3120
	ds_read_b32 v214, v219 offset:1536
	s_waitcnt lgkmcnt(12)
	v_mfma_f32_32x32x2_f32 v[4:19], v200, v208, v[4:19]
	ds_read_b32 v207, v218 offset:3640
	ds_read_b32 v215, v219 offset:1792
	s_waitcnt lgkmcnt(12)
	v_mfma_f32_32x32x2_f32 v[4:19], v201, v209, v[4:19]
	s_waitcnt lgkmcnt(10)
	v_mfma_f32_32x32x2_f32 v[4:19], v202, v210, v[4:19]
	s_waitcnt lgkmcnt(8)
	v_mfma_f32_32x32x2_f32 v[4:19], v203, v211, v[4:19]
	s_waitcnt lgkmcnt(6)
	v_mfma_f32_32x32x2_f32 v[4:19], v204, v212, v[4:19]
	s_waitcnt lgkmcnt(4)
	v_mfma_f32_32x32x2_f32 v[4:19], v205, v213, v[4:19]
	s_waitcnt lgkmcnt(2)
	v_mfma_f32_32x32x2_f32 v[4:19], v206, v214, v[4:19]
	s_waitcnt lgkmcnt(0)
	v_mfma_f32_32x32x2_f32 v[4:19], v207, v215, v[4:19]
	s_barrier
	global_load_dwordx4 v[32:35], v[94:95], off offset:1664
	global_load_dwordx4 v[20:23], v[76:77], off
	s_waitcnt vmcnt(3)
	v_cvt_f32_f16_sdwa v130, v28 dst_sel:DWORD dst_unused:UNUSED_PAD src0_sel:WORD_1
	v_cvt_f32_f16_e32 v28, v28
	v_cvt_f32_f16_e32 v131, v29
	v_cvt_f32_f16_sdwa v132, v30 dst_sel:DWORD dst_unused:UNUSED_PAD src0_sel:WORD_1
	v_cvt_f32_f16_e32 v135, v30
	ds_read_b128 v[36:39], v43 offset:15360
	ds_read_b128 v[98:101], v43 offset:15376
	ds_read_b128 v[122:125], v43 offset:19456
	ds_read_b128 v[126:129], v43 offset:19472
	v_cvt_f32_f16_sdwa v97, v29 dst_sel:DWORD dst_unused:UNUSED_PAD src0_sel:WORD_1
	v_cvt_f32_f16_sdwa v133, v31 dst_sel:DWORD dst_unused:UNUSED_PAD src0_sel:WORD_1
	v_cvt_f32_f16_e32 v134, v31
	v_sub_f32_e32 v28, v28, v0
	v_sub_f32_e32 v29, v130, v1
	v_sub_f32_e32 v30, v131, v2
	v_pk_mul_f32 v[28:29], v[90:91], v[28:29]
	v_sub_f32_e32 v130, v135, v0
	v_sub_f32_e32 v131, v132, v1
	v_sub_f32_e32 v31, v97, v3
	v_sub_f32_e32 v132, v134, v2
	v_sub_f32_e32 v133, v133, v3
	v_pk_mul_f32 v[130:131], v[90:91], v[130:131]
	s_waitcnt lgkmcnt(1)
	v_fma_f32 v28, v36, v28, v122
	v_fma_f32 v29, v37, v29, v123
	v_pk_mul_f32 v[30:31], v[92:93], v[30:31]
	v_pk_mul_f32 v[132:133], v[92:93], v[132:133]
	s_waitcnt lgkmcnt(0)
	v_fma_f32 v36, v98, v130, v126
	ds_write2_b32 v220, v28, v29 offset1:65
	v_fma_f32 v28, v99, v131, v127
	ds_write2_b32 v221, v36, v28 offset1:65
	v_fma_f32 v28, v38, v30, v124
	v_fma_f32 v29, v100, v132, v128
	v_fmac_f32_e32 v125, v39, v31
	v_fmac_f32_e32 v129, v101, v133
	ds_write2_b32 v220, v28, v125 offset0:130 offset1:195
	ds_write2_b32 v221, v29, v129 offset0:130 offset1:195
	s_waitcnt vmcnt(2)
	ds_write_b128 v104, v[24:27] offset:41984
	s_mov_b32 s16, 0
	v_mov_b32_e32 v24, v112
	s_waitcnt lgkmcnt(0)
	s_barrier
	ds_read_b32 v200, v218
	ds_read_b32 v208, v219
	ds_read_b32 v201, v218 offset:520
	ds_read_b32 v209, v219 offset:256
	ds_read_b32 v202, v218 offset:1040
	ds_read_b32 v210, v219 offset:512
	ds_read_b32 v203, v218 offset:1560
	ds_read_b32 v211, v219 offset:768
	ds_read_b32 v204, v218 offset:2080
	ds_read_b32 v212, v219 offset:1024
	ds_read_b32 v205, v218 offset:2600
	ds_read_b32 v213, v219 offset:1280
	ds_read_b32 v206, v218 offset:3120
	ds_read_b32 v214, v219 offset:1536
	s_waitcnt lgkmcnt(12)
	v_mfma_f32_32x32x2_f32 v[4:19], v200, v208, v[4:19]
	ds_read_b32 v207, v218 offset:3640
	ds_read_b32 v215, v219 offset:1792
	s_waitcnt lgkmcnt(12)
	v_mfma_f32_32x32x2_f32 v[4:19], v201, v209, v[4:19]
	s_waitcnt lgkmcnt(10)
	v_mfma_f32_32x32x2_f32 v[4:19], v202, v210, v[4:19]
	s_waitcnt lgkmcnt(8)
	v_mfma_f32_32x32x2_f32 v[4:19], v203, v211, v[4:19]
	s_waitcnt lgkmcnt(6)
	v_mfma_f32_32x32x2_f32 v[4:19], v204, v212, v[4:19]
	s_waitcnt lgkmcnt(4)
	v_mfma_f32_32x32x2_f32 v[4:19], v205, v213, v[4:19]
	s_waitcnt lgkmcnt(2)
	v_mfma_f32_32x32x2_f32 v[4:19], v206, v214, v[4:19]
	s_waitcnt lgkmcnt(0)
	v_mfma_f32_32x32x2_f32 v[4:19], v207, v215, v[4:19]
	s_barrier
	global_load_dwordx4 v[28:31], v[94:95], off offset:1792
	global_load_dwordx4 v[24:27], v[78:79], off
	s_waitcnt vmcnt(3)
	v_cvt_f32_f16_sdwa v130, v32 dst_sel:DWORD dst_unused:UNUSED_PAD src0_sel:WORD_1
	v_cvt_f32_f16_e32 v32, v32
	v_cvt_f32_f16_e32 v131, v33
	v_cvt_f32_f16_sdwa v132, v34 dst_sel:DWORD dst_unused:UNUSED_PAD src0_sel:WORD_1
	v_cvt_f32_f16_e32 v135, v34
	ds_read_b128 v[36:39], v43 offset:15616
	ds_read_b128 v[98:101], v43 offset:15632
	ds_read_b128 v[122:125], v43 offset:19712
	ds_read_b128 v[126:129], v43 offset:19728
	v_cvt_f32_f16_sdwa v97, v33 dst_sel:DWORD dst_unused:UNUSED_PAD src0_sel:WORD_1
	v_cvt_f32_f16_sdwa v133, v35 dst_sel:DWORD dst_unused:UNUSED_PAD src0_sel:WORD_1
	v_cvt_f32_f16_e32 v134, v35
	v_sub_f32_e32 v32, v32, v0
	v_sub_f32_e32 v33, v130, v1
	v_sub_f32_e32 v34, v131, v2
	v_pk_mul_f32 v[32:33], v[90:91], v[32:33]
	v_sub_f32_e32 v130, v135, v0
	v_sub_f32_e32 v131, v132, v1
	v_sub_f32_e32 v35, v97, v3
	v_sub_f32_e32 v132, v134, v2
	v_sub_f32_e32 v133, v133, v3
	v_pk_mul_f32 v[130:131], v[90:91], v[130:131]
	s_waitcnt lgkmcnt(1)
	v_fma_f32 v32, v36, v32, v122
	v_fma_f32 v33, v37, v33, v123
	v_pk_mul_f32 v[34:35], v[92:93], v[34:35]
	v_pk_mul_f32 v[132:133], v[92:93], v[132:133]
	s_waitcnt lgkmcnt(0)
	v_fma_f32 v36, v98, v130, v126
	ds_write2_b32 v220, v32, v33 offset1:65
	v_fma_f32 v32, v99, v131, v127
	ds_write2_b32 v221, v36, v32 offset1:65
	v_fma_f32 v32, v38, v34, v124
	v_fma_f32 v33, v100, v132, v128
	v_fmac_f32_e32 v125, v39, v35
	v_fmac_f32_e32 v129, v101, v133
	ds_write2_b32 v220, v32, v125 offset0:130 offset1:195
	ds_write2_b32 v221, v33, v129 offset0:130 offset1:195
	s_waitcnt vmcnt(2)
	ds_write_b128 v104, v[20:23] offset:41984
	s_mov_b32 s16, 0
	v_mov_b32_e32 v20, v112
	s_waitcnt lgkmcnt(0)
	s_barrier
	ds_read_b32 v200, v218
	ds_read_b32 v208, v219
	ds_read_b32 v201, v218 offset:520
	ds_read_b32 v209, v219 offset:256
	ds_read_b32 v202, v218 offset:1040
	ds_read_b32 v210, v219 offset:512
	ds_read_b32 v203, v218 offset:1560
	ds_read_b32 v211, v219 offset:768
	ds_read_b32 v204, v218 offset:2080
	ds_read_b32 v212, v219 offset:1024
	ds_read_b32 v205, v218 offset:2600
	ds_read_b32 v213, v219 offset:1280
	ds_read_b32 v206, v218 offset:3120
	ds_read_b32 v214, v219 offset:1536
	s_waitcnt lgkmcnt(12)
	v_mfma_f32_32x32x2_f32 v[4:19], v200, v208, v[4:19]
	ds_read_b32 v207, v218 offset:3640
	ds_read_b32 v215, v219 offset:1792
	s_waitcnt lgkmcnt(12)
	v_mfma_f32_32x32x2_f32 v[4:19], v201, v209, v[4:19]
	s_waitcnt lgkmcnt(10)
	v_mfma_f32_32x32x2_f32 v[4:19], v202, v210, v[4:19]
	s_waitcnt lgkmcnt(8)
	v_mfma_f32_32x32x2_f32 v[4:19], v203, v211, v[4:19]
	s_waitcnt lgkmcnt(6)
	v_mfma_f32_32x32x2_f32 v[4:19], v204, v212, v[4:19]
	s_waitcnt lgkmcnt(4)
	v_mfma_f32_32x32x2_f32 v[4:19], v205, v213, v[4:19]
	s_waitcnt lgkmcnt(2)
	v_mfma_f32_32x32x2_f32 v[4:19], v206, v214, v[4:19]
	s_waitcnt lgkmcnt(0)
	v_mfma_f32_32x32x2_f32 v[4:19], v207, v215, v[4:19]
	s_barrier
	global_load_dwordx4 v[32:35], v[94:95], off offset:1920
	global_load_dwordx4 v[20:23], v[80:81], off
	s_waitcnt vmcnt(3)
	v_cvt_f32_f16_sdwa v95, v28 dst_sel:DWORD dst_unused:UNUSED_PAD src0_sel:WORD_1
	v_cvt_f32_f16_e32 v28, v28
	v_cvt_f32_f16_sdwa v94, v29 dst_sel:DWORD dst_unused:UNUSED_PAD src0_sel:WORD_1
	v_cvt_f32_f16_sdwa v130, v30 dst_sel:DWORD dst_unused:UNUSED_PAD src0_sel:WORD_1
	v_cvt_f32_f16_e32 v133, v30
	ds_read_b128 v[36:39], v43 offset:15872
	ds_read_b128 v[98:101], v43 offset:15888
	ds_read_b128 v[122:125], v43 offset:19968
	ds_read_b128 v[126:129], v43 offset:19984
	v_cvt_f32_f16_e32 v97, v29
	v_cvt_f32_f16_sdwa v131, v31 dst_sel:DWORD dst_unused:UNUSED_PAD src0_sel:WORD_1
	v_cvt_f32_f16_e32 v132, v31
	v_sub_f32_e32 v28, v28, v0
	v_sub_f32_e32 v29, v95, v1
	v_sub_f32_e32 v31, v94, v3
	v_pk_mul_f32 v[28:29], v[90:91], v[28:29]
	v_sub_f32_e32 v94, v133, v0
	v_sub_f32_e32 v95, v130, v1
	v_sub_f32_e32 v30, v97, v2
	v_sub_f32_e32 v130, v132, v2
	v_sub_f32_e32 v131, v131, v3
	v_pk_mul_f32 v[94:95], v[90:91], v[94:95]
	s_waitcnt lgkmcnt(1)
	v_fma_f32 v28, v36, v28, v122
	v_fma_f32 v29, v37, v29, v123
	v_pk_mul_f32 v[30:31], v[92:93], v[30:31]
	v_pk_mul_f32 v[130:131], v[92:93], v[130:131]
	s_waitcnt lgkmcnt(0)
	v_fma_f32 v36, v98, v94, v126
	ds_write2_b32 v220, v28, v29 offset1:65
	v_fma_f32 v28, v99, v95, v127
	ds_write2_b32 v221, v36, v28 offset1:65
	v_fma_f32 v28, v38, v30, v124
	v_fma_f32 v29, v100, v130, v128
	v_fmac_f32_e32 v125, v39, v31
	v_fmac_f32_e32 v129, v101, v131
	ds_write2_b32 v220, v28, v125 offset0:130 offset1:195
	ds_write2_b32 v221, v29, v129 offset0:130 offset1:195
	s_waitcnt vmcnt(2)
	ds_write_b128 v104, v[24:27] offset:41984
	s_mov_b32 s16, 0
	v_mov_b32_e32 v24, v112
	s_waitcnt lgkmcnt(0)
	s_barrier
	ds_read_b32 v200, v218
	ds_read_b32 v208, v219
	ds_read_b32 v201, v218 offset:520
	ds_read_b32 v209, v219 offset:256
	ds_read_b32 v202, v218 offset:1040
	ds_read_b32 v210, v219 offset:512
	ds_read_b32 v203, v218 offset:1560
	ds_read_b32 v211, v219 offset:768
	ds_read_b32 v204, v218 offset:2080
	ds_read_b32 v212, v219 offset:1024
	ds_read_b32 v205, v218 offset:2600
	ds_read_b32 v213, v219 offset:1280
	ds_read_b32 v206, v218 offset:3120
	ds_read_b32 v214, v219 offset:1536
	s_waitcnt lgkmcnt(12)
	v_mfma_f32_32x32x2_f32 v[4:19], v200, v208, v[4:19]
	ds_read_b32 v207, v218 offset:3640
	ds_read_b32 v215, v219 offset:1792
	s_waitcnt lgkmcnt(12)
	v_mfma_f32_32x32x2_f32 v[4:19], v201, v209, v[4:19]
	s_waitcnt lgkmcnt(10)
	v_mfma_f32_32x32x2_f32 v[4:19], v202, v210, v[4:19]
	s_waitcnt lgkmcnt(8)
	v_mfma_f32_32x32x2_f32 v[4:19], v203, v211, v[4:19]
	s_waitcnt lgkmcnt(6)
	v_mfma_f32_32x32x2_f32 v[4:19], v204, v212, v[4:19]
	s_waitcnt lgkmcnt(4)
	v_mfma_f32_32x32x2_f32 v[4:19], v205, v213, v[4:19]
	s_waitcnt lgkmcnt(2)
	v_mfma_f32_32x32x2_f32 v[4:19], v206, v214, v[4:19]
	s_waitcnt lgkmcnt(0)
	v_mfma_f32_32x32x2_f32 v[4:19], v207, v215, v[4:19]
	s_waitcnt vmcnt(1)
	v_cvt_f32_f16_sdwa v95, v32 dst_sel:DWORD dst_unused:UNUSED_PAD src0_sel:WORD_1
	v_cvt_f32_f16_e32 v32, v32
	v_cvt_f32_f16_sdwa v123, v34 dst_sel:DWORD dst_unused:UNUSED_PAD src0_sel:WORD_1
	v_cvt_f32_f16_e32 v125, v34
	s_barrier
	ds_read_b128 v[24:27], v43 offset:16128
	ds_read_b128 v[28:31], v43 offset:16144
	ds_read_b128 v[36:39], v43 offset:20224
	ds_read_b128 v[98:101], v43 offset:20240
	v_cvt_f32_f16_sdwa v94, v33 dst_sel:DWORD dst_unused:UNUSED_PAD src0_sel:WORD_1
	v_cvt_f32_f16_e32 v97, v33
	v_cvt_f32_f16_sdwa v122, v35 dst_sel:DWORD dst_unused:UNUSED_PAD src0_sel:WORD_1
	v_cvt_f32_f16_e32 v124, v35
	v_sub_f32_e32 v32, v32, v0
	v_sub_f32_e32 v33, v95, v1
	v_sub_f32_e32 v0, v125, v0
	v_sub_f32_e32 v1, v123, v1
	v_sub_f32_e32 v34, v97, v2
	v_sub_f32_e32 v35, v94, v3
	v_pk_mul_f32 v[0:1], v[90:91], v[0:1]
	v_pk_mul_f32 v[34:35], v[92:93], v[34:35]
	v_sub_f32_e32 v2, v124, v2
	v_sub_f32_e32 v3, v122, v3
	s_waitcnt lgkmcnt(0)
	v_fma_f32 v0, v28, v0, v98
	v_fma_f32 v1, v29, v1, v99
	v_pk_mul_f32 v[32:33], v[90:91], v[32:33]
	v_pk_mul_f32 v[2:3], v[92:93], v[2:3]
	ds_write2_b32 v221, v0, v1 offset1:65
	v_fma_f32 v0, v26, v34, v38
	v_fmac_f32_e32 v39, v27, v35
	v_fma_f32 v24, v24, v32, v36
	v_fma_f32 v25, v25, v33, v37
	v_fma_f32 v1, v30, v2, v100
	ds_write2_b32 v220, v0, v39 offset0:130 offset1:195
	v_fmac_f32_e32 v101, v31, v3
	s_mov_b32 s16, 0
	v_mov_b32_e32 v0, v112
	ds_write2_b32 v220, v24, v25 offset1:65
	ds_write2_b32 v221, v1, v101 offset0:130 offset1:195
	s_waitcnt vmcnt(0)
	ds_write_b128 v104, v[20:23] offset:41984
	s_waitcnt lgkmcnt(0)
	s_barrier
	ds_read_b32 v200, v218
	ds_read_b32 v208, v219
	ds_read_b32 v201, v218 offset:520
	ds_read_b32 v209, v219 offset:256
	ds_read_b32 v202, v218 offset:1040
	ds_read_b32 v210, v219 offset:512
	ds_read_b32 v203, v218 offset:1560
	ds_read_b32 v211, v219 offset:768
	ds_read_b32 v204, v218 offset:2080
	ds_read_b32 v212, v219 offset:1024
	ds_read_b32 v205, v218 offset:2600
	ds_read_b32 v213, v219 offset:1280
	ds_read_b32 v206, v218 offset:3120
	ds_read_b32 v214, v219 offset:1536
	s_waitcnt lgkmcnt(12)
	v_mfma_f32_32x32x2_f32 v[4:19], v200, v208, v[4:19]
	ds_read_b32 v207, v218 offset:3640
	ds_read_b32 v215, v219 offset:1792
	s_waitcnt lgkmcnt(12)
	v_mfma_f32_32x32x2_f32 v[4:19], v201, v209, v[4:19]
	s_waitcnt lgkmcnt(10)
	v_mfma_f32_32x32x2_f32 v[4:19], v202, v210, v[4:19]
	s_waitcnt lgkmcnt(8)
	v_mfma_f32_32x32x2_f32 v[4:19], v203, v211, v[4:19]
	s_waitcnt lgkmcnt(6)
	v_mfma_f32_32x32x2_f32 v[4:19], v204, v212, v[4:19]
	s_waitcnt lgkmcnt(4)
	v_mfma_f32_32x32x2_f32 v[4:19], v205, v213, v[4:19]
	s_waitcnt lgkmcnt(2)
	v_mfma_f32_32x32x2_f32 v[4:19], v206, v214, v[4:19]
	s_waitcnt lgkmcnt(0)
	v_mfma_f32_32x32x2_f32 v[4:19], v207, v215, v[4:19]
	s_barrier
	s_nop 15
	s_nop 3
	ds_write_b32 v217, v4 offset:58752
	ds_write_b32 v217, v5 offset:58880
	ds_write_b32 v217, v6 offset:59008
	ds_write_b32 v217, v7 offset:59136
	ds_write_b32 v217, v8 offset:59776
	ds_write_b32 v217, v9 offset:59904
	ds_write_b32 v217, v10 offset:60032
	ds_write_b32 v217, v11 offset:60160
	ds_write_b32 v217, v12 offset:60800
	ds_write_b32 v217, v13 offset:60928
	ds_write_b32 v217, v14 offset:61056
	ds_write_b32 v217, v15 offset:61184
	ds_write_b32 v217, v16 offset:61824
	ds_write_b32 v217, v17 offset:61952
	ds_write_b32 v217, v18 offset:62080
	ds_write_b32 v217, v19 offset:62208
	s_waitcnt lgkmcnt(0)
	s_barrier
	global_load_dwordx4 v[0:3], v[50:51], off
	ds_read_b128 v[4:7], v106 offset:58752
	ds_read_b128 v[8:11], v107 offset:8192
	ds_read_b128 v[12:15], v107 offset:16384
	ds_read_b128 v[16:19], v107 offset:24576
	v_add_u32_e32 v20, 0xc400, v108
	v_add_u32_e32 v21, 0xc408, v108
	s_waitcnt lgkmcnt(2)
	v_pk_add_f32 v[4:5], v[4:5], v[8:9]
	v_pk_add_f32 v[6:7], v[6:7], v[10:11]
	s_waitcnt lgkmcnt(1)
	v_pk_add_f32 v[4:5], v[12:13], v[4:5]
	v_pk_add_f32 v[6:7], v[14:15], v[6:7]
	s_waitcnt lgkmcnt(0)
	v_pk_add_f32 v[4:5], v[16:17], v[4:5]
	v_pk_add_f32 v[6:7], v[18:19], v[6:7]
	s_waitcnt vmcnt(0)
	v_pk_add_f32 v[0:1], v[0:1], v[4:5]
	v_pk_add_f32 v[2:3], v[6:7], v[2:3]
	ds_write2_b32 v20, v0, v1 offset1:1
	ds_write2_b32 v21, v2, v3 offset1:1
	s_waitcnt lgkmcnt(0)
	s_barrier
	s_and_saveexec_b64 s[28:29], s[6:7]
	s_cbranch_execz .LBB0_687
	v_add_u32_e32 v0, 0xc400, v117
	v_add_u32_e32 v1, 0xc408, v117
	v_add_u32_e32 v2, 0xc410, v117
	v_add_u32_e32 v3, 0xc418, v117
	ds_read2_b32 v[34:35], v0 offset1:1
	ds_read2_b32 v[30:31], v1 offset1:1
	ds_read2_b32 v[22:23], v2 offset1:1
	ds_read2_b32 v[10:11], v3 offset1:1
	s_mov_b32 s16, 0xff61b1e6
	s_waitcnt lgkmcnt(3)
	v_max_f32_e32 v0, v34, v34
	v_max_f32_e32 v0, 0xff61b1e6, v0
	v_cmp_lt_f32_e32 vcc, s16, v34
	v_cmp_gt_f32_e64 s[16:17], v35, v0
	v_add_u32_e32 v2, 0xc420, v117
	ds_read2_b32 v[24:25], v2 offset1:1
	v_cndmask_b32_e64 v0, v0, v35, s[16:17]
	v_cndmask_b32_e64 v1, 0, 1, s[16:17]
	s_waitcnt lgkmcnt(3)
	v_cmp_gt_f32_e64 s[16:17], v30, v0
	v_add_u32_e32 v2, 0xc428, v117
	v_add_u32_e32 v3, 0xc430, v117
	v_cndmask_b32_e64 v0, v0, v30, s[16:17]
	v_cndmask_b32_e64 v1, v1, 2, s[16:17]
	v_cmp_gt_f32_e64 s[16:17], v31, v0
	v_add_u32_e32 v4, 0xc438, v117
	ds_read2_b32 v[32:33], v2 offset1:1
	ds_read2_b32 v[20:21], v3 offset1:1
	ds_read2_b32 v[6:7], v4 offset1:1
	v_cndmask_b32_e64 v0, v0, v31, s[16:17]
	v_cndmask_b32_e64 v1, v1, 3, s[16:17]
	s_waitcnt lgkmcnt(5)
	v_cmp_gt_f32_e64 s[16:17], v22, v0
	v_add_u32_e32 v2, 0xc440, v117
	ds_read2_b32 v[18:19], v2 offset1:1
	v_cndmask_b32_e64 v0, v0, v22, s[16:17]
	v_cndmask_b32_e64 v1, v1, 4, s[16:17]
	v_cmp_gt_f32_e64 s[16:17], v23, v0
	v_add_u32_e32 v2, 0xc448, v117
	v_add_u32_e32 v4, 0xc458, v117
	v_cndmask_b32_e64 v0, v0, v23, s[16:17]
	v_cndmask_b32_e64 v1, v1, 5, s[16:17]
	s_waitcnt lgkmcnt(5)
	v_cmp_gt_f32_e64 s[16:17], v10, v0
	v_add_u32_e32 v3, 0xc450, v117
	ds_read2_b32 v[26:27], v2 offset1:1
	ds_read2_b32 v[12:13], v3 offset1:1
	ds_read2_b32 v[4:5], v4 offset1:1
	v_cndmask_b32_e64 v0, v0, v10, s[16:17]
	v_cndmask_b32_e64 v1, v1, 6, s[16:17]
	v_cmp_gt_f32_e64 s[16:17], v11, v0
	v_add_u32_e32 v2, 0xc460, v117
	ds_read2_b32 v[14:15], v2 offset1:1
	v_cndmask_b32_e64 v0, v0, v11, s[16:17]
	v_cndmask_b32_e64 v1, v1, 7, s[16:17]
	s_waitcnt lgkmcnt(8)
	v_cmp_gt_f32_e64 s[16:17], v24, v0
	v_add_u32_e32 v2, 0xc468, v117
	v_add_u32_e32 v8, 0xc478, v117
	v_cndmask_b32_e64 v0, v0, v24, s[16:17]
	v_cndmask_b32_e64 v1, v1, 8, s[16:17]
	v_cmp_gt_f32_e64 s[16:17], v25, v0
	v_add_u32_e32 v3, 0xc470, v117
	ds_read2_b32 v[28:29], v2 offset1:1
	ds_read2_b32 v[16:17], v3 offset1:1
	ds_read2_b32 v[8:9], v8 offset1:1
	v_cndmask_b32_e64 v0, v0, v25, s[16:17]
	v_cndmask_b32_e64 v1, v1, 9, s[16:17]
	s_waitcnt lgkmcnt(10)
	v_cmp_gt_f32_e64 s[16:17], v32, v0
	s_nop 1
	v_cndmask_b32_e64 v0, v0, v32, s[16:17]
	v_cndmask_b32_e64 v1, v1, 10, s[16:17]
	v_cmp_gt_f32_e64 s[16:17], v33, v0
	s_nop 1
	v_cndmask_b32_e64 v0, v0, v33, s[16:17]
	v_cndmask_b32_e64 v1, v1, 11, s[16:17]
	s_waitcnt lgkmcnt(9)
	v_cmp_gt_f32_e64 s[16:17], v20, v0
	s_nop 1
	v_cndmask_b32_e64 v0, v0, v20, s[16:17]
	v_cndmask_b32_e64 v1, v1, 12, s[16:17]
	v_cmp_gt_f32_e64 s[16:17], v21, v0
	s_nop 1
	v_cndmask_b32_e64 v0, v0, v21, s[16:17]
	v_cndmask_b32_e64 v1, v1, 13, s[16:17]
	s_waitcnt lgkmcnt(8)
	v_cmp_gt_f32_e64 s[16:17], v6, v0
	s_nop 1
	v_cndmask_b32_e64 v0, v0, v6, s[16:17]
	v_cndmask_b32_e64 v1, v1, 14, s[16:17]
	v_cmp_gt_f32_e64 s[16:17], v7, v0
	s_nop 1
	v_cndmask_b32_e64 v0, v0, v7, s[16:17]
	v_cndmask_b32_e64 v1, v1, 15, s[16:17]
	s_waitcnt lgkmcnt(7)
	v_cmp_gt_f32_e64 s[16:17], v18, v0
	s_nop 1
	v_cndmask_b32_e64 v0, v0, v18, s[16:17]
	v_cndmask_b32_e64 v1, v1, 16, s[16:17]
	v_cmp_gt_f32_e64 s[16:17], v19, v0
	s_nop 1
	v_cndmask_b32_e64 v0, v0, v19, s[16:17]
	v_cndmask_b32_e64 v1, v1, 17, s[16:17]
	s_waitcnt lgkmcnt(6)
	v_cmp_gt_f32_e64 s[16:17], v26, v0
	s_nop 1
	v_cndmask_b32_e64 v0, v0, v26, s[16:17]
	v_cndmask_b32_e64 v1, v1, 18, s[16:17]
	v_cmp_gt_f32_e64 s[16:17], v27, v0
	s_nop 1
	v_cndmask_b32_e64 v0, v0, v27, s[16:17]
	v_cndmask_b32_e64 v1, v1, 19, s[16:17]
	s_waitcnt lgkmcnt(5)
	v_cmp_gt_f32_e64 s[16:17], v12, v0
	s_nop 1
	v_cndmask_b32_e64 v0, v0, v12, s[16:17]
	v_cndmask_b32_e64 v1, v1, 20, s[16:17]
	v_cmp_gt_f32_e64 s[16:17], v13, v0
	s_nop 1
	v_cndmask_b32_e64 v0, v0, v13, s[16:17]
	v_cndmask_b32_e64 v1, v1, 21, s[16:17]
	s_waitcnt lgkmcnt(4)
	v_cmp_gt_f32_e64 s[16:17], v4, v0
	s_nop 1
	v_cndmask_b32_e64 v0, v0, v4, s[16:17]
	v_cndmask_b32_e64 v1, v1, 22, s[16:17]
	v_cmp_gt_f32_e64 s[16:17], v5, v0
	s_nop 1
	v_cndmask_b32_e64 v0, v0, v5, s[16:17]
	v_cndmask_b32_e64 v1, v1, 23, s[16:17]
	s_waitcnt lgkmcnt(3)
	v_cmp_gt_f32_e64 s[16:17], v14, v0
	s_nop 1
	v_cndmask_b32_e64 v0, v0, v14, s[16:17]
	v_cndmask_b32_e64 v1, v1, 24, s[16:17]
	v_cmp_gt_f32_e64 s[16:17], v15, v0
	s_nop 1
	v_cndmask_b32_e64 v0, v0, v15, s[16:17]
	v_cndmask_b32_e64 v1, v1, 25, s[16:17]
	s_waitcnt lgkmcnt(2)
	v_cmp_gt_f32_e64 s[16:17], v28, v0
	s_nop 1
	v_cndmask_b32_e64 v0, v0, v28, s[16:17]
	v_cndmask_b32_e64 v1, v1, 26, s[16:17]
	v_cmp_gt_f32_e64 s[16:17], v29, v0
	s_nop 1
	v_cndmask_b32_e64 v0, v0, v29, s[16:17]
	v_cndmask_b32_e64 v1, v1, 27, s[16:17]
	s_waitcnt lgkmcnt(1)
	v_cmp_gt_f32_e64 s[16:17], v16, v0
	s_nop 1
	v_cndmask_b32_e64 v0, v0, v16, s[16:17]
	v_cndmask_b32_e64 v1, v1, 28, s[16:17]
	v_cmp_gt_f32_e64 s[16:17], v17, v0
	s_nop 1
	v_cndmask_b32_e64 v0, v0, v17, s[16:17]
	v_cndmask_b32_e64 v1, v1, 29, s[16:17]
	s_waitcnt lgkmcnt(0)
	v_cmp_gt_f32_e64 s[16:17], v8, v0
	s_nop 1
	v_cndmask_b32_e64 v0, v0, v8, s[16:17]
	v_cndmask_b32_e64 v1, v1, 30, s[16:17]
	v_cmp_gt_f32_e64 s[16:17], v9, v0
	s_nop 1
	v_cndmask_b32_e64 v36, v0, v9, s[16:17]
	v_cndmask_b32_e64 v0, v1, 31, s[16:17]
	v_cmp_ne_u32_e64 s[16:17], 0, v0
	v_lshlrev_b32_e64 v2, v0, 1
	s_and_b64 s[16:17], s[16:17], vcc
	v_cndmask_b32_e64 v1, v121, v34, s[16:17]
	v_and_b32_e32 v3, 2, v2
	v_cmp_eq_u32_e64 s[16:17], 0, v3
	v_cmp_gt_f32_e64 s[18:19], v35, v1
	s_and_b64 s[16:17], s[16:17], s[18:19]
	v_cndmask_b32_e64 v1, v1, v35, s[16:17]
	v_and_b32_e32 v37, 4, v2
	v_cndmask_b32_e64 v3, 0, 1, s[16:17]
	v_cmp_eq_u32_e64 s[16:17], 0, v37
	v_cmp_gt_f32_e64 s[18:19], v30, v1
	s_and_b64 s[16:17], s[16:17], s[18:19]
	v_cndmask_b32_e64 v1, v1, v30, s[16:17]
	v_and_b32_e32 v37, 8, v2
	v_cndmask_b32_e64 v3, v3, 2, s[16:17]
	v_cmp_eq_u32_e64 s[16:17], 0, v37
	v_cmp_gt_f32_e64 s[18:19], v31, v1
	s_and_b64 s[16:17], s[16:17], s[18:19]
	v_cndmask_b32_e64 v1, v1, v31, s[16:17]
	v_and_b32_e32 v37, 16, v2
	v_cndmask_b32_e64 v3, v3, 3, s[16:17]
	v_cmp_eq_u32_e64 s[16:17], 0, v37
	v_cmp_gt_f32_e64 s[18:19], v22, v1
	s_and_b64 s[16:17], s[16:17], s[18:19]
	v_cndmask_b32_e64 v1, v1, v22, s[16:17]
	v_and_b32_e32 v37, 32, v2
	v_cndmask_b32_e64 v3, v3, 4, s[16:17]
	v_cmp_eq_u32_e64 s[16:17], 0, v37
	v_cmp_gt_f32_e64 s[18:19], v23, v1
	s_and_b64 s[16:17], s[16:17], s[18:19]
	v_cndmask_b32_e64 v1, v1, v23, s[16:17]
	v_and_b32_e32 v37, 64, v2
	v_cndmask_b32_e64 v3, v3, 5, s[16:17]
	v_cmp_eq_u32_e64 s[16:17], 0, v37
	v_cmp_gt_f32_e64 s[18:19], v10, v1
	s_and_b64 s[16:17], s[16:17], s[18:19]
	v_cndmask_b32_e64 v1, v1, v10, s[16:17]
	v_and_b32_e32 v37, 0x80, v2
	v_cndmask_b32_e64 v3, v3, 6, s[16:17]
	v_cmp_eq_u32_e64 s[16:17], 0, v37
	v_cmp_gt_f32_e64 s[18:19], v11, v1
	s_and_b64 s[16:17], s[16:17], s[18:19]
	v_cndmask_b32_e64 v1, v1, v11, s[16:17]
	v_and_b32_e32 v37, 0x100, v2
	v_cndmask_b32_e64 v3, v3, 7, s[16:17]
	v_cmp_eq_u32_e64 s[16:17], 0, v37
	v_cmp_gt_f32_e64 s[18:19], v24, v1
	s_and_b64 s[16:17], s[16:17], s[18:19]
	v_cndmask_b32_e64 v1, v1, v24, s[16:17]
	v_and_b32_e32 v37, 0x200, v2
	v_cndmask_b32_e64 v3, v3, 8, s[16:17]
	v_cmp_eq_u32_e64 s[16:17], 0, v37
	v_cmp_gt_f32_e64 s[18:19], v25, v1
	s_and_b64 s[16:17], s[16:17], s[18:19]
	v_cndmask_b32_e64 v1, v1, v25, s[16:17]
	v_and_b32_e32 v37, 0x400, v2
	v_cndmask_b32_e64 v3, v3, 9, s[16:17]
	v_cmp_eq_u32_e64 s[16:17], 0, v37
	v_cmp_gt_f32_e64 s[18:19], v32, v1
	s_and_b64 s[16:17], s[16:17], s[18:19]
	v_cndmask_b32_e64 v1, v1, v32, s[16:17]
	v_and_b32_e32 v37, 0x800, v2
	v_cndmask_b32_e64 v3, v3, 10, s[16:17]
	v_cmp_eq_u32_e64 s[16:17], 0, v37
	v_cmp_gt_f32_e64 s[18:19], v33, v1
	s_and_b64 s[16:17], s[16:17], s[18:19]
	v_cndmask_b32_e64 v1, v1, v33, s[16:17]
	v_and_b32_e32 v37, 0x1000, v2
	v_cndmask_b32_e64 v3, v3, 11, s[16:17]
	v_cmp_eq_u32_e64 s[16:17], 0, v37
	v_cmp_gt_f32_e64 s[18:19], v20, v1
	s_and_b64 s[16:17], s[16:17], s[18:19]
	v_cndmask_b32_e64 v1, v1, v20, s[16:17]
	v_and_b32_e32 v37, 0x2000, v2
	v_cndmask_b32_e64 v3, v3, 12, s[16:17]
	v_cmp_eq_u32_e64 s[16:17], 0, v37
	v_cmp_gt_f32_e64 s[18:19], v21, v1
	s_and_b64 s[16:17], s[16:17], s[18:19]
	v_cndmask_b32_e64 v1, v1, v21, s[16:17]
	v_and_b32_e32 v37, 0x4000, v2
	v_cndmask_b32_e64 v3, v3, 13, s[16:17]
	v_cmp_eq_u32_e64 s[16:17], 0, v37
	v_cmp_gt_f32_e64 s[18:19], v6, v1
	s_and_b64 s[16:17], s[16:17], s[18:19]
	v_cndmask_b32_e64 v1, v1, v6, s[16:17]
	v_and_b32_e32 v37, 0x8000, v2
	v_cndmask_b32_e64 v3, v3, 14, s[16:17]
	v_cmp_eq_u32_e64 s[16:17], 0, v37
	v_cmp_gt_f32_e64 s[18:19], v7, v1
	s_and_b64 s[16:17], s[16:17], s[18:19]
	v_cndmask_b32_e64 v1, v1, v7, s[16:17]
	v_and_b32_e32 v37, 0x10000, v2
	v_cndmask_b32_e64 v3, v3, 15, s[16:17]
	v_cmp_eq_u32_e64 s[16:17], 0, v37
	v_cmp_gt_f32_e64 s[18:19], v18, v1
	s_and_b64 s[16:17], s[16:17], s[18:19]
	v_cndmask_b32_e64 v1, v1, v18, s[16:17]
	v_and_b32_e32 v37, 0x20000, v2
	v_cndmask_b32_e64 v3, v3, 16, s[16:17]
	v_cmp_eq_u32_e64 s[16:17], 0, v37
	v_cmp_gt_f32_e64 s[18:19], v19, v1
	s_and_b64 s[16:17], s[16:17], s[18:19]
	v_cndmask_b32_e64 v1, v1, v19, s[16:17]
	v_and_b32_e32 v37, 0x40000, v2
	v_cndmask_b32_e64 v3, v3, 17, s[16:17]
	v_cmp_eq_u32_e64 s[16:17], 0, v37
	v_cmp_gt_f32_e64 s[18:19], v26, v1
	s_and_b64 s[16:17], s[16:17], s[18:19]
	v_cndmask_b32_e64 v1, v1, v26, s[16:17]
	v_and_b32_e32 v37, 0x80000, v2
	v_cndmask_b32_e64 v3, v3, 18, s[16:17]
	v_cmp_eq_u32_e64 s[16:17], 0, v37
	v_cmp_gt_f32_e64 s[18:19], v27, v1
	s_and_b64 s[16:17], s[16:17], s[18:19]
	v_cndmask_b32_e64 v1, v1, v27, s[16:17]
	v_and_b32_e32 v37, 0x100000, v2
	v_cndmask_b32_e64 v3, v3, 19, s[16:17]
	v_cmp_eq_u32_e64 s[16:17], 0, v37
	v_cmp_gt_f32_e64 s[18:19], v12, v1
	s_and_b64 s[16:17], s[16:17], s[18:19]
	v_cndmask_b32_e64 v1, v1, v12, s[16:17]
	v_and_b32_e32 v37, 0x200000, v2
	v_cndmask_b32_e64 v3, v3, 20, s[16:17]
	v_cmp_eq_u32_e64 s[16:17], 0, v37
	v_cmp_gt_f32_e64 s[18:19], v13, v1
	s_and_b64 s[16:17], s[16:17], s[18:19]
	v_cndmask_b32_e64 v1, v1, v13, s[16:17]
	v_and_b32_e32 v37, 0x400000, v2
	v_cndmask_b32_e64 v3, v3, 21, s[16:17]
	v_cmp_eq_u32_e64 s[16:17], 0, v37
	v_cmp_gt_f32_e64 s[18:19], v4, v1
	s_and_b64 s[16:17], s[16:17], s[18:19]
	v_cndmask_b32_e64 v1, v1, v4, s[16:17]
	v_and_b32_e32 v37, 0x800000, v2
	v_cndmask_b32_e64 v3, v3, 22, s[16:17]
	v_cmp_eq_u32_e64 s[16:17], 0, v37
	v_cmp_gt_f32_e64 s[18:19], v5, v1
	s_and_b64 s[16:17], s[16:17], s[18:19]
	v_cndmask_b32_e64 v1, v1, v5, s[16:17]
	v_and_b32_e32 v37, 0x1000000, v2
	v_cndmask_b32_e64 v3, v3, 23, s[16:17]
	v_cmp_eq_u32_e64 s[16:17], 0, v37
	v_cmp_gt_f32_e64 s[18:19], v14, v1
	s_and_b64 s[16:17], s[16:17], s[18:19]
	v_cndmask_b32_e64 v1, v1, v14, s[16:17]
	v_and_b32_e32 v37, 0x2000000, v2
	v_cndmask_b32_e64 v3, v3, 24, s[16:17]
	v_cmp_eq_u32_e64 s[16:17], 0, v37
	v_cmp_gt_f32_e64 s[18:19], v15, v1
	s_and_b64 s[16:17], s[16:17], s[18:19]
	v_cndmask_b32_e64 v1, v1, v15, s[16:17]
	v_and_b32_e32 v37, 0x4000000, v2
	v_cndmask_b32_e64 v3, v3, 25, s[16:17]
	v_cmp_eq_u32_e64 s[16:17], 0, v37
	v_cmp_gt_f32_e64 s[18:19], v28, v1
	s_and_b64 s[16:17], s[16:17], s[18:19]
	v_cndmask_b32_e64 v1, v1, v28, s[16:17]
	v_and_b32_e32 v37, 0x8000000, v2
	v_cndmask_b32_e64 v3, v3, 26, s[16:17]
	v_cmp_eq_u32_e64 s[16:17], 0, v37
	v_cmp_gt_f32_e64 s[18:19], v29, v1
	s_and_b64 s[16:17], s[16:17], s[18:19]
	v_cndmask_b32_e64 v1, v1, v29, s[16:17]
	v_and_b32_e32 v37, 0x10000000, v2
	v_cndmask_b32_e64 v3, v3, 27, s[16:17]
	v_cmp_eq_u32_e64 s[16:17], 0, v37
	v_cmp_gt_f32_e64 s[18:19], v16, v1
	s_and_b64 s[16:17], s[16:17], s[18:19]
	v_cndmask_b32_e64 v1, v1, v16, s[16:17]
	v_and_b32_e32 v37, 0x20000000, v2
	v_cndmask_b32_e64 v3, v3, 28, s[16:17]
	v_cmp_eq_u32_e64 s[16:17], 0, v37
	v_cmp_gt_f32_e64 s[18:19], v17, v1
	s_and_b64 s[16:17], s[16:17], s[18:19]
	v_cndmask_b32_e64 v1, v1, v17, s[16:17]
	v_and_b32_e32 v37, 2.0, v2
	v_cndmask_b32_e64 v3, v3, 29, s[16:17]
	v_cmp_eq_u32_e64 s[16:17], 0, v37
	v_cmp_gt_f32_e64 s[18:19], v8, v1
	s_and_b64 s[16:17], s[16:17], s[18:19]
	v_cndmask_b32_e64 v1, v1, v8, s[16:17]
	v_cndmask_b32_e64 v3, v3, 30, s[16:17]
	v_cmp_ne_u32_e64 s[16:17], 31, v0
	v_cmp_gt_f32_e64 s[18:19], v9, v1
	s_and_b64 s[16:17], s[16:17], s[18:19]
	v_cndmask_b32_e64 v37, v1, v9, s[16:17]
	v_cndmask_b32_e64 v1, v3, 31, s[16:17]
	v_lshl_or_b32 v3, 1, v1, v2
	v_and_b32_e32 v2, 1, v3
	v_cmp_eq_u32_e64 s[16:17], 0, v2
	s_and_b64 s[16:17], s[16:17], vcc
	v_and_b32_e32 v38, 2, v3
	v_cndmask_b32_e64 v2, v121, v34, s[16:17]
	v_cmp_eq_u32_e64 s[16:17], 0, v38
	v_cmp_gt_f32_e64 s[18:19], v35, v2
	s_and_b64 s[16:17], s[16:17], s[18:19]
	v_cndmask_b32_e64 v2, v2, v35, s[16:17]
	v_and_b32_e32 v39, 4, v3
	v_cndmask_b32_e64 v38, 0, 1, s[16:17]
	v_cmp_eq_u32_e64 s[16:17], 0, v39
	v_cmp_gt_f32_e64 s[18:19], v30, v2
	s_and_b64 s[16:17], s[16:17], s[18:19]
	v_cndmask_b32_e64 v2, v2, v30, s[16:17]
	v_and_b32_e32 v39, 8, v3
	v_cndmask_b32_e64 v38, v38, 2, s[16:17]
	v_cmp_eq_u32_e64 s[16:17], 0, v39
	v_cmp_gt_f32_e64 s[18:19], v31, v2
	s_and_b64 s[16:17], s[16:17], s[18:19]
	v_cndmask_b32_e64 v2, v2, v31, s[16:17]
	v_and_b32_e32 v39, 16, v3
	v_cndmask_b32_e64 v38, v38, 3, s[16:17]
	v_cmp_eq_u32_e64 s[16:17], 0, v39
	v_cmp_gt_f32_e64 s[18:19], v22, v2
	s_and_b64 s[16:17], s[16:17], s[18:19]
	v_cndmask_b32_e64 v2, v2, v22, s[16:17]
	v_and_b32_e32 v39, 32, v3
	v_cndmask_b32_e64 v38, v38, 4, s[16:17]
	v_cmp_eq_u32_e64 s[16:17], 0, v39
	v_cmp_gt_f32_e64 s[18:19], v23, v2
	s_and_b64 s[16:17], s[16:17], s[18:19]
	v_cndmask_b32_e64 v2, v2, v23, s[16:17]
	v_and_b32_e32 v39, 64, v3
	v_cndmask_b32_e64 v38, v38, 5, s[16:17]
	v_cmp_eq_u32_e64 s[16:17], 0, v39
	v_cmp_gt_f32_e64 s[18:19], v10, v2
	s_and_b64 s[16:17], s[16:17], s[18:19]
	v_cndmask_b32_e64 v2, v2, v10, s[16:17]
	v_and_b32_e32 v39, 0x80, v3
	v_cndmask_b32_e64 v38, v38, 6, s[16:17]
	v_cmp_eq_u32_e64 s[16:17], 0, v39
	v_cmp_gt_f32_e64 s[18:19], v11, v2
	s_and_b64 s[16:17], s[16:17], s[18:19]
	v_cndmask_b32_e64 v2, v2, v11, s[16:17]
	v_and_b32_e32 v39, 0x100, v3
	v_cndmask_b32_e64 v38, v38, 7, s[16:17]
	v_cmp_eq_u32_e64 s[16:17], 0, v39
	v_cmp_gt_f32_e64 s[18:19], v24, v2
	s_and_b64 s[16:17], s[16:17], s[18:19]
	v_cndmask_b32_e64 v2, v2, v24, s[16:17]
	v_and_b32_e32 v39, 0x200, v3
	v_cndmask_b32_e64 v38, v38, 8, s[16:17]
	v_cmp_eq_u32_e64 s[16:17], 0, v39
	v_cmp_gt_f32_e64 s[18:19], v25, v2
	s_and_b64 s[16:17], s[16:17], s[18:19]
	v_cndmask_b32_e64 v2, v2, v25, s[16:17]
	v_and_b32_e32 v39, 0x400, v3
	v_cndmask_b32_e64 v38, v38, 9, s[16:17]
	v_cmp_eq_u32_e64 s[16:17], 0, v39
	v_cmp_gt_f32_e64 s[18:19], v32, v2
	s_and_b64 s[16:17], s[16:17], s[18:19]
	v_cndmask_b32_e64 v2, v2, v32, s[16:17]
	v_and_b32_e32 v39, 0x800, v3
	v_cndmask_b32_e64 v38, v38, 10, s[16:17]
	v_cmp_eq_u32_e64 s[16:17], 0, v39
	v_cmp_gt_f32_e64 s[18:19], v33, v2
	s_and_b64 s[16:17], s[16:17], s[18:19]
	v_cndmask_b32_e64 v2, v2, v33, s[16:17]
	v_and_b32_e32 v39, 0x1000, v3
	v_cndmask_b32_e64 v38, v38, 11, s[16:17]
	v_cmp_eq_u32_e64 s[16:17], 0, v39
	v_cmp_gt_f32_e64 s[18:19], v20, v2
	s_and_b64 s[16:17], s[16:17], s[18:19]
	v_cndmask_b32_e64 v2, v2, v20, s[16:17]
	v_and_b32_e32 v39, 0x2000, v3
	v_cndmask_b32_e64 v38, v38, 12, s[16:17]
	v_cmp_eq_u32_e64 s[16:17], 0, v39
	v_cmp_gt_f32_e64 s[18:19], v21, v2
	s_and_b64 s[16:17], s[16:17], s[18:19]
	v_cndmask_b32_e64 v2, v2, v21, s[16:17]
	v_and_b32_e32 v39, 0x4000, v3
	v_cndmask_b32_e64 v38, v38, 13, s[16:17]
	v_cmp_eq_u32_e64 s[16:17], 0, v39
	v_cmp_gt_f32_e64 s[18:19], v6, v2
	s_and_b64 s[16:17], s[16:17], s[18:19]
	v_cndmask_b32_e64 v2, v2, v6, s[16:17]
	v_and_b32_e32 v39, 0x8000, v3
	v_cndmask_b32_e64 v38, v38, 14, s[16:17]
	v_cmp_eq_u32_e64 s[16:17], 0, v39
	v_cmp_gt_f32_e64 s[18:19], v7, v2
	s_and_b64 s[16:17], s[16:17], s[18:19]
	v_cndmask_b32_e64 v2, v2, v7, s[16:17]
	v_and_b32_e32 v39, 0x10000, v3
	v_cndmask_b32_e64 v38, v38, 15, s[16:17]
	v_cmp_eq_u32_e64 s[16:17], 0, v39
	v_cmp_gt_f32_e64 s[18:19], v18, v2
	s_and_b64 s[16:17], s[16:17], s[18:19]
	v_cndmask_b32_e64 v2, v2, v18, s[16:17]
	v_and_b32_e32 v39, 0x20000, v3
	v_cndmask_b32_e64 v38, v38, 16, s[16:17]
	v_cmp_eq_u32_e64 s[16:17], 0, v39
	v_cmp_gt_f32_e64 s[18:19], v19, v2
	s_and_b64 s[16:17], s[16:17], s[18:19]
	v_cndmask_b32_e64 v2, v2, v19, s[16:17]
	v_and_b32_e32 v39, 0x40000, v3
	v_cndmask_b32_e64 v38, v38, 17, s[16:17]
	v_cmp_eq_u32_e64 s[16:17], 0, v39
	v_cmp_gt_f32_e64 s[18:19], v26, v2
	s_and_b64 s[16:17], s[16:17], s[18:19]
	v_cndmask_b32_e64 v2, v2, v26, s[16:17]
	v_and_b32_e32 v39, 0x80000, v3
	v_cndmask_b32_e64 v38, v38, 18, s[16:17]
	v_cmp_eq_u32_e64 s[16:17], 0, v39
	v_cmp_gt_f32_e64 s[18:19], v27, v2
	s_and_b64 s[16:17], s[16:17], s[18:19]
	v_cndmask_b32_e64 v2, v2, v27, s[16:17]
	v_and_b32_e32 v39, 0x100000, v3
	v_cndmask_b32_e64 v38, v38, 19, s[16:17]
	v_cmp_eq_u32_e64 s[16:17], 0, v39
	v_cmp_gt_f32_e64 s[18:19], v12, v2
	s_and_b64 s[16:17], s[16:17], s[18:19]
	v_cndmask_b32_e64 v2, v2, v12, s[16:17]
	v_and_b32_e32 v39, 0x200000, v3
	v_cndmask_b32_e64 v38, v38, 20, s[16:17]
	v_cmp_eq_u32_e64 s[16:17], 0, v39
	v_cmp_gt_f32_e64 s[18:19], v13, v2
	s_and_b64 s[16:17], s[16:17], s[18:19]
	v_cndmask_b32_e64 v2, v2, v13, s[16:17]
	v_and_b32_e32 v39, 0x400000, v3
	v_cndmask_b32_e64 v38, v38, 21, s[16:17]
	v_cmp_eq_u32_e64 s[16:17], 0, v39
	v_cmp_gt_f32_e64 s[18:19], v4, v2
	s_and_b64 s[16:17], s[16:17], s[18:19]
	v_cndmask_b32_e64 v2, v2, v4, s[16:17]
	v_and_b32_e32 v39, 0x800000, v3
	v_cndmask_b32_e64 v38, v38, 22, s[16:17]
	v_cmp_eq_u32_e64 s[16:17], 0, v39
	v_cmp_gt_f32_e64 s[18:19], v5, v2
	s_and_b64 s[16:17], s[16:17], s[18:19]
	v_cndmask_b32_e64 v2, v2, v5, s[16:17]
	v_and_b32_e32 v39, 0x1000000, v3
	v_cndmask_b32_e64 v38, v38, 23, s[16:17]
	v_cmp_eq_u32_e64 s[16:17], 0, v39
	v_cmp_gt_f32_e64 s[18:19], v14, v2
	s_and_b64 s[16:17], s[16:17], s[18:19]
	v_cndmask_b32_e64 v2, v2, v14, s[16:17]
	v_and_b32_e32 v39, 0x2000000, v3
	v_cndmask_b32_e64 v38, v38, 24, s[16:17]
	v_cmp_eq_u32_e64 s[16:17], 0, v39
	v_cmp_gt_f32_e64 s[18:19], v15, v2
	s_and_b64 s[16:17], s[16:17], s[18:19]
	v_cndmask_b32_e64 v2, v2, v15, s[16:17]
	v_and_b32_e32 v39, 0x4000000, v3
	v_cndmask_b32_e64 v38, v38, 25, s[16:17]
	v_cmp_eq_u32_e64 s[16:17], 0, v39
	v_cmp_gt_f32_e64 s[18:19], v28, v2
	s_and_b64 s[16:17], s[16:17], s[18:19]
	v_cndmask_b32_e64 v2, v2, v28, s[16:17]
	v_and_b32_e32 v39, 0x8000000, v3
	v_cndmask_b32_e64 v38, v38, 26, s[16:17]
	v_cmp_eq_u32_e64 s[16:17], 0, v39
	v_cmp_gt_f32_e64 s[18:19], v29, v2
	s_and_b64 s[16:17], s[16:17], s[18:19]
	v_cndmask_b32_e64 v2, v2, v29, s[16:17]
	v_and_b32_e32 v39, 0x10000000, v3
	v_cndmask_b32_e64 v38, v38, 27, s[16:17]
	v_cmp_eq_u32_e64 s[16:17], 0, v39
	v_cmp_gt_f32_e64 s[18:19], v16, v2
	s_and_b64 s[16:17], s[16:17], s[18:19]
	v_cndmask_b32_e64 v2, v2, v16, s[16:17]
	v_and_b32_e32 v39, 0x20000000, v3
	v_cndmask_b32_e64 v38, v38, 28, s[16:17]
	v_cmp_eq_u32_e64 s[16:17], 0, v39
	v_cmp_gt_f32_e64 s[18:19], v17, v2
	s_and_b64 s[16:17], s[16:17], s[18:19]
	v_cndmask_b32_e64 v2, v2, v17, s[16:17]
	v_and_b32_e32 v39, 2.0, v3
	v_cndmask_b32_e64 v38, v38, 29, s[16:17]
	v_cmp_eq_u32_e64 s[16:17], 0, v39
	v_cmp_gt_f32_e64 s[18:19], v8, v2
	s_and_b64 s[16:17], s[16:17], s[18:19]
	v_cndmask_b32_e64 v2, v2, v8, s[16:17]
	v_cndmask_b32_e64 v38, v38, 30, s[16:17]
	v_cmp_lt_i32_e64 s[16:17], -1, v3
	v_cmp_gt_f32_e64 s[18:19], v9, v2
	s_and_b64 s[16:17], s[16:17], s[18:19]
	v_cndmask_b32_e64 v39, v2, v9, s[16:17]
	v_cndmask_b32_e64 v2, v38, 31, s[16:17]
	v_lshlrev_b32_e64 v38, v2, 1
	v_bitop3_b32 v90, v38, 1, v3 bitop3:0xc8
	v_cmp_eq_u32_e64 s[16:17], 0, v90
	s_and_b64 vcc, s[16:17], vcc
	v_cndmask_b32_e32 v34, v121, v34, vcc
	v_bitop3_b32 v90, v38, 2, v3 bitop3:0xc8
	v_cmp_eq_u32_e32 vcc, 0, v90
	v_cmp_gt_f32_e64 s[16:17], v35, v34
	s_and_b64 vcc, vcc, s[16:17]
	v_cndmask_b32_e32 v34, v34, v35, vcc
	v_bitop3_b32 v90, v38, 4, v3 bitop3:0xc8
	v_cndmask_b32_e64 v35, 0, 1, vcc
	v_cmp_eq_u32_e32 vcc, 0, v90
	v_cmp_gt_f32_e64 s[16:17], v30, v34
	s_and_b64 vcc, vcc, s[16:17]
	v_cndmask_b32_e32 v30, v34, v30, vcc
	v_cndmask_b32_e64 v34, v35, 2, vcc
	v_bitop3_b32 v35, v38, 8, v3 bitop3:0xc8
	v_cmp_eq_u32_e32 vcc, 0, v35
	v_cmp_gt_f32_e64 s[16:17], v31, v30
	s_and_b64 vcc, vcc, s[16:17]
	v_cndmask_b32_e32 v30, v30, v31, vcc
	v_cndmask_b32_e64 v31, v34, 3, vcc
	v_bitop3_b32 v34, v38, 16, v3 bitop3:0xc8
	v_cmp_eq_u32_e32 vcc, 0, v34
	v_cmp_gt_f32_e64 s[16:17], v22, v30
	s_and_b64 vcc, vcc, s[16:17]
	v_cndmask_b32_e32 v22, v30, v22, vcc
	v_cndmask_b32_e64 v30, v31, 4, vcc
	v_bitop3_b32 v31, v38, 32, v3 bitop3:0xc8
	v_cmp_eq_u32_e32 vcc, 0, v31
	v_cmp_gt_f32_e64 s[16:17], v23, v22
	s_and_b64 vcc, vcc, s[16:17]
	v_cndmask_b32_e32 v22, v22, v23, vcc
	v_cndmask_b32_e64 v23, v30, 5, vcc
	v_bitop3_b32 v30, v38, 64, v3 bitop3:0xc8
	v_cmp_eq_u32_e32 vcc, 0, v30
	v_cmp_gt_f32_e64 s[16:17], v10, v22
	s_and_b64 vcc, vcc, s[16:17]
	s_movk_i32 s16, 0x80
	v_cndmask_b32_e32 v10, v22, v10, vcc
	v_cndmask_b32_e64 v22, v23, 6, vcc
	v_bitop3_b32 v23, v38, s16, v3 bitop3:0xc8
	v_cmp_eq_u32_e32 vcc, 0, v23
	v_cmp_gt_f32_e64 s[16:17], v11, v10
	s_and_b64 vcc, vcc, s[16:17]
	s_movk_i32 s16, 0x100
	v_cndmask_b32_e32 v10, v10, v11, vcc
	v_cndmask_b32_e64 v11, v22, 7, vcc
	v_bitop3_b32 v22, v38, s16, v3 bitop3:0xc8
	v_cmp_eq_u32_e32 vcc, 0, v22
	v_cmp_gt_f32_e64 s[16:17], v24, v10
	s_and_b64 vcc, vcc, s[16:17]
	s_movk_i32 s16, 0x200
	v_cndmask_b32_e32 v10, v10, v24, vcc
	v_bitop3_b32 v22, v38, s16, v3 bitop3:0xc8
	v_cndmask_b32_e64 v11, v11, 8, vcc
	v_cmp_eq_u32_e32 vcc, 0, v22
	v_cmp_gt_f32_e64 s[16:17], v25, v10
	s_and_b64 vcc, vcc, s[16:17]
	v_cndmask_b32_e32 v10, v10, v25, vcc
	v_bitop3_b32 v22, v38, s46, v3 bitop3:0xc8
	v_cndmask_b32_e64 v11, v11, 9, vcc
	v_cmp_eq_u32_e32 vcc, 0, v22
	v_cmp_gt_f32_e64 s[16:17], v32, v10
	s_and_b64 vcc, vcc, s[16:17]
	s_movk_i32 s16, 0x800
	v_cndmask_b32_e32 v10, v10, v32, vcc
	v_bitop3_b32 v22, v38, s16, v3 bitop3:0xc8
	v_cndmask_b32_e64 v11, v11, 10, vcc
	v_cmp_eq_u32_e32 vcc, 0, v22
	v_cmp_gt_f32_e64 s[16:17], v33, v10
	s_and_b64 vcc, vcc, s[16:17]
	s_movk_i32 s16, 0x1000
	v_cndmask_b32_e32 v10, v10, v33, vcc
	v_bitop3_b32 v22, v38, s16, v3 bitop3:0xc8
	v_cndmask_b32_e64 v11, v11, 11, vcc
	v_cmp_eq_u32_e32 vcc, 0, v22
	v_cmp_gt_f32_e64 s[16:17], v20, v10
	s_and_b64 vcc, vcc, s[16:17]
	s_movk_i32 s16, 0x2000
	v_cndmask_b32_e32 v10, v10, v20, vcc
	v_bitop3_b32 v20, v38, s16, v3 bitop3:0xc8
	v_cndmask_b32_e64 v11, v11, 12, vcc
	v_cmp_eq_u32_e32 vcc, 0, v20
	v_cmp_gt_f32_e64 s[16:17], v21, v10
	s_and_b64 vcc, vcc, s[16:17]
	s_movk_i32 s16, 0x4000
	v_cndmask_b32_e32 v10, v10, v21, vcc
	v_bitop3_b32 v20, v38, s16, v3 bitop3:0xc8
	v_cndmask_b32_e64 v11, v11, 13, vcc
	v_cmp_eq_u32_e32 vcc, 0, v20
	v_cmp_gt_f32_e64 s[16:17], v6, v10
	s_and_b64 vcc, vcc, s[16:17]
	s_mov_b32 s16, 0x8000
	v_cndmask_b32_e32 v6, v10, v6, vcc
	v_cndmask_b32_e64 v10, v11, 14, vcc
	v_bitop3_b32 v11, v38, s16, v3 bitop3:0xc8
	v_cmp_eq_u32_e32 vcc, 0, v11
	v_cmp_gt_f32_e64 s[16:17], v7, v6
	s_and_b64 vcc, vcc, s[16:17]
	s_mov_b32 s16, 0x10000
	v_cndmask_b32_e32 v6, v6, v7, vcc
	v_cndmask_b32_e64 v7, v10, 15, vcc
	v_bitop3_b32 v10, v38, s16, v3 bitop3:0xc8
	v_cmp_eq_u32_e32 vcc, 0, v10
	v_cmp_gt_f32_e64 s[16:17], v18, v6
	s_and_b64 vcc, vcc, s[16:17]
	s_mov_b32 s16, 0x20000
	v_cndmask_b32_e32 v6, v6, v18, vcc
	v_bitop3_b32 v10, v38, s16, v3 bitop3:0xc8
	v_cndmask_b32_e64 v7, v7, 16, vcc
	v_cmp_eq_u32_e32 vcc, 0, v10
	v_cmp_gt_f32_e64 s[16:17], v19, v6
	s_and_b64 vcc, vcc, s[16:17]
	s_mov_b32 s16, 0x40000
	v_cndmask_b32_e32 v6, v6, v19, vcc
	v_bitop3_b32 v10, v38, s16, v3 bitop3:0xc8
	v_cndmask_b32_e64 v7, v7, 17, vcc
	v_cmp_eq_u32_e32 vcc, 0, v10
	v_cmp_gt_f32_e64 s[16:17], v26, v6
	s_and_b64 vcc, vcc, s[16:17]
	s_mov_b32 s16, 0x80000
	v_cndmask_b32_e32 v6, v6, v26, vcc
	v_bitop3_b32 v10, v38, s16, v3 bitop3:0xc8
	v_cndmask_b32_e64 v7, v7, 18, vcc
	v_cmp_eq_u32_e32 vcc, 0, v10
	v_cmp_gt_f32_e64 s[16:17], v27, v6
	s_and_b64 vcc, vcc, s[16:17]
	s_mov_b32 s16, 0x100000
	v_cndmask_b32_e32 v6, v6, v27, vcc
	v_bitop3_b32 v10, v38, s16, v3 bitop3:0xc8
	v_cndmask_b32_e64 v7, v7, 19, vcc
	v_cmp_eq_u32_e32 vcc, 0, v10
	v_cmp_gt_f32_e64 s[16:17], v12, v6
	s_and_b64 vcc, vcc, s[16:17]
	s_mov_b32 s16, 0x200000
	v_cndmask_b32_e32 v6, v6, v12, vcc
	v_bitop3_b32 v10, v38, s16, v3 bitop3:0xc8
	v_cndmask_b32_e64 v7, v7, 20, vcc
	v_cmp_eq_u32_e32 vcc, 0, v10
	v_cmp_gt_f32_e64 s[16:17], v13, v6
	s_and_b64 vcc, vcc, s[16:17]
	s_mov_b32 s16, 0x400000
	v_cndmask_b32_e32 v6, v6, v13, vcc
	v_bitop3_b32 v10, v38, s16, v3 bitop3:0xc8
	v_cndmask_b32_e64 v7, v7, 21, vcc
	v_cmp_eq_u32_e32 vcc, 0, v10
	v_cmp_gt_f32_e64 s[16:17], v4, v6
	s_and_b64 vcc, vcc, s[16:17]
	s_mov_b32 s16, 0x800000
	v_cndmask_b32_e32 v4, v6, v4, vcc
	v_cndmask_b32_e64 v6, v7, 22, vcc
	v_bitop3_b32 v7, v38, s16, v3 bitop3:0xc8
	v_cmp_eq_u32_e32 vcc, 0, v7
	v_cmp_gt_f32_e64 s[16:17], v5, v4
	s_and_b64 vcc, vcc, s[16:17]
	v_cndmask_b32_e32 v4, v4, v5, vcc
	v_cndmask_b32_e64 v5, v6, 23, vcc
	v_bitop3_b32 v6, v38, s55, v3 bitop3:0xc8
	v_cmp_eq_u32_e32 vcc, 0, v6
	v_cmp_gt_f32_e64 s[16:17], v14, v4
	s_and_b64 vcc, vcc, s[16:17]
	v_cndmask_b32_e32 v4, v4, v14, vcc
	v_bitop3_b32 v6, v38, s56, v3 bitop3:0xc8
	v_cndmask_b32_e64 v5, v5, 24, vcc
	v_cmp_eq_u32_e32 vcc, 0, v6
	v_cmp_gt_f32_e64 s[16:17], v15, v4
	s_and_b64 vcc, vcc, s[16:17]
	v_cndmask_b32_e32 v4, v4, v15, vcc
	v_bitop3_b32 v6, v38, s57, v3 bitop3:0xc8
	v_cndmask_b32_e64 v5, v5, 25, vcc
	v_cmp_eq_u32_e32 vcc, 0, v6
	v_cmp_gt_f32_e64 s[16:17], v28, v4
	s_and_b64 vcc, vcc, s[16:17]
	v_cndmask_b32_e32 v4, v4, v28, vcc
	v_bitop3_b32 v6, v38, s58, v3 bitop3:0xc8
	v_cndmask_b32_e64 v5, v5, 26, vcc
	v_cmp_eq_u32_e32 vcc, 0, v6
	v_cmp_gt_f32_e64 s[16:17], v29, v4
	s_and_b64 vcc, vcc, s[16:17]
	v_cndmask_b32_e32 v4, v4, v29, vcc
	v_bitop3_b32 v6, v38, s59, v3 bitop3:0xc8
	v_cndmask_b32_e64 v5, v5, 27, vcc
	v_cmp_eq_u32_e32 vcc, 0, v6
	v_cmp_gt_f32_e64 s[16:17], v16, v4
	s_and_b64 vcc, vcc, s[16:17]
	v_cndmask_b32_e32 v4, v4, v16, vcc
	v_bitop3_b32 v6, v38, s60, v3 bitop3:0xc8
	v_cndmask_b32_e64 v5, v5, 28, vcc
	v_cmp_eq_u32_e32 vcc, 0, v6
	v_cmp_gt_f32_e64 s[16:17], v17, v4
	s_and_b64 vcc, vcc, s[16:17]
	v_or_b32_e32 v44, v38, v3
	v_cndmask_b32_e32 v4, v4, v17, vcc
	v_bitop3_b32 v3, v38, 2.0, v3 bitop3:0xc8
	v_cndmask_b32_e64 v5, v5, 29, vcc
	v_cmp_eq_u32_e32 vcc, 0, v3
	v_cmp_gt_f32_e64 s[16:17], v8, v4
	s_and_b64 vcc, vcc, s[16:17]
	v_cndmask_b32_e32 v3, v4, v8, vcc
	v_cndmask_b32_e64 v4, v5, 30, vcc
	v_cmp_lt_i32_e32 vcc, -1, v44
	v_cmp_gt_f32_e64 s[16:17], v9, v3
	s_and_b64 vcc, vcc, s[16:17]
	v_cndmask_b32_e32 v5, v3, v9, vcc
	v_cndmask_b32_e64 v3, v4, 31, vcc
	v_sub_f32_e32 v4, v36, v36
	v_mul_f32_e32 v4, 0x3fb8aa3b, v4
	v_exp_f32_e32 v10, v4
	v_sub_f32_e32 v4, v37, v36
	v_mul_f32_e32 v4, 0x3fb8aa3b, v4
	v_exp_f32_e32 v11, v4
	v_sub_f32_e32 v4, v39, v36
	v_mul_f32_e32 v4, 0x3fb8aa3b, v4
	v_exp_f32_e32 v12, v4
	v_sub_f32_e32 v4, v5, v36
	v_mul_f32_e32 v4, 0x3fb8aa3b, v4
	v_exp_f32_e32 v13, v4
	v_add_f32_e32 v4, 0, v10
	v_add_f32_e32 v4, v4, v11
	v_add_f32_e32 v4, v4, v12
	v_add_f32_e32 v14, v4, v13
	v_div_scale_f32 v15, s[16:17], v14, v14, v10
	v_rcp_f32_e32 v16, v15
	v_lshl_add_u32 v4, s61, 8, v102
	v_ashrrev_i32_e32 v5, 31, v4
	v_lshlrev_b64 v[6:7], 2, v[4:5]
	v_fma_f32 v5, -v15, v16, 1.0
	v_fmac_f32_e32 v16, v5, v16
	v_div_scale_f32 v5, vcc, v10, v14, v10
	v_mul_f32_e32 v17, v5, v16
	v_fma_f32 v18, -v15, v17, v5
	v_fmac_f32_e32 v17, v18, v16
	v_fma_f32 v5, -v15, v17, v5
	v_div_fmas_f32 v5, v5, v16, v17
	v_div_fixup_f32 v5, v5, v14, v10
	v_div_scale_f32 v10, s[16:17], v14, v14, v11
	v_rcp_f32_e32 v15, v10
	v_lshl_add_u64 v[8:9], s[20:21], 0, v[6:7]
	v_lshl_add_u64 v[6:7], s[22:23], 0, v[6:7]
	global_store_dword v[6:7], v5, off
	v_or_b32_e32 v6, 1, v4
	v_fma_f32 v4, -v10, v15, 1.0
	v_lshl_add_u32 v5, v0, 2, 0
	v_fmac_f32_e32 v15, v4, v15
	v_div_scale_f32 v4, vcc, v11, v14, v11
	ds_add_u32 v5, v118 offset:58624
	v_mul_f32_e32 v5, v4, v15
	v_fma_f32 v16, -v10, v5, v4
	v_fmac_f32_e32 v5, v16, v15
	v_fma_f32 v4, -v10, v5, v4
	v_div_fmas_f32 v4, v4, v15, v5
	v_div_scale_f32 v5, s[16:17], v14, v14, v12
	v_rcp_f32_e32 v15, v5
	v_ashrrev_i32_e32 v7, 31, v6
	v_div_fixup_f32 v4, v4, v14, v11
	v_lshl_add_u64 v[10:11], v[6:7], 2, s[22:23]
	v_lshl_add_u32 v6, v1, 2, 0
	ds_add_u32 v6, v118 offset:58624
	v_fma_f32 v6, -v5, v15, 1.0
	v_fmac_f32_e32 v15, v6, v15
	v_div_scale_f32 v6, vcc, v12, v14, v12
	v_mul_f32_e32 v7, v6, v15
	v_fma_f32 v16, -v5, v7, v6
	v_fmac_f32_e32 v7, v16, v15
	v_fma_f32 v5, -v5, v7, v6
	v_div_scale_f32 v6, s[16:17], v14, v14, v13
	v_div_fmas_f32 v5, v5, v15, v7
	v_rcp_f32_e32 v7, v6
	v_div_fixup_f32 v5, v5, v14, v12
	v_lshl_add_u32 v12, v2, 2, 0
	ds_add_u32 v12, v118 offset:58624
	global_store_dwordx4 v[8:9], v[0:3], off
	s_nop 1
	v_fma_f32 v0, -v6, v7, 1.0
	v_fmac_f32_e32 v7, v0, v7
	v_div_scale_f32 v0, vcc, v13, v14, v13
	v_mul_f32_e32 v1, v0, v7
	v_fma_f32 v2, -v6, v1, v0
	v_fmac_f32_e32 v1, v2, v7
	v_fma_f32 v0, -v6, v1, v0
	v_div_fmas_f32 v0, v0, v7, v1
	v_div_fixup_f32 v6, v0, v14, v13
	global_store_dwordx3 v[10:11], v[4:6], off
	v_lshl_add_u32 v0, v3, 2, 0
	ds_add_u32 v0, v118 offset:58624

.LBB0_1474:
	s_waitcnt vmcnt(0)
	s_barrier
	s_waitcnt vmcnt(0)
	buffer_inv sc1
	s_waitcnt vmcnt(0)
	v_readlane_b32 s98, v253, 20
	v_mbcnt_lo_u32_b32 v216, -1, 0
	v_mbcnt_hi_u32_b32 v216, -1, v216
	s_lshr_b32 s99, s98, 1
	s_and_b32 s100, s98, 1
	v_lshrrev_b32_e32 v217, 5, v216
	v_and_b32_e32 v216, 31, v216
	s_lshl_b32 s101, s99, 4
	v_add_u32_e32 v218, s101, v217
	v_lshlrev_b32_e32 v219, 7, v218
	v_lshl_add_u32 v219, v216, 2, v219
	v_add_u32_e32 v219, 0xa400, v219
	v_mul_u32_u24_e32 v218, 0x104, v218
	s_lshl_b32 s101, s100, 7
	v_add_u32_e32 v218, s101, v218
	v_lshl_add_u32 v218, v216, 2, v218
	v_add_u32_e32 v218, 0x6000, v218
	v_mov_b32_e32 v221, s98
	v_mbcnt_lo_u32_b32 v220, -1, 0
	v_mbcnt_hi_u32_b32 v220, -1, v220
	v_lshl_add_u32 v220, v221, 6, v220
	v_and_b32_e32 v221, 7, v220
	v_lshrrev_b32_e32 v220, 3, v220
	v_mul_u32_u24_e32 v221, 0x820, v221
	v_lshl_add_u32 v220, v220, 2, v221
	v_add_u32_e32 v220, 0x6000, v220
	v_add_u32_e32 v221, 0x410, v220
	s_lshl_b32 s101, s99, 13
	s_lshl_b32 s100, s100, 12
	s_add_i32 s101, s101, s100
	v_lshlrev_b32_e32 v217, 9, v217
	v_add_u32_e32 v217, s101, v217
	v_lshl_add_u32 v217, v216, 2, v217
	s_and_saveexec_b64 s[16:17], s[4:5]
	ds_write_b32 v95, v45 offset:58624
	s_or_b64 exec, exec, s[16:17]
	v_add_u32_e32 v0, s67, v42
	v_ashrrev_i32_e32 v1, 31, v0
	v_lshlrev_b64 v[0:1], 11, v[0:1]
	v_lshl_add_u64 v[92:93], v[46:47], 0, v[0:1]
	global_load_dwordx4 v[30:33], v[92:93], off
	global_load_dwordx4 v[34:37], v[48:49], off
	global_load_dwordx4 v[20:23], v[52:53], off
	global_load_dwordx4 v[24:27], v[92:93], off offset:128
	ds_read_b64 v[38:39], v106 offset:20480
	ds_read_b128 v[116:119], v43 offset:12288
	ds_read_b128 v[120:123], v43 offset:12304
	ds_read_b128 v[124:127], v43 offset:16384
	ds_read_b128 v[128:131], v43 offset:16400
	v_add_u32_e32 v114, 0x6000, v97
	v_mov_b32_e32 v4, 0
	s_waitcnt lgkmcnt(4)
	v_mov_b32_e32 v0, v38
	v_mov_b32_e32 v1, v38
	v_mov_b32_e32 v2, v38
	v_mov_b32_e32 v3, v38
	v_mov_b32_e32 v88, v39
	v_mov_b32_e32 v89, v39
	v_mov_b32_e32 v90, v39
	v_mov_b32_e32 v91, v39
	v_add_u32_e32 v113, 0x6400, v97
	s_mov_b32 s16, 0
	v_mov_b32_e32 v28, v103
	v_mov_b32_e32 v5, v4
	v_mov_b32_e32 v6, v4
	v_mov_b32_e32 v7, v4
	v_mov_b32_e32 v8, v4
	v_mov_b32_e32 v9, v4
	v_mov_b32_e32 v10, v4
	v_mov_b32_e32 v11, v4
	v_mov_b32_e32 v12, v4
	v_mov_b32_e32 v13, v4
	v_mov_b32_e32 v14, v4
	v_mov_b32_e32 v15, v4
	v_mov_b32_e32 v16, v4
	v_mov_b32_e32 v17, v4
	v_mov_b32_e32 v18, v4
	s_waitcnt vmcnt(3)
	v_cvt_f32_f16_sdwa v19, v31 dst_sel:DWORD dst_unused:UNUSED_PAD src0_sel:WORD_1
	v_cvt_f32_f16_e32 v29, v31
	v_cvt_f32_f16_sdwa v31, v30 dst_sel:DWORD dst_unused:UNUSED_PAD src0_sel:WORD_1
	v_cvt_f32_f16_e32 v30, v30
	v_cvt_f32_f16_sdwa v115, v33 dst_sel:DWORD dst_unused:UNUSED_PAD src0_sel:WORD_1
	v_cvt_f32_f16_e32 v134, v33
	v_cvt_f32_f16_sdwa v133, v32 dst_sel:DWORD dst_unused:UNUSED_PAD src0_sel:WORD_1
	v_cvt_f32_f16_e32 v132, v32
	v_sub_f32_e32 v30, v30, v38
	v_sub_f32_e32 v31, v31, v38
	v_sub_f32_e32 v32, v29, v38
	v_sub_f32_e32 v33, v19, v38
	v_sub_f32_e32 v132, v132, v38
	v_sub_f32_e32 v133, v133, v38
	v_sub_f32_e32 v134, v134, v38
	v_sub_f32_e32 v135, v115, v38
	v_pk_mul_f32 v[30:31], v[38:39], v[30:31] op_sel:[1,0]
	v_pk_mul_f32 v[32:33], v[38:39], v[32:33] op_sel:[1,0]
	v_pk_mul_f32 v[134:135], v[38:39], v[134:135] op_sel:[1,0]
	v_pk_mul_f32 v[38:39], v[38:39], v[132:133] op_sel:[1,0]
	s_waitcnt lgkmcnt(1)
	v_fma_f32 v19, v116, v30, v124
	v_fma_f32 v30, v117, v31, v125
	s_waitcnt lgkmcnt(0)
	v_fma_f32 v29, v120, v38, v128
	v_fma_f32 v31, v121, v39, v129
	v_fma_f32 v32, v118, v32, v126
	v_fma_f32 v38, v122, v134, v130
	v_fmac_f32_e32 v127, v119, v33
	v_fmac_f32_e32 v131, v123, v135
	ds_write2_b32 v220, v19, v30 offset1:65
	ds_write2_b32 v221, v29, v31 offset1:65
	ds_write2_b32 v220, v32, v127 offset0:130 offset1:195
	ds_write2_b32 v221, v38, v131 offset0:130 offset1:195
	s_waitcnt vmcnt(2)
	ds_write_b128 v96, v[34:37] offset:41984
	v_mov_b32_e32 v19, v4
	s_waitcnt lgkmcnt(0)
	s_barrier
	ds_read_b32 v200, v218
	ds_read_b32 v208, v219
	ds_read_b32 v201, v218 offset:520
	ds_read_b32 v209, v219 offset:256
	ds_read_b32 v202, v218 offset:1040
	ds_read_b32 v210, v219 offset:512
	ds_read_b32 v203, v218 offset:1560
	ds_read_b32 v211, v219 offset:768
	ds_read_b32 v204, v218 offset:2080
	ds_read_b32 v212, v219 offset:1024
	ds_read_b32 v205, v218 offset:2600
	ds_read_b32 v213, v219 offset:1280
	ds_read_b32 v206, v218 offset:3120
	ds_read_b32 v214, v219 offset:1536
	s_waitcnt lgkmcnt(12)
	v_mfma_f32_32x32x2_f32 v[4:19], v200, v208, v[4:19]
	ds_read_b32 v207, v218 offset:3640
	ds_read_b32 v215, v219 offset:1792
	s_waitcnt lgkmcnt(12)
	v_mfma_f32_32x32x2_f32 v[4:19], v201, v209, v[4:19]
	s_waitcnt lgkmcnt(10)
	v_mfma_f32_32x32x2_f32 v[4:19], v202, v210, v[4:19]
	s_waitcnt lgkmcnt(8)
	v_mfma_f32_32x32x2_f32 v[4:19], v203, v211, v[4:19]
	s_waitcnt lgkmcnt(6)
	v_mfma_f32_32x32x2_f32 v[4:19], v204, v212, v[4:19]
	s_waitcnt lgkmcnt(4)
	v_mfma_f32_32x32x2_f32 v[4:19], v205, v213, v[4:19]
	s_waitcnt lgkmcnt(2)
	v_mfma_f32_32x32x2_f32 v[4:19], v206, v214, v[4:19]
	s_waitcnt lgkmcnt(0)
	v_mfma_f32_32x32x2_f32 v[4:19], v207, v215, v[4:19]
	s_barrier
	global_load_dwordx4 v[32:35], v[92:93], off offset:256
	global_load_dwordx4 v[28:31], v[54:55], off
	s_waitcnt vmcnt(2)
	v_cvt_f32_f16_sdwa v128, v24 dst_sel:DWORD dst_unused:UNUSED_PAD src0_sel:WORD_1
	v_cvt_f32_f16_e32 v24, v24
	v_cvt_f32_f16_e32 v129, v25
	v_cvt_f32_f16_sdwa v130, v26 dst_sel:DWORD dst_unused:UNUSED_PAD src0_sel:WORD_1
	v_cvt_f32_f16_e32 v133, v26
	ds_read_b128 v[36:39], v43 offset:12544
	ds_read_b128 v[116:119], v43 offset:12560
	ds_read_b128 v[120:123], v43 offset:16640
	ds_read_b128 v[124:127], v43 offset:16656
	v_cvt_f32_f16_sdwa v115, v25 dst_sel:DWORD dst_unused:UNUSED_PAD src0_sel:WORD_1
	v_cvt_f32_f16_sdwa v131, v27 dst_sel:DWORD dst_unused:UNUSED_PAD src0_sel:WORD_1
	v_cvt_f32_f16_e32 v132, v27
	v_sub_f32_e32 v24, v24, v0
	v_sub_f32_e32 v25, v128, v1
	v_sub_f32_e32 v26, v129, v2
	v_pk_mul_f32 v[24:25], v[88:89], v[24:25]
	v_sub_f32_e32 v128, v133, v0
	v_sub_f32_e32 v129, v130, v1
	v_sub_f32_e32 v27, v115, v3
	v_sub_f32_e32 v130, v132, v2
	v_sub_f32_e32 v131, v131, v3
	v_pk_mul_f32 v[128:129], v[88:89], v[128:129]
	s_waitcnt lgkmcnt(1)
	v_fma_f32 v24, v36, v24, v120
	v_fma_f32 v25, v37, v25, v121
	v_pk_mul_f32 v[26:27], v[90:91], v[26:27]
	v_pk_mul_f32 v[130:131], v[90:91], v[130:131]
	s_waitcnt lgkmcnt(0)
	v_fma_f32 v36, v116, v128, v124
	ds_write2_b32 v220, v24, v25 offset1:65
	v_fma_f32 v24, v117, v129, v125
	ds_write2_b32 v221, v36, v24 offset1:65
	v_fma_f32 v24, v38, v26, v122
	v_fma_f32 v25, v118, v130, v126
	v_fmac_f32_e32 v123, v39, v27
	v_fmac_f32_e32 v127, v119, v131
	ds_write2_b32 v220, v24, v123 offset0:130 offset1:195
	ds_write2_b32 v221, v25, v127 offset0:130 offset1:195
	ds_write_b128 v96, v[20:23] offset:41984
	s_mov_b32 s16, 0
	v_mov_b32_e32 v20, v103
	s_waitcnt lgkmcnt(0)
	s_barrier
	ds_read_b32 v200, v218
	ds_read_b32 v208, v219
	ds_read_b32 v201, v218 offset:520
	ds_read_b32 v209, v219 offset:256
	ds_read_b32 v202, v218 offset:1040
	ds_read_b32 v210, v219 offset:512
	ds_read_b32 v203, v218 offset:1560
	ds_read_b32 v211, v219 offset:768
	ds_read_b32 v204, v218 offset:2080
	ds_read_b32 v212, v219 offset:1024
	ds_read_b32 v205, v218 offset:2600
	ds_read_b32 v213, v219 offset:1280
	ds_read_b32 v206, v218 offset:3120
	ds_read_b32 v214, v219 offset:1536
	s_waitcnt lgkmcnt(12)
	v_mfma_f32_32x32x2_f32 v[4:19], v200, v208, v[4:19]
	ds_read_b32 v207, v218 offset:3640
	ds_read_b32 v215, v219 offset:1792
	s_waitcnt lgkmcnt(12)
	v_mfma_f32_32x32x2_f32 v[4:19], v201, v209, v[4:19]
	s_waitcnt lgkmcnt(10)
	v_mfma_f32_32x32x2_f32 v[4:19], v202, v210, v[4:19]
	s_waitcnt lgkmcnt(8)
	v_mfma_f32_32x32x2_f32 v[4:19], v203, v211, v[4:19]
	s_waitcnt lgkmcnt(6)
	v_mfma_f32_32x32x2_f32 v[4:19], v204, v212, v[4:19]
	s_waitcnt lgkmcnt(4)
	v_mfma_f32_32x32x2_f32 v[4:19], v205, v213, v[4:19]
	s_waitcnt lgkmcnt(2)
	v_mfma_f32_32x32x2_f32 v[4:19], v206, v214, v[4:19]
	s_waitcnt lgkmcnt(0)
	v_mfma_f32_32x32x2_f32 v[4:19], v207, v215, v[4:19]
	s_barrier
	global_load_dwordx4 v[36:39], v[92:93], off offset:384
	global_load_dwordx4 v[20:23], v[56:57], off
	s_waitcnt vmcnt(3)
	v_cvt_f32_f16_sdwa v128, v32 dst_sel:DWORD dst_unused:UNUSED_PAD src0_sel:WORD_1
	v_cvt_f32_f16_e32 v32, v32
	v_cvt_f32_f16_e32 v129, v33
	v_cvt_f32_f16_sdwa v130, v34 dst_sel:DWORD dst_unused:UNUSED_PAD src0_sel:WORD_1
	v_cvt_f32_f16_e32 v133, v34
	ds_read_b128 v[24:27], v43 offset:12800
	ds_read_b128 v[116:119], v43 offset:12816
	ds_read_b128 v[120:123], v43 offset:16896
	ds_read_b128 v[124:127], v43 offset:16912
	v_cvt_f32_f16_sdwa v115, v33 dst_sel:DWORD dst_unused:UNUSED_PAD src0_sel:WORD_1
	v_cvt_f32_f16_sdwa v131, v35 dst_sel:DWORD dst_unused:UNUSED_PAD src0_sel:WORD_1
	v_cvt_f32_f16_e32 v132, v35
	v_sub_f32_e32 v32, v32, v0
	v_sub_f32_e32 v33, v128, v1
	v_sub_f32_e32 v34, v129, v2
	v_pk_mul_f32 v[32:33], v[88:89], v[32:33]
	v_sub_f32_e32 v128, v133, v0
	v_sub_f32_e32 v129, v130, v1
	v_sub_f32_e32 v35, v115, v3
	v_pk_mul_f32 v[128:129], v[88:89], v[128:129]
	s_waitcnt lgkmcnt(1)
	v_fma_f32 v24, v24, v32, v120
	v_fma_f32 v25, v25, v33, v121
	v_pk_mul_f32 v[34:35], v[90:91], v[34:35]
	v_sub_f32_e32 v130, v132, v2
	v_sub_f32_e32 v131, v131, v3
	s_waitcnt lgkmcnt(0)
	v_fma_f32 v32, v116, v128, v124
	ds_write2_b32 v220, v24, v25 offset1:65
	v_fma_f32 v24, v117, v129, v125
	v_pk_mul_f32 v[130:131], v[90:91], v[130:131]
	ds_write2_b32 v221, v32, v24 offset1:65
	v_fma_f32 v24, v26, v34, v122
	v_fmac_f32_e32 v123, v27, v35
	v_fma_f32 v25, v118, v130, v126
	ds_write2_b32 v220, v24, v123 offset0:130 offset1:195
	v_fmac_f32_e32 v127, v119, v131
	s_mov_b32 s16, 0
	v_mov_b32_e32 v24, v103
	ds_write2_b32 v221, v25, v127 offset0:130 offset1:195
	s_waitcnt vmcnt(2)
	ds_write_b128 v96, v[28:31] offset:41984
	s_waitcnt lgkmcnt(0)
	s_barrier
	ds_read_b32 v200, v218
	ds_read_b32 v208, v219
	ds_read_b32 v201, v218 offset:520
	ds_read_b32 v209, v219 offset:256
	ds_read_b32 v202, v218 offset:1040
	ds_read_b32 v210, v219 offset:512
	ds_read_b32 v203, v218 offset:1560
	ds_read_b32 v211, v219 offset:768
	ds_read_b32 v204, v218 offset:2080
	ds_read_b32 v212, v219 offset:1024
	ds_read_b32 v205, v218 offset:2600
	ds_read_b32 v213, v219 offset:1280
	ds_read_b32 v206, v218 offset:3120
	ds_read_b32 v214, v219 offset:1536
	s_waitcnt lgkmcnt(12)
	v_mfma_f32_32x32x2_f32 v[4:19], v200, v208, v[4:19]
	ds_read_b32 v207, v218 offset:3640
	ds_read_b32 v215, v219 offset:1792
	s_waitcnt lgkmcnt(12)
	v_mfma_f32_32x32x2_f32 v[4:19], v201, v209, v[4:19]
	s_waitcnt lgkmcnt(10)
	v_mfma_f32_32x32x2_f32 v[4:19], v202, v210, v[4:19]
	s_waitcnt lgkmcnt(8)
	v_mfma_f32_32x32x2_f32 v[4:19], v203, v211, v[4:19]
	s_waitcnt lgkmcnt(6)
	v_mfma_f32_32x32x2_f32 v[4:19], v204, v212, v[4:19]
	s_waitcnt lgkmcnt(4)
	v_mfma_f32_32x32x2_f32 v[4:19], v205, v213, v[4:19]
	s_waitcnt lgkmcnt(2)
	v_mfma_f32_32x32x2_f32 v[4:19], v206, v214, v[4:19]
	s_waitcnt lgkmcnt(0)
	v_mfma_f32_32x32x2_f32 v[4:19], v207, v215, v[4:19]
	s_barrier
	global_load_dwordx4 v[28:31], v[92:93], off offset:512
	global_load_dwordx4 v[24:27], v[58:59], off
	s_waitcnt vmcnt(3)
	v_cvt_f32_f16_sdwa v128, v36 dst_sel:DWORD dst_unused:UNUSED_PAD src0_sel:WORD_1
	v_cvt_f32_f16_e32 v36, v36
	v_cvt_f32_f16_e32 v129, v37
	v_cvt_f32_f16_sdwa v130, v38 dst_sel:DWORD dst_unused:UNUSED_PAD src0_sel:WORD_1
	v_cvt_f32_f16_e32 v133, v38
	ds_read_b128 v[32:35], v43 offset:13056
	ds_read_b128 v[116:119], v43 offset:13072
	ds_read_b128 v[120:123], v43 offset:17152
	ds_read_b128 v[124:127], v43 offset:17168
	v_cvt_f32_f16_sdwa v115, v37 dst_sel:DWORD dst_unused:UNUSED_PAD src0_sel:WORD_1
	v_cvt_f32_f16_sdwa v131, v39 dst_sel:DWORD dst_unused:UNUSED_PAD src0_sel:WORD_1
	v_cvt_f32_f16_e32 v132, v39
	v_sub_f32_e32 v36, v36, v0
	v_sub_f32_e32 v37, v128, v1
	v_sub_f32_e32 v38, v129, v2
	v_pk_mul_f32 v[36:37], v[88:89], v[36:37]
	v_sub_f32_e32 v128, v133, v0
	v_sub_f32_e32 v129, v130, v1
	v_sub_f32_e32 v39, v115, v3
	v_sub_f32_e32 v130, v132, v2
	v_sub_f32_e32 v131, v131, v3
	v_pk_mul_f32 v[128:129], v[88:89], v[128:129]
	s_waitcnt lgkmcnt(1)
	v_fma_f32 v32, v32, v36, v120
	v_fma_f32 v33, v33, v37, v121
	v_pk_mul_f32 v[38:39], v[90:91], v[38:39]
	v_pk_mul_f32 v[130:131], v[90:91], v[130:131]
	s_waitcnt lgkmcnt(0)
	v_fma_f32 v36, v116, v128, v124
	ds_write2_b32 v220, v32, v33 offset1:65
	v_fma_f32 v32, v117, v129, v125
	ds_write2_b32 v221, v36, v32 offset1:65
	v_fma_f32 v32, v34, v38, v122
	v_fma_f32 v33, v118, v130, v126
	v_fmac_f32_e32 v123, v35, v39
	v_fmac_f32_e32 v127, v119, v131
	ds_write2_b32 v220, v32, v123 offset0:130 offset1:195
	ds_write2_b32 v221, v33, v127 offset0:130 offset1:195
	s_waitcnt vmcnt(2)
	ds_write_b128 v96, v[20:23] offset:41984
	s_mov_b32 s16, 0
	v_mov_b32_e32 v20, v103
	s_waitcnt lgkmcnt(0)
	s_barrier
	ds_read_b32 v200, v218
	ds_read_b32 v208, v219
	ds_read_b32 v201, v218 offset:520
	ds_read_b32 v209, v219 offset:256
	ds_read_b32 v202, v218 offset:1040
	ds_read_b32 v210, v219 offset:512
	ds_read_b32 v203, v218 offset:1560
	ds_read_b32 v211, v219 offset:768
	ds_read_b32 v204, v218 offset:2080
	ds_read_b32 v212, v219 offset:1024
	ds_read_b32 v205, v218 offset:2600
	ds_read_b32 v213, v219 offset:1280
	ds_read_b32 v206, v218 offset:3120
	ds_read_b32 v214, v219 offset:1536
	s_waitcnt lgkmcnt(12)
	v_mfma_f32_32x32x2_f32 v[4:19], v200, v208, v[4:19]
	ds_read_b32 v207, v218 offset:3640
	ds_read_b32 v215, v219 offset:1792
	s_waitcnt lgkmcnt(12)
	v_mfma_f32_32x32x2_f32 v[4:19], v201, v209, v[4:19]
	s_waitcnt lgkmcnt(10)
	v_mfma_f32_32x32x2_f32 v[4:19], v202, v210, v[4:19]
	s_waitcnt lgkmcnt(8)
	v_mfma_f32_32x32x2_f32 v[4:19], v203, v211, v[4:19]
	s_waitcnt lgkmcnt(6)
	v_mfma_f32_32x32x2_f32 v[4:19], v204, v212, v[4:19]
	s_waitcnt lgkmcnt(4)
	v_mfma_f32_32x32x2_f32 v[4:19], v205, v213, v[4:19]
	s_waitcnt lgkmcnt(2)
	v_mfma_f32_32x32x2_f32 v[4:19], v206, v214, v[4:19]
	s_waitcnt lgkmcnt(0)
	v_mfma_f32_32x32x2_f32 v[4:19], v207, v215, v[4:19]
	s_barrier
	global_load_dwordx4 v[32:35], v[92:93], off offset:640
	global_load_dwordx4 v[20:23], v[60:61], off
	s_waitcnt vmcnt(3)
	v_cvt_f32_f16_sdwa v128, v28 dst_sel:DWORD dst_unused:UNUSED_PAD src0_sel:WORD_1
	v_cvt_f32_f16_e32 v28, v28
	v_cvt_f32_f16_e32 v129, v29
	v_cvt_f32_f16_sdwa v130, v30 dst_sel:DWORD dst_unused:UNUSED_PAD src0_sel:WORD_1
	v_cvt_f32_f16_e32 v133, v30
	ds_read_b128 v[36:39], v43 offset:13312
	ds_read_b128 v[116:119], v43 offset:13328
	ds_read_b128 v[120:123], v43 offset:17408
	ds_read_b128 v[124:127], v43 offset:17424
	v_cvt_f32_f16_sdwa v115, v29 dst_sel:DWORD dst_unused:UNUSED_PAD src0_sel:WORD_1
	v_cvt_f32_f16_sdwa v131, v31 dst_sel:DWORD dst_unused:UNUSED_PAD src0_sel:WORD_1
	v_cvt_f32_f16_e32 v132, v31
	v_sub_f32_e32 v28, v28, v0
	v_sub_f32_e32 v29, v128, v1
	v_sub_f32_e32 v30, v129, v2
	v_pk_mul_f32 v[28:29], v[88:89], v[28:29]
	v_sub_f32_e32 v128, v133, v0
	v_sub_f32_e32 v129, v130, v1
	v_sub_f32_e32 v31, v115, v3
	v_sub_f32_e32 v130, v132, v2
	v_sub_f32_e32 v131, v131, v3
	v_pk_mul_f32 v[128:129], v[88:89], v[128:129]
	s_waitcnt lgkmcnt(1)
	v_fma_f32 v28, v36, v28, v120
	v_fma_f32 v29, v37, v29, v121
	v_pk_mul_f32 v[30:31], v[90:91], v[30:31]
	v_pk_mul_f32 v[130:131], v[90:91], v[130:131]
	s_waitcnt lgkmcnt(0)
	v_fma_f32 v36, v116, v128, v124
	ds_write2_b32 v220, v28, v29 offset1:65
	v_fma_f32 v28, v117, v129, v125
	ds_write2_b32 v221, v36, v28 offset1:65
	v_fma_f32 v28, v38, v30, v122
	v_fma_f32 v29, v118, v130, v126
	v_fmac_f32_e32 v123, v39, v31
	v_fmac_f32_e32 v127, v119, v131
	ds_write2_b32 v220, v28, v123 offset0:130 offset1:195
	ds_write2_b32 v221, v29, v127 offset0:130 offset1:195
	s_waitcnt vmcnt(2)
	ds_write_b128 v96, v[24:27] offset:41984
	s_mov_b32 s16, 0
	v_mov_b32_e32 v24, v103
	s_waitcnt lgkmcnt(0)
	s_barrier
	ds_read_b32 v200, v218
	ds_read_b32 v208, v219
	ds_read_b32 v201, v218 offset:520
	ds_read_b32 v209, v219 offset:256
	ds_read_b32 v202, v218 offset:1040
	ds_read_b32 v210, v219 offset:512
	ds_read_b32 v203, v218 offset:1560
	ds_read_b32 v211, v219 offset:768
	ds_read_b32 v204, v218 offset:2080
	ds_read_b32 v212, v219 offset:1024
	ds_read_b32 v205, v218 offset:2600
	ds_read_b32 v213, v219 offset:1280
	ds_read_b32 v206, v218 offset:3120
	ds_read_b32 v214, v219 offset:1536
	s_waitcnt lgkmcnt(12)
	v_mfma_f32_32x32x2_f32 v[4:19], v200, v208, v[4:19]
	ds_read_b32 v207, v218 offset:3640
	ds_read_b32 v215, v219 offset:1792
	s_waitcnt lgkmcnt(12)
	v_mfma_f32_32x32x2_f32 v[4:19], v201, v209, v[4:19]
	s_waitcnt lgkmcnt(10)
	v_mfma_f32_32x32x2_f32 v[4:19], v202, v210, v[4:19]
	s_waitcnt lgkmcnt(8)
	v_mfma_f32_32x32x2_f32 v[4:19], v203, v211, v[4:19]
	s_waitcnt lgkmcnt(6)
	v_mfma_f32_32x32x2_f32 v[4:19], v204, v212, v[4:19]
	s_waitcnt lgkmcnt(4)
	v_mfma_f32_32x32x2_f32 v[4:19], v205, v213, v[4:19]
	s_waitcnt lgkmcnt(2)
	v_mfma_f32_32x32x2_f32 v[4:19], v206, v214, v[4:19]
	s_waitcnt lgkmcnt(0)
	v_mfma_f32_32x32x2_f32 v[4:19], v207, v215, v[4:19]
	s_barrier
	global_load_dwordx4 v[28:31], v[92:93], off offset:768
	global_load_dwordx4 v[24:27], v[62:63], off
	s_waitcnt vmcnt(3)
	v_cvt_f32_f16_sdwa v128, v32 dst_sel:DWORD dst_unused:UNUSED_PAD src0_sel:WORD_1
	v_cvt_f32_f16_e32 v32, v32
	v_cvt_f32_f16_e32 v129, v33
	v_cvt_f32_f16_sdwa v130, v34 dst_sel:DWORD dst_unused:UNUSED_PAD src0_sel:WORD_1
	v_cvt_f32_f16_e32 v133, v34
	ds_read_b128 v[36:39], v43 offset:13568
	ds_read_b128 v[116:119], v43 offset:13584
	ds_read_b128 v[120:123], v43 offset:17664
	ds_read_b128 v[124:127], v43 offset:17680
	v_cvt_f32_f16_sdwa v115, v33 dst_sel:DWORD dst_unused:UNUSED_PAD src0_sel:WORD_1
	v_cvt_f32_f16_sdwa v131, v35 dst_sel:DWORD dst_unused:UNUSED_PAD src0_sel:WORD_1
	v_cvt_f32_f16_e32 v132, v35
	v_sub_f32_e32 v32, v32, v0
	v_sub_f32_e32 v33, v128, v1
	v_sub_f32_e32 v34, v129, v2
	v_pk_mul_f32 v[32:33], v[88:89], v[32:33]
	v_sub_f32_e32 v128, v133, v0
	v_sub_f32_e32 v129, v130, v1
	v_sub_f32_e32 v35, v115, v3
	v_sub_f32_e32 v130, v132, v2
	v_sub_f32_e32 v131, v131, v3
	v_pk_mul_f32 v[128:129], v[88:89], v[128:129]
	s_waitcnt lgkmcnt(1)
	v_fma_f32 v32, v36, v32, v120
	v_fma_f32 v33, v37, v33, v121
	v_pk_mul_f32 v[34:35], v[90:91], v[34:35]
	v_pk_mul_f32 v[130:131], v[90:91], v[130:131]
	s_waitcnt lgkmcnt(0)
	v_fma_f32 v36, v116, v128, v124
	ds_write2_b32 v220, v32, v33 offset1:65
	v_fma_f32 v32, v117, v129, v125
	ds_write2_b32 v221, v36, v32 offset1:65
	v_fma_f32 v32, v38, v34, v122
	v_fma_f32 v33, v118, v130, v126
	v_fmac_f32_e32 v123, v39, v35
	v_fmac_f32_e32 v127, v119, v131
	ds_write2_b32 v220, v32, v123 offset0:130 offset1:195
	ds_write2_b32 v221, v33, v127 offset0:130 offset1:195
	s_waitcnt vmcnt(2)
	ds_write_b128 v96, v[20:23] offset:41984
	s_mov_b32 s16, 0
	v_mov_b32_e32 v20, v103
	s_waitcnt lgkmcnt(0)
	s_barrier
	ds_read_b32 v200, v218
	ds_read_b32 v208, v219
	ds_read_b32 v201, v218 offset:520
	ds_read_b32 v209, v219 offset:256
	ds_read_b32 v202, v218 offset:1040
	ds_read_b32 v210, v219 offset:512
	ds_read_b32 v203, v218 offset:1560
	ds_read_b32 v211, v219 offset:768
	ds_read_b32 v204, v218 offset:2080
	ds_read_b32 v212, v219 offset:1024
	ds_read_b32 v205, v218 offset:2600
	ds_read_b32 v213, v219 offset:1280
	ds_read_b32 v206, v218 offset:3120
	ds_read_b32 v214, v219 offset:1536
	s_waitcnt lgkmcnt(12)
	v_mfma_f32_32x32x2_f32 v[4:19], v200, v208, v[4:19]
	ds_read_b32 v207, v218 offset:3640
	ds_read_b32 v215, v219 offset:1792
	s_waitcnt lgkmcnt(12)
	v_mfma_f32_32x32x2_f32 v[4:19], v201, v209, v[4:19]
	s_waitcnt lgkmcnt(10)
	v_mfma_f32_32x32x2_f32 v[4:19], v202, v210, v[4:19]
	s_waitcnt lgkmcnt(8)
	v_mfma_f32_32x32x2_f32 v[4:19], v203, v211, v[4:19]
	s_waitcnt lgkmcnt(6)
	v_mfma_f32_32x32x2_f32 v[4:19], v204, v212, v[4:19]
	s_waitcnt lgkmcnt(4)
	v_mfma_f32_32x32x2_f32 v[4:19], v205, v213, v[4:19]
	s_waitcnt lgkmcnt(2)
	v_mfma_f32_32x32x2_f32 v[4:19], v206, v214, v[4:19]
	s_waitcnt lgkmcnt(0)
	v_mfma_f32_32x32x2_f32 v[4:19], v207, v215, v[4:19]
	s_barrier
	global_load_dwordx4 v[32:35], v[92:93], off offset:896
	global_load_dwordx4 v[20:23], v[64:65], off
	s_waitcnt vmcnt(3)
	v_cvt_f32_f16_sdwa v128, v28 dst_sel:DWORD dst_unused:UNUSED_PAD src0_sel:WORD_1
	v_cvt_f32_f16_e32 v28, v28
	v_cvt_f32_f16_e32 v129, v29
	v_cvt_f32_f16_sdwa v130, v30 dst_sel:DWORD dst_unused:UNUSED_PAD src0_sel:WORD_1
	v_cvt_f32_f16_e32 v133, v30
	ds_read_b128 v[36:39], v43 offset:13824
	ds_read_b128 v[116:119], v43 offset:13840
	ds_read_b128 v[120:123], v43 offset:17920
	ds_read_b128 v[124:127], v43 offset:17936
	v_cvt_f32_f16_sdwa v115, v29 dst_sel:DWORD dst_unused:UNUSED_PAD src0_sel:WORD_1
	v_cvt_f32_f16_sdwa v131, v31 dst_sel:DWORD dst_unused:UNUSED_PAD src0_sel:WORD_1
	v_cvt_f32_f16_e32 v132, v31
	v_sub_f32_e32 v28, v28, v0
	v_sub_f32_e32 v29, v128, v1
	v_sub_f32_e32 v30, v129, v2
	v_pk_mul_f32 v[28:29], v[88:89], v[28:29]
	v_sub_f32_e32 v128, v133, v0
	v_sub_f32_e32 v129, v130, v1
	v_sub_f32_e32 v31, v115, v3
	v_sub_f32_e32 v130, v132, v2
	v_sub_f32_e32 v131, v131, v3
	v_pk_mul_f32 v[128:129], v[88:89], v[128:129]
	s_waitcnt lgkmcnt(1)
	v_fma_f32 v28, v36, v28, v120
	v_fma_f32 v29, v37, v29, v121
	v_pk_mul_f32 v[30:31], v[90:91], v[30:31]
	v_pk_mul_f32 v[130:131], v[90:91], v[130:131]
	s_waitcnt lgkmcnt(0)
	v_fma_f32 v36, v116, v128, v124
	ds_write2_b32 v220, v28, v29 offset1:65
	v_fma_f32 v28, v117, v129, v125
	ds_write2_b32 v221, v36, v28 offset1:65
	v_fma_f32 v28, v38, v30, v122
	v_fma_f32 v29, v118, v130, v126
	v_fmac_f32_e32 v123, v39, v31
	v_fmac_f32_e32 v127, v119, v131
	ds_write2_b32 v220, v28, v123 offset0:130 offset1:195
	ds_write2_b32 v221, v29, v127 offset0:130 offset1:195
	s_waitcnt vmcnt(2)
	ds_write_b128 v96, v[24:27] offset:41984
	s_mov_b32 s16, 0
	v_mov_b32_e32 v24, v103
	s_waitcnt lgkmcnt(0)
	s_barrier
	ds_read_b32 v200, v218
	ds_read_b32 v208, v219
	ds_read_b32 v201, v218 offset:520
	ds_read_b32 v209, v219 offset:256
	ds_read_b32 v202, v218 offset:1040
	ds_read_b32 v210, v219 offset:512
	ds_read_b32 v203, v218 offset:1560
	ds_read_b32 v211, v219 offset:768
	ds_read_b32 v204, v218 offset:2080
	ds_read_b32 v212, v219 offset:1024
	ds_read_b32 v205, v218 offset:2600
	ds_read_b32 v213, v219 offset:1280
	ds_read_b32 v206, v218 offset:3120
	ds_read_b32 v214, v219 offset:1536
	s_waitcnt lgkmcnt(12)
	v_mfma_f32_32x32x2_f32 v[4:19], v200, v208, v[4:19]
	ds_read_b32 v207, v218 offset:3640
	ds_read_b32 v215, v219 offset:1792
	s_waitcnt lgkmcnt(12)
	v_mfma_f32_32x32x2_f32 v[4:19], v201, v209, v[4:19]
	s_waitcnt lgkmcnt(10)
	v_mfma_f32_32x32x2_f32 v[4:19], v202, v210, v[4:19]
	s_waitcnt lgkmcnt(8)
	v_mfma_f32_32x32x2_f32 v[4:19], v203, v211, v[4:19]
	s_waitcnt lgkmcnt(6)
	v_mfma_f32_32x32x2_f32 v[4:19], v204, v212, v[4:19]
	s_waitcnt lgkmcnt(4)
	v_mfma_f32_32x32x2_f32 v[4:19], v205, v213, v[4:19]
	s_waitcnt lgkmcnt(2)
	v_mfma_f32_32x32x2_f32 v[4:19], v206, v214, v[4:19]
	s_waitcnt lgkmcnt(0)
	v_mfma_f32_32x32x2_f32 v[4:19], v207, v215, v[4:19]
	s_barrier
	global_load_dwordx4 v[28:31], v[92:93], off offset:1024
	global_load_dwordx4 v[24:27], v[66:67], off
	s_waitcnt vmcnt(3)
	v_cvt_f32_f16_sdwa v128, v32 dst_sel:DWORD dst_unused:UNUSED_PAD src0_sel:WORD_1
	v_cvt_f32_f16_e32 v32, v32
	v_cvt_f32_f16_e32 v129, v33
	v_cvt_f32_f16_sdwa v130, v34 dst_sel:DWORD dst_unused:UNUSED_PAD src0_sel:WORD_1
	v_cvt_f32_f16_e32 v133, v34
	ds_read_b128 v[36:39], v43 offset:14080
	ds_read_b128 v[116:119], v43 offset:14096
	ds_read_b128 v[120:123], v43 offset:18176
	ds_read_b128 v[124:127], v43 offset:18192
	v_cvt_f32_f16_sdwa v115, v33 dst_sel:DWORD dst_unused:UNUSED_PAD src0_sel:WORD_1
	v_cvt_f32_f16_sdwa v131, v35 dst_sel:DWORD dst_unused:UNUSED_PAD src0_sel:WORD_1
	v_cvt_f32_f16_e32 v132, v35
	v_sub_f32_e32 v32, v32, v0
	v_sub_f32_e32 v33, v128, v1
	v_sub_f32_e32 v34, v129, v2
	v_pk_mul_f32 v[32:33], v[88:89], v[32:33]
	v_sub_f32_e32 v128, v133, v0
	v_sub_f32_e32 v129, v130, v1
	v_sub_f32_e32 v35, v115, v3
	v_sub_f32_e32 v130, v132, v2
	v_sub_f32_e32 v131, v131, v3
	v_pk_mul_f32 v[128:129], v[88:89], v[128:129]
	s_waitcnt lgkmcnt(1)
	v_fma_f32 v32, v36, v32, v120
	v_fma_f32 v33, v37, v33, v121
	v_pk_mul_f32 v[34:35], v[90:91], v[34:35]
	v_pk_mul_f32 v[130:131], v[90:91], v[130:131]
	s_waitcnt lgkmcnt(0)
	v_fma_f32 v36, v116, v128, v124
	ds_write2_b32 v220, v32, v33 offset1:65
	v_fma_f32 v32, v117, v129, v125
	ds_write2_b32 v221, v36, v32 offset1:65
	v_fma_f32 v32, v38, v34, v122
	v_fma_f32 v33, v118, v130, v126
	v_fmac_f32_e32 v123, v39, v35
	v_fmac_f32_e32 v127, v119, v131
	ds_write2_b32 v220, v32, v123 offset0:130 offset1:195
	ds_write2_b32 v221, v33, v127 offset0:130 offset1:195
	s_waitcnt vmcnt(2)
	ds_write_b128 v96, v[20:23] offset:41984
	s_mov_b32 s16, 0
	v_mov_b32_e32 v20, v103
	s_waitcnt lgkmcnt(0)
	s_barrier
	ds_read_b32 v200, v218
	ds_read_b32 v208, v219
	ds_read_b32 v201, v218 offset:520
	ds_read_b32 v209, v219 offset:256
	ds_read_b32 v202, v218 offset:1040
	ds_read_b32 v210, v219 offset:512
	ds_read_b32 v203, v218 offset:1560
	ds_read_b32 v211, v219 offset:768
	ds_read_b32 v204, v218 offset:2080
	ds_read_b32 v212, v219 offset:1024
	ds_read_b32 v205, v218 offset:2600
	ds_read_b32 v213, v219 offset:1280
	ds_read_b32 v206, v218 offset:3120
	ds_read_b32 v214, v219 offset:1536
	s_waitcnt lgkmcnt(12)
	v_mfma_f32_32x32x2_f32 v[4:19], v200, v208, v[4:19]
	ds_read_b32 v207, v218 offset:3640
	ds_read_b32 v215, v219 offset:1792
	s_waitcnt lgkmcnt(12)
	v_mfma_f32_32x32x2_f32 v[4:19], v201, v209, v[4:19]
	s_waitcnt lgkmcnt(10)
	v_mfma_f32_32x32x2_f32 v[4:19], v202, v210, v[4:19]
	s_waitcnt lgkmcnt(8)
	v_mfma_f32_32x32x2_f32 v[4:19], v203, v211, v[4:19]
	s_waitcnt lgkmcnt(6)
	v_mfma_f32_32x32x2_f32 v[4:19], v204, v212, v[4:19]
	s_waitcnt lgkmcnt(4)
	v_mfma_f32_32x32x2_f32 v[4:19], v205, v213, v[4:19]
	s_waitcnt lgkmcnt(2)
	v_mfma_f32_32x32x2_f32 v[4:19], v206, v214, v[4:19]
	s_waitcnt lgkmcnt(0)
	v_mfma_f32_32x32x2_f32 v[4:19], v207, v215, v[4:19]
	s_barrier
	global_load_dwordx4 v[32:35], v[92:93], off offset:1152
	global_load_dwordx4 v[20:23], v[68:69], off
	s_waitcnt vmcnt(3)
	v_cvt_f32_f16_sdwa v128, v28 dst_sel:DWORD dst_unused:UNUSED_PAD src0_sel:WORD_1
	v_cvt_f32_f16_e32 v28, v28
	v_cvt_f32_f16_e32 v129, v29
	v_cvt_f32_f16_sdwa v130, v30 dst_sel:DWORD dst_unused:UNUSED_PAD src0_sel:WORD_1
	v_cvt_f32_f16_e32 v133, v30
	ds_read_b128 v[36:39], v43 offset:14336
	ds_read_b128 v[116:119], v43 offset:14352
	ds_read_b128 v[120:123], v43 offset:18432
	ds_read_b128 v[124:127], v43 offset:18448
	v_cvt_f32_f16_sdwa v115, v29 dst_sel:DWORD dst_unused:UNUSED_PAD src0_sel:WORD_1
	v_cvt_f32_f16_sdwa v131, v31 dst_sel:DWORD dst_unused:UNUSED_PAD src0_sel:WORD_1
	v_cvt_f32_f16_e32 v132, v31
	v_sub_f32_e32 v28, v28, v0
	v_sub_f32_e32 v29, v128, v1
	v_sub_f32_e32 v30, v129, v2
	v_pk_mul_f32 v[28:29], v[88:89], v[28:29]
	v_sub_f32_e32 v128, v133, v0
	v_sub_f32_e32 v129, v130, v1
	v_sub_f32_e32 v31, v115, v3
	v_sub_f32_e32 v130, v132, v2
	v_sub_f32_e32 v131, v131, v3
	v_pk_mul_f32 v[128:129], v[88:89], v[128:129]
	s_waitcnt lgkmcnt(1)
	v_fma_f32 v28, v36, v28, v120
	v_fma_f32 v29, v37, v29, v121
	v_pk_mul_f32 v[30:31], v[90:91], v[30:31]
	v_pk_mul_f32 v[130:131], v[90:91], v[130:131]
	s_waitcnt lgkmcnt(0)
	v_fma_f32 v36, v116, v128, v124
	ds_write2_b32 v220, v28, v29 offset1:65
	v_fma_f32 v28, v117, v129, v125
	ds_write2_b32 v221, v36, v28 offset1:65
	v_fma_f32 v28, v38, v30, v122
	v_fma_f32 v29, v118, v130, v126
	v_fmac_f32_e32 v123, v39, v31
	v_fmac_f32_e32 v127, v119, v131
	ds_write2_b32 v220, v28, v123 offset0:130 offset1:195
	ds_write2_b32 v221, v29, v127 offset0:130 offset1:195
	s_waitcnt vmcnt(2)
	ds_write_b128 v96, v[24:27] offset:41984
	s_mov_b32 s16, 0
	v_mov_b32_e32 v24, v103
	s_waitcnt lgkmcnt(0)
	s_barrier
	ds_read_b32 v200, v218
	ds_read_b32 v208, v219
	ds_read_b32 v201, v218 offset:520
	ds_read_b32 v209, v219 offset:256
	ds_read_b32 v202, v218 offset:1040
	ds_read_b32 v210, v219 offset:512
	ds_read_b32 v203, v218 offset:1560
	ds_read_b32 v211, v219 offset:768
	ds_read_b32 v204, v218 offset:2080
	ds_read_b32 v212, v219 offset:1024
	ds_read_b32 v205, v218 offset:2600
	ds_read_b32 v213, v219 offset:1280
	ds_read_b32 v206, v218 offset:3120
	ds_read_b32 v214, v219 offset:1536
	s_waitcnt lgkmcnt(12)
	v_mfma_f32_32x32x2_f32 v[4:19], v200, v208, v[4:19]
	ds_read_b32 v207, v218 offset:3640
	ds_read_b32 v215, v219 offset:1792
	s_waitcnt lgkmcnt(12)
	v_mfma_f32_32x32x2_f32 v[4:19], v201, v209, v[4:19]
	s_waitcnt lgkmcnt(10)
	v_mfma_f32_32x32x2_f32 v[4:19], v202, v210, v[4:19]
	s_waitcnt lgkmcnt(8)
	v_mfma_f32_32x32x2_f32 v[4:19], v203, v211, v[4:19]
	s_waitcnt lgkmcnt(6)
	v_mfma_f32_32x32x2_f32 v[4:19], v204, v212, v[4:19]
	s_waitcnt lgkmcnt(4)
	v_mfma_f32_32x32x2_f32 v[4:19], v205, v213, v[4:19]
	s_waitcnt lgkmcnt(2)
	v_mfma_f32_32x32x2_f32 v[4:19], v206, v214, v[4:19]
	s_waitcnt lgkmcnt(0)
	v_mfma_f32_32x32x2_f32 v[4:19], v207, v215, v[4:19]
	s_barrier
	global_load_dwordx4 v[28:31], v[92:93], off offset:1280
	global_load_dwordx4 v[24:27], v[70:71], off
	s_waitcnt vmcnt(3)
	v_cvt_f32_f16_sdwa v128, v32 dst_sel:DWORD dst_unused:UNUSED_PAD src0_sel:WORD_1
	v_cvt_f32_f16_e32 v32, v32
	v_cvt_f32_f16_e32 v129, v33
	v_cvt_f32_f16_sdwa v130, v34 dst_sel:DWORD dst_unused:UNUSED_PAD src0_sel:WORD_1
	v_cvt_f32_f16_e32 v133, v34
	ds_read_b128 v[36:39], v43 offset:14592
	ds_read_b128 v[116:119], v43 offset:14608
	ds_read_b128 v[120:123], v43 offset:18688
	ds_read_b128 v[124:127], v43 offset:18704
	v_cvt_f32_f16_sdwa v115, v33 dst_sel:DWORD dst_unused:UNUSED_PAD src0_sel:WORD_1
	v_cvt_f32_f16_sdwa v131, v35 dst_sel:DWORD dst_unused:UNUSED_PAD src0_sel:WORD_1
	v_cvt_f32_f16_e32 v132, v35
	v_sub_f32_e32 v32, v32, v0
	v_sub_f32_e32 v33, v128, v1
	v_sub_f32_e32 v34, v129, v2
	v_pk_mul_f32 v[32:33], v[88:89], v[32:33]
	v_sub_f32_e32 v128, v133, v0
	v_sub_f32_e32 v129, v130, v1
	v_sub_f32_e32 v35, v115, v3
	v_sub_f32_e32 v130, v132, v2
	v_sub_f32_e32 v131, v131, v3
	v_pk_mul_f32 v[128:129], v[88:89], v[128:129]
	s_waitcnt lgkmcnt(1)
	v_fma_f32 v32, v36, v32, v120
	v_fma_f32 v33, v37, v33, v121
	v_pk_mul_f32 v[34:35], v[90:91], v[34:35]
	v_pk_mul_f32 v[130:131], v[90:91], v[130:131]
	s_waitcnt lgkmcnt(0)
	v_fma_f32 v36, v116, v128, v124
	ds_write2_b32 v220, v32, v33 offset1:65
	v_fma_f32 v32, v117, v129, v125
	ds_write2_b32 v221, v36, v32 offset1:65
	v_fma_f32 v32, v38, v34, v122
	v_fma_f32 v33, v118, v130, v126
	v_fmac_f32_e32 v123, v39, v35
	v_fmac_f32_e32 v127, v119, v131
	ds_write2_b32 v220, v32, v123 offset0:130 offset1:195
	ds_write2_b32 v221, v33, v127 offset0:130 offset1:195
	s_waitcnt vmcnt(2)
	ds_write_b128 v96, v[20:23] offset:41984
	s_mov_b32 s16, 0
	v_mov_b32_e32 v20, v103
	s_waitcnt lgkmcnt(0)
	s_barrier
	ds_read_b32 v200, v218
	ds_read_b32 v208, v219
	ds_read_b32 v201, v218 offset:520
	ds_read_b32 v209, v219 offset:256
	ds_read_b32 v202, v218 offset:1040
	ds_read_b32 v210, v219 offset:512
	ds_read_b32 v203, v218 offset:1560
	ds_read_b32 v211, v219 offset:768
	ds_read_b32 v204, v218 offset:2080
	ds_read_b32 v212, v219 offset:1024
	ds_read_b32 v205, v218 offset:2600
	ds_read_b32 v213, v219 offset:1280
	ds_read_b32 v206, v218 offset:3120
	ds_read_b32 v214, v219 offset:1536
	s_waitcnt lgkmcnt(12)
	v_mfma_f32_32x32x2_f32 v[4:19], v200, v208, v[4:19]
	ds_read_b32 v207, v218 offset:3640
	ds_read_b32 v215, v219 offset:1792
	s_waitcnt lgkmcnt(12)
	v_mfma_f32_32x32x2_f32 v[4:19], v201, v209, v[4:19]
	s_waitcnt lgkmcnt(10)
	v_mfma_f32_32x32x2_f32 v[4:19], v202, v210, v[4:19]
	s_waitcnt lgkmcnt(8)
	v_mfma_f32_32x32x2_f32 v[4:19], v203, v211, v[4:19]
	s_waitcnt lgkmcnt(6)
	v_mfma_f32_32x32x2_f32 v[4:19], v204, v212, v[4:19]
	s_waitcnt lgkmcnt(4)
	v_mfma_f32_32x32x2_f32 v[4:19], v205, v213, v[4:19]
	s_waitcnt lgkmcnt(2)
	v_mfma_f32_32x32x2_f32 v[4:19], v206, v214, v[4:19]
	s_waitcnt lgkmcnt(0)
	v_mfma_f32_32x32x2_f32 v[4:19], v207, v215, v[4:19]
	s_barrier
	global_load_dwordx4 v[32:35], v[92:93], off offset:1408
	global_load_dwordx4 v[20:23], v[72:73], off
	s_waitcnt vmcnt(3)
	v_cvt_f32_f16_sdwa v128, v28 dst_sel:DWORD dst_unused:UNUSED_PAD src0_sel:WORD_1
	v_cvt_f32_f16_e32 v28, v28
	v_cvt_f32_f16_e32 v129, v29
	v_cvt_f32_f16_sdwa v130, v30 dst_sel:DWORD dst_unused:UNUSED_PAD src0_sel:WORD_1
	v_cvt_f32_f16_e32 v133, v30
	ds_read_b128 v[36:39], v43 offset:14848
	ds_read_b128 v[116:119], v43 offset:14864
	ds_read_b128 v[120:123], v43 offset:18944
	ds_read_b128 v[124:127], v43 offset:18960
	v_cvt_f32_f16_sdwa v115, v29 dst_sel:DWORD dst_unused:UNUSED_PAD src0_sel:WORD_1
	v_cvt_f32_f16_sdwa v131, v31 dst_sel:DWORD dst_unused:UNUSED_PAD src0_sel:WORD_1
	v_cvt_f32_f16_e32 v132, v31
	v_sub_f32_e32 v28, v28, v0
	v_sub_f32_e32 v29, v128, v1
	v_sub_f32_e32 v30, v129, v2
	v_pk_mul_f32 v[28:29], v[88:89], v[28:29]
	v_sub_f32_e32 v128, v133, v0
	v_sub_f32_e32 v129, v130, v1
	v_sub_f32_e32 v31, v115, v3
	v_sub_f32_e32 v130, v132, v2
	v_sub_f32_e32 v131, v131, v3
	v_pk_mul_f32 v[128:129], v[88:89], v[128:129]
	s_waitcnt lgkmcnt(1)
	v_fma_f32 v28, v36, v28, v120
	v_fma_f32 v29, v37, v29, v121
	v_pk_mul_f32 v[30:31], v[90:91], v[30:31]
	v_pk_mul_f32 v[130:131], v[90:91], v[130:131]
	s_waitcnt lgkmcnt(0)
	v_fma_f32 v36, v116, v128, v124
	ds_write2_b32 v220, v28, v29 offset1:65
	v_fma_f32 v28, v117, v129, v125
	ds_write2_b32 v221, v36, v28 offset1:65
	v_fma_f32 v28, v38, v30, v122
	v_fma_f32 v29, v118, v130, v126
	v_fmac_f32_e32 v123, v39, v31
	v_fmac_f32_e32 v127, v119, v131
	ds_write2_b32 v220, v28, v123 offset0:130 offset1:195
	ds_write2_b32 v221, v29, v127 offset0:130 offset1:195
	s_waitcnt vmcnt(2)
	ds_write_b128 v96, v[24:27] offset:41984
	s_mov_b32 s16, 0
	v_mov_b32_e32 v24, v103
	s_waitcnt lgkmcnt(0)
	s_barrier
	ds_read_b32 v200, v218
	ds_read_b32 v208, v219
	ds_read_b32 v201, v218 offset:520
	ds_read_b32 v209, v219 offset:256
	ds_read_b32 v202, v218 offset:1040
	ds_read_b32 v210, v219 offset:512
	ds_read_b32 v203, v218 offset:1560
	ds_read_b32 v211, v219 offset:768
	ds_read_b32 v204, v218 offset:2080
	ds_read_b32 v212, v219 offset:1024
	ds_read_b32 v205, v218 offset:2600
	ds_read_b32 v213, v219 offset:1280
	ds_read_b32 v206, v218 offset:3120
	ds_read_b32 v214, v219 offset:1536
	s_waitcnt lgkmcnt(12)
	v_mfma_f32_32x32x2_f32 v[4:19], v200, v208, v[4:19]
	ds_read_b32 v207, v218 offset:3640
	ds_read_b32 v215, v219 offset:1792
	s_waitcnt lgkmcnt(12)
	v_mfma_f32_32x32x2_f32 v[4:19], v201, v209, v[4:19]
	s_waitcnt lgkmcnt(10)
	v_mfma_f32_32x32x2_f32 v[4:19], v202, v210, v[4:19]
	s_waitcnt lgkmcnt(8)
	v_mfma_f32_32x32x2_f32 v[4:19], v203, v211, v[4:19]
	s_waitcnt lgkmcnt(6)
	v_mfma_f32_32x32x2_f32 v[4:19], v204, v212, v[4:19]
	s_waitcnt lgkmcnt(4)
	v_mfma_f32_32x32x2_f32 v[4:19], v205, v213, v[4:19]
	s_waitcnt lgkmcnt(2)
	v_mfma_f32_32x32x2_f32 v[4:19], v206, v214, v[4:19]
	s_waitcnt lgkmcnt(0)
	v_mfma_f32_32x32x2_f32 v[4:19], v207, v215, v[4:19]
	s_barrier
	global_load_dwordx4 v[28:31], v[92:93], off offset:1536
	global_load_dwordx4 v[24:27], v[74:75], off
	s_waitcnt vmcnt(3)
	v_cvt_f32_f16_sdwa v128, v32 dst_sel:DWORD dst_unused:UNUSED_PAD src0_sel:WORD_1
	v_cvt_f32_f16_e32 v32, v32
	v_cvt_f32_f16_e32 v129, v33
	v_cvt_f32_f16_sdwa v130, v34 dst_sel:DWORD dst_unused:UNUSED_PAD src0_sel:WORD_1
	v_cvt_f32_f16_e32 v133, v34
	ds_read_b128 v[36:39], v43 offset:15104
	ds_read_b128 v[116:119], v43 offset:15120
	ds_read_b128 v[120:123], v43 offset:19200
	ds_read_b128 v[124:127], v43 offset:19216
	v_cvt_f32_f16_sdwa v115, v33 dst_sel:DWORD dst_unused:UNUSED_PAD src0_sel:WORD_1
	v_cvt_f32_f16_sdwa v131, v35 dst_sel:DWORD dst_unused:UNUSED_PAD src0_sel:WORD_1
	v_cvt_f32_f16_e32 v132, v35
	v_sub_f32_e32 v32, v32, v0
	v_sub_f32_e32 v33, v128, v1
	v_sub_f32_e32 v34, v129, v2
	v_pk_mul_f32 v[32:33], v[88:89], v[32:33]
	v_sub_f32_e32 v128, v133, v0
	v_sub_f32_e32 v129, v130, v1
	v_sub_f32_e32 v35, v115, v3
	v_sub_f32_e32 v130, v132, v2
	v_sub_f32_e32 v131, v131, v3
	v_pk_mul_f32 v[128:129], v[88:89], v[128:129]
	s_waitcnt lgkmcnt(1)
	v_fma_f32 v32, v36, v32, v120
	v_fma_f32 v33, v37, v33, v121
	v_pk_mul_f32 v[34:35], v[90:91], v[34:35]
	v_pk_mul_f32 v[130:131], v[90:91], v[130:131]
	s_waitcnt lgkmcnt(0)
	v_fma_f32 v36, v116, v128, v124
	ds_write2_b32 v220, v32, v33 offset1:65
	v_fma_f32 v32, v117, v129, v125
	ds_write2_b32 v221, v36, v32 offset1:65
	v_fma_f32 v32, v38, v34, v122
	v_fma_f32 v33, v118, v130, v126
	v_fmac_f32_e32 v123, v39, v35
	v_fmac_f32_e32 v127, v119, v131
	ds_write2_b32 v220, v32, v123 offset0:130 offset1:195
	ds_write2_b32 v221, v33, v127 offset0:130 offset1:195
	s_waitcnt vmcnt(2)
	ds_write_b128 v96, v[20:23] offset:41984
	s_mov_b32 s16, 0
	v_mov_b32_e32 v20, v103
	s_waitcnt lgkmcnt(0)
	s_barrier
	ds_read_b32 v200, v218
	ds_read_b32 v208, v219
	ds_read_b32 v201, v218 offset:520
	ds_read_b32 v209, v219 offset:256
	ds_read_b32 v202, v218 offset:1040
	ds_read_b32 v210, v219 offset:512
	ds_read_b32 v203, v218 offset:1560
	ds_read_b32 v211, v219 offset:768
	ds_read_b32 v204, v218 offset:2080
	ds_read_b32 v212, v219 offset:1024
	ds_read_b32 v205, v218 offset:2600
	ds_read_b32 v213, v219 offset:1280
	ds_read_b32 v206, v218 offset:3120
	ds_read_b32 v214, v219 offset:1536
	s_waitcnt lgkmcnt(12)
	v_mfma_f32_32x32x2_f32 v[4:19], v200, v208, v[4:19]
	ds_read_b32 v207, v218 offset:3640
	ds_read_b32 v215, v219 offset:1792
	s_waitcnt lgkmcnt(12)
	v_mfma_f32_32x32x2_f32 v[4:19], v201, v209, v[4:19]
	s_waitcnt lgkmcnt(10)
	v_mfma_f32_32x32x2_f32 v[4:19], v202, v210, v[4:19]
	s_waitcnt lgkmcnt(8)
	v_mfma_f32_32x32x2_f32 v[4:19], v203, v211, v[4:19]
	s_waitcnt lgkmcnt(6)
	v_mfma_f32_32x32x2_f32 v[4:19], v204, v212, v[4:19]
	s_waitcnt lgkmcnt(4)
	v_mfma_f32_32x32x2_f32 v[4:19], v205, v213, v[4:19]
	s_waitcnt lgkmcnt(2)
	v_mfma_f32_32x32x2_f32 v[4:19], v206, v214, v[4:19]
	s_waitcnt lgkmcnt(0)
	v_mfma_f32_32x32x2_f32 v[4:19], v207, v215, v[4:19]
	s_barrier
	global_load_dwordx4 v[32:35], v[92:93], off offset:1664
	global_load_dwordx4 v[20:23], v[76:77], off
	s_waitcnt vmcnt(3)
	v_cvt_f32_f16_sdwa v128, v28 dst_sel:DWORD dst_unused:UNUSED_PAD src0_sel:WORD_1
	v_cvt_f32_f16_e32 v28, v28
	v_cvt_f32_f16_e32 v129, v29
	v_cvt_f32_f16_sdwa v130, v30 dst_sel:DWORD dst_unused:UNUSED_PAD src0_sel:WORD_1
	v_cvt_f32_f16_e32 v133, v30
	ds_read_b128 v[36:39], v43 offset:15360
	ds_read_b128 v[116:119], v43 offset:15376
	ds_read_b128 v[120:123], v43 offset:19456
	ds_read_b128 v[124:127], v43 offset:19472
	v_cvt_f32_f16_sdwa v115, v29 dst_sel:DWORD dst_unused:UNUSED_PAD src0_sel:WORD_1
	v_cvt_f32_f16_sdwa v131, v31 dst_sel:DWORD dst_unused:UNUSED_PAD src0_sel:WORD_1
	v_cvt_f32_f16_e32 v132, v31
	v_sub_f32_e32 v28, v28, v0
	v_sub_f32_e32 v29, v128, v1
	v_sub_f32_e32 v30, v129, v2
	v_pk_mul_f32 v[28:29], v[88:89], v[28:29]
	v_sub_f32_e32 v128, v133, v0
	v_sub_f32_e32 v129, v130, v1
	v_sub_f32_e32 v31, v115, v3
	v_sub_f32_e32 v130, v132, v2
	v_sub_f32_e32 v131, v131, v3
	v_pk_mul_f32 v[128:129], v[88:89], v[128:129]
	s_waitcnt lgkmcnt(1)
	v_fma_f32 v28, v36, v28, v120
	v_fma_f32 v29, v37, v29, v121
	v_pk_mul_f32 v[30:31], v[90:91], v[30:31]
	v_pk_mul_f32 v[130:131], v[90:91], v[130:131]
	s_waitcnt lgkmcnt(0)
	v_fma_f32 v36, v116, v128, v124
	ds_write2_b32 v220, v28, v29 offset1:65
	v_fma_f32 v28, v117, v129, v125
	ds_write2_b32 v221, v36, v28 offset1:65
	v_fma_f32 v28, v38, v30, v122
	v_fma_f32 v29, v118, v130, v126
	v_fmac_f32_e32 v123, v39, v31
	v_fmac_f32_e32 v127, v119, v131
	ds_write2_b32 v220, v28, v123 offset0:130 offset1:195
	ds_write2_b32 v221, v29, v127 offset0:130 offset1:195
	s_waitcnt vmcnt(2)
	ds_write_b128 v96, v[24:27] offset:41984
	s_mov_b32 s16, 0
	v_mov_b32_e32 v24, v103
	s_waitcnt lgkmcnt(0)
	s_barrier
	ds_read_b32 v200, v218
	ds_read_b32 v208, v219
	ds_read_b32 v201, v218 offset:520
	ds_read_b32 v209, v219 offset:256
	ds_read_b32 v202, v218 offset:1040
	ds_read_b32 v210, v219 offset:512
	ds_read_b32 v203, v218 offset:1560
	ds_read_b32 v211, v219 offset:768
	ds_read_b32 v204, v218 offset:2080
	ds_read_b32 v212, v219 offset:1024
	ds_read_b32 v205, v218 offset:2600
	ds_read_b32 v213, v219 offset:1280
	ds_read_b32 v206, v218 offset:3120
	ds_read_b32 v214, v219 offset:1536
	s_waitcnt lgkmcnt(12)
	v_mfma_f32_32x32x2_f32 v[4:19], v200, v208, v[4:19]
	ds_read_b32 v207, v218 offset:3640
	ds_read_b32 v215, v219 offset:1792
	s_waitcnt lgkmcnt(12)
	v_mfma_f32_32x32x2_f32 v[4:19], v201, v209, v[4:19]
	s_waitcnt lgkmcnt(10)
	v_mfma_f32_32x32x2_f32 v[4:19], v202, v210, v[4:19]
	s_waitcnt lgkmcnt(8)
	v_mfma_f32_32x32x2_f32 v[4:19], v203, v211, v[4:19]
	s_waitcnt lgkmcnt(6)
	v_mfma_f32_32x32x2_f32 v[4:19], v204, v212, v[4:19]
	s_waitcnt lgkmcnt(4)
	v_mfma_f32_32x32x2_f32 v[4:19], v205, v213, v[4:19]
	s_waitcnt lgkmcnt(2)
	v_mfma_f32_32x32x2_f32 v[4:19], v206, v214, v[4:19]
	s_waitcnt lgkmcnt(0)
	v_mfma_f32_32x32x2_f32 v[4:19], v207, v215, v[4:19]
	s_barrier
	global_load_dwordx4 v[28:31], v[92:93], off offset:1792
	global_load_dwordx4 v[24:27], v[78:79], off
	s_waitcnt vmcnt(3)
	v_cvt_f32_f16_sdwa v128, v32 dst_sel:DWORD dst_unused:UNUSED_PAD src0_sel:WORD_1
	v_cvt_f32_f16_e32 v32, v32
	v_cvt_f32_f16_e32 v129, v33
	v_cvt_f32_f16_sdwa v130, v34 dst_sel:DWORD dst_unused:UNUSED_PAD src0_sel:WORD_1
	v_cvt_f32_f16_e32 v133, v34
	ds_read_b128 v[36:39], v43 offset:15616
	ds_read_b128 v[116:119], v43 offset:15632
	ds_read_b128 v[120:123], v43 offset:19712
	ds_read_b128 v[124:127], v43 offset:19728
	v_cvt_f32_f16_sdwa v115, v33 dst_sel:DWORD dst_unused:UNUSED_PAD src0_sel:WORD_1
	v_cvt_f32_f16_sdwa v131, v35 dst_sel:DWORD dst_unused:UNUSED_PAD src0_sel:WORD_1
	v_cvt_f32_f16_e32 v132, v35
	v_sub_f32_e32 v32, v32, v0
	v_sub_f32_e32 v33, v128, v1
	v_sub_f32_e32 v34, v129, v2
	v_pk_mul_f32 v[32:33], v[88:89], v[32:33]
	v_sub_f32_e32 v128, v133, v0
	v_sub_f32_e32 v129, v130, v1
	v_sub_f32_e32 v35, v115, v3
	v_sub_f32_e32 v130, v132, v2
	v_sub_f32_e32 v131, v131, v3
	v_pk_mul_f32 v[128:129], v[88:89], v[128:129]
	s_waitcnt lgkmcnt(1)
	v_fma_f32 v32, v36, v32, v120
	v_fma_f32 v33, v37, v33, v121
	v_pk_mul_f32 v[34:35], v[90:91], v[34:35]
	v_pk_mul_f32 v[130:131], v[90:91], v[130:131]
	s_waitcnt lgkmcnt(0)
	v_fma_f32 v36, v116, v128, v124
	ds_write2_b32 v220, v32, v33 offset1:65
	v_fma_f32 v32, v117, v129, v125
	ds_write2_b32 v221, v36, v32 offset1:65
	v_fma_f32 v32, v38, v34, v122
	v_fma_f32 v33, v118, v130, v126
	v_fmac_f32_e32 v123, v39, v35
	v_fmac_f32_e32 v127, v119, v131
	ds_write2_b32 v220, v32, v123 offset0:130 offset1:195
	ds_write2_b32 v221, v33, v127 offset0:130 offset1:195
	s_waitcnt vmcnt(2)
	ds_write_b128 v96, v[20:23] offset:41984
	s_mov_b32 s16, 0
	v_mov_b32_e32 v20, v103
	s_waitcnt lgkmcnt(0)
	s_barrier
	ds_read_b32 v200, v218
	ds_read_b32 v208, v219
	ds_read_b32 v201, v218 offset:520
	ds_read_b32 v209, v219 offset:256
	ds_read_b32 v202, v218 offset:1040
	ds_read_b32 v210, v219 offset:512
	ds_read_b32 v203, v218 offset:1560
	ds_read_b32 v211, v219 offset:768
	ds_read_b32 v204, v218 offset:2080
	ds_read_b32 v212, v219 offset:1024
	ds_read_b32 v205, v218 offset:2600
	ds_read_b32 v213, v219 offset:1280
	ds_read_b32 v206, v218 offset:3120
	ds_read_b32 v214, v219 offset:1536
	s_waitcnt lgkmcnt(12)
	v_mfma_f32_32x32x2_f32 v[4:19], v200, v208, v[4:19]
	ds_read_b32 v207, v218 offset:3640
	ds_read_b32 v215, v219 offset:1792
	s_waitcnt lgkmcnt(12)
	v_mfma_f32_32x32x2_f32 v[4:19], v201, v209, v[4:19]
	s_waitcnt lgkmcnt(10)
	v_mfma_f32_32x32x2_f32 v[4:19], v202, v210, v[4:19]
	s_waitcnt lgkmcnt(8)
	v_mfma_f32_32x32x2_f32 v[4:19], v203, v211, v[4:19]
	s_waitcnt lgkmcnt(6)
	v_mfma_f32_32x32x2_f32 v[4:19], v204, v212, v[4:19]
	s_waitcnt lgkmcnt(4)
	v_mfma_f32_32x32x2_f32 v[4:19], v205, v213, v[4:19]
	s_waitcnt lgkmcnt(2)
	v_mfma_f32_32x32x2_f32 v[4:19], v206, v214, v[4:19]
	s_waitcnt lgkmcnt(0)
	v_mfma_f32_32x32x2_f32 v[4:19], v207, v215, v[4:19]
	s_barrier
	global_load_dwordx4 v[32:35], v[92:93], off offset:1920
	global_load_dwordx4 v[20:23], v[80:81], off
	s_waitcnt vmcnt(3)
	v_cvt_f32_f16_sdwa v93, v28 dst_sel:DWORD dst_unused:UNUSED_PAD src0_sel:WORD_1
	v_cvt_f32_f16_e32 v28, v28
	v_cvt_f32_f16_sdwa v92, v29 dst_sel:DWORD dst_unused:UNUSED_PAD src0_sel:WORD_1
	v_cvt_f32_f16_sdwa v128, v30 dst_sel:DWORD dst_unused:UNUSED_PAD src0_sel:WORD_1
	v_cvt_f32_f16_e32 v131, v30
	ds_read_b128 v[36:39], v43 offset:15872
	ds_read_b128 v[116:119], v43 offset:15888
	ds_read_b128 v[120:123], v43 offset:19968
	ds_read_b128 v[124:127], v43 offset:19984
	v_cvt_f32_f16_e32 v115, v29
	v_cvt_f32_f16_sdwa v129, v31 dst_sel:DWORD dst_unused:UNUSED_PAD src0_sel:WORD_1
	v_cvt_f32_f16_e32 v130, v31
	v_sub_f32_e32 v28, v28, v0
	v_sub_f32_e32 v29, v93, v1
	v_sub_f32_e32 v31, v92, v3
	v_pk_mul_f32 v[28:29], v[88:89], v[28:29]
	v_sub_f32_e32 v92, v131, v0
	v_sub_f32_e32 v93, v128, v1
	v_sub_f32_e32 v30, v115, v2
	v_sub_f32_e32 v128, v130, v2
	v_sub_f32_e32 v129, v129, v3
	v_pk_mul_f32 v[92:93], v[88:89], v[92:93]
	s_waitcnt lgkmcnt(1)
	v_fma_f32 v28, v36, v28, v120
	v_fma_f32 v29, v37, v29, v121
	v_pk_mul_f32 v[30:31], v[90:91], v[30:31]
	v_pk_mul_f32 v[128:129], v[90:91], v[128:129]
	s_waitcnt lgkmcnt(0)
	v_fma_f32 v36, v116, v92, v124
	ds_write2_b32 v220, v28, v29 offset1:65
	v_fma_f32 v28, v117, v93, v125
	ds_write2_b32 v221, v36, v28 offset1:65
	v_fma_f32 v28, v38, v30, v122
	v_fma_f32 v29, v118, v128, v126
	v_fmac_f32_e32 v123, v39, v31
	v_fmac_f32_e32 v127, v119, v129
	ds_write2_b32 v220, v28, v123 offset0:130 offset1:195
	ds_write2_b32 v221, v29, v127 offset0:130 offset1:195
	s_waitcnt vmcnt(2)
	ds_write_b128 v96, v[24:27] offset:41984
	s_mov_b32 s16, 0
	v_mov_b32_e32 v24, v103
	s_waitcnt lgkmcnt(0)
	s_barrier
	ds_read_b32 v200, v218
	ds_read_b32 v208, v219
	ds_read_b32 v201, v218 offset:520
	ds_read_b32 v209, v219 offset:256
	ds_read_b32 v202, v218 offset:1040
	ds_read_b32 v210, v219 offset:512
	ds_read_b32 v203, v218 offset:1560
	ds_read_b32 v211, v219 offset:768
	ds_read_b32 v204, v218 offset:2080
	ds_read_b32 v212, v219 offset:1024
	ds_read_b32 v205, v218 offset:2600
	ds_read_b32 v213, v219 offset:1280
	ds_read_b32 v206, v218 offset:3120
	ds_read_b32 v214, v219 offset:1536
	s_waitcnt lgkmcnt(12)
	v_mfma_f32_32x32x2_f32 v[4:19], v200, v208, v[4:19]
	ds_read_b32 v207, v218 offset:3640
	ds_read_b32 v215, v219 offset:1792
	s_waitcnt lgkmcnt(12)
	v_mfma_f32_32x32x2_f32 v[4:19], v201, v209, v[4:19]
	s_waitcnt lgkmcnt(10)
	v_mfma_f32_32x32x2_f32 v[4:19], v202, v210, v[4:19]
	s_waitcnt lgkmcnt(8)
	v_mfma_f32_32x32x2_f32 v[4:19], v203, v211, v[4:19]
	s_waitcnt lgkmcnt(6)
	v_mfma_f32_32x32x2_f32 v[4:19], v204, v212, v[4:19]
	s_waitcnt lgkmcnt(4)
	v_mfma_f32_32x32x2_f32 v[4:19], v205, v213, v[4:19]
	s_waitcnt lgkmcnt(2)
	v_mfma_f32_32x32x2_f32 v[4:19], v206, v214, v[4:19]
	s_waitcnt lgkmcnt(0)
	v_mfma_f32_32x32x2_f32 v[4:19], v207, v215, v[4:19]
	s_waitcnt vmcnt(1)
	v_cvt_f32_f16_sdwa v93, v32 dst_sel:DWORD dst_unused:UNUSED_PAD src0_sel:WORD_1
	v_cvt_f32_f16_e32 v32, v32
	v_cvt_f32_f16_sdwa v121, v34 dst_sel:DWORD dst_unused:UNUSED_PAD src0_sel:WORD_1
	v_cvt_f32_f16_e32 v123, v34
	s_barrier
	ds_read_b128 v[24:27], v43 offset:16128
	ds_read_b128 v[28:31], v43 offset:16144
	ds_read_b128 v[36:39], v43 offset:20224
	ds_read_b128 v[116:119], v43 offset:20240
	v_cvt_f32_f16_sdwa v92, v33 dst_sel:DWORD dst_unused:UNUSED_PAD src0_sel:WORD_1
	v_cvt_f32_f16_e32 v115, v33
	v_cvt_f32_f16_sdwa v120, v35 dst_sel:DWORD dst_unused:UNUSED_PAD src0_sel:WORD_1
	v_cvt_f32_f16_e32 v122, v35
	v_sub_f32_e32 v32, v32, v0
	v_sub_f32_e32 v33, v93, v1
	v_sub_f32_e32 v0, v123, v0
	v_sub_f32_e32 v1, v121, v1
	v_sub_f32_e32 v34, v115, v2
	v_sub_f32_e32 v35, v92, v3
	v_pk_mul_f32 v[0:1], v[88:89], v[0:1]
	v_pk_mul_f32 v[34:35], v[90:91], v[34:35]
	v_sub_f32_e32 v2, v122, v2
	v_sub_f32_e32 v3, v120, v3
	s_waitcnt lgkmcnt(0)
	v_fma_f32 v0, v28, v0, v116
	v_fma_f32 v1, v29, v1, v117
	v_pk_mul_f32 v[32:33], v[88:89], v[32:33]
	v_pk_mul_f32 v[2:3], v[90:91], v[2:3]
	ds_write2_b32 v221, v0, v1 offset1:65
	v_fma_f32 v0, v26, v34, v38
	v_fmac_f32_e32 v39, v27, v35
	v_fma_f32 v24, v24, v32, v36
	v_fma_f32 v25, v25, v33, v37
	v_fma_f32 v1, v30, v2, v118
	ds_write2_b32 v220, v0, v39 offset0:130 offset1:195
	v_fmac_f32_e32 v119, v31, v3
	s_mov_b32 s16, 0
	v_mov_b32_e32 v0, v103
	ds_write2_b32 v220, v24, v25 offset1:65
	ds_write2_b32 v221, v1, v119 offset0:130 offset1:195
	s_waitcnt vmcnt(0)
	ds_write_b128 v96, v[20:23] offset:41984
	s_waitcnt lgkmcnt(0)
	s_barrier
	ds_read_b32 v200, v218
	ds_read_b32 v208, v219
	ds_read_b32 v201, v218 offset:520
	ds_read_b32 v209, v219 offset:256
	ds_read_b32 v202, v218 offset:1040
	ds_read_b32 v210, v219 offset:512
	ds_read_b32 v203, v218 offset:1560
	ds_read_b32 v211, v219 offset:768
	ds_read_b32 v204, v218 offset:2080
	ds_read_b32 v212, v219 offset:1024
	ds_read_b32 v205, v218 offset:2600
	ds_read_b32 v213, v219 offset:1280
	ds_read_b32 v206, v218 offset:3120
	ds_read_b32 v214, v219 offset:1536
	s_waitcnt lgkmcnt(12)
	v_mfma_f32_32x32x2_f32 v[4:19], v200, v208, v[4:19]
	ds_read_b32 v207, v218 offset:3640
	ds_read_b32 v215, v219 offset:1792
	s_waitcnt lgkmcnt(12)
	v_mfma_f32_32x32x2_f32 v[4:19], v201, v209, v[4:19]
	s_waitcnt lgkmcnt(10)
	v_mfma_f32_32x32x2_f32 v[4:19], v202, v210, v[4:19]
	s_waitcnt lgkmcnt(8)
	v_mfma_f32_32x32x2_f32 v[4:19], v203, v211, v[4:19]
	s_waitcnt lgkmcnt(6)
	v_mfma_f32_32x32x2_f32 v[4:19], v204, v212, v[4:19]
	s_waitcnt lgkmcnt(4)
	v_mfma_f32_32x32x2_f32 v[4:19], v205, v213, v[4:19]
	s_waitcnt lgkmcnt(2)
	v_mfma_f32_32x32x2_f32 v[4:19], v206, v214, v[4:19]
	s_waitcnt lgkmcnt(0)
	v_mfma_f32_32x32x2_f32 v[4:19], v207, v215, v[4:19]
	s_barrier
	s_nop 15
	s_nop 3
	ds_write_b32 v217, v4 offset:58752
	ds_write_b32 v217, v5 offset:58880
	ds_write_b32 v217, v6 offset:59008
	ds_write_b32 v217, v7 offset:59136
	ds_write_b32 v217, v8 offset:59776
	ds_write_b32 v217, v9 offset:59904
	ds_write_b32 v217, v10 offset:60032
	ds_write_b32 v217, v11 offset:60160
	ds_write_b32 v217, v12 offset:60800
	ds_write_b32 v217, v13 offset:60928
	ds_write_b32 v217, v14 offset:61056
	ds_write_b32 v217, v15 offset:61184
	ds_write_b32 v217, v16 offset:61824
	ds_write_b32 v217, v17 offset:61952
	ds_write_b32 v217, v18 offset:62080
	ds_write_b32 v217, v19 offset:62208
	s_waitcnt lgkmcnt(0)
	s_barrier
	global_load_dwordx4 v[0:3], v[50:51], off offset:128
	ds_read_b128 v[4:7], v98 offset:58752
	ds_read_b128 v[8:11], v99 offset:8192
	ds_read_b128 v[12:15], v99 offset:16384
	ds_read_b128 v[16:19], v99 offset:24576
	v_add_u32_e32 v20, 0xc400, v100
	v_add_u32_e32 v21, 0xc408, v100
	s_waitcnt lgkmcnt(2)
	v_pk_add_f32 v[4:5], v[4:5], v[8:9]
	v_pk_add_f32 v[6:7], v[6:7], v[10:11]
	s_waitcnt lgkmcnt(1)
	v_pk_add_f32 v[4:5], v[12:13], v[4:5]
	v_pk_add_f32 v[6:7], v[14:15], v[6:7]
	s_waitcnt lgkmcnt(0)
	v_pk_add_f32 v[4:5], v[16:17], v[4:5]
	v_pk_add_f32 v[6:7], v[18:19], v[6:7]
	s_waitcnt vmcnt(0)
	v_pk_add_f32 v[0:1], v[0:1], v[4:5]
	v_pk_add_f32 v[2:3], v[6:7], v[2:3]
	ds_write2_b32 v20, v0, v1 offset1:1
	ds_write2_b32 v21, v2, v3 offset1:1
	s_waitcnt lgkmcnt(0)
	s_barrier
	s_and_saveexec_b64 s[36:37], s[6:7]
	s_cbranch_execz .LBB0_1510
	v_add_u32_e32 v0, 0xc400, v108
	v_add_u32_e32 v1, 0xc408, v108
	v_add_u32_e32 v2, 0xc410, v108
	v_add_u32_e32 v3, 0xc418, v108
	ds_read2_b32 v[34:35], v0 offset1:1
	ds_read2_b32 v[30:31], v1 offset1:1
	ds_read2_b32 v[22:23], v2 offset1:1
	ds_read2_b32 v[10:11], v3 offset1:1
	s_mov_b32 s16, 0xff61b1e6
	s_waitcnt lgkmcnt(3)
	v_max_f32_e32 v0, v34, v34
	v_max_f32_e32 v0, 0xff61b1e6, v0
	v_cmp_lt_f32_e32 vcc, s16, v34
	v_cmp_gt_f32_e64 s[16:17], v35, v0
	v_add_u32_e32 v2, 0xc420, v108
	ds_read2_b32 v[24:25], v2 offset1:1
	v_cndmask_b32_e64 v0, v0, v35, s[16:17]
	v_cndmask_b32_e64 v1, 0, 1, s[16:17]
	s_waitcnt lgkmcnt(3)
	v_cmp_gt_f32_e64 s[16:17], v30, v0
	v_add_u32_e32 v2, 0xc428, v108
	v_add_u32_e32 v3, 0xc430, v108
	v_cndmask_b32_e64 v0, v0, v30, s[16:17]
	v_cndmask_b32_e64 v1, v1, 2, s[16:17]
	v_cmp_gt_f32_e64 s[16:17], v31, v0
	v_add_u32_e32 v4, 0xc438, v108
	ds_read2_b32 v[32:33], v2 offset1:1
	ds_read2_b32 v[20:21], v3 offset1:1
	ds_read2_b32 v[6:7], v4 offset1:1
	v_cndmask_b32_e64 v0, v0, v31, s[16:17]
	v_cndmask_b32_e64 v1, v1, 3, s[16:17]
	s_waitcnt lgkmcnt(5)
	v_cmp_gt_f32_e64 s[16:17], v22, v0
	v_add_u32_e32 v2, 0xc440, v108
	ds_read2_b32 v[18:19], v2 offset1:1
	v_cndmask_b32_e64 v0, v0, v22, s[16:17]
	v_cndmask_b32_e64 v1, v1, 4, s[16:17]
	v_cmp_gt_f32_e64 s[16:17], v23, v0
	v_add_u32_e32 v2, 0xc448, v108
	v_add_u32_e32 v4, 0xc458, v108
	v_cndmask_b32_e64 v0, v0, v23, s[16:17]
	v_cndmask_b32_e64 v1, v1, 5, s[16:17]
	s_waitcnt lgkmcnt(5)
	v_cmp_gt_f32_e64 s[16:17], v10, v0
	v_add_u32_e32 v3, 0xc450, v108
	ds_read2_b32 v[28:29], v2 offset1:1
	ds_read2_b32 v[12:13], v3 offset1:1
	ds_read2_b32 v[4:5], v4 offset1:1
	v_cndmask_b32_e64 v0, v0, v10, s[16:17]
	v_cndmask_b32_e64 v1, v1, 6, s[16:17]
	v_cmp_gt_f32_e64 s[16:17], v11, v0
	v_add_u32_e32 v2, 0xc460, v108
	ds_read2_b32 v[14:15], v2 offset1:1
	v_cndmask_b32_e64 v0, v0, v11, s[16:17]
	v_cndmask_b32_e64 v1, v1, 7, s[16:17]
	s_waitcnt lgkmcnt(8)
	v_cmp_gt_f32_e64 s[16:17], v24, v0
	v_add_u32_e32 v2, 0xc468, v108
	v_add_u32_e32 v8, 0xc478, v108
	v_cndmask_b32_e64 v0, v0, v24, s[16:17]
	v_cndmask_b32_e64 v1, v1, 8, s[16:17]
	v_cmp_gt_f32_e64 s[16:17], v25, v0
	v_add_u32_e32 v3, 0xc470, v108
	ds_read2_b32 v[26:27], v2 offset1:1
	ds_read2_b32 v[16:17], v3 offset1:1
	ds_read2_b32 v[8:9], v8 offset1:1
	v_cndmask_b32_e64 v0, v0, v25, s[16:17]
	v_cndmask_b32_e64 v1, v1, 9, s[16:17]
	s_waitcnt lgkmcnt(10)
	v_cmp_gt_f32_e64 s[16:17], v32, v0
	s_nop 1
	v_cndmask_b32_e64 v0, v0, v32, s[16:17]
	v_cndmask_b32_e64 v1, v1, 10, s[16:17]
	v_cmp_gt_f32_e64 s[16:17], v33, v0
	s_nop 1
	v_cndmask_b32_e64 v0, v0, v33, s[16:17]
	v_cndmask_b32_e64 v1, v1, 11, s[16:17]
	s_waitcnt lgkmcnt(9)
	v_cmp_gt_f32_e64 s[16:17], v20, v0
	s_nop 1
	v_cndmask_b32_e64 v0, v0, v20, s[16:17]
	v_cndmask_b32_e64 v1, v1, 12, s[16:17]
	v_cmp_gt_f32_e64 s[16:17], v21, v0
	s_nop 1
	v_cndmask_b32_e64 v0, v0, v21, s[16:17]
	v_cndmask_b32_e64 v1, v1, 13, s[16:17]
	s_waitcnt lgkmcnt(8)
	v_cmp_gt_f32_e64 s[16:17], v6, v0
	s_nop 1
	v_cndmask_b32_e64 v0, v0, v6, s[16:17]
	v_cndmask_b32_e64 v1, v1, 14, s[16:17]
	v_cmp_gt_f32_e64 s[16:17], v7, v0
	s_nop 1
	v_cndmask_b32_e64 v0, v0, v7, s[16:17]
	v_cndmask_b32_e64 v1, v1, 15, s[16:17]
	s_waitcnt lgkmcnt(7)
	v_cmp_gt_f32_e64 s[16:17], v18, v0
	s_nop 1
	v_cndmask_b32_e64 v0, v0, v18, s[16:17]
	v_cndmask_b32_e64 v1, v1, 16, s[16:17]
	v_cmp_gt_f32_e64 s[16:17], v19, v0
	s_nop 1
	v_cndmask_b32_e64 v0, v0, v19, s[16:17]
	v_cndmask_b32_e64 v1, v1, 17, s[16:17]
	s_waitcnt lgkmcnt(6)
	v_cmp_gt_f32_e64 s[16:17], v28, v0
	s_nop 1
	v_cndmask_b32_e64 v0, v0, v28, s[16:17]
	v_cndmask_b32_e64 v1, v1, 18, s[16:17]
	v_cmp_gt_f32_e64 s[16:17], v29, v0
	s_nop 1
	v_cndmask_b32_e64 v0, v0, v29, s[16:17]
	v_cndmask_b32_e64 v1, v1, 19, s[16:17]
	s_waitcnt lgkmcnt(5)
	v_cmp_gt_f32_e64 s[16:17], v12, v0
	s_nop 1
	v_cndmask_b32_e64 v0, v0, v12, s[16:17]
	v_cndmask_b32_e64 v1, v1, 20, s[16:17]
	v_cmp_gt_f32_e64 s[16:17], v13, v0
	s_nop 1
	v_cndmask_b32_e64 v0, v0, v13, s[16:17]
	v_cndmask_b32_e64 v1, v1, 21, s[16:17]
	s_waitcnt lgkmcnt(4)
	v_cmp_gt_f32_e64 s[16:17], v4, v0
	s_nop 1
	v_cndmask_b32_e64 v0, v0, v4, s[16:17]
	v_cndmask_b32_e64 v1, v1, 22, s[16:17]
	v_cmp_gt_f32_e64 s[16:17], v5, v0
	s_nop 1
	v_cndmask_b32_e64 v0, v0, v5, s[16:17]
	v_cndmask_b32_e64 v1, v1, 23, s[16:17]
	s_waitcnt lgkmcnt(3)
	v_cmp_gt_f32_e64 s[16:17], v14, v0
	s_nop 1
	v_cndmask_b32_e64 v0, v0, v14, s[16:17]
	v_cndmask_b32_e64 v1, v1, 24, s[16:17]
	v_cmp_gt_f32_e64 s[16:17], v15, v0
	s_nop 1
	v_cndmask_b32_e64 v0, v0, v15, s[16:17]
	v_cndmask_b32_e64 v1, v1, 25, s[16:17]
	s_waitcnt lgkmcnt(2)
	v_cmp_gt_f32_e64 s[16:17], v26, v0
	s_nop 1
	v_cndmask_b32_e64 v0, v0, v26, s[16:17]
	v_cndmask_b32_e64 v1, v1, 26, s[16:17]
	v_cmp_gt_f32_e64 s[16:17], v27, v0
	s_nop 1
	v_cndmask_b32_e64 v0, v0, v27, s[16:17]
	v_cndmask_b32_e64 v1, v1, 27, s[16:17]
	s_waitcnt lgkmcnt(1)
	v_cmp_gt_f32_e64 s[16:17], v16, v0
	s_nop 1
	v_cndmask_b32_e64 v0, v0, v16, s[16:17]
	v_cndmask_b32_e64 v1, v1, 28, s[16:17]
	v_cmp_gt_f32_e64 s[16:17], v17, v0
	s_nop 1
	v_cndmask_b32_e64 v0, v0, v17, s[16:17]
	v_cndmask_b32_e64 v1, v1, 29, s[16:17]
	s_waitcnt lgkmcnt(0)
	v_cmp_gt_f32_e64 s[16:17], v8, v0
	s_nop 1
	v_cndmask_b32_e64 v0, v0, v8, s[16:17]
	v_cndmask_b32_e64 v1, v1, 30, s[16:17]
	v_cmp_gt_f32_e64 s[16:17], v9, v0
	s_nop 1
	v_cndmask_b32_e64 v36, v0, v9, s[16:17]
	v_cndmask_b32_e64 v0, v1, 31, s[16:17]
	v_cmp_ne_u32_e64 s[16:17], 0, v0
	v_lshlrev_b32_e64 v2, v0, 1
	s_and_b64 s[16:17], s[16:17], vcc
	v_cndmask_b32_e64 v1, v112, v34, s[16:17]
	v_and_b32_e32 v3, 2, v2
	v_cmp_eq_u32_e64 s[16:17], 0, v3
	v_cmp_gt_f32_e64 s[18:19], v35, v1
	s_and_b64 s[16:17], s[16:17], s[18:19]
	v_cndmask_b32_e64 v1, v1, v35, s[16:17]
	v_and_b32_e32 v37, 4, v2
	v_cndmask_b32_e64 v3, 0, 1, s[16:17]
	v_cmp_eq_u32_e64 s[16:17], 0, v37
	v_cmp_gt_f32_e64 s[18:19], v30, v1
	s_and_b64 s[16:17], s[16:17], s[18:19]
	v_cndmask_b32_e64 v1, v1, v30, s[16:17]
	v_and_b32_e32 v37, 8, v2
	v_cndmask_b32_e64 v3, v3, 2, s[16:17]
	v_cmp_eq_u32_e64 s[16:17], 0, v37
	v_cmp_gt_f32_e64 s[18:19], v31, v1
	s_and_b64 s[16:17], s[16:17], s[18:19]
	v_cndmask_b32_e64 v1, v1, v31, s[16:17]
	v_and_b32_e32 v37, 16, v2
	v_cndmask_b32_e64 v3, v3, 3, s[16:17]
	v_cmp_eq_u32_e64 s[16:17], 0, v37
	v_cmp_gt_f32_e64 s[18:19], v22, v1
	s_and_b64 s[16:17], s[16:17], s[18:19]
	v_cndmask_b32_e64 v1, v1, v22, s[16:17]
	v_and_b32_e32 v37, 32, v2
	v_cndmask_b32_e64 v3, v3, 4, s[16:17]
	v_cmp_eq_u32_e64 s[16:17], 0, v37
	v_cmp_gt_f32_e64 s[18:19], v23, v1
	s_and_b64 s[16:17], s[16:17], s[18:19]
	v_cndmask_b32_e64 v1, v1, v23, s[16:17]
	v_and_b32_e32 v37, 64, v2
	v_cndmask_b32_e64 v3, v3, 5, s[16:17]
	v_cmp_eq_u32_e64 s[16:17], 0, v37
	v_cmp_gt_f32_e64 s[18:19], v10, v1
	s_and_b64 s[16:17], s[16:17], s[18:19]
	v_cndmask_b32_e64 v1, v1, v10, s[16:17]
	v_and_b32_e32 v37, 0x80, v2
	v_cndmask_b32_e64 v3, v3, 6, s[16:17]
	v_cmp_eq_u32_e64 s[16:17], 0, v37
	v_cmp_gt_f32_e64 s[18:19], v11, v1
	s_and_b64 s[16:17], s[16:17], s[18:19]
	v_cndmask_b32_e64 v1, v1, v11, s[16:17]
	v_and_b32_e32 v37, 0x100, v2
	v_cndmask_b32_e64 v3, v3, 7, s[16:17]
	v_cmp_eq_u32_e64 s[16:17], 0, v37
	v_cmp_gt_f32_e64 s[18:19], v24, v1
	s_and_b64 s[16:17], s[16:17], s[18:19]
	v_cndmask_b32_e64 v1, v1, v24, s[16:17]
	v_and_b32_e32 v37, 0x200, v2
	v_cndmask_b32_e64 v3, v3, 8, s[16:17]
	v_cmp_eq_u32_e64 s[16:17], 0, v37
	v_cmp_gt_f32_e64 s[18:19], v25, v1
	s_and_b64 s[16:17], s[16:17], s[18:19]
	v_cndmask_b32_e64 v1, v1, v25, s[16:17]
	v_and_b32_e32 v37, 0x400, v2
	v_cndmask_b32_e64 v3, v3, 9, s[16:17]
	v_cmp_eq_u32_e64 s[16:17], 0, v37
	v_cmp_gt_f32_e64 s[18:19], v32, v1
	s_and_b64 s[16:17], s[16:17], s[18:19]
	v_cndmask_b32_e64 v1, v1, v32, s[16:17]
	v_and_b32_e32 v37, 0x800, v2
	v_cndmask_b32_e64 v3, v3, 10, s[16:17]
	v_cmp_eq_u32_e64 s[16:17], 0, v37
	v_cmp_gt_f32_e64 s[18:19], v33, v1
	s_and_b64 s[16:17], s[16:17], s[18:19]
	v_cndmask_b32_e64 v1, v1, v33, s[16:17]
	v_and_b32_e32 v37, 0x1000, v2
	v_cndmask_b32_e64 v3, v3, 11, s[16:17]
	v_cmp_eq_u32_e64 s[16:17], 0, v37
	v_cmp_gt_f32_e64 s[18:19], v20, v1
	s_and_b64 s[16:17], s[16:17], s[18:19]
	v_cndmask_b32_e64 v1, v1, v20, s[16:17]
	v_and_b32_e32 v37, 0x2000, v2
	v_cndmask_b32_e64 v3, v3, 12, s[16:17]
	v_cmp_eq_u32_e64 s[16:17], 0, v37
	v_cmp_gt_f32_e64 s[18:19], v21, v1
	s_and_b64 s[16:17], s[16:17], s[18:19]
	v_cndmask_b32_e64 v1, v1, v21, s[16:17]
	v_and_b32_e32 v37, 0x4000, v2
	v_cndmask_b32_e64 v3, v3, 13, s[16:17]
	v_cmp_eq_u32_e64 s[16:17], 0, v37
	v_cmp_gt_f32_e64 s[18:19], v6, v1
	s_and_b64 s[16:17], s[16:17], s[18:19]
	v_cndmask_b32_e64 v1, v1, v6, s[16:17]
	v_and_b32_e32 v37, 0x8000, v2
	v_cndmask_b32_e64 v3, v3, 14, s[16:17]
	v_cmp_eq_u32_e64 s[16:17], 0, v37
	v_cmp_gt_f32_e64 s[18:19], v7, v1
	s_and_b64 s[16:17], s[16:17], s[18:19]
	v_cndmask_b32_e64 v1, v1, v7, s[16:17]
	v_and_b32_e32 v37, 0x10000, v2
	v_cndmask_b32_e64 v3, v3, 15, s[16:17]
	v_cmp_eq_u32_e64 s[16:17], 0, v37
	v_cmp_gt_f32_e64 s[18:19], v18, v1
	s_and_b64 s[16:17], s[16:17], s[18:19]
	v_cndmask_b32_e64 v1, v1, v18, s[16:17]
	v_and_b32_e32 v37, 0x20000, v2
	v_cndmask_b32_e64 v3, v3, 16, s[16:17]
	v_cmp_eq_u32_e64 s[16:17], 0, v37
	v_cmp_gt_f32_e64 s[18:19], v19, v1
	s_and_b64 s[16:17], s[16:17], s[18:19]
	v_cndmask_b32_e64 v1, v1, v19, s[16:17]
	v_and_b32_e32 v37, 0x40000, v2
	v_cndmask_b32_e64 v3, v3, 17, s[16:17]
	v_cmp_eq_u32_e64 s[16:17], 0, v37
	v_cmp_gt_f32_e64 s[18:19], v28, v1
	s_and_b64 s[16:17], s[16:17], s[18:19]
	v_cndmask_b32_e64 v1, v1, v28, s[16:17]
	v_and_b32_e32 v37, 0x80000, v2
	v_cndmask_b32_e64 v3, v3, 18, s[16:17]
	v_cmp_eq_u32_e64 s[16:17], 0, v37
	v_cmp_gt_f32_e64 s[18:19], v29, v1
	s_and_b64 s[16:17], s[16:17], s[18:19]
	v_cndmask_b32_e64 v1, v1, v29, s[16:17]
	v_and_b32_e32 v37, 0x100000, v2
	v_cndmask_b32_e64 v3, v3, 19, s[16:17]
	v_cmp_eq_u32_e64 s[16:17], 0, v37
	v_cmp_gt_f32_e64 s[18:19], v12, v1
	s_and_b64 s[16:17], s[16:17], s[18:19]
	v_cndmask_b32_e64 v1, v1, v12, s[16:17]
	v_and_b32_e32 v37, 0x200000, v2
	v_cndmask_b32_e64 v3, v3, 20, s[16:17]
	v_cmp_eq_u32_e64 s[16:17], 0, v37
	v_cmp_gt_f32_e64 s[18:19], v13, v1
	s_and_b64 s[16:17], s[16:17], s[18:19]
	v_cndmask_b32_e64 v1, v1, v13, s[16:17]
	v_and_b32_e32 v37, 0x400000, v2
	v_cndmask_b32_e64 v3, v3, 21, s[16:17]
	v_cmp_eq_u32_e64 s[16:17], 0, v37
	v_cmp_gt_f32_e64 s[18:19], v4, v1
	s_and_b64 s[16:17], s[16:17], s[18:19]
	v_cndmask_b32_e64 v1, v1, v4, s[16:17]
	v_and_b32_e32 v37, 0x800000, v2
	v_cndmask_b32_e64 v3, v3, 22, s[16:17]
	v_cmp_eq_u32_e64 s[16:17], 0, v37
	v_cmp_gt_f32_e64 s[18:19], v5, v1
	s_and_b64 s[16:17], s[16:17], s[18:19]
	v_cndmask_b32_e64 v1, v1, v5, s[16:17]
	v_and_b32_e32 v37, 0x1000000, v2
	v_cndmask_b32_e64 v3, v3, 23, s[16:17]
	v_cmp_eq_u32_e64 s[16:17], 0, v37
	v_cmp_gt_f32_e64 s[18:19], v14, v1
	s_and_b64 s[16:17], s[16:17], s[18:19]
	v_cndmask_b32_e64 v1, v1, v14, s[16:17]
	v_and_b32_e32 v37, 0x2000000, v2
	v_cndmask_b32_e64 v3, v3, 24, s[16:17]
	v_cmp_eq_u32_e64 s[16:17], 0, v37
	v_cmp_gt_f32_e64 s[18:19], v15, v1
	s_and_b64 s[16:17], s[16:17], s[18:19]
	v_cndmask_b32_e64 v1, v1, v15, s[16:17]
	v_and_b32_e32 v37, 0x4000000, v2
	v_cndmask_b32_e64 v3, v3, 25, s[16:17]
	v_cmp_eq_u32_e64 s[16:17], 0, v37
	v_cmp_gt_f32_e64 s[18:19], v26, v1
	s_and_b64 s[16:17], s[16:17], s[18:19]
	v_cndmask_b32_e64 v1, v1, v26, s[16:17]
	v_and_b32_e32 v37, 0x8000000, v2
	v_cndmask_b32_e64 v3, v3, 26, s[16:17]
	v_cmp_eq_u32_e64 s[16:17], 0, v37
	v_cmp_gt_f32_e64 s[18:19], v27, v1
	s_and_b64 s[16:17], s[16:17], s[18:19]
	v_cndmask_b32_e64 v1, v1, v27, s[16:17]
	v_and_b32_e32 v37, 0x10000000, v2
	v_cndmask_b32_e64 v3, v3, 27, s[16:17]
	v_cmp_eq_u32_e64 s[16:17], 0, v37
	v_cmp_gt_f32_e64 s[18:19], v16, v1
	s_and_b64 s[16:17], s[16:17], s[18:19]
	v_cndmask_b32_e64 v1, v1, v16, s[16:17]
	v_and_b32_e32 v37, 0x20000000, v2
	v_cndmask_b32_e64 v3, v3, 28, s[16:17]
	v_cmp_eq_u32_e64 s[16:17], 0, v37
	v_cmp_gt_f32_e64 s[18:19], v17, v1
	s_and_b64 s[16:17], s[16:17], s[18:19]
	v_cndmask_b32_e64 v1, v1, v17, s[16:17]
	v_and_b32_e32 v37, 2.0, v2
	v_cndmask_b32_e64 v3, v3, 29, s[16:17]
	v_cmp_eq_u32_e64 s[16:17], 0, v37
	v_cmp_gt_f32_e64 s[18:19], v8, v1
	s_and_b64 s[16:17], s[16:17], s[18:19]
	v_cndmask_b32_e64 v1, v1, v8, s[16:17]
	v_cndmask_b32_e64 v3, v3, 30, s[16:17]
	v_cmp_ne_u32_e64 s[16:17], 31, v0
	v_cmp_gt_f32_e64 s[18:19], v9, v1
	s_and_b64 s[16:17], s[16:17], s[18:19]
	v_cndmask_b32_e64 v37, v1, v9, s[16:17]
	v_cndmask_b32_e64 v1, v3, 31, s[16:17]
	v_lshl_or_b32 v3, 1, v1, v2
	v_and_b32_e32 v2, 1, v3
	v_cmp_eq_u32_e64 s[16:17], 0, v2
	s_and_b64 s[16:17], s[16:17], vcc
	v_and_b32_e32 v38, 2, v3
	v_cndmask_b32_e64 v2, v112, v34, s[16:17]
	v_cmp_eq_u32_e64 s[16:17], 0, v38
	v_cmp_gt_f32_e64 s[18:19], v35, v2
	s_and_b64 s[16:17], s[16:17], s[18:19]
	v_cndmask_b32_e64 v2, v2, v35, s[16:17]
	v_and_b32_e32 v39, 4, v3
	v_cndmask_b32_e64 v38, 0, 1, s[16:17]
	v_cmp_eq_u32_e64 s[16:17], 0, v39
	v_cmp_gt_f32_e64 s[18:19], v30, v2
	s_and_b64 s[16:17], s[16:17], s[18:19]
	v_cndmask_b32_e64 v2, v2, v30, s[16:17]
	v_and_b32_e32 v39, 8, v3
	v_cndmask_b32_e64 v38, v38, 2, s[16:17]
	v_cmp_eq_u32_e64 s[16:17], 0, v39
	v_cmp_gt_f32_e64 s[18:19], v31, v2
	s_and_b64 s[16:17], s[16:17], s[18:19]
	v_cndmask_b32_e64 v2, v2, v31, s[16:17]
	v_and_b32_e32 v39, 16, v3
	v_cndmask_b32_e64 v38, v38, 3, s[16:17]
	v_cmp_eq_u32_e64 s[16:17], 0, v39
	v_cmp_gt_f32_e64 s[18:19], v22, v2
	s_and_b64 s[16:17], s[16:17], s[18:19]
	v_cndmask_b32_e64 v2, v2, v22, s[16:17]
	v_and_b32_e32 v39, 32, v3
	v_cndmask_b32_e64 v38, v38, 4, s[16:17]
	v_cmp_eq_u32_e64 s[16:17], 0, v39
	v_cmp_gt_f32_e64 s[18:19], v23, v2
	s_and_b64 s[16:17], s[16:17], s[18:19]
	v_cndmask_b32_e64 v2, v2, v23, s[16:17]
	v_and_b32_e32 v39, 64, v3
	v_cndmask_b32_e64 v38, v38, 5, s[16:17]
	v_cmp_eq_u32_e64 s[16:17], 0, v39
	v_cmp_gt_f32_e64 s[18:19], v10, v2
	s_and_b64 s[16:17], s[16:17], s[18:19]
	v_cndmask_b32_e64 v2, v2, v10, s[16:17]
	v_and_b32_e32 v39, 0x80, v3
	v_cndmask_b32_e64 v38, v38, 6, s[16:17]
	v_cmp_eq_u32_e64 s[16:17], 0, v39
	v_cmp_gt_f32_e64 s[18:19], v11, v2
	s_and_b64 s[16:17], s[16:17], s[18:19]
	v_cndmask_b32_e64 v2, v2, v11, s[16:17]
	v_and_b32_e32 v39, 0x100, v3
	v_cndmask_b32_e64 v38, v38, 7, s[16:17]
	v_cmp_eq_u32_e64 s[16:17], 0, v39
	v_cmp_gt_f32_e64 s[18:19], v24, v2
	s_and_b64 s[16:17], s[16:17], s[18:19]
	v_cndmask_b32_e64 v2, v2, v24, s[16:17]
	v_and_b32_e32 v39, 0x200, v3
	v_cndmask_b32_e64 v38, v38, 8, s[16:17]
	v_cmp_eq_u32_e64 s[16:17], 0, v39
	v_cmp_gt_f32_e64 s[18:19], v25, v2
	s_and_b64 s[16:17], s[16:17], s[18:19]
	v_cndmask_b32_e64 v2, v2, v25, s[16:17]
	v_and_b32_e32 v39, 0x400, v3
	v_cndmask_b32_e64 v38, v38, 9, s[16:17]
	v_cmp_eq_u32_e64 s[16:17], 0, v39
	v_cmp_gt_f32_e64 s[18:19], v32, v2
	s_and_b64 s[16:17], s[16:17], s[18:19]
	v_cndmask_b32_e64 v2, v2, v32, s[16:17]
	v_and_b32_e32 v39, 0x800, v3
	v_cndmask_b32_e64 v38, v38, 10, s[16:17]
	v_cmp_eq_u32_e64 s[16:17], 0, v39
	v_cmp_gt_f32_e64 s[18:19], v33, v2
	s_and_b64 s[16:17], s[16:17], s[18:19]
	v_cndmask_b32_e64 v2, v2, v33, s[16:17]
	v_and_b32_e32 v39, 0x1000, v3
	v_cndmask_b32_e64 v38, v38, 11, s[16:17]
	v_cmp_eq_u32_e64 s[16:17], 0, v39
	v_cmp_gt_f32_e64 s[18:19], v20, v2
	s_and_b64 s[16:17], s[16:17], s[18:19]
	v_cndmask_b32_e64 v2, v2, v20, s[16:17]
	v_and_b32_e32 v39, 0x2000, v3
	v_cndmask_b32_e64 v38, v38, 12, s[16:17]
	v_cmp_eq_u32_e64 s[16:17], 0, v39
	v_cmp_gt_f32_e64 s[18:19], v21, v2
	s_and_b64 s[16:17], s[16:17], s[18:19]
	v_cndmask_b32_e64 v2, v2, v21, s[16:17]
	v_and_b32_e32 v39, 0x4000, v3
	v_cndmask_b32_e64 v38, v38, 13, s[16:17]
	v_cmp_eq_u32_e64 s[16:17], 0, v39
	v_cmp_gt_f32_e64 s[18:19], v6, v2
	s_and_b64 s[16:17], s[16:17], s[18:19]
	v_cndmask_b32_e64 v2, v2, v6, s[16:17]
	v_and_b32_e32 v39, 0x8000, v3
	v_cndmask_b32_e64 v38, v38, 14, s[16:17]
	v_cmp_eq_u32_e64 s[16:17], 0, v39
	v_cmp_gt_f32_e64 s[18:19], v7, v2
	s_and_b64 s[16:17], s[16:17], s[18:19]
	v_cndmask_b32_e64 v2, v2, v7, s[16:17]
	v_and_b32_e32 v39, 0x10000, v3
	v_cndmask_b32_e64 v38, v38, 15, s[16:17]
	v_cmp_eq_u32_e64 s[16:17], 0, v39
	v_cmp_gt_f32_e64 s[18:19], v18, v2
	s_and_b64 s[16:17], s[16:17], s[18:19]
	v_cndmask_b32_e64 v2, v2, v18, s[16:17]
	v_and_b32_e32 v39, 0x20000, v3
	v_cndmask_b32_e64 v38, v38, 16, s[16:17]
	v_cmp_eq_u32_e64 s[16:17], 0, v39
	v_cmp_gt_f32_e64 s[18:19], v19, v2
	s_and_b64 s[16:17], s[16:17], s[18:19]
	v_cndmask_b32_e64 v2, v2, v19, s[16:17]
	v_and_b32_e32 v39, 0x40000, v3
	v_cndmask_b32_e64 v38, v38, 17, s[16:17]
	v_cmp_eq_u32_e64 s[16:17], 0, v39
	v_cmp_gt_f32_e64 s[18:19], v28, v2
	s_and_b64 s[16:17], s[16:17], s[18:19]
	v_cndmask_b32_e64 v2, v2, v28, s[16:17]
	v_and_b32_e32 v39, 0x80000, v3
	v_cndmask_b32_e64 v38, v38, 18, s[16:17]
	v_cmp_eq_u32_e64 s[16:17], 0, v39
	v_cmp_gt_f32_e64 s[18:19], v29, v2
	s_and_b64 s[16:17], s[16:17], s[18:19]
	v_cndmask_b32_e64 v2, v2, v29, s[16:17]
	v_and_b32_e32 v39, 0x100000, v3
	v_cndmask_b32_e64 v38, v38, 19, s[16:17]
	v_cmp_eq_u32_e64 s[16:17], 0, v39
	v_cmp_gt_f32_e64 s[18:19], v12, v2
	s_and_b64 s[16:17], s[16:17], s[18:19]
	v_cndmask_b32_e64 v2, v2, v12, s[16:17]
	v_and_b32_e32 v39, 0x200000, v3
	v_cndmask_b32_e64 v38, v38, 20, s[16:17]
	v_cmp_eq_u32_e64 s[16:17], 0, v39
	v_cmp_gt_f32_e64 s[18:19], v13, v2
	s_and_b64 s[16:17], s[16:17], s[18:19]
	v_cndmask_b32_e64 v2, v2, v13, s[16:17]
	v_and_b32_e32 v39, 0x400000, v3
	v_cndmask_b32_e64 v38, v38, 21, s[16:17]
	v_cmp_eq_u32_e64 s[16:17], 0, v39
	v_cmp_gt_f32_e64 s[18:19], v4, v2
	s_and_b64 s[16:17], s[16:17], s[18:19]
	v_cndmask_b32_e64 v2, v2, v4, s[16:17]
	v_and_b32_e32 v39, 0x800000, v3
	v_cndmask_b32_e64 v38, v38, 22, s[16:17]
	v_cmp_eq_u32_e64 s[16:17], 0, v39
	v_cmp_gt_f32_e64 s[18:19], v5, v2
	s_and_b64 s[16:17], s[16:17], s[18:19]
	v_cndmask_b32_e64 v2, v2, v5, s[16:17]
	v_and_b32_e32 v39, 0x1000000, v3
	v_cndmask_b32_e64 v38, v38, 23, s[16:17]
	v_cmp_eq_u32_e64 s[16:17], 0, v39
	v_cmp_gt_f32_e64 s[18:19], v14, v2
	s_and_b64 s[16:17], s[16:17], s[18:19]
	v_cndmask_b32_e64 v2, v2, v14, s[16:17]
	v_and_b32_e32 v39, 0x2000000, v3
	v_cndmask_b32_e64 v38, v38, 24, s[16:17]
	v_cmp_eq_u32_e64 s[16:17], 0, v39
	v_cmp_gt_f32_e64 s[18:19], v15, v2
	s_and_b64 s[16:17], s[16:17], s[18:19]
	v_cndmask_b32_e64 v2, v2, v15, s[16:17]
	v_and_b32_e32 v39, 0x4000000, v3
	v_cndmask_b32_e64 v38, v38, 25, s[16:17]
	v_cmp_eq_u32_e64 s[16:17], 0, v39
	v_cmp_gt_f32_e64 s[18:19], v26, v2
	s_and_b64 s[16:17], s[16:17], s[18:19]
	v_cndmask_b32_e64 v2, v2, v26, s[16:17]
	v_and_b32_e32 v39, 0x8000000, v3
	v_cndmask_b32_e64 v38, v38, 26, s[16:17]
	v_cmp_eq_u32_e64 s[16:17], 0, v39
	v_cmp_gt_f32_e64 s[18:19], v27, v2
	s_and_b64 s[16:17], s[16:17], s[18:19]
	v_cndmask_b32_e64 v2, v2, v27, s[16:17]
	v_and_b32_e32 v39, 0x10000000, v3
	v_cndmask_b32_e64 v38, v38, 27, s[16:17]
	v_cmp_eq_u32_e64 s[16:17], 0, v39
	v_cmp_gt_f32_e64 s[18:19], v16, v2
	s_and_b64 s[16:17], s[16:17], s[18:19]
	v_cndmask_b32_e64 v2, v2, v16, s[16:17]
	v_and_b32_e32 v39, 0x20000000, v3
	v_cndmask_b32_e64 v38, v38, 28, s[16:17]
	v_cmp_eq_u32_e64 s[16:17], 0, v39
	v_cmp_gt_f32_e64 s[18:19], v17, v2
	s_and_b64 s[16:17], s[16:17], s[18:19]
	v_cndmask_b32_e64 v2, v2, v17, s[16:17]
	v_and_b32_e32 v39, 2.0, v3
	v_cndmask_b32_e64 v38, v38, 29, s[16:17]
	v_cmp_eq_u32_e64 s[16:17], 0, v39
	v_cmp_gt_f32_e64 s[18:19], v8, v2
	s_and_b64 s[16:17], s[16:17], s[18:19]
	v_cndmask_b32_e64 v2, v2, v8, s[16:17]
	v_cndmask_b32_e64 v38, v38, 30, s[16:17]
	v_cmp_lt_i32_e64 s[16:17], -1, v3
	v_cmp_gt_f32_e64 s[18:19], v9, v2
	s_and_b64 s[16:17], s[16:17], s[18:19]
	v_cndmask_b32_e64 v39, v2, v9, s[16:17]
	v_cndmask_b32_e64 v2, v38, 31, s[16:17]
	v_lshlrev_b32_e64 v38, v2, 1
	v_bitop3_b32 v89, v38, 1, v3 bitop3:0xc8
	v_cmp_eq_u32_e64 s[16:17], 0, v89
	s_and_b64 vcc, s[16:17], vcc
	v_cndmask_b32_e32 v34, v112, v34, vcc
	v_bitop3_b32 v89, v38, 2, v3 bitop3:0xc8
	v_cmp_eq_u32_e32 vcc, 0, v89
	v_cmp_gt_f32_e64 s[16:17], v35, v34
	s_and_b64 vcc, vcc, s[16:17]
	v_cndmask_b32_e32 v34, v34, v35, vcc
	v_bitop3_b32 v89, v38, 4, v3 bitop3:0xc8
	v_cndmask_b32_e64 v35, 0, 1, vcc
	v_cmp_eq_u32_e32 vcc, 0, v89
	v_cmp_gt_f32_e64 s[16:17], v30, v34
	s_and_b64 vcc, vcc, s[16:17]
	v_cndmask_b32_e32 v30, v34, v30, vcc
	v_cndmask_b32_e64 v34, v35, 2, vcc
	v_bitop3_b32 v35, v38, 8, v3 bitop3:0xc8
	v_cmp_eq_u32_e32 vcc, 0, v35
	v_cmp_gt_f32_e64 s[16:17], v31, v30
	s_and_b64 vcc, vcc, s[16:17]
	v_cndmask_b32_e32 v30, v30, v31, vcc
	v_cndmask_b32_e64 v31, v34, 3, vcc
	v_bitop3_b32 v34, v38, 16, v3 bitop3:0xc8
	v_cmp_eq_u32_e32 vcc, 0, v34
	v_cmp_gt_f32_e64 s[16:17], v22, v30
	s_and_b64 vcc, vcc, s[16:17]
	v_cndmask_b32_e32 v22, v30, v22, vcc
	v_cndmask_b32_e64 v30, v31, 4, vcc
	v_bitop3_b32 v31, v38, 32, v3 bitop3:0xc8
	v_cmp_eq_u32_e32 vcc, 0, v31
	v_cmp_gt_f32_e64 s[16:17], v23, v22
	s_and_b64 vcc, vcc, s[16:17]
	v_cndmask_b32_e32 v22, v22, v23, vcc
	v_cndmask_b32_e64 v23, v30, 5, vcc
	v_bitop3_b32 v30, v38, 64, v3 bitop3:0xc8
	v_cmp_eq_u32_e32 vcc, 0, v30
	v_cmp_gt_f32_e64 s[16:17], v10, v22
	s_and_b64 vcc, vcc, s[16:17]
	s_movk_i32 s16, 0x80
	v_cndmask_b32_e32 v10, v22, v10, vcc
	v_cndmask_b32_e64 v22, v23, 6, vcc
	v_bitop3_b32 v23, v38, s16, v3 bitop3:0xc8
	v_cmp_eq_u32_e32 vcc, 0, v23
	v_cmp_gt_f32_e64 s[16:17], v11, v10
	s_and_b64 vcc, vcc, s[16:17]
	s_movk_i32 s16, 0x100
	v_cndmask_b32_e32 v10, v10, v11, vcc
	v_cndmask_b32_e64 v11, v22, 7, vcc
	v_bitop3_b32 v22, v38, s16, v3 bitop3:0xc8
	v_cmp_eq_u32_e32 vcc, 0, v22
	v_cmp_gt_f32_e64 s[16:17], v24, v10
	s_and_b64 vcc, vcc, s[16:17]
	s_movk_i32 s16, 0x200
	v_cndmask_b32_e32 v10, v10, v24, vcc
	v_bitop3_b32 v22, v38, s16, v3 bitop3:0xc8
	v_cndmask_b32_e64 v11, v11, 8, vcc
	v_cmp_eq_u32_e32 vcc, 0, v22
	v_cmp_gt_f32_e64 s[16:17], v25, v10
	s_and_b64 vcc, vcc, s[16:17]
	v_cndmask_b32_e32 v10, v10, v25, vcc
	v_bitop3_b32 v22, v38, s52, v3 bitop3:0xc8
	v_cndmask_b32_e64 v11, v11, 9, vcc
	v_cmp_eq_u32_e32 vcc, 0, v22
	v_cmp_gt_f32_e64 s[16:17], v32, v10
	s_and_b64 vcc, vcc, s[16:17]
	s_movk_i32 s16, 0x800
	v_cndmask_b32_e32 v10, v10, v32, vcc
	v_bitop3_b32 v22, v38, s16, v3 bitop3:0xc8
	v_cndmask_b32_e64 v11, v11, 10, vcc
	v_cmp_eq_u32_e32 vcc, 0, v22
	v_cmp_gt_f32_e64 s[16:17], v33, v10
	s_and_b64 vcc, vcc, s[16:17]
	s_movk_i32 s16, 0x1000
	v_cndmask_b32_e32 v10, v10, v33, vcc
	v_bitop3_b32 v22, v38, s16, v3 bitop3:0xc8
	v_cndmask_b32_e64 v11, v11, 11, vcc
	v_cmp_eq_u32_e32 vcc, 0, v22
	v_cmp_gt_f32_e64 s[16:17], v20, v10
	s_and_b64 vcc, vcc, s[16:17]
	s_movk_i32 s16, 0x2000
	v_cndmask_b32_e32 v10, v10, v20, vcc
	v_bitop3_b32 v20, v38, s16, v3 bitop3:0xc8
	v_cndmask_b32_e64 v11, v11, 12, vcc
	v_cmp_eq_u32_e32 vcc, 0, v20
	v_cmp_gt_f32_e64 s[16:17], v21, v10
	s_and_b64 vcc, vcc, s[16:17]
	s_movk_i32 s16, 0x4000
	v_cndmask_b32_e32 v10, v10, v21, vcc
	v_bitop3_b32 v20, v38, s16, v3 bitop3:0xc8
	v_cndmask_b32_e64 v11, v11, 13, vcc
	v_cmp_eq_u32_e32 vcc, 0, v20
	v_cmp_gt_f32_e64 s[16:17], v6, v10
	s_and_b64 vcc, vcc, s[16:17]
	s_mov_b32 s16, 0x8000
	v_cndmask_b32_e32 v6, v10, v6, vcc
	v_cndmask_b32_e64 v10, v11, 14, vcc
	v_bitop3_b32 v11, v38, s16, v3 bitop3:0xc8
	v_cmp_eq_u32_e32 vcc, 0, v11
	v_cmp_gt_f32_e64 s[16:17], v7, v6
	s_and_b64 vcc, vcc, s[16:17]
	s_mov_b32 s16, 0x10000
	v_cndmask_b32_e32 v6, v6, v7, vcc
	v_cndmask_b32_e64 v7, v10, 15, vcc
	v_bitop3_b32 v10, v38, s16, v3 bitop3:0xc8
	v_cmp_eq_u32_e32 vcc, 0, v10
	v_cmp_gt_f32_e64 s[16:17], v18, v6
	s_and_b64 vcc, vcc, s[16:17]
	s_mov_b32 s16, 0x20000
	v_cndmask_b32_e32 v6, v6, v18, vcc
	v_bitop3_b32 v10, v38, s16, v3 bitop3:0xc8
	v_cndmask_b32_e64 v7, v7, 16, vcc
	v_cmp_eq_u32_e32 vcc, 0, v10
	v_cmp_gt_f32_e64 s[16:17], v19, v6
	s_and_b64 vcc, vcc, s[16:17]
	s_mov_b32 s16, 0x40000
	v_cndmask_b32_e32 v6, v6, v19, vcc
	v_bitop3_b32 v10, v38, s16, v3 bitop3:0xc8
	v_cndmask_b32_e64 v7, v7, 17, vcc
	v_cmp_eq_u32_e32 vcc, 0, v10
	v_cmp_gt_f32_e64 s[16:17], v28, v6
	s_and_b64 vcc, vcc, s[16:17]
	s_mov_b32 s16, 0x80000
	v_cndmask_b32_e32 v6, v6, v28, vcc
	v_bitop3_b32 v10, v38, s16, v3 bitop3:0xc8
	v_cndmask_b32_e64 v7, v7, 18, vcc
	v_cmp_eq_u32_e32 vcc, 0, v10
	v_cmp_gt_f32_e64 s[16:17], v29, v6
	s_and_b64 vcc, vcc, s[16:17]
	s_mov_b32 s16, 0x100000
	v_cndmask_b32_e32 v6, v6, v29, vcc
	v_bitop3_b32 v10, v38, s16, v3 bitop3:0xc8
	v_cndmask_b32_e64 v7, v7, 19, vcc
	v_cmp_eq_u32_e32 vcc, 0, v10
	v_cmp_gt_f32_e64 s[16:17], v12, v6
	s_and_b64 vcc, vcc, s[16:17]
	s_mov_b32 s16, 0x200000
	v_cndmask_b32_e32 v6, v6, v12, vcc
	v_bitop3_b32 v10, v38, s16, v3 bitop3:0xc8
	v_cndmask_b32_e64 v7, v7, 20, vcc
	v_cmp_eq_u32_e32 vcc, 0, v10
	v_cmp_gt_f32_e64 s[16:17], v13, v6
	s_and_b64 vcc, vcc, s[16:17]
	s_mov_b32 s16, 0x400000
	v_cndmask_b32_e32 v6, v6, v13, vcc
	v_bitop3_b32 v10, v38, s16, v3 bitop3:0xc8
	v_cndmask_b32_e64 v7, v7, 21, vcc
	v_cmp_eq_u32_e32 vcc, 0, v10
	v_cmp_gt_f32_e64 s[16:17], v4, v6
	s_and_b64 vcc, vcc, s[16:17]
	s_mov_b32 s16, 0x800000
	v_cndmask_b32_e32 v4, v6, v4, vcc
	v_cndmask_b32_e64 v6, v7, 22, vcc
	v_bitop3_b32 v7, v38, s16, v3 bitop3:0xc8
	v_cmp_eq_u32_e32 vcc, 0, v7
	v_cmp_gt_f32_e64 s[16:17], v5, v4
	s_and_b64 vcc, vcc, s[16:17]
	s_mov_b32 s16, 0x1000000
	v_cndmask_b32_e32 v4, v4, v5, vcc
	v_cndmask_b32_e64 v5, v6, 23, vcc
	v_bitop3_b32 v6, v38, s16, v3 bitop3:0xc8
	v_cmp_eq_u32_e32 vcc, 0, v6
	v_cmp_gt_f32_e64 s[16:17], v14, v4
	s_and_b64 vcc, vcc, s[16:17]
	v_cndmask_b32_e32 v4, v4, v14, vcc
	v_bitop3_b32 v6, v38, s61, v3 bitop3:0xc8
	v_cndmask_b32_e64 v5, v5, 24, vcc
	v_cmp_eq_u32_e32 vcc, 0, v6
	v_cmp_gt_f32_e64 s[16:17], v15, v4
	s_and_b64 vcc, vcc, s[16:17]
	v_cndmask_b32_e32 v4, v4, v15, vcc
	v_bitop3_b32 v6, v38, s62, v3 bitop3:0xc8
	v_cndmask_b32_e64 v5, v5, 25, vcc
	v_cmp_eq_u32_e32 vcc, 0, v6
	v_cmp_gt_f32_e64 s[16:17], v26, v4
	s_and_b64 vcc, vcc, s[16:17]
	v_cndmask_b32_e32 v4, v4, v26, vcc
	v_bitop3_b32 v6, v38, s63, v3 bitop3:0xc8
	v_cndmask_b32_e64 v5, v5, 26, vcc
	v_cmp_eq_u32_e32 vcc, 0, v6
	v_cmp_gt_f32_e64 s[16:17], v27, v4
	s_and_b64 vcc, vcc, s[16:17]
	v_cndmask_b32_e32 v4, v4, v27, vcc
	v_bitop3_b32 v6, v38, s64, v3 bitop3:0xc8
	v_cndmask_b32_e64 v5, v5, 27, vcc
	v_cmp_eq_u32_e32 vcc, 0, v6
	v_cmp_gt_f32_e64 s[16:17], v16, v4
	s_and_b64 vcc, vcc, s[16:17]
	v_cndmask_b32_e32 v4, v4, v16, vcc
	v_bitop3_b32 v6, v38, s65, v3 bitop3:0xc8
	v_cndmask_b32_e64 v5, v5, 28, vcc
	v_cmp_eq_u32_e32 vcc, 0, v6
	v_cmp_gt_f32_e64 s[16:17], v17, v4
	s_and_b64 vcc, vcc, s[16:17]
	v_or_b32_e32 v88, v38, v3
	v_cndmask_b32_e32 v4, v4, v17, vcc
	v_bitop3_b32 v3, v38, 2.0, v3 bitop3:0xc8
	v_cndmask_b32_e64 v5, v5, 29, vcc
	v_cmp_eq_u32_e32 vcc, 0, v3
	v_cmp_gt_f32_e64 s[16:17], v8, v4
	s_and_b64 vcc, vcc, s[16:17]
	v_cndmask_b32_e32 v3, v4, v8, vcc
	v_cndmask_b32_e64 v4, v5, 30, vcc
	v_cmp_lt_i32_e32 vcc, -1, v88
	v_cmp_gt_f32_e64 s[16:17], v9, v3
	s_and_b64 vcc, vcc, s[16:17]
	v_cndmask_b32_e32 v5, v3, v9, vcc
	v_cndmask_b32_e64 v3, v4, 31, vcc
	v_sub_f32_e32 v4, v36, v36
	v_mul_f32_e32 v4, 0x3fb8aa3b, v4
	v_exp_f32_e32 v10, v4
	v_sub_f32_e32 v4, v37, v36
	v_mul_f32_e32 v4, 0x3fb8aa3b, v4
	v_exp_f32_e32 v11, v4
	v_sub_f32_e32 v4, v39, v36
	v_mul_f32_e32 v4, 0x3fb8aa3b, v4
	v_exp_f32_e32 v12, v4
	v_sub_f32_e32 v4, v5, v36
	v_mul_f32_e32 v4, 0x3fb8aa3b, v4
	v_exp_f32_e32 v13, v4
	v_add_f32_e32 v4, 0, v10
	v_add_f32_e32 v4, v4, v11
	v_add_f32_e32 v4, v4, v12
	v_add_f32_e32 v14, v4, v13
	v_div_scale_f32 v15, s[16:17], v14, v14, v10
	v_rcp_f32_e32 v16, v15
	v_lshl_add_u32 v4, s66, 8, v94
	v_ashrrev_i32_e32 v5, 31, v4
	v_lshlrev_b64 v[6:7], 2, v[4:5]
	v_fma_f32 v5, -v15, v16, 1.0
	v_fmac_f32_e32 v16, v5, v16
	v_div_scale_f32 v5, vcc, v10, v14, v10
	v_mul_f32_e32 v17, v5, v16
	v_fma_f32 v18, -v15, v17, v5
	v_fmac_f32_e32 v17, v18, v16
	v_fma_f32 v5, -v15, v17, v5
	v_div_fmas_f32 v5, v5, v16, v17
	v_div_fixup_f32 v5, v5, v14, v10
	v_div_scale_f32 v10, s[16:17], v14, v14, v11
	v_rcp_f32_e32 v15, v10
	v_lshl_add_u64 v[8:9], s[20:21], 0, v[6:7]
	v_lshl_add_u64 v[6:7], s[22:23], 0, v[6:7]
	global_store_dword v[6:7], v5, off
	v_or_b32_e32 v6, 1, v4
	v_fma_f32 v4, -v10, v15, 1.0
	v_lshl_add_u32 v5, v0, 2, 0
	v_fmac_f32_e32 v15, v4, v15
	v_div_scale_f32 v4, vcc, v11, v14, v11
	ds_add_u32 v5, v109 offset:58624
	v_mul_f32_e32 v5, v4, v15
	v_fma_f32 v16, -v10, v5, v4
	v_fmac_f32_e32 v5, v16, v15
	v_fma_f32 v4, -v10, v5, v4
	v_div_fmas_f32 v4, v4, v15, v5
	v_div_scale_f32 v5, s[16:17], v14, v14, v12
	v_rcp_f32_e32 v15, v5
	v_ashrrev_i32_e32 v7, 31, v6
	v_div_fixup_f32 v4, v4, v14, v11
	v_lshl_add_u64 v[10:11], v[6:7], 2, s[22:23]
	v_lshl_add_u32 v6, v1, 2, 0
	ds_add_u32 v6, v109 offset:58624
	v_fma_f32 v6, -v5, v15, 1.0
	v_fmac_f32_e32 v15, v6, v15
	v_div_scale_f32 v6, vcc, v12, v14, v12
	v_mul_f32_e32 v7, v6, v15
	v_fma_f32 v16, -v5, v7, v6
	v_fmac_f32_e32 v7, v16, v15
	v_fma_f32 v5, -v5, v7, v6
	v_div_scale_f32 v6, s[16:17], v14, v14, v13
	v_div_fmas_f32 v5, v5, v15, v7
	v_rcp_f32_e32 v7, v6
	v_div_fixup_f32 v5, v5, v14, v12
	v_lshl_add_u32 v12, v2, 2, 0
	ds_add_u32 v12, v109 offset:58624
	global_store_dwordx4 v[8:9], v[0:3], off
	s_nop 1
	v_fma_f32 v0, -v6, v7, 1.0
	v_fmac_f32_e32 v7, v0, v7
	v_div_scale_f32 v0, vcc, v13, v14, v13
	v_mul_f32_e32 v1, v0, v7
	v_fma_f32 v2, -v6, v1, v0
	v_fmac_f32_e32 v1, v2, v7
	v_fma_f32 v0, -v6, v1, v0
	v_div_fmas_f32 v0, v0, v7, v1
	v_div_fixup_f32 v6, v0, v14, v13
	global_store_dwordx3 v[10:11], v[4:6], off
	v_lshl_add_u32 v0, v3, 2, 0
	ds_add_u32 v0, v109 offset:58624

.LBB0_2382:
	s_waitcnt vmcnt(0)
	s_barrier
	s_waitcnt vmcnt(0)
	buffer_inv sc1
	s_waitcnt vmcnt(0)
	v_readlane_b32 s98, v253, 20
	v_mbcnt_lo_u32_b32 v216, -1, 0
	v_mbcnt_hi_u32_b32 v216, -1, v216
	s_lshr_b32 s99, s98, 1
	s_and_b32 s100, s98, 1
	v_lshrrev_b32_e32 v217, 5, v216
	v_and_b32_e32 v216, 31, v216
	s_lshl_b32 s101, s99, 4
	v_add_u32_e32 v218, s101, v217
	v_lshlrev_b32_e32 v219, 7, v218
	v_lshl_add_u32 v219, v216, 2, v219
	v_add_u32_e32 v219, 0xa400, v219
	v_mul_u32_u24_e32 v218, 0x104, v218
	s_lshl_b32 s101, s100, 7
	v_add_u32_e32 v218, s101, v218
	v_lshl_add_u32 v218, v216, 2, v218
	v_add_u32_e32 v218, 0x6000, v218
	v_mov_b32_e32 v221, s98
	v_mbcnt_lo_u32_b32 v220, -1, 0
	v_mbcnt_hi_u32_b32 v220, -1, v220
	v_lshl_add_u32 v220, v221, 6, v220
	v_and_b32_e32 v221, 7, v220
	v_lshrrev_b32_e32 v220, 3, v220
	v_mul_u32_u24_e32 v221, 0x820, v221
	v_lshl_add_u32 v220, v220, 2, v221
	v_add_u32_e32 v220, 0x6000, v220
	v_add_u32_e32 v221, 0x410, v220
	s_lshl_b32 s101, s99, 13
	s_lshl_b32 s100, s100, 12
	s_add_i32 s101, s101, s100
	v_lshlrev_b32_e32 v217, 9, v217
	v_add_u32_e32 v217, s101, v217
	v_lshl_add_u32 v217, v216, 2, v217
	s_and_saveexec_b64 s[16:17], s[4:5]
	ds_write_b32 v95, v45 offset:58624
	s_or_b64 exec, exec, s[16:17]
	v_add_u32_e32 v0, s67, v42
	v_ashrrev_i32_e32 v1, 31, v0
	v_lshlrev_b64 v[0:1], 11, v[0:1]
	v_lshl_add_u64 v[92:93], v[46:47], 0, v[0:1]
	global_load_dwordx4 v[30:33], v[92:93], off
	global_load_dwordx4 v[34:37], v[48:49], off
	global_load_dwordx4 v[20:23], v[52:53], off
	global_load_dwordx4 v[24:27], v[92:93], off offset:128
	ds_read_b64 v[38:39], v106 offset:20480
	ds_read_b128 v[116:119], v43 offset:12288
	ds_read_b128 v[120:123], v43 offset:12304
	ds_read_b128 v[124:127], v43 offset:16384
	ds_read_b128 v[128:131], v43 offset:16400
	v_add_u32_e32 v114, 0x6000, v97
	v_mov_b32_e32 v4, 0
	s_waitcnt lgkmcnt(4)
	v_mov_b32_e32 v0, v38
	v_mov_b32_e32 v1, v38
	v_mov_b32_e32 v2, v38
	v_mov_b32_e32 v3, v38
	v_mov_b32_e32 v88, v39
	v_mov_b32_e32 v89, v39
	v_mov_b32_e32 v90, v39
	v_mov_b32_e32 v91, v39
	v_add_u32_e32 v113, 0x6400, v97
	s_mov_b32 s16, 0
	v_mov_b32_e32 v28, v103
	v_mov_b32_e32 v5, v4
	v_mov_b32_e32 v6, v4
	v_mov_b32_e32 v7, v4
	v_mov_b32_e32 v8, v4
	v_mov_b32_e32 v9, v4
	v_mov_b32_e32 v10, v4
	v_mov_b32_e32 v11, v4
	v_mov_b32_e32 v12, v4
	v_mov_b32_e32 v13, v4
	v_mov_b32_e32 v14, v4
	v_mov_b32_e32 v15, v4
	v_mov_b32_e32 v16, v4
	v_mov_b32_e32 v17, v4
	v_mov_b32_e32 v18, v4
	s_waitcnt vmcnt(3)
	v_cvt_f32_f16_sdwa v19, v31 dst_sel:DWORD dst_unused:UNUSED_PAD src0_sel:WORD_1
	v_cvt_f32_f16_e32 v29, v31
	v_cvt_f32_f16_sdwa v31, v30 dst_sel:DWORD dst_unused:UNUSED_PAD src0_sel:WORD_1
	v_cvt_f32_f16_e32 v30, v30
	v_cvt_f32_f16_sdwa v115, v33 dst_sel:DWORD dst_unused:UNUSED_PAD src0_sel:WORD_1
	v_cvt_f32_f16_e32 v134, v33
	v_cvt_f32_f16_sdwa v133, v32 dst_sel:DWORD dst_unused:UNUSED_PAD src0_sel:WORD_1
	v_cvt_f32_f16_e32 v132, v32
	v_sub_f32_e32 v30, v30, v38
	v_sub_f32_e32 v31, v31, v38
	v_sub_f32_e32 v32, v29, v38
	v_sub_f32_e32 v33, v19, v38
	v_sub_f32_e32 v132, v132, v38
	v_sub_f32_e32 v133, v133, v38
	v_sub_f32_e32 v134, v134, v38
	v_sub_f32_e32 v135, v115, v38
	v_pk_mul_f32 v[30:31], v[38:39], v[30:31] op_sel:[1,0]
	v_pk_mul_f32 v[32:33], v[38:39], v[32:33] op_sel:[1,0]
	v_pk_mul_f32 v[134:135], v[38:39], v[134:135] op_sel:[1,0]
	v_pk_mul_f32 v[38:39], v[38:39], v[132:133] op_sel:[1,0]
	s_waitcnt lgkmcnt(1)
	v_fma_f32 v19, v116, v30, v124
	v_fma_f32 v30, v117, v31, v125
	s_waitcnt lgkmcnt(0)
	v_fma_f32 v29, v120, v38, v128
	v_fma_f32 v31, v121, v39, v129
	v_fma_f32 v32, v118, v32, v126
	v_fma_f32 v38, v122, v134, v130
	v_fmac_f32_e32 v127, v119, v33
	v_fmac_f32_e32 v131, v123, v135
	ds_write2_b32 v220, v19, v30 offset1:65
	ds_write2_b32 v221, v29, v31 offset1:65
	ds_write2_b32 v220, v32, v127 offset0:130 offset1:195
	ds_write2_b32 v221, v38, v131 offset0:130 offset1:195
	s_waitcnt vmcnt(2)
	ds_write_b128 v96, v[34:37] offset:41984
	v_mov_b32_e32 v19, v4
	s_waitcnt lgkmcnt(0)
	s_barrier
	ds_read_b32 v200, v218
	ds_read_b32 v208, v219
	ds_read_b32 v201, v218 offset:520
	ds_read_b32 v209, v219 offset:256
	ds_read_b32 v202, v218 offset:1040
	ds_read_b32 v210, v219 offset:512
	ds_read_b32 v203, v218 offset:1560
	ds_read_b32 v211, v219 offset:768
	ds_read_b32 v204, v218 offset:2080
	ds_read_b32 v212, v219 offset:1024
	ds_read_b32 v205, v218 offset:2600
	ds_read_b32 v213, v219 offset:1280
	ds_read_b32 v206, v218 offset:3120
	ds_read_b32 v214, v219 offset:1536
	s_waitcnt lgkmcnt(12)
	v_mfma_f32_32x32x2_f32 v[4:19], v200, v208, v[4:19]
	ds_read_b32 v207, v218 offset:3640
	ds_read_b32 v215, v219 offset:1792
	s_waitcnt lgkmcnt(12)
	v_mfma_f32_32x32x2_f32 v[4:19], v201, v209, v[4:19]
	s_waitcnt lgkmcnt(10)
	v_mfma_f32_32x32x2_f32 v[4:19], v202, v210, v[4:19]
	s_waitcnt lgkmcnt(8)
	v_mfma_f32_32x32x2_f32 v[4:19], v203, v211, v[4:19]
	s_waitcnt lgkmcnt(6)
	v_mfma_f32_32x32x2_f32 v[4:19], v204, v212, v[4:19]
	s_waitcnt lgkmcnt(4)
	v_mfma_f32_32x32x2_f32 v[4:19], v205, v213, v[4:19]
	s_waitcnt lgkmcnt(2)
	v_mfma_f32_32x32x2_f32 v[4:19], v206, v214, v[4:19]
	s_waitcnt lgkmcnt(0)
	v_mfma_f32_32x32x2_f32 v[4:19], v207, v215, v[4:19]
	s_barrier
	global_load_dwordx4 v[32:35], v[92:93], off offset:256
	global_load_dwordx4 v[28:31], v[54:55], off
	s_waitcnt vmcnt(2)
	v_cvt_f32_f16_sdwa v128, v24 dst_sel:DWORD dst_unused:UNUSED_PAD src0_sel:WORD_1
	v_cvt_f32_f16_e32 v24, v24
	v_cvt_f32_f16_e32 v129, v25
	v_cvt_f32_f16_sdwa v130, v26 dst_sel:DWORD dst_unused:UNUSED_PAD src0_sel:WORD_1
	v_cvt_f32_f16_e32 v133, v26
	ds_read_b128 v[36:39], v43 offset:12544
	ds_read_b128 v[116:119], v43 offset:12560
	ds_read_b128 v[120:123], v43 offset:16640
	ds_read_b128 v[124:127], v43 offset:16656
	v_cvt_f32_f16_sdwa v115, v25 dst_sel:DWORD dst_unused:UNUSED_PAD src0_sel:WORD_1
	v_cvt_f32_f16_sdwa v131, v27 dst_sel:DWORD dst_unused:UNUSED_PAD src0_sel:WORD_1
	v_cvt_f32_f16_e32 v132, v27
	v_sub_f32_e32 v24, v24, v0
	v_sub_f32_e32 v25, v128, v1
	v_sub_f32_e32 v26, v129, v2
	v_pk_mul_f32 v[24:25], v[88:89], v[24:25]
	v_sub_f32_e32 v128, v133, v0
	v_sub_f32_e32 v129, v130, v1
	v_sub_f32_e32 v27, v115, v3
	v_sub_f32_e32 v130, v132, v2
	v_sub_f32_e32 v131, v131, v3
	v_pk_mul_f32 v[128:129], v[88:89], v[128:129]
	s_waitcnt lgkmcnt(1)
	v_fma_f32 v24, v36, v24, v120
	v_fma_f32 v25, v37, v25, v121
	v_pk_mul_f32 v[26:27], v[90:91], v[26:27]
	v_pk_mul_f32 v[130:131], v[90:91], v[130:131]
	s_waitcnt lgkmcnt(0)
	v_fma_f32 v36, v116, v128, v124
	ds_write2_b32 v220, v24, v25 offset1:65
	v_fma_f32 v24, v117, v129, v125
	ds_write2_b32 v221, v36, v24 offset1:65
	v_fma_f32 v24, v38, v26, v122
	v_fma_f32 v25, v118, v130, v126
	v_fmac_f32_e32 v123, v39, v27
	v_fmac_f32_e32 v127, v119, v131
	ds_write2_b32 v220, v24, v123 offset0:130 offset1:195
	ds_write2_b32 v221, v25, v127 offset0:130 offset1:195
	ds_write_b128 v96, v[20:23] offset:41984
	s_mov_b32 s16, 0
	v_mov_b32_e32 v20, v103
	s_waitcnt lgkmcnt(0)
	s_barrier
	ds_read_b32 v200, v218
	ds_read_b32 v208, v219
	ds_read_b32 v201, v218 offset:520
	ds_read_b32 v209, v219 offset:256
	ds_read_b32 v202, v218 offset:1040
	ds_read_b32 v210, v219 offset:512
	ds_read_b32 v203, v218 offset:1560
	ds_read_b32 v211, v219 offset:768
	ds_read_b32 v204, v218 offset:2080
	ds_read_b32 v212, v219 offset:1024
	ds_read_b32 v205, v218 offset:2600
	ds_read_b32 v213, v219 offset:1280
	ds_read_b32 v206, v218 offset:3120
	ds_read_b32 v214, v219 offset:1536
	s_waitcnt lgkmcnt(12)
	v_mfma_f32_32x32x2_f32 v[4:19], v200, v208, v[4:19]
	ds_read_b32 v207, v218 offset:3640
	ds_read_b32 v215, v219 offset:1792
	s_waitcnt lgkmcnt(12)
	v_mfma_f32_32x32x2_f32 v[4:19], v201, v209, v[4:19]
	s_waitcnt lgkmcnt(10)
	v_mfma_f32_32x32x2_f32 v[4:19], v202, v210, v[4:19]
	s_waitcnt lgkmcnt(8)
	v_mfma_f32_32x32x2_f32 v[4:19], v203, v211, v[4:19]
	s_waitcnt lgkmcnt(6)
	v_mfma_f32_32x32x2_f32 v[4:19], v204, v212, v[4:19]
	s_waitcnt lgkmcnt(4)
	v_mfma_f32_32x32x2_f32 v[4:19], v205, v213, v[4:19]
	s_waitcnt lgkmcnt(2)
	v_mfma_f32_32x32x2_f32 v[4:19], v206, v214, v[4:19]
	s_waitcnt lgkmcnt(0)
	v_mfma_f32_32x32x2_f32 v[4:19], v207, v215, v[4:19]
	s_barrier
	global_load_dwordx4 v[36:39], v[92:93], off offset:384
	global_load_dwordx4 v[20:23], v[56:57], off
	s_waitcnt vmcnt(3)
	v_cvt_f32_f16_sdwa v128, v32 dst_sel:DWORD dst_unused:UNUSED_PAD src0_sel:WORD_1
	v_cvt_f32_f16_e32 v32, v32
	v_cvt_f32_f16_e32 v129, v33
	v_cvt_f32_f16_sdwa v130, v34 dst_sel:DWORD dst_unused:UNUSED_PAD src0_sel:WORD_1
	v_cvt_f32_f16_e32 v133, v34
	ds_read_b128 v[24:27], v43 offset:12800
	ds_read_b128 v[116:119], v43 offset:12816
	ds_read_b128 v[120:123], v43 offset:16896
	ds_read_b128 v[124:127], v43 offset:16912
	v_cvt_f32_f16_sdwa v115, v33 dst_sel:DWORD dst_unused:UNUSED_PAD src0_sel:WORD_1
	v_cvt_f32_f16_sdwa v131, v35 dst_sel:DWORD dst_unused:UNUSED_PAD src0_sel:WORD_1
	v_cvt_f32_f16_e32 v132, v35
	v_sub_f32_e32 v32, v32, v0
	v_sub_f32_e32 v33, v128, v1
	v_sub_f32_e32 v34, v129, v2
	v_pk_mul_f32 v[32:33], v[88:89], v[32:33]
	v_sub_f32_e32 v128, v133, v0
	v_sub_f32_e32 v129, v130, v1
	v_sub_f32_e32 v35, v115, v3
	v_pk_mul_f32 v[128:129], v[88:89], v[128:129]
	s_waitcnt lgkmcnt(1)
	v_fma_f32 v24, v24, v32, v120
	v_fma_f32 v25, v25, v33, v121
	v_pk_mul_f32 v[34:35], v[90:91], v[34:35]
	v_sub_f32_e32 v130, v132, v2
	v_sub_f32_e32 v131, v131, v3
	s_waitcnt lgkmcnt(0)
	v_fma_f32 v32, v116, v128, v124
	ds_write2_b32 v220, v24, v25 offset1:65
	v_fma_f32 v24, v117, v129, v125
	v_pk_mul_f32 v[130:131], v[90:91], v[130:131]
	ds_write2_b32 v221, v32, v24 offset1:65
	v_fma_f32 v24, v26, v34, v122
	v_fmac_f32_e32 v123, v27, v35
	v_fma_f32 v25, v118, v130, v126
	ds_write2_b32 v220, v24, v123 offset0:130 offset1:195
	v_fmac_f32_e32 v127, v119, v131
	s_mov_b32 s16, 0
	v_mov_b32_e32 v24, v103
	ds_write2_b32 v221, v25, v127 offset0:130 offset1:195
	s_waitcnt vmcnt(2)
	ds_write_b128 v96, v[28:31] offset:41984
	s_waitcnt lgkmcnt(0)
	s_barrier
	ds_read_b32 v200, v218
	ds_read_b32 v208, v219
	ds_read_b32 v201, v218 offset:520
	ds_read_b32 v209, v219 offset:256
	ds_read_b32 v202, v218 offset:1040
	ds_read_b32 v210, v219 offset:512
	ds_read_b32 v203, v218 offset:1560
	ds_read_b32 v211, v219 offset:768
	ds_read_b32 v204, v218 offset:2080
	ds_read_b32 v212, v219 offset:1024
	ds_read_b32 v205, v218 offset:2600
	ds_read_b32 v213, v219 offset:1280
	ds_read_b32 v206, v218 offset:3120
	ds_read_b32 v214, v219 offset:1536
	s_waitcnt lgkmcnt(12)
	v_mfma_f32_32x32x2_f32 v[4:19], v200, v208, v[4:19]
	ds_read_b32 v207, v218 offset:3640
	ds_read_b32 v215, v219 offset:1792
	s_waitcnt lgkmcnt(12)
	v_mfma_f32_32x32x2_f32 v[4:19], v201, v209, v[4:19]
	s_waitcnt lgkmcnt(10)
	v_mfma_f32_32x32x2_f32 v[4:19], v202, v210, v[4:19]
	s_waitcnt lgkmcnt(8)
	v_mfma_f32_32x32x2_f32 v[4:19], v203, v211, v[4:19]
	s_waitcnt lgkmcnt(6)
	v_mfma_f32_32x32x2_f32 v[4:19], v204, v212, v[4:19]
	s_waitcnt lgkmcnt(4)
	v_mfma_f32_32x32x2_f32 v[4:19], v205, v213, v[4:19]
	s_waitcnt lgkmcnt(2)
	v_mfma_f32_32x32x2_f32 v[4:19], v206, v214, v[4:19]
	s_waitcnt lgkmcnt(0)
	v_mfma_f32_32x32x2_f32 v[4:19], v207, v215, v[4:19]
	s_barrier
	global_load_dwordx4 v[28:31], v[92:93], off offset:512
	global_load_dwordx4 v[24:27], v[58:59], off
	s_waitcnt vmcnt(3)
	v_cvt_f32_f16_sdwa v128, v36 dst_sel:DWORD dst_unused:UNUSED_PAD src0_sel:WORD_1
	v_cvt_f32_f16_e32 v36, v36
	v_cvt_f32_f16_e32 v129, v37
	v_cvt_f32_f16_sdwa v130, v38 dst_sel:DWORD dst_unused:UNUSED_PAD src0_sel:WORD_1
	v_cvt_f32_f16_e32 v133, v38
	ds_read_b128 v[32:35], v43 offset:13056
	ds_read_b128 v[116:119], v43 offset:13072
	ds_read_b128 v[120:123], v43 offset:17152
	ds_read_b128 v[124:127], v43 offset:17168
	v_cvt_f32_f16_sdwa v115, v37 dst_sel:DWORD dst_unused:UNUSED_PAD src0_sel:WORD_1
	v_cvt_f32_f16_sdwa v131, v39 dst_sel:DWORD dst_unused:UNUSED_PAD src0_sel:WORD_1
	v_cvt_f32_f16_e32 v132, v39
	v_sub_f32_e32 v36, v36, v0
	v_sub_f32_e32 v37, v128, v1
	v_sub_f32_e32 v38, v129, v2
	v_pk_mul_f32 v[36:37], v[88:89], v[36:37]
	v_sub_f32_e32 v128, v133, v0
	v_sub_f32_e32 v129, v130, v1
	v_sub_f32_e32 v39, v115, v3
	v_sub_f32_e32 v130, v132, v2
	v_sub_f32_e32 v131, v131, v3
	v_pk_mul_f32 v[128:129], v[88:89], v[128:129]
	s_waitcnt lgkmcnt(1)
	v_fma_f32 v32, v32, v36, v120
	v_fma_f32 v33, v33, v37, v121
	v_pk_mul_f32 v[38:39], v[90:91], v[38:39]
	v_pk_mul_f32 v[130:131], v[90:91], v[130:131]
	s_waitcnt lgkmcnt(0)
	v_fma_f32 v36, v116, v128, v124
	ds_write2_b32 v220, v32, v33 offset1:65
	v_fma_f32 v32, v117, v129, v125
	ds_write2_b32 v221, v36, v32 offset1:65
	v_fma_f32 v32, v34, v38, v122
	v_fma_f32 v33, v118, v130, v126
	v_fmac_f32_e32 v123, v35, v39
	v_fmac_f32_e32 v127, v119, v131
	ds_write2_b32 v220, v32, v123 offset0:130 offset1:195
	ds_write2_b32 v221, v33, v127 offset0:130 offset1:195
	s_waitcnt vmcnt(2)
	ds_write_b128 v96, v[20:23] offset:41984
	s_mov_b32 s16, 0
	v_mov_b32_e32 v20, v103
	s_waitcnt lgkmcnt(0)
	s_barrier
	ds_read_b32 v200, v218
	ds_read_b32 v208, v219
	ds_read_b32 v201, v218 offset:520
	ds_read_b32 v209, v219 offset:256
	ds_read_b32 v202, v218 offset:1040
	ds_read_b32 v210, v219 offset:512
	ds_read_b32 v203, v218 offset:1560
	ds_read_b32 v211, v219 offset:768
	ds_read_b32 v204, v218 offset:2080
	ds_read_b32 v212, v219 offset:1024
	ds_read_b32 v205, v218 offset:2600
	ds_read_b32 v213, v219 offset:1280
	ds_read_b32 v206, v218 offset:3120
	ds_read_b32 v214, v219 offset:1536
	s_waitcnt lgkmcnt(12)
	v_mfma_f32_32x32x2_f32 v[4:19], v200, v208, v[4:19]
	ds_read_b32 v207, v218 offset:3640
	ds_read_b32 v215, v219 offset:1792
	s_waitcnt lgkmcnt(12)
	v_mfma_f32_32x32x2_f32 v[4:19], v201, v209, v[4:19]
	s_waitcnt lgkmcnt(10)
	v_mfma_f32_32x32x2_f32 v[4:19], v202, v210, v[4:19]
	s_waitcnt lgkmcnt(8)
	v_mfma_f32_32x32x2_f32 v[4:19], v203, v211, v[4:19]
	s_waitcnt lgkmcnt(6)
	v_mfma_f32_32x32x2_f32 v[4:19], v204, v212, v[4:19]
	s_waitcnt lgkmcnt(4)
	v_mfma_f32_32x32x2_f32 v[4:19], v205, v213, v[4:19]
	s_waitcnt lgkmcnt(2)
	v_mfma_f32_32x32x2_f32 v[4:19], v206, v214, v[4:19]
	s_waitcnt lgkmcnt(0)
	v_mfma_f32_32x32x2_f32 v[4:19], v207, v215, v[4:19]
	s_barrier
	global_load_dwordx4 v[32:35], v[92:93], off offset:640
	global_load_dwordx4 v[20:23], v[60:61], off
	s_waitcnt vmcnt(3)
	v_cvt_f32_f16_sdwa v128, v28 dst_sel:DWORD dst_unused:UNUSED_PAD src0_sel:WORD_1
	v_cvt_f32_f16_e32 v28, v28
	v_cvt_f32_f16_e32 v129, v29
	v_cvt_f32_f16_sdwa v130, v30 dst_sel:DWORD dst_unused:UNUSED_PAD src0_sel:WORD_1
	v_cvt_f32_f16_e32 v133, v30
	ds_read_b128 v[36:39], v43 offset:13312
	ds_read_b128 v[116:119], v43 offset:13328
	ds_read_b128 v[120:123], v43 offset:17408
	ds_read_b128 v[124:127], v43 offset:17424
	v_cvt_f32_f16_sdwa v115, v29 dst_sel:DWORD dst_unused:UNUSED_PAD src0_sel:WORD_1
	v_cvt_f32_f16_sdwa v131, v31 dst_sel:DWORD dst_unused:UNUSED_PAD src0_sel:WORD_1
	v_cvt_f32_f16_e32 v132, v31
	v_sub_f32_e32 v28, v28, v0
	v_sub_f32_e32 v29, v128, v1
	v_sub_f32_e32 v30, v129, v2
	v_pk_mul_f32 v[28:29], v[88:89], v[28:29]
	v_sub_f32_e32 v128, v133, v0
	v_sub_f32_e32 v129, v130, v1
	v_sub_f32_e32 v31, v115, v3
	v_sub_f32_e32 v130, v132, v2
	v_sub_f32_e32 v131, v131, v3
	v_pk_mul_f32 v[128:129], v[88:89], v[128:129]
	s_waitcnt lgkmcnt(1)
	v_fma_f32 v28, v36, v28, v120
	v_fma_f32 v29, v37, v29, v121
	v_pk_mul_f32 v[30:31], v[90:91], v[30:31]
	v_pk_mul_f32 v[130:131], v[90:91], v[130:131]
	s_waitcnt lgkmcnt(0)
	v_fma_f32 v36, v116, v128, v124
	ds_write2_b32 v220, v28, v29 offset1:65
	v_fma_f32 v28, v117, v129, v125
	ds_write2_b32 v221, v36, v28 offset1:65
	v_fma_f32 v28, v38, v30, v122
	v_fma_f32 v29, v118, v130, v126
	v_fmac_f32_e32 v123, v39, v31
	v_fmac_f32_e32 v127, v119, v131
	ds_write2_b32 v220, v28, v123 offset0:130 offset1:195
	ds_write2_b32 v221, v29, v127 offset0:130 offset1:195
	s_waitcnt vmcnt(2)
	ds_write_b128 v96, v[24:27] offset:41984
	s_mov_b32 s16, 0
	v_mov_b32_e32 v24, v103
	s_waitcnt lgkmcnt(0)
	s_barrier
	ds_read_b32 v200, v218
	ds_read_b32 v208, v219
	ds_read_b32 v201, v218 offset:520
	ds_read_b32 v209, v219 offset:256
	ds_read_b32 v202, v218 offset:1040
	ds_read_b32 v210, v219 offset:512
	ds_read_b32 v203, v218 offset:1560
	ds_read_b32 v211, v219 offset:768
	ds_read_b32 v204, v218 offset:2080
	ds_read_b32 v212, v219 offset:1024
	ds_read_b32 v205, v218 offset:2600
	ds_read_b32 v213, v219 offset:1280
	ds_read_b32 v206, v218 offset:3120
	ds_read_b32 v214, v219 offset:1536
	s_waitcnt lgkmcnt(12)
	v_mfma_f32_32x32x2_f32 v[4:19], v200, v208, v[4:19]
	ds_read_b32 v207, v218 offset:3640
	ds_read_b32 v215, v219 offset:1792
	s_waitcnt lgkmcnt(12)
	v_mfma_f32_32x32x2_f32 v[4:19], v201, v209, v[4:19]
	s_waitcnt lgkmcnt(10)
	v_mfma_f32_32x32x2_f32 v[4:19], v202, v210, v[4:19]
	s_waitcnt lgkmcnt(8)
	v_mfma_f32_32x32x2_f32 v[4:19], v203, v211, v[4:19]
	s_waitcnt lgkmcnt(6)
	v_mfma_f32_32x32x2_f32 v[4:19], v204, v212, v[4:19]
	s_waitcnt lgkmcnt(4)
	v_mfma_f32_32x32x2_f32 v[4:19], v205, v213, v[4:19]
	s_waitcnt lgkmcnt(2)
	v_mfma_f32_32x32x2_f32 v[4:19], v206, v214, v[4:19]
	s_waitcnt lgkmcnt(0)
	v_mfma_f32_32x32x2_f32 v[4:19], v207, v215, v[4:19]
	s_barrier
	global_load_dwordx4 v[28:31], v[92:93], off offset:768
	global_load_dwordx4 v[24:27], v[62:63], off
	s_waitcnt vmcnt(3)
	v_cvt_f32_f16_sdwa v128, v32 dst_sel:DWORD dst_unused:UNUSED_PAD src0_sel:WORD_1
	v_cvt_f32_f16_e32 v32, v32
	v_cvt_f32_f16_e32 v129, v33
	v_cvt_f32_f16_sdwa v130, v34 dst_sel:DWORD dst_unused:UNUSED_PAD src0_sel:WORD_1
	v_cvt_f32_f16_e32 v133, v34
	ds_read_b128 v[36:39], v43 offset:13568
	ds_read_b128 v[116:119], v43 offset:13584
	ds_read_b128 v[120:123], v43 offset:17664
	ds_read_b128 v[124:127], v43 offset:17680
	v_cvt_f32_f16_sdwa v115, v33 dst_sel:DWORD dst_unused:UNUSED_PAD src0_sel:WORD_1
	v_cvt_f32_f16_sdwa v131, v35 dst_sel:DWORD dst_unused:UNUSED_PAD src0_sel:WORD_1
	v_cvt_f32_f16_e32 v132, v35
	v_sub_f32_e32 v32, v32, v0
	v_sub_f32_e32 v33, v128, v1
	v_sub_f32_e32 v34, v129, v2
	v_pk_mul_f32 v[32:33], v[88:89], v[32:33]
	v_sub_f32_e32 v128, v133, v0
	v_sub_f32_e32 v129, v130, v1
	v_sub_f32_e32 v35, v115, v3
	v_sub_f32_e32 v130, v132, v2
	v_sub_f32_e32 v131, v131, v3
	v_pk_mul_f32 v[128:129], v[88:89], v[128:129]
	s_waitcnt lgkmcnt(1)
	v_fma_f32 v32, v36, v32, v120
	v_fma_f32 v33, v37, v33, v121
	v_pk_mul_f32 v[34:35], v[90:91], v[34:35]
	v_pk_mul_f32 v[130:131], v[90:91], v[130:131]
	s_waitcnt lgkmcnt(0)
	v_fma_f32 v36, v116, v128, v124
	ds_write2_b32 v220, v32, v33 offset1:65
	v_fma_f32 v32, v117, v129, v125
	ds_write2_b32 v221, v36, v32 offset1:65
	v_fma_f32 v32, v38, v34, v122
	v_fma_f32 v33, v118, v130, v126
	v_fmac_f32_e32 v123, v39, v35
	v_fmac_f32_e32 v127, v119, v131
	ds_write2_b32 v220, v32, v123 offset0:130 offset1:195
	ds_write2_b32 v221, v33, v127 offset0:130 offset1:195
	s_waitcnt vmcnt(2)
	ds_write_b128 v96, v[20:23] offset:41984
	s_mov_b32 s16, 0
	v_mov_b32_e32 v20, v103
	s_waitcnt lgkmcnt(0)
	s_barrier
	ds_read_b32 v200, v218
	ds_read_b32 v208, v219
	ds_read_b32 v201, v218 offset:520
	ds_read_b32 v209, v219 offset:256
	ds_read_b32 v202, v218 offset:1040
	ds_read_b32 v210, v219 offset:512
	ds_read_b32 v203, v218 offset:1560
	ds_read_b32 v211, v219 offset:768
	ds_read_b32 v204, v218 offset:2080
	ds_read_b32 v212, v219 offset:1024
	ds_read_b32 v205, v218 offset:2600
	ds_read_b32 v213, v219 offset:1280
	ds_read_b32 v206, v218 offset:3120
	ds_read_b32 v214, v219 offset:1536
	s_waitcnt lgkmcnt(12)
	v_mfma_f32_32x32x2_f32 v[4:19], v200, v208, v[4:19]
	ds_read_b32 v207, v218 offset:3640
	ds_read_b32 v215, v219 offset:1792
	s_waitcnt lgkmcnt(12)
	v_mfma_f32_32x32x2_f32 v[4:19], v201, v209, v[4:19]
	s_waitcnt lgkmcnt(10)
	v_mfma_f32_32x32x2_f32 v[4:19], v202, v210, v[4:19]
	s_waitcnt lgkmcnt(8)
	v_mfma_f32_32x32x2_f32 v[4:19], v203, v211, v[4:19]
	s_waitcnt lgkmcnt(6)
	v_mfma_f32_32x32x2_f32 v[4:19], v204, v212, v[4:19]
	s_waitcnt lgkmcnt(4)
	v_mfma_f32_32x32x2_f32 v[4:19], v205, v213, v[4:19]
	s_waitcnt lgkmcnt(2)
	v_mfma_f32_32x32x2_f32 v[4:19], v206, v214, v[4:19]
	s_waitcnt lgkmcnt(0)
	v_mfma_f32_32x32x2_f32 v[4:19], v207, v215, v[4:19]
	s_barrier
	global_load_dwordx4 v[32:35], v[92:93], off offset:896
	global_load_dwordx4 v[20:23], v[64:65], off
	s_waitcnt vmcnt(3)
	v_cvt_f32_f16_sdwa v128, v28 dst_sel:DWORD dst_unused:UNUSED_PAD src0_sel:WORD_1
	v_cvt_f32_f16_e32 v28, v28
	v_cvt_f32_f16_e32 v129, v29
	v_cvt_f32_f16_sdwa v130, v30 dst_sel:DWORD dst_unused:UNUSED_PAD src0_sel:WORD_1
	v_cvt_f32_f16_e32 v133, v30
	ds_read_b128 v[36:39], v43 offset:13824
	ds_read_b128 v[116:119], v43 offset:13840
	ds_read_b128 v[120:123], v43 offset:17920
	ds_read_b128 v[124:127], v43 offset:17936
	v_cvt_f32_f16_sdwa v115, v29 dst_sel:DWORD dst_unused:UNUSED_PAD src0_sel:WORD_1
	v_cvt_f32_f16_sdwa v131, v31 dst_sel:DWORD dst_unused:UNUSED_PAD src0_sel:WORD_1
	v_cvt_f32_f16_e32 v132, v31
	v_sub_f32_e32 v28, v28, v0
	v_sub_f32_e32 v29, v128, v1
	v_sub_f32_e32 v30, v129, v2
	v_pk_mul_f32 v[28:29], v[88:89], v[28:29]
	v_sub_f32_e32 v128, v133, v0
	v_sub_f32_e32 v129, v130, v1
	v_sub_f32_e32 v31, v115, v3
	v_sub_f32_e32 v130, v132, v2
	v_sub_f32_e32 v131, v131, v3
	v_pk_mul_f32 v[128:129], v[88:89], v[128:129]
	s_waitcnt lgkmcnt(1)
	v_fma_f32 v28, v36, v28, v120
	v_fma_f32 v29, v37, v29, v121
	v_pk_mul_f32 v[30:31], v[90:91], v[30:31]
	v_pk_mul_f32 v[130:131], v[90:91], v[130:131]
	s_waitcnt lgkmcnt(0)
	v_fma_f32 v36, v116, v128, v124
	ds_write2_b32 v220, v28, v29 offset1:65
	v_fma_f32 v28, v117, v129, v125
	ds_write2_b32 v221, v36, v28 offset1:65
	v_fma_f32 v28, v38, v30, v122
	v_fma_f32 v29, v118, v130, v126
	v_fmac_f32_e32 v123, v39, v31
	v_fmac_f32_e32 v127, v119, v131
	ds_write2_b32 v220, v28, v123 offset0:130 offset1:195
	ds_write2_b32 v221, v29, v127 offset0:130 offset1:195
	s_waitcnt vmcnt(2)
	ds_write_b128 v96, v[24:27] offset:41984
	s_mov_b32 s16, 0
	v_mov_b32_e32 v24, v103
	s_waitcnt lgkmcnt(0)
	s_barrier
	ds_read_b32 v200, v218
	ds_read_b32 v208, v219
	ds_read_b32 v201, v218 offset:520
	ds_read_b32 v209, v219 offset:256
	ds_read_b32 v202, v218 offset:1040
	ds_read_b32 v210, v219 offset:512
	ds_read_b32 v203, v218 offset:1560
	ds_read_b32 v211, v219 offset:768
	ds_read_b32 v204, v218 offset:2080
	ds_read_b32 v212, v219 offset:1024
	ds_read_b32 v205, v218 offset:2600
	ds_read_b32 v213, v219 offset:1280
	ds_read_b32 v206, v218 offset:3120
	ds_read_b32 v214, v219 offset:1536
	s_waitcnt lgkmcnt(12)
	v_mfma_f32_32x32x2_f32 v[4:19], v200, v208, v[4:19]
	ds_read_b32 v207, v218 offset:3640
	ds_read_b32 v215, v219 offset:1792
	s_waitcnt lgkmcnt(12)
	v_mfma_f32_32x32x2_f32 v[4:19], v201, v209, v[4:19]
	s_waitcnt lgkmcnt(10)
	v_mfma_f32_32x32x2_f32 v[4:19], v202, v210, v[4:19]
	s_waitcnt lgkmcnt(8)
	v_mfma_f32_32x32x2_f32 v[4:19], v203, v211, v[4:19]
	s_waitcnt lgkmcnt(6)
	v_mfma_f32_32x32x2_f32 v[4:19], v204, v212, v[4:19]
	s_waitcnt lgkmcnt(4)
	v_mfma_f32_32x32x2_f32 v[4:19], v205, v213, v[4:19]
	s_waitcnt lgkmcnt(2)
	v_mfma_f32_32x32x2_f32 v[4:19], v206, v214, v[4:19]
	s_waitcnt lgkmcnt(0)
	v_mfma_f32_32x32x2_f32 v[4:19], v207, v215, v[4:19]
	s_barrier
	global_load_dwordx4 v[28:31], v[92:93], off offset:1024
	global_load_dwordx4 v[24:27], v[66:67], off
	s_waitcnt vmcnt(3)
	v_cvt_f32_f16_sdwa v128, v32 dst_sel:DWORD dst_unused:UNUSED_PAD src0_sel:WORD_1
	v_cvt_f32_f16_e32 v32, v32
	v_cvt_f32_f16_e32 v129, v33
	v_cvt_f32_f16_sdwa v130, v34 dst_sel:DWORD dst_unused:UNUSED_PAD src0_sel:WORD_1
	v_cvt_f32_f16_e32 v133, v34
	ds_read_b128 v[36:39], v43 offset:14080
	ds_read_b128 v[116:119], v43 offset:14096
	ds_read_b128 v[120:123], v43 offset:18176
	ds_read_b128 v[124:127], v43 offset:18192
	v_cvt_f32_f16_sdwa v115, v33 dst_sel:DWORD dst_unused:UNUSED_PAD src0_sel:WORD_1
	v_cvt_f32_f16_sdwa v131, v35 dst_sel:DWORD dst_unused:UNUSED_PAD src0_sel:WORD_1
	v_cvt_f32_f16_e32 v132, v35
	v_sub_f32_e32 v32, v32, v0
	v_sub_f32_e32 v33, v128, v1
	v_sub_f32_e32 v34, v129, v2
	v_pk_mul_f32 v[32:33], v[88:89], v[32:33]
	v_sub_f32_e32 v128, v133, v0
	v_sub_f32_e32 v129, v130, v1
	v_sub_f32_e32 v35, v115, v3
	v_sub_f32_e32 v130, v132, v2
	v_sub_f32_e32 v131, v131, v3
	v_pk_mul_f32 v[128:129], v[88:89], v[128:129]
	s_waitcnt lgkmcnt(1)
	v_fma_f32 v32, v36, v32, v120
	v_fma_f32 v33, v37, v33, v121
	v_pk_mul_f32 v[34:35], v[90:91], v[34:35]
	v_pk_mul_f32 v[130:131], v[90:91], v[130:131]
	s_waitcnt lgkmcnt(0)
	v_fma_f32 v36, v116, v128, v124
	ds_write2_b32 v220, v32, v33 offset1:65
	v_fma_f32 v32, v117, v129, v125
	ds_write2_b32 v221, v36, v32 offset1:65
	v_fma_f32 v32, v38, v34, v122
	v_fma_f32 v33, v118, v130, v126
	v_fmac_f32_e32 v123, v39, v35
	v_fmac_f32_e32 v127, v119, v131
	ds_write2_b32 v220, v32, v123 offset0:130 offset1:195
	ds_write2_b32 v221, v33, v127 offset0:130 offset1:195
	s_waitcnt vmcnt(2)
	ds_write_b128 v96, v[20:23] offset:41984
	s_mov_b32 s16, 0
	v_mov_b32_e32 v20, v103
	s_waitcnt lgkmcnt(0)
	s_barrier
	ds_read_b32 v200, v218
	ds_read_b32 v208, v219
	ds_read_b32 v201, v218 offset:520
	ds_read_b32 v209, v219 offset:256
	ds_read_b32 v202, v218 offset:1040
	ds_read_b32 v210, v219 offset:512
	ds_read_b32 v203, v218 offset:1560
	ds_read_b32 v211, v219 offset:768
	ds_read_b32 v204, v218 offset:2080
	ds_read_b32 v212, v219 offset:1024
	ds_read_b32 v205, v218 offset:2600
	ds_read_b32 v213, v219 offset:1280
	ds_read_b32 v206, v218 offset:3120
	ds_read_b32 v214, v219 offset:1536
	s_waitcnt lgkmcnt(12)
	v_mfma_f32_32x32x2_f32 v[4:19], v200, v208, v[4:19]
	ds_read_b32 v207, v218 offset:3640
	ds_read_b32 v215, v219 offset:1792
	s_waitcnt lgkmcnt(12)
	v_mfma_f32_32x32x2_f32 v[4:19], v201, v209, v[4:19]
	s_waitcnt lgkmcnt(10)
	v_mfma_f32_32x32x2_f32 v[4:19], v202, v210, v[4:19]
	s_waitcnt lgkmcnt(8)
	v_mfma_f32_32x32x2_f32 v[4:19], v203, v211, v[4:19]
	s_waitcnt lgkmcnt(6)
	v_mfma_f32_32x32x2_f32 v[4:19], v204, v212, v[4:19]
	s_waitcnt lgkmcnt(4)
	v_mfma_f32_32x32x2_f32 v[4:19], v205, v213, v[4:19]
	s_waitcnt lgkmcnt(2)
	v_mfma_f32_32x32x2_f32 v[4:19], v206, v214, v[4:19]
	s_waitcnt lgkmcnt(0)
	v_mfma_f32_32x32x2_f32 v[4:19], v207, v215, v[4:19]
	s_barrier
	global_load_dwordx4 v[32:35], v[92:93], off offset:1152
	global_load_dwordx4 v[20:23], v[68:69], off
	s_waitcnt vmcnt(3)
	v_cvt_f32_f16_sdwa v128, v28 dst_sel:DWORD dst_unused:UNUSED_PAD src0_sel:WORD_1
	v_cvt_f32_f16_e32 v28, v28
	v_cvt_f32_f16_e32 v129, v29
	v_cvt_f32_f16_sdwa v130, v30 dst_sel:DWORD dst_unused:UNUSED_PAD src0_sel:WORD_1
	v_cvt_f32_f16_e32 v133, v30
	ds_read_b128 v[36:39], v43 offset:14336
	ds_read_b128 v[116:119], v43 offset:14352
	ds_read_b128 v[120:123], v43 offset:18432
	ds_read_b128 v[124:127], v43 offset:18448
	v_cvt_f32_f16_sdwa v115, v29 dst_sel:DWORD dst_unused:UNUSED_PAD src0_sel:WORD_1
	v_cvt_f32_f16_sdwa v131, v31 dst_sel:DWORD dst_unused:UNUSED_PAD src0_sel:WORD_1
	v_cvt_f32_f16_e32 v132, v31
	v_sub_f32_e32 v28, v28, v0
	v_sub_f32_e32 v29, v128, v1
	v_sub_f32_e32 v30, v129, v2
	v_pk_mul_f32 v[28:29], v[88:89], v[28:29]
	v_sub_f32_e32 v128, v133, v0
	v_sub_f32_e32 v129, v130, v1
	v_sub_f32_e32 v31, v115, v3
	v_sub_f32_e32 v130, v132, v2
	v_sub_f32_e32 v131, v131, v3
	v_pk_mul_f32 v[128:129], v[88:89], v[128:129]
	s_waitcnt lgkmcnt(1)
	v_fma_f32 v28, v36, v28, v120
	v_fma_f32 v29, v37, v29, v121
	v_pk_mul_f32 v[30:31], v[90:91], v[30:31]
	v_pk_mul_f32 v[130:131], v[90:91], v[130:131]
	s_waitcnt lgkmcnt(0)
	v_fma_f32 v36, v116, v128, v124
	ds_write2_b32 v220, v28, v29 offset1:65
	v_fma_f32 v28, v117, v129, v125
	ds_write2_b32 v221, v36, v28 offset1:65
	v_fma_f32 v28, v38, v30, v122
	v_fma_f32 v29, v118, v130, v126
	v_fmac_f32_e32 v123, v39, v31
	v_fmac_f32_e32 v127, v119, v131
	ds_write2_b32 v220, v28, v123 offset0:130 offset1:195
	ds_write2_b32 v221, v29, v127 offset0:130 offset1:195
	s_waitcnt vmcnt(2)
	ds_write_b128 v96, v[24:27] offset:41984
	s_mov_b32 s16, 0
	v_mov_b32_e32 v24, v103
	s_waitcnt lgkmcnt(0)
	s_barrier
	ds_read_b32 v200, v218
	ds_read_b32 v208, v219
	ds_read_b32 v201, v218 offset:520
	ds_read_b32 v209, v219 offset:256
	ds_read_b32 v202, v218 offset:1040
	ds_read_b32 v210, v219 offset:512
	ds_read_b32 v203, v218 offset:1560
	ds_read_b32 v211, v219 offset:768
	ds_read_b32 v204, v218 offset:2080
	ds_read_b32 v212, v219 offset:1024
	ds_read_b32 v205, v218 offset:2600
	ds_read_b32 v213, v219 offset:1280
	ds_read_b32 v206, v218 offset:3120
	ds_read_b32 v214, v219 offset:1536
	s_waitcnt lgkmcnt(12)
	v_mfma_f32_32x32x2_f32 v[4:19], v200, v208, v[4:19]
	ds_read_b32 v207, v218 offset:3640
	ds_read_b32 v215, v219 offset:1792
	s_waitcnt lgkmcnt(12)
	v_mfma_f32_32x32x2_f32 v[4:19], v201, v209, v[4:19]
	s_waitcnt lgkmcnt(10)
	v_mfma_f32_32x32x2_f32 v[4:19], v202, v210, v[4:19]
	s_waitcnt lgkmcnt(8)
	v_mfma_f32_32x32x2_f32 v[4:19], v203, v211, v[4:19]
	s_waitcnt lgkmcnt(6)
	v_mfma_f32_32x32x2_f32 v[4:19], v204, v212, v[4:19]
	s_waitcnt lgkmcnt(4)
	v_mfma_f32_32x32x2_f32 v[4:19], v205, v213, v[4:19]
	s_waitcnt lgkmcnt(2)
	v_mfma_f32_32x32x2_f32 v[4:19], v206, v214, v[4:19]
	s_waitcnt lgkmcnt(0)
	v_mfma_f32_32x32x2_f32 v[4:19], v207, v215, v[4:19]
	s_barrier
	global_load_dwordx4 v[28:31], v[92:93], off offset:1280
	global_load_dwordx4 v[24:27], v[70:71], off
	s_waitcnt vmcnt(3)
	v_cvt_f32_f16_sdwa v128, v32 dst_sel:DWORD dst_unused:UNUSED_PAD src0_sel:WORD_1
	v_cvt_f32_f16_e32 v32, v32
	v_cvt_f32_f16_e32 v129, v33
	v_cvt_f32_f16_sdwa v130, v34 dst_sel:DWORD dst_unused:UNUSED_PAD src0_sel:WORD_1
	v_cvt_f32_f16_e32 v133, v34
	ds_read_b128 v[36:39], v43 offset:14592
	ds_read_b128 v[116:119], v43 offset:14608
	ds_read_b128 v[120:123], v43 offset:18688
	ds_read_b128 v[124:127], v43 offset:18704
	v_cvt_f32_f16_sdwa v115, v33 dst_sel:DWORD dst_unused:UNUSED_PAD src0_sel:WORD_1
	v_cvt_f32_f16_sdwa v131, v35 dst_sel:DWORD dst_unused:UNUSED_PAD src0_sel:WORD_1
	v_cvt_f32_f16_e32 v132, v35
	v_sub_f32_e32 v32, v32, v0
	v_sub_f32_e32 v33, v128, v1
	v_sub_f32_e32 v34, v129, v2
	v_pk_mul_f32 v[32:33], v[88:89], v[32:33]
	v_sub_f32_e32 v128, v133, v0
	v_sub_f32_e32 v129, v130, v1
	v_sub_f32_e32 v35, v115, v3
	v_sub_f32_e32 v130, v132, v2
	v_sub_f32_e32 v131, v131, v3
	v_pk_mul_f32 v[128:129], v[88:89], v[128:129]
	s_waitcnt lgkmcnt(1)
	v_fma_f32 v32, v36, v32, v120
	v_fma_f32 v33, v37, v33, v121
	v_pk_mul_f32 v[34:35], v[90:91], v[34:35]
	v_pk_mul_f32 v[130:131], v[90:91], v[130:131]
	s_waitcnt lgkmcnt(0)
	v_fma_f32 v36, v116, v128, v124
	ds_write2_b32 v220, v32, v33 offset1:65
	v_fma_f32 v32, v117, v129, v125
	ds_write2_b32 v221, v36, v32 offset1:65
	v_fma_f32 v32, v38, v34, v122
	v_fma_f32 v33, v118, v130, v126
	v_fmac_f32_e32 v123, v39, v35
	v_fmac_f32_e32 v127, v119, v131
	ds_write2_b32 v220, v32, v123 offset0:130 offset1:195
	ds_write2_b32 v221, v33, v127 offset0:130 offset1:195
	s_waitcnt vmcnt(2)
	ds_write_b128 v96, v[20:23] offset:41984
	s_mov_b32 s16, 0
	v_mov_b32_e32 v20, v103
	s_waitcnt lgkmcnt(0)
	s_barrier
	ds_read_b32 v200, v218
	ds_read_b32 v208, v219
	ds_read_b32 v201, v218 offset:520
	ds_read_b32 v209, v219 offset:256
	ds_read_b32 v202, v218 offset:1040
	ds_read_b32 v210, v219 offset:512
	ds_read_b32 v203, v218 offset:1560
	ds_read_b32 v211, v219 offset:768
	ds_read_b32 v204, v218 offset:2080
	ds_read_b32 v212, v219 offset:1024
	ds_read_b32 v205, v218 offset:2600
	ds_read_b32 v213, v219 offset:1280
	ds_read_b32 v206, v218 offset:3120
	ds_read_b32 v214, v219 offset:1536
	s_waitcnt lgkmcnt(12)
	v_mfma_f32_32x32x2_f32 v[4:19], v200, v208, v[4:19]
	ds_read_b32 v207, v218 offset:3640
	ds_read_b32 v215, v219 offset:1792
	s_waitcnt lgkmcnt(12)
	v_mfma_f32_32x32x2_f32 v[4:19], v201, v209, v[4:19]
	s_waitcnt lgkmcnt(10)
	v_mfma_f32_32x32x2_f32 v[4:19], v202, v210, v[4:19]
	s_waitcnt lgkmcnt(8)
	v_mfma_f32_32x32x2_f32 v[4:19], v203, v211, v[4:19]
	s_waitcnt lgkmcnt(6)
	v_mfma_f32_32x32x2_f32 v[4:19], v204, v212, v[4:19]
	s_waitcnt lgkmcnt(4)
	v_mfma_f32_32x32x2_f32 v[4:19], v205, v213, v[4:19]
	s_waitcnt lgkmcnt(2)
	v_mfma_f32_32x32x2_f32 v[4:19], v206, v214, v[4:19]
	s_waitcnt lgkmcnt(0)
	v_mfma_f32_32x32x2_f32 v[4:19], v207, v215, v[4:19]
	s_barrier
	global_load_dwordx4 v[32:35], v[92:93], off offset:1408
	global_load_dwordx4 v[20:23], v[72:73], off
	s_waitcnt vmcnt(3)
	v_cvt_f32_f16_sdwa v128, v28 dst_sel:DWORD dst_unused:UNUSED_PAD src0_sel:WORD_1
	v_cvt_f32_f16_e32 v28, v28
	v_cvt_f32_f16_e32 v129, v29
	v_cvt_f32_f16_sdwa v130, v30 dst_sel:DWORD dst_unused:UNUSED_PAD src0_sel:WORD_1
	v_cvt_f32_f16_e32 v133, v30
	ds_read_b128 v[36:39], v43 offset:14848
	ds_read_b128 v[116:119], v43 offset:14864
	ds_read_b128 v[120:123], v43 offset:18944
	ds_read_b128 v[124:127], v43 offset:18960
	v_cvt_f32_f16_sdwa v115, v29 dst_sel:DWORD dst_unused:UNUSED_PAD src0_sel:WORD_1
	v_cvt_f32_f16_sdwa v131, v31 dst_sel:DWORD dst_unused:UNUSED_PAD src0_sel:WORD_1
	v_cvt_f32_f16_e32 v132, v31
	v_sub_f32_e32 v28, v28, v0
	v_sub_f32_e32 v29, v128, v1
	v_sub_f32_e32 v30, v129, v2
	v_pk_mul_f32 v[28:29], v[88:89], v[28:29]
	v_sub_f32_e32 v128, v133, v0
	v_sub_f32_e32 v129, v130, v1
	v_sub_f32_e32 v31, v115, v3
	v_sub_f32_e32 v130, v132, v2
	v_sub_f32_e32 v131, v131, v3
	v_pk_mul_f32 v[128:129], v[88:89], v[128:129]
	s_waitcnt lgkmcnt(1)
	v_fma_f32 v28, v36, v28, v120
	v_fma_f32 v29, v37, v29, v121
	v_pk_mul_f32 v[30:31], v[90:91], v[30:31]
	v_pk_mul_f32 v[130:131], v[90:91], v[130:131]
	s_waitcnt lgkmcnt(0)
	v_fma_f32 v36, v116, v128, v124
	ds_write2_b32 v220, v28, v29 offset1:65
	v_fma_f32 v28, v117, v129, v125
	ds_write2_b32 v221, v36, v28 offset1:65
	v_fma_f32 v28, v38, v30, v122
	v_fma_f32 v29, v118, v130, v126
	v_fmac_f32_e32 v123, v39, v31
	v_fmac_f32_e32 v127, v119, v131
	ds_write2_b32 v220, v28, v123 offset0:130 offset1:195
	ds_write2_b32 v221, v29, v127 offset0:130 offset1:195
	s_waitcnt vmcnt(2)
	ds_write_b128 v96, v[24:27] offset:41984
	s_mov_b32 s16, 0
	v_mov_b32_e32 v24, v103
	s_waitcnt lgkmcnt(0)
	s_barrier
	ds_read_b32 v200, v218
	ds_read_b32 v208, v219
	ds_read_b32 v201, v218 offset:520
	ds_read_b32 v209, v219 offset:256
	ds_read_b32 v202, v218 offset:1040
	ds_read_b32 v210, v219 offset:512
	ds_read_b32 v203, v218 offset:1560
	ds_read_b32 v211, v219 offset:768
	ds_read_b32 v204, v218 offset:2080
	ds_read_b32 v212, v219 offset:1024
	ds_read_b32 v205, v218 offset:2600
	ds_read_b32 v213, v219 offset:1280
	ds_read_b32 v206, v218 offset:3120
	ds_read_b32 v214, v219 offset:1536
	s_waitcnt lgkmcnt(12)
	v_mfma_f32_32x32x2_f32 v[4:19], v200, v208, v[4:19]
	ds_read_b32 v207, v218 offset:3640
	ds_read_b32 v215, v219 offset:1792
	s_waitcnt lgkmcnt(12)
	v_mfma_f32_32x32x2_f32 v[4:19], v201, v209, v[4:19]
	s_waitcnt lgkmcnt(10)
	v_mfma_f32_32x32x2_f32 v[4:19], v202, v210, v[4:19]
	s_waitcnt lgkmcnt(8)
	v_mfma_f32_32x32x2_f32 v[4:19], v203, v211, v[4:19]
	s_waitcnt lgkmcnt(6)
	v_mfma_f32_32x32x2_f32 v[4:19], v204, v212, v[4:19]
	s_waitcnt lgkmcnt(4)
	v_mfma_f32_32x32x2_f32 v[4:19], v205, v213, v[4:19]
	s_waitcnt lgkmcnt(2)
	v_mfma_f32_32x32x2_f32 v[4:19], v206, v214, v[4:19]
	s_waitcnt lgkmcnt(0)
	v_mfma_f32_32x32x2_f32 v[4:19], v207, v215, v[4:19]
	s_barrier
	global_load_dwordx4 v[28:31], v[92:93], off offset:1536
	global_load_dwordx4 v[24:27], v[74:75], off
	s_waitcnt vmcnt(3)
	v_cvt_f32_f16_sdwa v128, v32 dst_sel:DWORD dst_unused:UNUSED_PAD src0_sel:WORD_1
	v_cvt_f32_f16_e32 v32, v32
	v_cvt_f32_f16_e32 v129, v33
	v_cvt_f32_f16_sdwa v130, v34 dst_sel:DWORD dst_unused:UNUSED_PAD src0_sel:WORD_1
	v_cvt_f32_f16_e32 v133, v34
	ds_read_b128 v[36:39], v43 offset:15104
	ds_read_b128 v[116:119], v43 offset:15120
	ds_read_b128 v[120:123], v43 offset:19200
	ds_read_b128 v[124:127], v43 offset:19216
	v_cvt_f32_f16_sdwa v115, v33 dst_sel:DWORD dst_unused:UNUSED_PAD src0_sel:WORD_1
	v_cvt_f32_f16_sdwa v131, v35 dst_sel:DWORD dst_unused:UNUSED_PAD src0_sel:WORD_1
	v_cvt_f32_f16_e32 v132, v35
	v_sub_f32_e32 v32, v32, v0
	v_sub_f32_e32 v33, v128, v1
	v_sub_f32_e32 v34, v129, v2
	v_pk_mul_f32 v[32:33], v[88:89], v[32:33]
	v_sub_f32_e32 v128, v133, v0
	v_sub_f32_e32 v129, v130, v1
	v_sub_f32_e32 v35, v115, v3
	v_sub_f32_e32 v130, v132, v2
	v_sub_f32_e32 v131, v131, v3
	v_pk_mul_f32 v[128:129], v[88:89], v[128:129]
	s_waitcnt lgkmcnt(1)
	v_fma_f32 v32, v36, v32, v120
	v_fma_f32 v33, v37, v33, v121
	v_pk_mul_f32 v[34:35], v[90:91], v[34:35]
	v_pk_mul_f32 v[130:131], v[90:91], v[130:131]
	s_waitcnt lgkmcnt(0)
	v_fma_f32 v36, v116, v128, v124
	ds_write2_b32 v220, v32, v33 offset1:65
	v_fma_f32 v32, v117, v129, v125
	ds_write2_b32 v221, v36, v32 offset1:65
	v_fma_f32 v32, v38, v34, v122
	v_fma_f32 v33, v118, v130, v126
	v_fmac_f32_e32 v123, v39, v35
	v_fmac_f32_e32 v127, v119, v131
	ds_write2_b32 v220, v32, v123 offset0:130 offset1:195
	ds_write2_b32 v221, v33, v127 offset0:130 offset1:195
	s_waitcnt vmcnt(2)
	ds_write_b128 v96, v[20:23] offset:41984
	s_mov_b32 s16, 0
	v_mov_b32_e32 v20, v103
	s_waitcnt lgkmcnt(0)
	s_barrier
	ds_read_b32 v200, v218
	ds_read_b32 v208, v219
	ds_read_b32 v201, v218 offset:520
	ds_read_b32 v209, v219 offset:256
	ds_read_b32 v202, v218 offset:1040
	ds_read_b32 v210, v219 offset:512
	ds_read_b32 v203, v218 offset:1560
	ds_read_b32 v211, v219 offset:768
	ds_read_b32 v204, v218 offset:2080
	ds_read_b32 v212, v219 offset:1024
	ds_read_b32 v205, v218 offset:2600
	ds_read_b32 v213, v219 offset:1280
	ds_read_b32 v206, v218 offset:3120
	ds_read_b32 v214, v219 offset:1536
	s_waitcnt lgkmcnt(12)
	v_mfma_f32_32x32x2_f32 v[4:19], v200, v208, v[4:19]
	ds_read_b32 v207, v218 offset:3640
	ds_read_b32 v215, v219 offset:1792
	s_waitcnt lgkmcnt(12)
	v_mfma_f32_32x32x2_f32 v[4:19], v201, v209, v[4:19]
	s_waitcnt lgkmcnt(10)
	v_mfma_f32_32x32x2_f32 v[4:19], v202, v210, v[4:19]
	s_waitcnt lgkmcnt(8)
	v_mfma_f32_32x32x2_f32 v[4:19], v203, v211, v[4:19]
	s_waitcnt lgkmcnt(6)
	v_mfma_f32_32x32x2_f32 v[4:19], v204, v212, v[4:19]
	s_waitcnt lgkmcnt(4)
	v_mfma_f32_32x32x2_f32 v[4:19], v205, v213, v[4:19]
	s_waitcnt lgkmcnt(2)
	v_mfma_f32_32x32x2_f32 v[4:19], v206, v214, v[4:19]
	s_waitcnt lgkmcnt(0)
	v_mfma_f32_32x32x2_f32 v[4:19], v207, v215, v[4:19]
	s_barrier
	global_load_dwordx4 v[32:35], v[92:93], off offset:1664
	global_load_dwordx4 v[20:23], v[76:77], off
	s_waitcnt vmcnt(3)
	v_cvt_f32_f16_sdwa v128, v28 dst_sel:DWORD dst_unused:UNUSED_PAD src0_sel:WORD_1
	v_cvt_f32_f16_e32 v28, v28
	v_cvt_f32_f16_e32 v129, v29
	v_cvt_f32_f16_sdwa v130, v30 dst_sel:DWORD dst_unused:UNUSED_PAD src0_sel:WORD_1
	v_cvt_f32_f16_e32 v133, v30
	ds_read_b128 v[36:39], v43 offset:15360
	ds_read_b128 v[116:119], v43 offset:15376
	ds_read_b128 v[120:123], v43 offset:19456
	ds_read_b128 v[124:127], v43 offset:19472
	v_cvt_f32_f16_sdwa v115, v29 dst_sel:DWORD dst_unused:UNUSED_PAD src0_sel:WORD_1
	v_cvt_f32_f16_sdwa v131, v31 dst_sel:DWORD dst_unused:UNUSED_PAD src0_sel:WORD_1
	v_cvt_f32_f16_e32 v132, v31
	v_sub_f32_e32 v28, v28, v0
	v_sub_f32_e32 v29, v128, v1
	v_sub_f32_e32 v30, v129, v2
	v_pk_mul_f32 v[28:29], v[88:89], v[28:29]
	v_sub_f32_e32 v128, v133, v0
	v_sub_f32_e32 v129, v130, v1
	v_sub_f32_e32 v31, v115, v3
	v_sub_f32_e32 v130, v132, v2
	v_sub_f32_e32 v131, v131, v3
	v_pk_mul_f32 v[128:129], v[88:89], v[128:129]
	s_waitcnt lgkmcnt(1)
	v_fma_f32 v28, v36, v28, v120
	v_fma_f32 v29, v37, v29, v121
	v_pk_mul_f32 v[30:31], v[90:91], v[30:31]
	v_pk_mul_f32 v[130:131], v[90:91], v[130:131]
	s_waitcnt lgkmcnt(0)
	v_fma_f32 v36, v116, v128, v124
	ds_write2_b32 v220, v28, v29 offset1:65
	v_fma_f32 v28, v117, v129, v125
	ds_write2_b32 v221, v36, v28 offset1:65
	v_fma_f32 v28, v38, v30, v122
	v_fma_f32 v29, v118, v130, v126
	v_fmac_f32_e32 v123, v39, v31
	v_fmac_f32_e32 v127, v119, v131
	ds_write2_b32 v220, v28, v123 offset0:130 offset1:195
	ds_write2_b32 v221, v29, v127 offset0:130 offset1:195
	s_waitcnt vmcnt(2)
	ds_write_b128 v96, v[24:27] offset:41984
	s_mov_b32 s16, 0
	v_mov_b32_e32 v24, v103
	s_waitcnt lgkmcnt(0)
	s_barrier
	ds_read_b32 v200, v218
	ds_read_b32 v208, v219
	ds_read_b32 v201, v218 offset:520
	ds_read_b32 v209, v219 offset:256
	ds_read_b32 v202, v218 offset:1040
	ds_read_b32 v210, v219 offset:512
	ds_read_b32 v203, v218 offset:1560
	ds_read_b32 v211, v219 offset:768
	ds_read_b32 v204, v218 offset:2080
	ds_read_b32 v212, v219 offset:1024
	ds_read_b32 v205, v218 offset:2600
	ds_read_b32 v213, v219 offset:1280
	ds_read_b32 v206, v218 offset:3120
	ds_read_b32 v214, v219 offset:1536
	s_waitcnt lgkmcnt(12)
	v_mfma_f32_32x32x2_f32 v[4:19], v200, v208, v[4:19]
	ds_read_b32 v207, v218 offset:3640
	ds_read_b32 v215, v219 offset:1792
	s_waitcnt lgkmcnt(12)
	v_mfma_f32_32x32x2_f32 v[4:19], v201, v209, v[4:19]
	s_waitcnt lgkmcnt(10)
	v_mfma_f32_32x32x2_f32 v[4:19], v202, v210, v[4:19]
	s_waitcnt lgkmcnt(8)
	v_mfma_f32_32x32x2_f32 v[4:19], v203, v211, v[4:19]
	s_waitcnt lgkmcnt(6)
	v_mfma_f32_32x32x2_f32 v[4:19], v204, v212, v[4:19]
	s_waitcnt lgkmcnt(4)
	v_mfma_f32_32x32x2_f32 v[4:19], v205, v213, v[4:19]
	s_waitcnt lgkmcnt(2)
	v_mfma_f32_32x32x2_f32 v[4:19], v206, v214, v[4:19]
	s_waitcnt lgkmcnt(0)
	v_mfma_f32_32x32x2_f32 v[4:19], v207, v215, v[4:19]
	s_barrier
	global_load_dwordx4 v[28:31], v[92:93], off offset:1792
	global_load_dwordx4 v[24:27], v[78:79], off
	s_waitcnt vmcnt(3)
	v_cvt_f32_f16_sdwa v128, v32 dst_sel:DWORD dst_unused:UNUSED_PAD src0_sel:WORD_1
	v_cvt_f32_f16_e32 v32, v32
	v_cvt_f32_f16_e32 v129, v33
	v_cvt_f32_f16_sdwa v130, v34 dst_sel:DWORD dst_unused:UNUSED_PAD src0_sel:WORD_1
	v_cvt_f32_f16_e32 v133, v34
	ds_read_b128 v[36:39], v43 offset:15616
	ds_read_b128 v[116:119], v43 offset:15632
	ds_read_b128 v[120:123], v43 offset:19712
	ds_read_b128 v[124:127], v43 offset:19728
	v_cvt_f32_f16_sdwa v115, v33 dst_sel:DWORD dst_unused:UNUSED_PAD src0_sel:WORD_1
	v_cvt_f32_f16_sdwa v131, v35 dst_sel:DWORD dst_unused:UNUSED_PAD src0_sel:WORD_1
	v_cvt_f32_f16_e32 v132, v35
	v_sub_f32_e32 v32, v32, v0
	v_sub_f32_e32 v33, v128, v1
	v_sub_f32_e32 v34, v129, v2
	v_pk_mul_f32 v[32:33], v[88:89], v[32:33]
	v_sub_f32_e32 v128, v133, v0
	v_sub_f32_e32 v129, v130, v1
	v_sub_f32_e32 v35, v115, v3
	v_sub_f32_e32 v130, v132, v2
	v_sub_f32_e32 v131, v131, v3
	v_pk_mul_f32 v[128:129], v[88:89], v[128:129]
	s_waitcnt lgkmcnt(1)
	v_fma_f32 v32, v36, v32, v120
	v_fma_f32 v33, v37, v33, v121
	v_pk_mul_f32 v[34:35], v[90:91], v[34:35]
	v_pk_mul_f32 v[130:131], v[90:91], v[130:131]
	s_waitcnt lgkmcnt(0)
	v_fma_f32 v36, v116, v128, v124
	ds_write2_b32 v220, v32, v33 offset1:65
	v_fma_f32 v32, v117, v129, v125
	ds_write2_b32 v221, v36, v32 offset1:65
	v_fma_f32 v32, v38, v34, v122
	v_fma_f32 v33, v118, v130, v126
	v_fmac_f32_e32 v123, v39, v35
	v_fmac_f32_e32 v127, v119, v131
	ds_write2_b32 v220, v32, v123 offset0:130 offset1:195
	ds_write2_b32 v221, v33, v127 offset0:130 offset1:195
	s_waitcnt vmcnt(2)
	ds_write_b128 v96, v[20:23] offset:41984
	s_mov_b32 s16, 0
	v_mov_b32_e32 v20, v103
	s_waitcnt lgkmcnt(0)
	s_barrier
	ds_read_b32 v200, v218
	ds_read_b32 v208, v219
	ds_read_b32 v201, v218 offset:520
	ds_read_b32 v209, v219 offset:256
	ds_read_b32 v202, v218 offset:1040
	ds_read_b32 v210, v219 offset:512
	ds_read_b32 v203, v218 offset:1560
	ds_read_b32 v211, v219 offset:768
	ds_read_b32 v204, v218 offset:2080
	ds_read_b32 v212, v219 offset:1024
	ds_read_b32 v205, v218 offset:2600
	ds_read_b32 v213, v219 offset:1280
	ds_read_b32 v206, v218 offset:3120
	ds_read_b32 v214, v219 offset:1536
	s_waitcnt lgkmcnt(12)
	v_mfma_f32_32x32x2_f32 v[4:19], v200, v208, v[4:19]
	ds_read_b32 v207, v218 offset:3640
	ds_read_b32 v215, v219 offset:1792
	s_waitcnt lgkmcnt(12)
	v_mfma_f32_32x32x2_f32 v[4:19], v201, v209, v[4:19]
	s_waitcnt lgkmcnt(10)
	v_mfma_f32_32x32x2_f32 v[4:19], v202, v210, v[4:19]
	s_waitcnt lgkmcnt(8)
	v_mfma_f32_32x32x2_f32 v[4:19], v203, v211, v[4:19]
	s_waitcnt lgkmcnt(6)
	v_mfma_f32_32x32x2_f32 v[4:19], v204, v212, v[4:19]
	s_waitcnt lgkmcnt(4)
	v_mfma_f32_32x32x2_f32 v[4:19], v205, v213, v[4:19]
	s_waitcnt lgkmcnt(2)
	v_mfma_f32_32x32x2_f32 v[4:19], v206, v214, v[4:19]
	s_waitcnt lgkmcnt(0)
	v_mfma_f32_32x32x2_f32 v[4:19], v207, v215, v[4:19]
	s_barrier
	global_load_dwordx4 v[32:35], v[92:93], off offset:1920
	global_load_dwordx4 v[20:23], v[80:81], off
	s_waitcnt vmcnt(3)
	v_cvt_f32_f16_sdwa v93, v28 dst_sel:DWORD dst_unused:UNUSED_PAD src0_sel:WORD_1
	v_cvt_f32_f16_e32 v28, v28
	v_cvt_f32_f16_sdwa v92, v29 dst_sel:DWORD dst_unused:UNUSED_PAD src0_sel:WORD_1
	v_cvt_f32_f16_sdwa v128, v30 dst_sel:DWORD dst_unused:UNUSED_PAD src0_sel:WORD_1
	v_cvt_f32_f16_e32 v131, v30
	ds_read_b128 v[36:39], v43 offset:15872
	ds_read_b128 v[116:119], v43 offset:15888
	ds_read_b128 v[120:123], v43 offset:19968
	ds_read_b128 v[124:127], v43 offset:19984
	v_cvt_f32_f16_e32 v115, v29
	v_cvt_f32_f16_sdwa v129, v31 dst_sel:DWORD dst_unused:UNUSED_PAD src0_sel:WORD_1
	v_cvt_f32_f16_e32 v130, v31
	v_sub_f32_e32 v28, v28, v0
	v_sub_f32_e32 v29, v93, v1
	v_sub_f32_e32 v31, v92, v3
	v_pk_mul_f32 v[28:29], v[88:89], v[28:29]
	v_sub_f32_e32 v92, v131, v0
	v_sub_f32_e32 v93, v128, v1
	v_sub_f32_e32 v30, v115, v2
	v_sub_f32_e32 v128, v130, v2
	v_sub_f32_e32 v129, v129, v3
	v_pk_mul_f32 v[92:93], v[88:89], v[92:93]
	s_waitcnt lgkmcnt(1)
	v_fma_f32 v28, v36, v28, v120
	v_fma_f32 v29, v37, v29, v121
	v_pk_mul_f32 v[30:31], v[90:91], v[30:31]
	v_pk_mul_f32 v[128:129], v[90:91], v[128:129]
	s_waitcnt lgkmcnt(0)
	v_fma_f32 v36, v116, v92, v124
	ds_write2_b32 v220, v28, v29 offset1:65
	v_fma_f32 v28, v117, v93, v125
	ds_write2_b32 v221, v36, v28 offset1:65
	v_fma_f32 v28, v38, v30, v122
	v_fma_f32 v29, v118, v128, v126
	v_fmac_f32_e32 v123, v39, v31
	v_fmac_f32_e32 v127, v119, v129
	ds_write2_b32 v220, v28, v123 offset0:130 offset1:195
	ds_write2_b32 v221, v29, v127 offset0:130 offset1:195
	s_waitcnt vmcnt(2)
	ds_write_b128 v96, v[24:27] offset:41984
	s_mov_b32 s16, 0
	v_mov_b32_e32 v24, v103
	s_waitcnt lgkmcnt(0)
	s_barrier
	ds_read_b32 v200, v218
	ds_read_b32 v208, v219
	ds_read_b32 v201, v218 offset:520
	ds_read_b32 v209, v219 offset:256
	ds_read_b32 v202, v218 offset:1040
	ds_read_b32 v210, v219 offset:512
	ds_read_b32 v203, v218 offset:1560
	ds_read_b32 v211, v219 offset:768
	ds_read_b32 v204, v218 offset:2080
	ds_read_b32 v212, v219 offset:1024
	ds_read_b32 v205, v218 offset:2600
	ds_read_b32 v213, v219 offset:1280
	ds_read_b32 v206, v218 offset:3120
	ds_read_b32 v214, v219 offset:1536
	s_waitcnt lgkmcnt(12)
	v_mfma_f32_32x32x2_f32 v[4:19], v200, v208, v[4:19]
	ds_read_b32 v207, v218 offset:3640
	ds_read_b32 v215, v219 offset:1792
	s_waitcnt lgkmcnt(12)
	v_mfma_f32_32x32x2_f32 v[4:19], v201, v209, v[4:19]
	s_waitcnt lgkmcnt(10)
	v_mfma_f32_32x32x2_f32 v[4:19], v202, v210, v[4:19]
	s_waitcnt lgkmcnt(8)
	v_mfma_f32_32x32x2_f32 v[4:19], v203, v211, v[4:19]
	s_waitcnt lgkmcnt(6)
	v_mfma_f32_32x32x2_f32 v[4:19], v204, v212, v[4:19]
	s_waitcnt lgkmcnt(4)
	v_mfma_f32_32x32x2_f32 v[4:19], v205, v213, v[4:19]
	s_waitcnt lgkmcnt(2)
	v_mfma_f32_32x32x2_f32 v[4:19], v206, v214, v[4:19]
	s_waitcnt lgkmcnt(0)
	v_mfma_f32_32x32x2_f32 v[4:19], v207, v215, v[4:19]
	s_waitcnt vmcnt(1)
	v_cvt_f32_f16_sdwa v93, v32 dst_sel:DWORD dst_unused:UNUSED_PAD src0_sel:WORD_1
	v_cvt_f32_f16_e32 v32, v32
	v_cvt_f32_f16_sdwa v121, v34 dst_sel:DWORD dst_unused:UNUSED_PAD src0_sel:WORD_1
	v_cvt_f32_f16_e32 v123, v34
	s_barrier
	ds_read_b128 v[24:27], v43 offset:16128
	ds_read_b128 v[28:31], v43 offset:16144
	ds_read_b128 v[36:39], v43 offset:20224
	ds_read_b128 v[116:119], v43 offset:20240
	v_cvt_f32_f16_sdwa v92, v33 dst_sel:DWORD dst_unused:UNUSED_PAD src0_sel:WORD_1
	v_cvt_f32_f16_e32 v115, v33
	v_cvt_f32_f16_sdwa v120, v35 dst_sel:DWORD dst_unused:UNUSED_PAD src0_sel:WORD_1
	v_cvt_f32_f16_e32 v122, v35
	v_sub_f32_e32 v32, v32, v0
	v_sub_f32_e32 v33, v93, v1
	v_sub_f32_e32 v0, v123, v0
	v_sub_f32_e32 v1, v121, v1
	v_sub_f32_e32 v34, v115, v2
	v_sub_f32_e32 v35, v92, v3
	v_pk_mul_f32 v[0:1], v[88:89], v[0:1]
	v_pk_mul_f32 v[34:35], v[90:91], v[34:35]
	v_sub_f32_e32 v2, v122, v2
	v_sub_f32_e32 v3, v120, v3
	s_waitcnt lgkmcnt(0)
	v_fma_f32 v0, v28, v0, v116
	v_fma_f32 v1, v29, v1, v117
	v_pk_mul_f32 v[32:33], v[88:89], v[32:33]
	v_pk_mul_f32 v[2:3], v[90:91], v[2:3]
	ds_write2_b32 v221, v0, v1 offset1:65
	v_fma_f32 v0, v26, v34, v38
	v_fmac_f32_e32 v39, v27, v35
	v_fma_f32 v24, v24, v32, v36
	v_fma_f32 v25, v25, v33, v37
	v_fma_f32 v1, v30, v2, v118
	ds_write2_b32 v220, v0, v39 offset0:130 offset1:195
	v_fmac_f32_e32 v119, v31, v3
	s_mov_b32 s16, 0
	v_mov_b32_e32 v0, v103
	ds_write2_b32 v220, v24, v25 offset1:65
	ds_write2_b32 v221, v1, v119 offset0:130 offset1:195
	s_waitcnt vmcnt(0)
	ds_write_b128 v96, v[20:23] offset:41984
	s_waitcnt lgkmcnt(0)
	s_barrier
	ds_read_b32 v200, v218
	ds_read_b32 v208, v219
	ds_read_b32 v201, v218 offset:520
	ds_read_b32 v209, v219 offset:256
	ds_read_b32 v202, v218 offset:1040
	ds_read_b32 v210, v219 offset:512
	ds_read_b32 v203, v218 offset:1560
	ds_read_b32 v211, v219 offset:768
	ds_read_b32 v204, v218 offset:2080
	ds_read_b32 v212, v219 offset:1024
	ds_read_b32 v205, v218 offset:2600
	ds_read_b32 v213, v219 offset:1280
	ds_read_b32 v206, v218 offset:3120
	ds_read_b32 v214, v219 offset:1536
	s_waitcnt lgkmcnt(12)
	v_mfma_f32_32x32x2_f32 v[4:19], v200, v208, v[4:19]
	ds_read_b32 v207, v218 offset:3640
	ds_read_b32 v215, v219 offset:1792
	s_waitcnt lgkmcnt(12)
	v_mfma_f32_32x32x2_f32 v[4:19], v201, v209, v[4:19]
	s_waitcnt lgkmcnt(10)
	v_mfma_f32_32x32x2_f32 v[4:19], v202, v210, v[4:19]
	s_waitcnt lgkmcnt(8)
	v_mfma_f32_32x32x2_f32 v[4:19], v203, v211, v[4:19]
	s_waitcnt lgkmcnt(6)
	v_mfma_f32_32x32x2_f32 v[4:19], v204, v212, v[4:19]
	s_waitcnt lgkmcnt(4)
	v_mfma_f32_32x32x2_f32 v[4:19], v205, v213, v[4:19]
	s_waitcnt lgkmcnt(2)
	v_mfma_f32_32x32x2_f32 v[4:19], v206, v214, v[4:19]
	s_waitcnt lgkmcnt(0)
	v_mfma_f32_32x32x2_f32 v[4:19], v207, v215, v[4:19]
	s_barrier
	s_nop 15
	s_nop 3
	ds_write_b32 v217, v4 offset:58752
	ds_write_b32 v217, v5 offset:58880
	ds_write_b32 v217, v6 offset:59008
	ds_write_b32 v217, v7 offset:59136
	ds_write_b32 v217, v8 offset:59776
	ds_write_b32 v217, v9 offset:59904
	ds_write_b32 v217, v10 offset:60032
	ds_write_b32 v217, v11 offset:60160
	ds_write_b32 v217, v12 offset:60800
	ds_write_b32 v217, v13 offset:60928
	ds_write_b32 v217, v14 offset:61056
	ds_write_b32 v217, v15 offset:61184
	ds_write_b32 v217, v16 offset:61824
	ds_write_b32 v217, v17 offset:61952
	ds_write_b32 v217, v18 offset:62080
	ds_write_b32 v217, v19 offset:62208
	s_waitcnt lgkmcnt(0)
	s_barrier
	global_load_dwordx4 v[0:3], v[50:51], off offset:256
	ds_read_b128 v[4:7], v98 offset:58752
	ds_read_b128 v[8:11], v99 offset:8192
	ds_read_b128 v[12:15], v99 offset:16384
	ds_read_b128 v[16:19], v99 offset:24576
	v_add_u32_e32 v20, 0xc400, v100
	v_add_u32_e32 v21, 0xc408, v100
	s_waitcnt lgkmcnt(2)
	v_pk_add_f32 v[4:5], v[4:5], v[8:9]
	v_pk_add_f32 v[6:7], v[6:7], v[10:11]
	s_waitcnt lgkmcnt(1)
	v_pk_add_f32 v[4:5], v[12:13], v[4:5]
	v_pk_add_f32 v[6:7], v[14:15], v[6:7]
	s_waitcnt lgkmcnt(0)
	v_pk_add_f32 v[4:5], v[16:17], v[4:5]
	v_pk_add_f32 v[6:7], v[18:19], v[6:7]
	s_waitcnt vmcnt(0)
	v_pk_add_f32 v[0:1], v[0:1], v[4:5]
	v_pk_add_f32 v[2:3], v[6:7], v[2:3]
	ds_write2_b32 v20, v0, v1 offset1:1
	ds_write2_b32 v21, v2, v3 offset1:1
	s_waitcnt lgkmcnt(0)
	s_barrier
	s_and_saveexec_b64 s[36:37], s[6:7]
	s_cbranch_execz .LBB0_2418
	v_add_u32_e32 v0, 0xc400, v108
	v_add_u32_e32 v1, 0xc408, v108
	v_add_u32_e32 v2, 0xc410, v108
	v_add_u32_e32 v3, 0xc418, v108
	ds_read2_b32 v[34:35], v0 offset1:1
	ds_read2_b32 v[30:31], v1 offset1:1
	ds_read2_b32 v[22:23], v2 offset1:1
	ds_read2_b32 v[10:11], v3 offset1:1
	s_mov_b32 s16, 0xff61b1e6
	s_waitcnt lgkmcnt(3)
	v_max_f32_e32 v0, v34, v34
	v_max_f32_e32 v0, 0xff61b1e6, v0
	v_cmp_lt_f32_e32 vcc, s16, v34
	v_cmp_gt_f32_e64 s[16:17], v35, v0
	v_add_u32_e32 v2, 0xc420, v108
	ds_read2_b32 v[24:25], v2 offset1:1
	v_cndmask_b32_e64 v0, v0, v35, s[16:17]
	v_cndmask_b32_e64 v1, 0, 1, s[16:17]
	s_waitcnt lgkmcnt(3)
	v_cmp_gt_f32_e64 s[16:17], v30, v0
	v_add_u32_e32 v2, 0xc428, v108
	v_add_u32_e32 v3, 0xc430, v108
	v_cndmask_b32_e64 v0, v0, v30, s[16:17]
	v_cndmask_b32_e64 v1, v1, 2, s[16:17]
	v_cmp_gt_f32_e64 s[16:17], v31, v0
	v_add_u32_e32 v4, 0xc438, v108
	ds_read2_b32 v[32:33], v2 offset1:1
	ds_read2_b32 v[20:21], v3 offset1:1
	ds_read2_b32 v[6:7], v4 offset1:1
	v_cndmask_b32_e64 v0, v0, v31, s[16:17]
	v_cndmask_b32_e64 v1, v1, 3, s[16:17]
	s_waitcnt lgkmcnt(5)
	v_cmp_gt_f32_e64 s[16:17], v22, v0
	v_add_u32_e32 v2, 0xc440, v108
	ds_read2_b32 v[18:19], v2 offset1:1
	v_cndmask_b32_e64 v0, v0, v22, s[16:17]
	v_cndmask_b32_e64 v1, v1, 4, s[16:17]
	v_cmp_gt_f32_e64 s[16:17], v23, v0
	v_add_u32_e32 v2, 0xc448, v108
	v_add_u32_e32 v4, 0xc458, v108
	v_cndmask_b32_e64 v0, v0, v23, s[16:17]
	v_cndmask_b32_e64 v1, v1, 5, s[16:17]
	s_waitcnt lgkmcnt(5)
	v_cmp_gt_f32_e64 s[16:17], v10, v0
	v_add_u32_e32 v3, 0xc450, v108
	ds_read2_b32 v[28:29], v2 offset1:1
	ds_read2_b32 v[12:13], v3 offset1:1
	ds_read2_b32 v[4:5], v4 offset1:1
	v_cndmask_b32_e64 v0, v0, v10, s[16:17]
	v_cndmask_b32_e64 v1, v1, 6, s[16:17]
	v_cmp_gt_f32_e64 s[16:17], v11, v0
	v_add_u32_e32 v2, 0xc460, v108
	ds_read2_b32 v[14:15], v2 offset1:1
	v_cndmask_b32_e64 v0, v0, v11, s[16:17]
	v_cndmask_b32_e64 v1, v1, 7, s[16:17]
	s_waitcnt lgkmcnt(8)
	v_cmp_gt_f32_e64 s[16:17], v24, v0
	v_add_u32_e32 v2, 0xc468, v108
	v_add_u32_e32 v8, 0xc478, v108
	v_cndmask_b32_e64 v0, v0, v24, s[16:17]
	v_cndmask_b32_e64 v1, v1, 8, s[16:17]
	v_cmp_gt_f32_e64 s[16:17], v25, v0
	v_add_u32_e32 v3, 0xc470, v108
	ds_read2_b32 v[26:27], v2 offset1:1
	ds_read2_b32 v[16:17], v3 offset1:1
	ds_read2_b32 v[8:9], v8 offset1:1
	v_cndmask_b32_e64 v0, v0, v25, s[16:17]
	v_cndmask_b32_e64 v1, v1, 9, s[16:17]
	s_waitcnt lgkmcnt(10)
	v_cmp_gt_f32_e64 s[16:17], v32, v0
	s_nop 1
	v_cndmask_b32_e64 v0, v0, v32, s[16:17]
	v_cndmask_b32_e64 v1, v1, 10, s[16:17]
	v_cmp_gt_f32_e64 s[16:17], v33, v0
	s_nop 1
	v_cndmask_b32_e64 v0, v0, v33, s[16:17]
	v_cndmask_b32_e64 v1, v1, 11, s[16:17]
	s_waitcnt lgkmcnt(9)
	v_cmp_gt_f32_e64 s[16:17], v20, v0
	s_nop 1
	v_cndmask_b32_e64 v0, v0, v20, s[16:17]
	v_cndmask_b32_e64 v1, v1, 12, s[16:17]
	v_cmp_gt_f32_e64 s[16:17], v21, v0
	s_nop 1
	v_cndmask_b32_e64 v0, v0, v21, s[16:17]
	v_cndmask_b32_e64 v1, v1, 13, s[16:17]
	s_waitcnt lgkmcnt(8)
	v_cmp_gt_f32_e64 s[16:17], v6, v0
	s_nop 1
	v_cndmask_b32_e64 v0, v0, v6, s[16:17]
	v_cndmask_b32_e64 v1, v1, 14, s[16:17]
	v_cmp_gt_f32_e64 s[16:17], v7, v0
	s_nop 1
	v_cndmask_b32_e64 v0, v0, v7, s[16:17]
	v_cndmask_b32_e64 v1, v1, 15, s[16:17]
	s_waitcnt lgkmcnt(7)
	v_cmp_gt_f32_e64 s[16:17], v18, v0
	s_nop 1
	v_cndmask_b32_e64 v0, v0, v18, s[16:17]
	v_cndmask_b32_e64 v1, v1, 16, s[16:17]
	v_cmp_gt_f32_e64 s[16:17], v19, v0
	s_nop 1
	v_cndmask_b32_e64 v0, v0, v19, s[16:17]
	v_cndmask_b32_e64 v1, v1, 17, s[16:17]
	s_waitcnt lgkmcnt(6)
	v_cmp_gt_f32_e64 s[16:17], v28, v0
	s_nop 1
	v_cndmask_b32_e64 v0, v0, v28, s[16:17]
	v_cndmask_b32_e64 v1, v1, 18, s[16:17]
	v_cmp_gt_f32_e64 s[16:17], v29, v0
	s_nop 1
	v_cndmask_b32_e64 v0, v0, v29, s[16:17]
	v_cndmask_b32_e64 v1, v1, 19, s[16:17]
	s_waitcnt lgkmcnt(5)
	v_cmp_gt_f32_e64 s[16:17], v12, v0
	s_nop 1
	v_cndmask_b32_e64 v0, v0, v12, s[16:17]
	v_cndmask_b32_e64 v1, v1, 20, s[16:17]
	v_cmp_gt_f32_e64 s[16:17], v13, v0
	s_nop 1
	v_cndmask_b32_e64 v0, v0, v13, s[16:17]
	v_cndmask_b32_e64 v1, v1, 21, s[16:17]
	s_waitcnt lgkmcnt(4)
	v_cmp_gt_f32_e64 s[16:17], v4, v0
	s_nop 1
	v_cndmask_b32_e64 v0, v0, v4, s[16:17]
	v_cndmask_b32_e64 v1, v1, 22, s[16:17]
	v_cmp_gt_f32_e64 s[16:17], v5, v0
	s_nop 1
	v_cndmask_b32_e64 v0, v0, v5, s[16:17]
	v_cndmask_b32_e64 v1, v1, 23, s[16:17]
	s_waitcnt lgkmcnt(3)
	v_cmp_gt_f32_e64 s[16:17], v14, v0
	s_nop 1
	v_cndmask_b32_e64 v0, v0, v14, s[16:17]
	v_cndmask_b32_e64 v1, v1, 24, s[16:17]
	v_cmp_gt_f32_e64 s[16:17], v15, v0
	s_nop 1
	v_cndmask_b32_e64 v0, v0, v15, s[16:17]
	v_cndmask_b32_e64 v1, v1, 25, s[16:17]
	s_waitcnt lgkmcnt(2)
	v_cmp_gt_f32_e64 s[16:17], v26, v0
	s_nop 1
	v_cndmask_b32_e64 v0, v0, v26, s[16:17]
	v_cndmask_b32_e64 v1, v1, 26, s[16:17]
	v_cmp_gt_f32_e64 s[16:17], v27, v0
	s_nop 1
	v_cndmask_b32_e64 v0, v0, v27, s[16:17]
	v_cndmask_b32_e64 v1, v1, 27, s[16:17]
	s_waitcnt lgkmcnt(1)
	v_cmp_gt_f32_e64 s[16:17], v16, v0
	s_nop 1
	v_cndmask_b32_e64 v0, v0, v16, s[16:17]
	v_cndmask_b32_e64 v1, v1, 28, s[16:17]
	v_cmp_gt_f32_e64 s[16:17], v17, v0
	s_nop 1
	v_cndmask_b32_e64 v0, v0, v17, s[16:17]
	v_cndmask_b32_e64 v1, v1, 29, s[16:17]
	s_waitcnt lgkmcnt(0)
	v_cmp_gt_f32_e64 s[16:17], v8, v0
	s_nop 1
	v_cndmask_b32_e64 v0, v0, v8, s[16:17]
	v_cndmask_b32_e64 v1, v1, 30, s[16:17]
	v_cmp_gt_f32_e64 s[16:17], v9, v0
	s_nop 1
	v_cndmask_b32_e64 v36, v0, v9, s[16:17]
	v_cndmask_b32_e64 v0, v1, 31, s[16:17]
	v_cmp_ne_u32_e64 s[16:17], 0, v0
	v_lshlrev_b32_e64 v2, v0, 1
	s_and_b64 s[16:17], s[16:17], vcc
	v_cndmask_b32_e64 v1, v112, v34, s[16:17]
	v_and_b32_e32 v3, 2, v2
	v_cmp_eq_u32_e64 s[16:17], 0, v3
	v_cmp_gt_f32_e64 s[18:19], v35, v1
	s_and_b64 s[16:17], s[16:17], s[18:19]
	v_cndmask_b32_e64 v1, v1, v35, s[16:17]
	v_and_b32_e32 v37, 4, v2
	v_cndmask_b32_e64 v3, 0, 1, s[16:17]
	v_cmp_eq_u32_e64 s[16:17], 0, v37
	v_cmp_gt_f32_e64 s[18:19], v30, v1
	s_and_b64 s[16:17], s[16:17], s[18:19]
	v_cndmask_b32_e64 v1, v1, v30, s[16:17]
	v_and_b32_e32 v37, 8, v2
	v_cndmask_b32_e64 v3, v3, 2, s[16:17]
	v_cmp_eq_u32_e64 s[16:17], 0, v37
	v_cmp_gt_f32_e64 s[18:19], v31, v1
	s_and_b64 s[16:17], s[16:17], s[18:19]
	v_cndmask_b32_e64 v1, v1, v31, s[16:17]
	v_and_b32_e32 v37, 16, v2
	v_cndmask_b32_e64 v3, v3, 3, s[16:17]
	v_cmp_eq_u32_e64 s[16:17], 0, v37
	v_cmp_gt_f32_e64 s[18:19], v22, v1
	s_and_b64 s[16:17], s[16:17], s[18:19]
	v_cndmask_b32_e64 v1, v1, v22, s[16:17]
	v_and_b32_e32 v37, 32, v2
	v_cndmask_b32_e64 v3, v3, 4, s[16:17]
	v_cmp_eq_u32_e64 s[16:17], 0, v37
	v_cmp_gt_f32_e64 s[18:19], v23, v1
	s_and_b64 s[16:17], s[16:17], s[18:19]
	v_cndmask_b32_e64 v1, v1, v23, s[16:17]
	v_and_b32_e32 v37, 64, v2
	v_cndmask_b32_e64 v3, v3, 5, s[16:17]
	v_cmp_eq_u32_e64 s[16:17], 0, v37
	v_cmp_gt_f32_e64 s[18:19], v10, v1
	s_and_b64 s[16:17], s[16:17], s[18:19]
	v_cndmask_b32_e64 v1, v1, v10, s[16:17]
	v_and_b32_e32 v37, 0x80, v2
	v_cndmask_b32_e64 v3, v3, 6, s[16:17]
	v_cmp_eq_u32_e64 s[16:17], 0, v37
	v_cmp_gt_f32_e64 s[18:19], v11, v1
	s_and_b64 s[16:17], s[16:17], s[18:19]
	v_cndmask_b32_e64 v1, v1, v11, s[16:17]
	v_and_b32_e32 v37, 0x100, v2
	v_cndmask_b32_e64 v3, v3, 7, s[16:17]
	v_cmp_eq_u32_e64 s[16:17], 0, v37
	v_cmp_gt_f32_e64 s[18:19], v24, v1
	s_and_b64 s[16:17], s[16:17], s[18:19]
	v_cndmask_b32_e64 v1, v1, v24, s[16:17]
	v_and_b32_e32 v37, 0x200, v2
	v_cndmask_b32_e64 v3, v3, 8, s[16:17]
	v_cmp_eq_u32_e64 s[16:17], 0, v37
	v_cmp_gt_f32_e64 s[18:19], v25, v1
	s_and_b64 s[16:17], s[16:17], s[18:19]
	v_cndmask_b32_e64 v1, v1, v25, s[16:17]
	v_and_b32_e32 v37, 0x400, v2
	v_cndmask_b32_e64 v3, v3, 9, s[16:17]
	v_cmp_eq_u32_e64 s[16:17], 0, v37
	v_cmp_gt_f32_e64 s[18:19], v32, v1
	s_and_b64 s[16:17], s[16:17], s[18:19]
	v_cndmask_b32_e64 v1, v1, v32, s[16:17]
	v_and_b32_e32 v37, 0x800, v2
	v_cndmask_b32_e64 v3, v3, 10, s[16:17]
	v_cmp_eq_u32_e64 s[16:17], 0, v37
	v_cmp_gt_f32_e64 s[18:19], v33, v1
	s_and_b64 s[16:17], s[16:17], s[18:19]
	v_cndmask_b32_e64 v1, v1, v33, s[16:17]
	v_and_b32_e32 v37, 0x1000, v2
	v_cndmask_b32_e64 v3, v3, 11, s[16:17]
	v_cmp_eq_u32_e64 s[16:17], 0, v37
	v_cmp_gt_f32_e64 s[18:19], v20, v1
	s_and_b64 s[16:17], s[16:17], s[18:19]
	v_cndmask_b32_e64 v1, v1, v20, s[16:17]
	v_and_b32_e32 v37, 0x2000, v2
	v_cndmask_b32_e64 v3, v3, 12, s[16:17]
	v_cmp_eq_u32_e64 s[16:17], 0, v37
	v_cmp_gt_f32_e64 s[18:19], v21, v1
	s_and_b64 s[16:17], s[16:17], s[18:19]
	v_cndmask_b32_e64 v1, v1, v21, s[16:17]
	v_and_b32_e32 v37, 0x4000, v2
	v_cndmask_b32_e64 v3, v3, 13, s[16:17]
	v_cmp_eq_u32_e64 s[16:17], 0, v37
	v_cmp_gt_f32_e64 s[18:19], v6, v1
	s_and_b64 s[16:17], s[16:17], s[18:19]
	v_cndmask_b32_e64 v1, v1, v6, s[16:17]
	v_and_b32_e32 v37, 0x8000, v2
	v_cndmask_b32_e64 v3, v3, 14, s[16:17]
	v_cmp_eq_u32_e64 s[16:17], 0, v37
	v_cmp_gt_f32_e64 s[18:19], v7, v1
	s_and_b64 s[16:17], s[16:17], s[18:19]
	v_cndmask_b32_e64 v1, v1, v7, s[16:17]
	v_and_b32_e32 v37, 0x10000, v2
	v_cndmask_b32_e64 v3, v3, 15, s[16:17]
	v_cmp_eq_u32_e64 s[16:17], 0, v37
	v_cmp_gt_f32_e64 s[18:19], v18, v1
	s_and_b64 s[16:17], s[16:17], s[18:19]
	v_cndmask_b32_e64 v1, v1, v18, s[16:17]
	v_and_b32_e32 v37, 0x20000, v2
	v_cndmask_b32_e64 v3, v3, 16, s[16:17]
	v_cmp_eq_u32_e64 s[16:17], 0, v37
	v_cmp_gt_f32_e64 s[18:19], v19, v1
	s_and_b64 s[16:17], s[16:17], s[18:19]
	v_cndmask_b32_e64 v1, v1, v19, s[16:17]
	v_and_b32_e32 v37, 0x40000, v2
	v_cndmask_b32_e64 v3, v3, 17, s[16:17]
	v_cmp_eq_u32_e64 s[16:17], 0, v37
	v_cmp_gt_f32_e64 s[18:19], v28, v1
	s_and_b64 s[16:17], s[16:17], s[18:19]
	v_cndmask_b32_e64 v1, v1, v28, s[16:17]
	v_and_b32_e32 v37, 0x80000, v2
	v_cndmask_b32_e64 v3, v3, 18, s[16:17]
	v_cmp_eq_u32_e64 s[16:17], 0, v37
	v_cmp_gt_f32_e64 s[18:19], v29, v1
	s_and_b64 s[16:17], s[16:17], s[18:19]
	v_cndmask_b32_e64 v1, v1, v29, s[16:17]
	v_and_b32_e32 v37, 0x100000, v2
	v_cndmask_b32_e64 v3, v3, 19, s[16:17]
	v_cmp_eq_u32_e64 s[16:17], 0, v37
	v_cmp_gt_f32_e64 s[18:19], v12, v1
	s_and_b64 s[16:17], s[16:17], s[18:19]
	v_cndmask_b32_e64 v1, v1, v12, s[16:17]
	v_and_b32_e32 v37, 0x200000, v2
	v_cndmask_b32_e64 v3, v3, 20, s[16:17]
	v_cmp_eq_u32_e64 s[16:17], 0, v37
	v_cmp_gt_f32_e64 s[18:19], v13, v1
	s_and_b64 s[16:17], s[16:17], s[18:19]
	v_cndmask_b32_e64 v1, v1, v13, s[16:17]
	v_and_b32_e32 v37, 0x400000, v2
	v_cndmask_b32_e64 v3, v3, 21, s[16:17]
	v_cmp_eq_u32_e64 s[16:17], 0, v37
	v_cmp_gt_f32_e64 s[18:19], v4, v1
	s_and_b64 s[16:17], s[16:17], s[18:19]
	v_cndmask_b32_e64 v1, v1, v4, s[16:17]
	v_and_b32_e32 v37, 0x800000, v2
	v_cndmask_b32_e64 v3, v3, 22, s[16:17]
	v_cmp_eq_u32_e64 s[16:17], 0, v37
	v_cmp_gt_f32_e64 s[18:19], v5, v1
	s_and_b64 s[16:17], s[16:17], s[18:19]
	v_cndmask_b32_e64 v1, v1, v5, s[16:17]
	v_and_b32_e32 v37, 0x1000000, v2
	v_cndmask_b32_e64 v3, v3, 23, s[16:17]
	v_cmp_eq_u32_e64 s[16:17], 0, v37
	v_cmp_gt_f32_e64 s[18:19], v14, v1
	s_and_b64 s[16:17], s[16:17], s[18:19]
	v_cndmask_b32_e64 v1, v1, v14, s[16:17]
	v_and_b32_e32 v37, 0x2000000, v2
	v_cndmask_b32_e64 v3, v3, 24, s[16:17]
	v_cmp_eq_u32_e64 s[16:17], 0, v37
	v_cmp_gt_f32_e64 s[18:19], v15, v1
	s_and_b64 s[16:17], s[16:17], s[18:19]
	v_cndmask_b32_e64 v1, v1, v15, s[16:17]
	v_and_b32_e32 v37, 0x4000000, v2
	v_cndmask_b32_e64 v3, v3, 25, s[16:17]
	v_cmp_eq_u32_e64 s[16:17], 0, v37
	v_cmp_gt_f32_e64 s[18:19], v26, v1
	s_and_b64 s[16:17], s[16:17], s[18:19]
	v_cndmask_b32_e64 v1, v1, v26, s[16:17]
	v_and_b32_e32 v37, 0x8000000, v2
	v_cndmask_b32_e64 v3, v3, 26, s[16:17]
	v_cmp_eq_u32_e64 s[16:17], 0, v37
	v_cmp_gt_f32_e64 s[18:19], v27, v1
	s_and_b64 s[16:17], s[16:17], s[18:19]
	v_cndmask_b32_e64 v1, v1, v27, s[16:17]
	v_and_b32_e32 v37, 0x10000000, v2
	v_cndmask_b32_e64 v3, v3, 27, s[16:17]
	v_cmp_eq_u32_e64 s[16:17], 0, v37
	v_cmp_gt_f32_e64 s[18:19], v16, v1
	s_and_b64 s[16:17], s[16:17], s[18:19]
	v_cndmask_b32_e64 v1, v1, v16, s[16:17]
	v_and_b32_e32 v37, 0x20000000, v2
	v_cndmask_b32_e64 v3, v3, 28, s[16:17]
	v_cmp_eq_u32_e64 s[16:17], 0, v37
	v_cmp_gt_f32_e64 s[18:19], v17, v1
	s_and_b64 s[16:17], s[16:17], s[18:19]
	v_cndmask_b32_e64 v1, v1, v17, s[16:17]
	v_and_b32_e32 v37, 2.0, v2
	v_cndmask_b32_e64 v3, v3, 29, s[16:17]
	v_cmp_eq_u32_e64 s[16:17], 0, v37
	v_cmp_gt_f32_e64 s[18:19], v8, v1
	s_and_b64 s[16:17], s[16:17], s[18:19]
	v_cndmask_b32_e64 v1, v1, v8, s[16:17]
	v_cndmask_b32_e64 v3, v3, 30, s[16:17]
	v_cmp_ne_u32_e64 s[16:17], 31, v0
	v_cmp_gt_f32_e64 s[18:19], v9, v1
	s_and_b64 s[16:17], s[16:17], s[18:19]
	v_cndmask_b32_e64 v37, v1, v9, s[16:17]
	v_cndmask_b32_e64 v1, v3, 31, s[16:17]
	v_lshl_or_b32 v3, 1, v1, v2
	v_and_b32_e32 v2, 1, v3
	v_cmp_eq_u32_e64 s[16:17], 0, v2
	s_and_b64 s[16:17], s[16:17], vcc
	v_and_b32_e32 v38, 2, v3
	v_cndmask_b32_e64 v2, v112, v34, s[16:17]
	v_cmp_eq_u32_e64 s[16:17], 0, v38
	v_cmp_gt_f32_e64 s[18:19], v35, v2
	s_and_b64 s[16:17], s[16:17], s[18:19]
	v_cndmask_b32_e64 v2, v2, v35, s[16:17]
	v_and_b32_e32 v39, 4, v3
	v_cndmask_b32_e64 v38, 0, 1, s[16:17]
	v_cmp_eq_u32_e64 s[16:17], 0, v39
	v_cmp_gt_f32_e64 s[18:19], v30, v2
	s_and_b64 s[16:17], s[16:17], s[18:19]
	v_cndmask_b32_e64 v2, v2, v30, s[16:17]
	v_and_b32_e32 v39, 8, v3
	v_cndmask_b32_e64 v38, v38, 2, s[16:17]
	v_cmp_eq_u32_e64 s[16:17], 0, v39
	v_cmp_gt_f32_e64 s[18:19], v31, v2
	s_and_b64 s[16:17], s[16:17], s[18:19]
	v_cndmask_b32_e64 v2, v2, v31, s[16:17]
	v_and_b32_e32 v39, 16, v3
	v_cndmask_b32_e64 v38, v38, 3, s[16:17]
	v_cmp_eq_u32_e64 s[16:17], 0, v39
	v_cmp_gt_f32_e64 s[18:19], v22, v2
	s_and_b64 s[16:17], s[16:17], s[18:19]
	v_cndmask_b32_e64 v2, v2, v22, s[16:17]
	v_and_b32_e32 v39, 32, v3
	v_cndmask_b32_e64 v38, v38, 4, s[16:17]
	v_cmp_eq_u32_e64 s[16:17], 0, v39
	v_cmp_gt_f32_e64 s[18:19], v23, v2
	s_and_b64 s[16:17], s[16:17], s[18:19]
	v_cndmask_b32_e64 v2, v2, v23, s[16:17]
	v_and_b32_e32 v39, 64, v3
	v_cndmask_b32_e64 v38, v38, 5, s[16:17]
	v_cmp_eq_u32_e64 s[16:17], 0, v39
	v_cmp_gt_f32_e64 s[18:19], v10, v2
	s_and_b64 s[16:17], s[16:17], s[18:19]
	v_cndmask_b32_e64 v2, v2, v10, s[16:17]
	v_and_b32_e32 v39, 0x80, v3
	v_cndmask_b32_e64 v38, v38, 6, s[16:17]
	v_cmp_eq_u32_e64 s[16:17], 0, v39
	v_cmp_gt_f32_e64 s[18:19], v11, v2
	s_and_b64 s[16:17], s[16:17], s[18:19]
	v_cndmask_b32_e64 v2, v2, v11, s[16:17]
	v_and_b32_e32 v39, 0x100, v3
	v_cndmask_b32_e64 v38, v38, 7, s[16:17]
	v_cmp_eq_u32_e64 s[16:17], 0, v39
	v_cmp_gt_f32_e64 s[18:19], v24, v2
	s_and_b64 s[16:17], s[16:17], s[18:19]
	v_cndmask_b32_e64 v2, v2, v24, s[16:17]
	v_and_b32_e32 v39, 0x200, v3
	v_cndmask_b32_e64 v38, v38, 8, s[16:17]
	v_cmp_eq_u32_e64 s[16:17], 0, v39
	v_cmp_gt_f32_e64 s[18:19], v25, v2
	s_and_b64 s[16:17], s[16:17], s[18:19]
	v_cndmask_b32_e64 v2, v2, v25, s[16:17]
	v_and_b32_e32 v39, 0x400, v3
	v_cndmask_b32_e64 v38, v38, 9, s[16:17]
	v_cmp_eq_u32_e64 s[16:17], 0, v39
	v_cmp_gt_f32_e64 s[18:19], v32, v2
	s_and_b64 s[16:17], s[16:17], s[18:19]
	v_cndmask_b32_e64 v2, v2, v32, s[16:17]
	v_and_b32_e32 v39, 0x800, v3
	v_cndmask_b32_e64 v38, v38, 10, s[16:17]
	v_cmp_eq_u32_e64 s[16:17], 0, v39
	v_cmp_gt_f32_e64 s[18:19], v33, v2
	s_and_b64 s[16:17], s[16:17], s[18:19]
	v_cndmask_b32_e64 v2, v2, v33, s[16:17]
	v_and_b32_e32 v39, 0x1000, v3
	v_cndmask_b32_e64 v38, v38, 11, s[16:17]
	v_cmp_eq_u32_e64 s[16:17], 0, v39
	v_cmp_gt_f32_e64 s[18:19], v20, v2
	s_and_b64 s[16:17], s[16:17], s[18:19]
	v_cndmask_b32_e64 v2, v2, v20, s[16:17]
	v_and_b32_e32 v39, 0x2000, v3
	v_cndmask_b32_e64 v38, v38, 12, s[16:17]
	v_cmp_eq_u32_e64 s[16:17], 0, v39
	v_cmp_gt_f32_e64 s[18:19], v21, v2
	s_and_b64 s[16:17], s[16:17], s[18:19]
	v_cndmask_b32_e64 v2, v2, v21, s[16:17]
	v_and_b32_e32 v39, 0x4000, v3
	v_cndmask_b32_e64 v38, v38, 13, s[16:17]
	v_cmp_eq_u32_e64 s[16:17], 0, v39
	v_cmp_gt_f32_e64 s[18:19], v6, v2
	s_and_b64 s[16:17], s[16:17], s[18:19]
	v_cndmask_b32_e64 v2, v2, v6, s[16:17]
	v_and_b32_e32 v39, 0x8000, v3
	v_cndmask_b32_e64 v38, v38, 14, s[16:17]
	v_cmp_eq_u32_e64 s[16:17], 0, v39
	v_cmp_gt_f32_e64 s[18:19], v7, v2
	s_and_b64 s[16:17], s[16:17], s[18:19]
	v_cndmask_b32_e64 v2, v2, v7, s[16:17]
	v_and_b32_e32 v39, 0x10000, v3
	v_cndmask_b32_e64 v38, v38, 15, s[16:17]
	v_cmp_eq_u32_e64 s[16:17], 0, v39
	v_cmp_gt_f32_e64 s[18:19], v18, v2
	s_and_b64 s[16:17], s[16:17], s[18:19]
	v_cndmask_b32_e64 v2, v2, v18, s[16:17]
	v_and_b32_e32 v39, 0x20000, v3
	v_cndmask_b32_e64 v38, v38, 16, s[16:17]
	v_cmp_eq_u32_e64 s[16:17], 0, v39
	v_cmp_gt_f32_e64 s[18:19], v19, v2
	s_and_b64 s[16:17], s[16:17], s[18:19]
	v_cndmask_b32_e64 v2, v2, v19, s[16:17]
	v_and_b32_e32 v39, 0x40000, v3
	v_cndmask_b32_e64 v38, v38, 17, s[16:17]
	v_cmp_eq_u32_e64 s[16:17], 0, v39
	v_cmp_gt_f32_e64 s[18:19], v28, v2
	s_and_b64 s[16:17], s[16:17], s[18:19]
	v_cndmask_b32_e64 v2, v2, v28, s[16:17]
	v_and_b32_e32 v39, 0x80000, v3
	v_cndmask_b32_e64 v38, v38, 18, s[16:17]
	v_cmp_eq_u32_e64 s[16:17], 0, v39
	v_cmp_gt_f32_e64 s[18:19], v29, v2
	s_and_b64 s[16:17], s[16:17], s[18:19]
	v_cndmask_b32_e64 v2, v2, v29, s[16:17]
	v_and_b32_e32 v39, 0x100000, v3
	v_cndmask_b32_e64 v38, v38, 19, s[16:17]
	v_cmp_eq_u32_e64 s[16:17], 0, v39
	v_cmp_gt_f32_e64 s[18:19], v12, v2
	s_and_b64 s[16:17], s[16:17], s[18:19]
	v_cndmask_b32_e64 v2, v2, v12, s[16:17]
	v_and_b32_e32 v39, 0x200000, v3
	v_cndmask_b32_e64 v38, v38, 20, s[16:17]
	v_cmp_eq_u32_e64 s[16:17], 0, v39
	v_cmp_gt_f32_e64 s[18:19], v13, v2
	s_and_b64 s[16:17], s[16:17], s[18:19]
	v_cndmask_b32_e64 v2, v2, v13, s[16:17]
	v_and_b32_e32 v39, 0x400000, v3
	v_cndmask_b32_e64 v38, v38, 21, s[16:17]
	v_cmp_eq_u32_e64 s[16:17], 0, v39
	v_cmp_gt_f32_e64 s[18:19], v4, v2
	s_and_b64 s[16:17], s[16:17], s[18:19]
	v_cndmask_b32_e64 v2, v2, v4, s[16:17]
	v_and_b32_e32 v39, 0x800000, v3
	v_cndmask_b32_e64 v38, v38, 22, s[16:17]
	v_cmp_eq_u32_e64 s[16:17], 0, v39
	v_cmp_gt_f32_e64 s[18:19], v5, v2
	s_and_b64 s[16:17], s[16:17], s[18:19]
	v_cndmask_b32_e64 v2, v2, v5, s[16:17]
	v_and_b32_e32 v39, 0x1000000, v3
	v_cndmask_b32_e64 v38, v38, 23, s[16:17]
	v_cmp_eq_u32_e64 s[16:17], 0, v39
	v_cmp_gt_f32_e64 s[18:19], v14, v2
	s_and_b64 s[16:17], s[16:17], s[18:19]
	v_cndmask_b32_e64 v2, v2, v14, s[16:17]
	v_and_b32_e32 v39, 0x2000000, v3
	v_cndmask_b32_e64 v38, v38, 24, s[16:17]
	v_cmp_eq_u32_e64 s[16:17], 0, v39
	v_cmp_gt_f32_e64 s[18:19], v15, v2
	s_and_b64 s[16:17], s[16:17], s[18:19]
	v_cndmask_b32_e64 v2, v2, v15, s[16:17]
	v_and_b32_e32 v39, 0x4000000, v3
	v_cndmask_b32_e64 v38, v38, 25, s[16:17]
	v_cmp_eq_u32_e64 s[16:17], 0, v39
	v_cmp_gt_f32_e64 s[18:19], v26, v2
	s_and_b64 s[16:17], s[16:17], s[18:19]
	v_cndmask_b32_e64 v2, v2, v26, s[16:17]
	v_and_b32_e32 v39, 0x8000000, v3
	v_cndmask_b32_e64 v38, v38, 26, s[16:17]
	v_cmp_eq_u32_e64 s[16:17], 0, v39
	v_cmp_gt_f32_e64 s[18:19], v27, v2
	s_and_b64 s[16:17], s[16:17], s[18:19]
	v_cndmask_b32_e64 v2, v2, v27, s[16:17]
	v_and_b32_e32 v39, 0x10000000, v3
	v_cndmask_b32_e64 v38, v38, 27, s[16:17]
	v_cmp_eq_u32_e64 s[16:17], 0, v39
	v_cmp_gt_f32_e64 s[18:19], v16, v2
	s_and_b64 s[16:17], s[16:17], s[18:19]
	v_cndmask_b32_e64 v2, v2, v16, s[16:17]
	v_and_b32_e32 v39, 0x20000000, v3
	v_cndmask_b32_e64 v38, v38, 28, s[16:17]
	v_cmp_eq_u32_e64 s[16:17], 0, v39
	v_cmp_gt_f32_e64 s[18:19], v17, v2
	s_and_b64 s[16:17], s[16:17], s[18:19]
	v_cndmask_b32_e64 v2, v2, v17, s[16:17]
	v_and_b32_e32 v39, 2.0, v3
	v_cndmask_b32_e64 v38, v38, 29, s[16:17]
	v_cmp_eq_u32_e64 s[16:17], 0, v39
	v_cmp_gt_f32_e64 s[18:19], v8, v2
	s_and_b64 s[16:17], s[16:17], s[18:19]
	v_cndmask_b32_e64 v2, v2, v8, s[16:17]
	v_cndmask_b32_e64 v38, v38, 30, s[16:17]
	v_cmp_lt_i32_e64 s[16:17], -1, v3
	v_cmp_gt_f32_e64 s[18:19], v9, v2
	s_and_b64 s[16:17], s[16:17], s[18:19]
	v_cndmask_b32_e64 v39, v2, v9, s[16:17]
	v_cndmask_b32_e64 v2, v38, 31, s[16:17]
	v_lshlrev_b32_e64 v38, v2, 1
	v_bitop3_b32 v89, v38, 1, v3 bitop3:0xc8
	v_cmp_eq_u32_e64 s[16:17], 0, v89
	s_and_b64 vcc, s[16:17], vcc
	v_cndmask_b32_e32 v34, v112, v34, vcc
	v_bitop3_b32 v89, v38, 2, v3 bitop3:0xc8
	v_cmp_eq_u32_e32 vcc, 0, v89
	v_cmp_gt_f32_e64 s[16:17], v35, v34
	s_and_b64 vcc, vcc, s[16:17]
	v_cndmask_b32_e32 v34, v34, v35, vcc
	v_bitop3_b32 v89, v38, 4, v3 bitop3:0xc8
	v_cndmask_b32_e64 v35, 0, 1, vcc
	v_cmp_eq_u32_e32 vcc, 0, v89
	v_cmp_gt_f32_e64 s[16:17], v30, v34
	s_and_b64 vcc, vcc, s[16:17]
	v_cndmask_b32_e32 v30, v34, v30, vcc
	v_cndmask_b32_e64 v34, v35, 2, vcc
	v_bitop3_b32 v35, v38, 8, v3 bitop3:0xc8
	v_cmp_eq_u32_e32 vcc, 0, v35
	v_cmp_gt_f32_e64 s[16:17], v31, v30
	s_and_b64 vcc, vcc, s[16:17]
	v_cndmask_b32_e32 v30, v30, v31, vcc
	v_cndmask_b32_e64 v31, v34, 3, vcc
	v_bitop3_b32 v34, v38, 16, v3 bitop3:0xc8
	v_cmp_eq_u32_e32 vcc, 0, v34
	v_cmp_gt_f32_e64 s[16:17], v22, v30
	s_and_b64 vcc, vcc, s[16:17]
	v_cndmask_b32_e32 v22, v30, v22, vcc
	v_cndmask_b32_e64 v30, v31, 4, vcc
	v_bitop3_b32 v31, v38, 32, v3 bitop3:0xc8
	v_cmp_eq_u32_e32 vcc, 0, v31
	v_cmp_gt_f32_e64 s[16:17], v23, v22
	s_and_b64 vcc, vcc, s[16:17]
	v_cndmask_b32_e32 v22, v22, v23, vcc
	v_cndmask_b32_e64 v23, v30, 5, vcc
	v_bitop3_b32 v30, v38, 64, v3 bitop3:0xc8
	v_cmp_eq_u32_e32 vcc, 0, v30
	v_cmp_gt_f32_e64 s[16:17], v10, v22
	s_and_b64 vcc, vcc, s[16:17]
	s_movk_i32 s16, 0x80
	v_cndmask_b32_e32 v10, v22, v10, vcc
	v_cndmask_b32_e64 v22, v23, 6, vcc
	v_bitop3_b32 v23, v38, s16, v3 bitop3:0xc8
	v_cmp_eq_u32_e32 vcc, 0, v23
	v_cmp_gt_f32_e64 s[16:17], v11, v10
	s_and_b64 vcc, vcc, s[16:17]
	s_movk_i32 s16, 0x100
	v_cndmask_b32_e32 v10, v10, v11, vcc
	v_cndmask_b32_e64 v11, v22, 7, vcc
	v_bitop3_b32 v22, v38, s16, v3 bitop3:0xc8
	v_cmp_eq_u32_e32 vcc, 0, v22
	v_cmp_gt_f32_e64 s[16:17], v24, v10
	s_and_b64 vcc, vcc, s[16:17]
	s_movk_i32 s16, 0x200
	v_cndmask_b32_e32 v10, v10, v24, vcc
	v_bitop3_b32 v22, v38, s16, v3 bitop3:0xc8
	v_cndmask_b32_e64 v11, v11, 8, vcc
	v_cmp_eq_u32_e32 vcc, 0, v22
	v_cmp_gt_f32_e64 s[16:17], v25, v10
	s_and_b64 vcc, vcc, s[16:17]
	v_cndmask_b32_e32 v10, v10, v25, vcc
	v_bitop3_b32 v22, v38, s52, v3 bitop3:0xc8
	v_cndmask_b32_e64 v11, v11, 9, vcc
	v_cmp_eq_u32_e32 vcc, 0, v22
	v_cmp_gt_f32_e64 s[16:17], v32, v10
	s_and_b64 vcc, vcc, s[16:17]
	s_movk_i32 s16, 0x800
	v_cndmask_b32_e32 v10, v10, v32, vcc
	v_bitop3_b32 v22, v38, s16, v3 bitop3:0xc8
	v_cndmask_b32_e64 v11, v11, 10, vcc
	v_cmp_eq_u32_e32 vcc, 0, v22
	v_cmp_gt_f32_e64 s[16:17], v33, v10
	s_and_b64 vcc, vcc, s[16:17]
	s_movk_i32 s16, 0x1000
	v_cndmask_b32_e32 v10, v10, v33, vcc
	v_bitop3_b32 v22, v38, s16, v3 bitop3:0xc8
	v_cndmask_b32_e64 v11, v11, 11, vcc
	v_cmp_eq_u32_e32 vcc, 0, v22
	v_cmp_gt_f32_e64 s[16:17], v20, v10
	s_and_b64 vcc, vcc, s[16:17]
	s_movk_i32 s16, 0x2000
	v_cndmask_b32_e32 v10, v10, v20, vcc
	v_bitop3_b32 v20, v38, s16, v3 bitop3:0xc8
	v_cndmask_b32_e64 v11, v11, 12, vcc
	v_cmp_eq_u32_e32 vcc, 0, v20
	v_cmp_gt_f32_e64 s[16:17], v21, v10
	s_and_b64 vcc, vcc, s[16:17]
	s_movk_i32 s16, 0x4000
	v_cndmask_b32_e32 v10, v10, v21, vcc
	v_bitop3_b32 v20, v38, s16, v3 bitop3:0xc8
	v_cndmask_b32_e64 v11, v11, 13, vcc
	v_cmp_eq_u32_e32 vcc, 0, v20
	v_cmp_gt_f32_e64 s[16:17], v6, v10
	s_and_b64 vcc, vcc, s[16:17]
	s_mov_b32 s16, 0x8000
	v_cndmask_b32_e32 v6, v10, v6, vcc
	v_cndmask_b32_e64 v10, v11, 14, vcc
	v_bitop3_b32 v11, v38, s16, v3 bitop3:0xc8
	v_cmp_eq_u32_e32 vcc, 0, v11
	v_cmp_gt_f32_e64 s[16:17], v7, v6
	s_and_b64 vcc, vcc, s[16:17]
	s_mov_b32 s16, 0x10000
	v_cndmask_b32_e32 v6, v6, v7, vcc
	v_cndmask_b32_e64 v7, v10, 15, vcc
	v_bitop3_b32 v10, v38, s16, v3 bitop3:0xc8
	v_cmp_eq_u32_e32 vcc, 0, v10
	v_cmp_gt_f32_e64 s[16:17], v18, v6
	s_and_b64 vcc, vcc, s[16:17]
	s_mov_b32 s16, 0x20000
	v_cndmask_b32_e32 v6, v6, v18, vcc
	v_bitop3_b32 v10, v38, s16, v3 bitop3:0xc8
	v_cndmask_b32_e64 v7, v7, 16, vcc
	v_cmp_eq_u32_e32 vcc, 0, v10
	v_cmp_gt_f32_e64 s[16:17], v19, v6
	s_and_b64 vcc, vcc, s[16:17]
	s_mov_b32 s16, 0x40000
	v_cndmask_b32_e32 v6, v6, v19, vcc
	v_bitop3_b32 v10, v38, s16, v3 bitop3:0xc8
	v_cndmask_b32_e64 v7, v7, 17, vcc
	v_cmp_eq_u32_e32 vcc, 0, v10
	v_cmp_gt_f32_e64 s[16:17], v28, v6
	s_and_b64 vcc, vcc, s[16:17]
	s_mov_b32 s16, 0x80000
	v_cndmask_b32_e32 v6, v6, v28, vcc
	v_bitop3_b32 v10, v38, s16, v3 bitop3:0xc8
	v_cndmask_b32_e64 v7, v7, 18, vcc
	v_cmp_eq_u32_e32 vcc, 0, v10
	v_cmp_gt_f32_e64 s[16:17], v29, v6
	s_and_b64 vcc, vcc, s[16:17]
	s_mov_b32 s16, 0x100000
	v_cndmask_b32_e32 v6, v6, v29, vcc
	v_bitop3_b32 v10, v38, s16, v3 bitop3:0xc8
	v_cndmask_b32_e64 v7, v7, 19, vcc
	v_cmp_eq_u32_e32 vcc, 0, v10
	v_cmp_gt_f32_e64 s[16:17], v12, v6
	s_and_b64 vcc, vcc, s[16:17]
	s_mov_b32 s16, 0x200000
	v_cndmask_b32_e32 v6, v6, v12, vcc
	v_bitop3_b32 v10, v38, s16, v3 bitop3:0xc8
	v_cndmask_b32_e64 v7, v7, 20, vcc
	v_cmp_eq_u32_e32 vcc, 0, v10
	v_cmp_gt_f32_e64 s[16:17], v13, v6
	s_and_b64 vcc, vcc, s[16:17]
	s_mov_b32 s16, 0x400000
	v_cndmask_b32_e32 v6, v6, v13, vcc
	v_bitop3_b32 v10, v38, s16, v3 bitop3:0xc8
	v_cndmask_b32_e64 v7, v7, 21, vcc
	v_cmp_eq_u32_e32 vcc, 0, v10
	v_cmp_gt_f32_e64 s[16:17], v4, v6
	s_and_b64 vcc, vcc, s[16:17]
	s_mov_b32 s16, 0x800000
	v_cndmask_b32_e32 v4, v6, v4, vcc
	v_cndmask_b32_e64 v6, v7, 22, vcc
	v_bitop3_b32 v7, v38, s16, v3 bitop3:0xc8
	v_cmp_eq_u32_e32 vcc, 0, v7
	v_cmp_gt_f32_e64 s[16:17], v5, v4
	s_and_b64 vcc, vcc, s[16:17]
	s_mov_b32 s16, 0x1000000
	v_cndmask_b32_e32 v4, v4, v5, vcc
	v_cndmask_b32_e64 v5, v6, 23, vcc
	v_bitop3_b32 v6, v38, s16, v3 bitop3:0xc8
	v_cmp_eq_u32_e32 vcc, 0, v6
	v_cmp_gt_f32_e64 s[16:17], v14, v4
	s_and_b64 vcc, vcc, s[16:17]
	v_cndmask_b32_e32 v4, v4, v14, vcc
	v_bitop3_b32 v6, v38, s61, v3 bitop3:0xc8
	v_cndmask_b32_e64 v5, v5, 24, vcc
	v_cmp_eq_u32_e32 vcc, 0, v6
	v_cmp_gt_f32_e64 s[16:17], v15, v4
	s_and_b64 vcc, vcc, s[16:17]
	v_cndmask_b32_e32 v4, v4, v15, vcc
	v_bitop3_b32 v6, v38, s62, v3 bitop3:0xc8
	v_cndmask_b32_e64 v5, v5, 25, vcc
	v_cmp_eq_u32_e32 vcc, 0, v6
	v_cmp_gt_f32_e64 s[16:17], v26, v4
	s_and_b64 vcc, vcc, s[16:17]
	v_cndmask_b32_e32 v4, v4, v26, vcc
	v_bitop3_b32 v6, v38, s63, v3 bitop3:0xc8
	v_cndmask_b32_e64 v5, v5, 26, vcc
	v_cmp_eq_u32_e32 vcc, 0, v6
	v_cmp_gt_f32_e64 s[16:17], v27, v4
	s_and_b64 vcc, vcc, s[16:17]
	v_cndmask_b32_e32 v4, v4, v27, vcc
	v_bitop3_b32 v6, v38, s64, v3 bitop3:0xc8
	v_cndmask_b32_e64 v5, v5, 27, vcc
	v_cmp_eq_u32_e32 vcc, 0, v6
	v_cmp_gt_f32_e64 s[16:17], v16, v4
	s_and_b64 vcc, vcc, s[16:17]
	v_cndmask_b32_e32 v4, v4, v16, vcc
	v_bitop3_b32 v6, v38, s65, v3 bitop3:0xc8
	v_cndmask_b32_e64 v5, v5, 28, vcc
	v_cmp_eq_u32_e32 vcc, 0, v6
	v_cmp_gt_f32_e64 s[16:17], v17, v4
	s_and_b64 vcc, vcc, s[16:17]
	v_or_b32_e32 v88, v38, v3
	v_cndmask_b32_e32 v4, v4, v17, vcc
	v_bitop3_b32 v3, v38, 2.0, v3 bitop3:0xc8
	v_cndmask_b32_e64 v5, v5, 29, vcc
	v_cmp_eq_u32_e32 vcc, 0, v3
	v_cmp_gt_f32_e64 s[16:17], v8, v4
	s_and_b64 vcc, vcc, s[16:17]
	v_cndmask_b32_e32 v3, v4, v8, vcc
	v_cndmask_b32_e64 v4, v5, 30, vcc
	v_cmp_lt_i32_e32 vcc, -1, v88
	v_cmp_gt_f32_e64 s[16:17], v9, v3
	s_and_b64 vcc, vcc, s[16:17]
	v_cndmask_b32_e32 v5, v3, v9, vcc
	v_cndmask_b32_e64 v3, v4, 31, vcc
	v_sub_f32_e32 v4, v36, v36
	v_mul_f32_e32 v4, 0x3fb8aa3b, v4
	v_exp_f32_e32 v10, v4
	v_sub_f32_e32 v4, v37, v36
	v_mul_f32_e32 v4, 0x3fb8aa3b, v4
	v_exp_f32_e32 v11, v4
	v_sub_f32_e32 v4, v39, v36
	v_mul_f32_e32 v4, 0x3fb8aa3b, v4
	v_exp_f32_e32 v12, v4
	v_sub_f32_e32 v4, v5, v36
	v_mul_f32_e32 v4, 0x3fb8aa3b, v4
	v_exp_f32_e32 v13, v4
	v_add_f32_e32 v4, 0, v10
	v_add_f32_e32 v4, v4, v11
	v_add_f32_e32 v4, v4, v12
	v_add_f32_e32 v14, v4, v13
	v_div_scale_f32 v15, s[16:17], v14, v14, v10
	v_rcp_f32_e32 v16, v15
	v_lshl_add_u32 v4, s66, 8, v94
	v_ashrrev_i32_e32 v5, 31, v4
	v_lshlrev_b64 v[6:7], 2, v[4:5]
	v_fma_f32 v5, -v15, v16, 1.0
	v_fmac_f32_e32 v16, v5, v16
	v_div_scale_f32 v5, vcc, v10, v14, v10
	v_mul_f32_e32 v17, v5, v16
	v_fma_f32 v18, -v15, v17, v5
	v_fmac_f32_e32 v17, v18, v16
	v_fma_f32 v5, -v15, v17, v5
	v_div_fmas_f32 v5, v5, v16, v17
	v_div_fixup_f32 v5, v5, v14, v10
	v_div_scale_f32 v10, s[16:17], v14, v14, v11
	v_rcp_f32_e32 v15, v10
	v_lshl_add_u64 v[8:9], s[20:21], 0, v[6:7]
	v_lshl_add_u64 v[6:7], s[22:23], 0, v[6:7]
	global_store_dword v[6:7], v5, off
	v_or_b32_e32 v6, 1, v4
	v_fma_f32 v4, -v10, v15, 1.0
	v_lshl_add_u32 v5, v0, 2, 0
	v_fmac_f32_e32 v15, v4, v15
	v_div_scale_f32 v4, vcc, v11, v14, v11
	ds_add_u32 v5, v109 offset:58624
	v_mul_f32_e32 v5, v4, v15
	v_fma_f32 v16, -v10, v5, v4
	v_fmac_f32_e32 v5, v16, v15
	v_fma_f32 v4, -v10, v5, v4
	v_div_fmas_f32 v4, v4, v15, v5
	v_div_scale_f32 v5, s[16:17], v14, v14, v12
	v_rcp_f32_e32 v15, v5
	v_ashrrev_i32_e32 v7, 31, v6
	v_div_fixup_f32 v4, v4, v14, v11
	v_lshl_add_u64 v[10:11], v[6:7], 2, s[22:23]
	v_lshl_add_u32 v6, v1, 2, 0
	ds_add_u32 v6, v109 offset:58624
	v_fma_f32 v6, -v5, v15, 1.0
	v_fmac_f32_e32 v15, v6, v15
	v_div_scale_f32 v6, vcc, v12, v14, v12
	v_mul_f32_e32 v7, v6, v15
	v_fma_f32 v16, -v5, v7, v6
	v_fmac_f32_e32 v7, v16, v15
	v_fma_f32 v5, -v5, v7, v6
	v_div_scale_f32 v6, s[16:17], v14, v14, v13
	v_div_fmas_f32 v5, v5, v15, v7
	v_rcp_f32_e32 v7, v6
	v_div_fixup_f32 v5, v5, v14, v12
	v_lshl_add_u32 v12, v2, 2, 0
	ds_add_u32 v12, v109 offset:58624
	global_store_dwordx4 v[8:9], v[0:3], off
	s_nop 1
	v_fma_f32 v0, -v6, v7, 1.0
	v_fmac_f32_e32 v7, v0, v7
	v_div_scale_f32 v0, vcc, v13, v14, v13
	v_mul_f32_e32 v1, v0, v7
	v_fma_f32 v2, -v6, v1, v0
	v_fmac_f32_e32 v1, v2, v7
	v_fma_f32 v0, -v6, v1, v0
	v_div_fmas_f32 v0, v0, v7, v1
	v_div_fixup_f32 v6, v0, v14, v13
	global_store_dwordx3 v[10:11], v[4:6], off
	v_lshl_add_u32 v0, v3, 2, 0
	ds_add_u32 v0, v109 offset:58624

.LBB0_3329:
	s_waitcnt vmcnt(0)
	s_barrier
	s_waitcnt vmcnt(0)
	buffer_inv sc1
	s_waitcnt vmcnt(0)
	v_readlane_b32 s98, v253, 20
	v_mbcnt_lo_u32_b32 v216, -1, 0
	v_mbcnt_hi_u32_b32 v216, -1, v216
	s_lshr_b32 s99, s98, 1
	s_and_b32 s100, s98, 1
	v_lshrrev_b32_e32 v217, 5, v216
	v_and_b32_e32 v216, 31, v216
	s_lshl_b32 s101, s99, 4
	v_add_u32_e32 v218, s101, v217
	v_lshlrev_b32_e32 v219, 7, v218
	v_lshl_add_u32 v219, v216, 2, v219
	v_add_u32_e32 v219, 0xa400, v219
	v_mul_u32_u24_e32 v218, 0x104, v218
	s_lshl_b32 s101, s100, 7
	v_add_u32_e32 v218, s101, v218
	v_lshl_add_u32 v218, v216, 2, v218
	v_add_u32_e32 v218, 0x6000, v218
	v_mov_b32_e32 v221, s98
	v_mbcnt_lo_u32_b32 v220, -1, 0
	v_mbcnt_hi_u32_b32 v220, -1, v220
	v_lshl_add_u32 v220, v221, 6, v220
	v_and_b32_e32 v221, 7, v220
	v_lshrrev_b32_e32 v220, 3, v220
	v_mul_u32_u24_e32 v221, 0x820, v221
	v_lshl_add_u32 v220, v220, 2, v221
	v_add_u32_e32 v220, 0x6000, v220
	v_add_u32_e32 v221, 0x410, v220
	s_lshl_b32 s101, s99, 13
	s_lshl_b32 s100, s100, 12
	s_add_i32 s101, s101, s100
	v_lshlrev_b32_e32 v217, 9, v217
	v_add_u32_e32 v217, s101, v217
	v_lshl_add_u32 v217, v216, 2, v217
	s_and_saveexec_b64 s[16:17], s[4:5]
	ds_write_b32 v95, v45 offset:58624
	s_or_b64 exec, exec, s[16:17]
	v_add_u32_e32 v0, s96, v42
	v_ashrrev_i32_e32 v1, 31, v0
	v_lshlrev_b64 v[0:1], 11, v[0:1]
	v_lshl_add_u64 v[92:93], v[46:47], 0, v[0:1]
	global_load_dwordx4 v[30:33], v[92:93], off
	global_load_dwordx4 v[34:37], v[48:49], off
	global_load_dwordx4 v[20:23], v[52:53], off
	global_load_dwordx4 v[24:27], v[92:93], off offset:128
	ds_read_b64 v[38:39], v106 offset:20480
	ds_read_b128 v[116:119], v43 offset:12288
	ds_read_b128 v[120:123], v43 offset:12304
	ds_read_b128 v[124:127], v43 offset:16384
	ds_read_b128 v[128:131], v43 offset:16400
	v_add_u32_e32 v114, 0x6000, v97
	v_mov_b32_e32 v4, 0
	s_waitcnt lgkmcnt(4)
	v_mov_b32_e32 v0, v38
	v_mov_b32_e32 v1, v38
	v_mov_b32_e32 v2, v38
	v_mov_b32_e32 v3, v38
	v_mov_b32_e32 v88, v39
	v_mov_b32_e32 v89, v39
	v_mov_b32_e32 v90, v39
	v_mov_b32_e32 v91, v39
	v_add_u32_e32 v113, 0x6400, v97
	s_mov_b32 s16, 0
	v_mov_b32_e32 v28, v103
	v_mov_b32_e32 v5, v4
	v_mov_b32_e32 v6, v4
	v_mov_b32_e32 v7, v4
	v_mov_b32_e32 v8, v4
	v_mov_b32_e32 v9, v4
	v_mov_b32_e32 v10, v4
	v_mov_b32_e32 v11, v4
	v_mov_b32_e32 v12, v4
	v_mov_b32_e32 v13, v4
	v_mov_b32_e32 v14, v4
	v_mov_b32_e32 v15, v4
	v_mov_b32_e32 v16, v4
	v_mov_b32_e32 v17, v4
	v_mov_b32_e32 v18, v4
	s_waitcnt vmcnt(3)
	v_cvt_f32_f16_sdwa v19, v31 dst_sel:DWORD dst_unused:UNUSED_PAD src0_sel:WORD_1
	v_cvt_f32_f16_e32 v29, v31
	v_cvt_f32_f16_sdwa v31, v30 dst_sel:DWORD dst_unused:UNUSED_PAD src0_sel:WORD_1
	v_cvt_f32_f16_e32 v30, v30
	v_cvt_f32_f16_sdwa v115, v33 dst_sel:DWORD dst_unused:UNUSED_PAD src0_sel:WORD_1
	v_cvt_f32_f16_e32 v134, v33
	v_cvt_f32_f16_sdwa v133, v32 dst_sel:DWORD dst_unused:UNUSED_PAD src0_sel:WORD_1
	v_cvt_f32_f16_e32 v132, v32
	v_sub_f32_e32 v30, v30, v38
	v_sub_f32_e32 v31, v31, v38
	v_sub_f32_e32 v32, v29, v38
	v_sub_f32_e32 v33, v19, v38
	v_sub_f32_e32 v132, v132, v38
	v_sub_f32_e32 v133, v133, v38
	v_sub_f32_e32 v134, v134, v38
	v_sub_f32_e32 v135, v115, v38
	v_pk_mul_f32 v[30:31], v[38:39], v[30:31] op_sel:[1,0]
	v_pk_mul_f32 v[32:33], v[38:39], v[32:33] op_sel:[1,0]
	v_pk_mul_f32 v[134:135], v[38:39], v[134:135] op_sel:[1,0]
	v_pk_mul_f32 v[38:39], v[38:39], v[132:133] op_sel:[1,0]
	s_waitcnt lgkmcnt(1)
	v_fma_f32 v19, v116, v30, v124
	v_fma_f32 v30, v117, v31, v125
	s_waitcnt lgkmcnt(0)
	v_fma_f32 v29, v120, v38, v128
	v_fma_f32 v31, v121, v39, v129
	v_fma_f32 v32, v118, v32, v126
	v_fma_f32 v38, v122, v134, v130
	v_fmac_f32_e32 v127, v119, v33
	v_fmac_f32_e32 v131, v123, v135
	ds_write2_b32 v220, v19, v30 offset1:65
	ds_write2_b32 v221, v29, v31 offset1:65
	ds_write2_b32 v220, v32, v127 offset0:130 offset1:195
	ds_write2_b32 v221, v38, v131 offset0:130 offset1:195
	s_waitcnt vmcnt(2)
	ds_write_b128 v96, v[34:37] offset:41984
	v_mov_b32_e32 v19, v4
	s_waitcnt lgkmcnt(0)
	s_barrier
	ds_read_b32 v200, v218
	ds_read_b32 v208, v219
	ds_read_b32 v201, v218 offset:520
	ds_read_b32 v209, v219 offset:256
	ds_read_b32 v202, v218 offset:1040
	ds_read_b32 v210, v219 offset:512
	ds_read_b32 v203, v218 offset:1560
	ds_read_b32 v211, v219 offset:768
	ds_read_b32 v204, v218 offset:2080
	ds_read_b32 v212, v219 offset:1024
	ds_read_b32 v205, v218 offset:2600
	ds_read_b32 v213, v219 offset:1280
	ds_read_b32 v206, v218 offset:3120
	ds_read_b32 v214, v219 offset:1536
	s_waitcnt lgkmcnt(12)
	v_mfma_f32_32x32x2_f32 v[4:19], v200, v208, v[4:19]
	ds_read_b32 v207, v218 offset:3640
	ds_read_b32 v215, v219 offset:1792
	s_waitcnt lgkmcnt(12)
	v_mfma_f32_32x32x2_f32 v[4:19], v201, v209, v[4:19]
	s_waitcnt lgkmcnt(10)
	v_mfma_f32_32x32x2_f32 v[4:19], v202, v210, v[4:19]
	s_waitcnt lgkmcnt(8)
	v_mfma_f32_32x32x2_f32 v[4:19], v203, v211, v[4:19]
	s_waitcnt lgkmcnt(6)
	v_mfma_f32_32x32x2_f32 v[4:19], v204, v212, v[4:19]
	s_waitcnt lgkmcnt(4)
	v_mfma_f32_32x32x2_f32 v[4:19], v205, v213, v[4:19]
	s_waitcnt lgkmcnt(2)
	v_mfma_f32_32x32x2_f32 v[4:19], v206, v214, v[4:19]
	s_waitcnt lgkmcnt(0)
	v_mfma_f32_32x32x2_f32 v[4:19], v207, v215, v[4:19]
	s_barrier
	global_load_dwordx4 v[32:35], v[92:93], off offset:256
	global_load_dwordx4 v[28:31], v[54:55], off
	s_waitcnt vmcnt(2)
	v_cvt_f32_f16_sdwa v128, v24 dst_sel:DWORD dst_unused:UNUSED_PAD src0_sel:WORD_1
	v_cvt_f32_f16_e32 v24, v24
	v_cvt_f32_f16_e32 v129, v25
	v_cvt_f32_f16_sdwa v130, v26 dst_sel:DWORD dst_unused:UNUSED_PAD src0_sel:WORD_1
	v_cvt_f32_f16_e32 v133, v26
	ds_read_b128 v[36:39], v43 offset:12544
	ds_read_b128 v[116:119], v43 offset:12560
	ds_read_b128 v[120:123], v43 offset:16640
	ds_read_b128 v[124:127], v43 offset:16656
	v_cvt_f32_f16_sdwa v115, v25 dst_sel:DWORD dst_unused:UNUSED_PAD src0_sel:WORD_1
	v_cvt_f32_f16_sdwa v131, v27 dst_sel:DWORD dst_unused:UNUSED_PAD src0_sel:WORD_1
	v_cvt_f32_f16_e32 v132, v27
	v_sub_f32_e32 v24, v24, v0
	v_sub_f32_e32 v25, v128, v1
	v_sub_f32_e32 v26, v129, v2
	v_pk_mul_f32 v[24:25], v[88:89], v[24:25]
	v_sub_f32_e32 v128, v133, v0
	v_sub_f32_e32 v129, v130, v1
	v_sub_f32_e32 v27, v115, v3
	v_sub_f32_e32 v130, v132, v2
	v_sub_f32_e32 v131, v131, v3
	v_pk_mul_f32 v[128:129], v[88:89], v[128:129]
	s_waitcnt lgkmcnt(1)
	v_fma_f32 v24, v36, v24, v120
	v_fma_f32 v25, v37, v25, v121
	v_pk_mul_f32 v[26:27], v[90:91], v[26:27]
	v_pk_mul_f32 v[130:131], v[90:91], v[130:131]
	s_waitcnt lgkmcnt(0)
	v_fma_f32 v36, v116, v128, v124
	ds_write2_b32 v220, v24, v25 offset1:65
	v_fma_f32 v24, v117, v129, v125
	ds_write2_b32 v221, v36, v24 offset1:65
	v_fma_f32 v24, v38, v26, v122
	v_fma_f32 v25, v118, v130, v126
	v_fmac_f32_e32 v123, v39, v27
	v_fmac_f32_e32 v127, v119, v131
	ds_write2_b32 v220, v24, v123 offset0:130 offset1:195
	ds_write2_b32 v221, v25, v127 offset0:130 offset1:195
	ds_write_b128 v96, v[20:23] offset:41984
	s_mov_b32 s16, 0
	v_mov_b32_e32 v20, v103
	s_waitcnt lgkmcnt(0)
	s_barrier
	ds_read_b32 v200, v218
	ds_read_b32 v208, v219
	ds_read_b32 v201, v218 offset:520
	ds_read_b32 v209, v219 offset:256
	ds_read_b32 v202, v218 offset:1040
	ds_read_b32 v210, v219 offset:512
	ds_read_b32 v203, v218 offset:1560
	ds_read_b32 v211, v219 offset:768
	ds_read_b32 v204, v218 offset:2080
	ds_read_b32 v212, v219 offset:1024
	ds_read_b32 v205, v218 offset:2600
	ds_read_b32 v213, v219 offset:1280
	ds_read_b32 v206, v218 offset:3120
	ds_read_b32 v214, v219 offset:1536
	s_waitcnt lgkmcnt(12)
	v_mfma_f32_32x32x2_f32 v[4:19], v200, v208, v[4:19]
	ds_read_b32 v207, v218 offset:3640
	ds_read_b32 v215, v219 offset:1792
	s_waitcnt lgkmcnt(12)
	v_mfma_f32_32x32x2_f32 v[4:19], v201, v209, v[4:19]
	s_waitcnt lgkmcnt(10)
	v_mfma_f32_32x32x2_f32 v[4:19], v202, v210, v[4:19]
	s_waitcnt lgkmcnt(8)
	v_mfma_f32_32x32x2_f32 v[4:19], v203, v211, v[4:19]
	s_waitcnt lgkmcnt(6)
	v_mfma_f32_32x32x2_f32 v[4:19], v204, v212, v[4:19]
	s_waitcnt lgkmcnt(4)
	v_mfma_f32_32x32x2_f32 v[4:19], v205, v213, v[4:19]
	s_waitcnt lgkmcnt(2)
	v_mfma_f32_32x32x2_f32 v[4:19], v206, v214, v[4:19]
	s_waitcnt lgkmcnt(0)
	v_mfma_f32_32x32x2_f32 v[4:19], v207, v215, v[4:19]
	s_barrier
	global_load_dwordx4 v[36:39], v[92:93], off offset:384
	global_load_dwordx4 v[20:23], v[56:57], off
	s_waitcnt vmcnt(3)
	v_cvt_f32_f16_sdwa v128, v32 dst_sel:DWORD dst_unused:UNUSED_PAD src0_sel:WORD_1
	v_cvt_f32_f16_e32 v32, v32
	v_cvt_f32_f16_e32 v129, v33
	v_cvt_f32_f16_sdwa v130, v34 dst_sel:DWORD dst_unused:UNUSED_PAD src0_sel:WORD_1
	v_cvt_f32_f16_e32 v133, v34
	ds_read_b128 v[24:27], v43 offset:12800
	ds_read_b128 v[116:119], v43 offset:12816
	ds_read_b128 v[120:123], v43 offset:16896
	ds_read_b128 v[124:127], v43 offset:16912
	v_cvt_f32_f16_sdwa v115, v33 dst_sel:DWORD dst_unused:UNUSED_PAD src0_sel:WORD_1
	v_cvt_f32_f16_sdwa v131, v35 dst_sel:DWORD dst_unused:UNUSED_PAD src0_sel:WORD_1
	v_cvt_f32_f16_e32 v132, v35
	v_sub_f32_e32 v32, v32, v0
	v_sub_f32_e32 v33, v128, v1
	v_sub_f32_e32 v34, v129, v2
	v_pk_mul_f32 v[32:33], v[88:89], v[32:33]
	v_sub_f32_e32 v128, v133, v0
	v_sub_f32_e32 v129, v130, v1
	v_sub_f32_e32 v35, v115, v3
	v_pk_mul_f32 v[128:129], v[88:89], v[128:129]
	s_waitcnt lgkmcnt(1)
	v_fma_f32 v24, v24, v32, v120
	v_fma_f32 v25, v25, v33, v121
	v_pk_mul_f32 v[34:35], v[90:91], v[34:35]
	v_sub_f32_e32 v130, v132, v2
	v_sub_f32_e32 v131, v131, v3
	s_waitcnt lgkmcnt(0)
	v_fma_f32 v32, v116, v128, v124
	ds_write2_b32 v220, v24, v25 offset1:65
	v_fma_f32 v24, v117, v129, v125
	v_pk_mul_f32 v[130:131], v[90:91], v[130:131]
	ds_write2_b32 v221, v32, v24 offset1:65
	v_fma_f32 v24, v26, v34, v122
	v_fmac_f32_e32 v123, v27, v35
	v_fma_f32 v25, v118, v130, v126
	ds_write2_b32 v220, v24, v123 offset0:130 offset1:195
	v_fmac_f32_e32 v127, v119, v131
	s_mov_b32 s16, 0
	v_mov_b32_e32 v24, v103
	ds_write2_b32 v221, v25, v127 offset0:130 offset1:195
	s_waitcnt vmcnt(2)
	ds_write_b128 v96, v[28:31] offset:41984
	s_waitcnt lgkmcnt(0)
	s_barrier
	ds_read_b32 v200, v218
	ds_read_b32 v208, v219
	ds_read_b32 v201, v218 offset:520
	ds_read_b32 v209, v219 offset:256
	ds_read_b32 v202, v218 offset:1040
	ds_read_b32 v210, v219 offset:512
	ds_read_b32 v203, v218 offset:1560
	ds_read_b32 v211, v219 offset:768
	ds_read_b32 v204, v218 offset:2080
	ds_read_b32 v212, v219 offset:1024
	ds_read_b32 v205, v218 offset:2600
	ds_read_b32 v213, v219 offset:1280
	ds_read_b32 v206, v218 offset:3120
	ds_read_b32 v214, v219 offset:1536
	s_waitcnt lgkmcnt(12)
	v_mfma_f32_32x32x2_f32 v[4:19], v200, v208, v[4:19]
	ds_read_b32 v207, v218 offset:3640
	ds_read_b32 v215, v219 offset:1792
	s_waitcnt lgkmcnt(12)
	v_mfma_f32_32x32x2_f32 v[4:19], v201, v209, v[4:19]
	s_waitcnt lgkmcnt(10)
	v_mfma_f32_32x32x2_f32 v[4:19], v202, v210, v[4:19]
	s_waitcnt lgkmcnt(8)
	v_mfma_f32_32x32x2_f32 v[4:19], v203, v211, v[4:19]
	s_waitcnt lgkmcnt(6)
	v_mfma_f32_32x32x2_f32 v[4:19], v204, v212, v[4:19]
	s_waitcnt lgkmcnt(4)
	v_mfma_f32_32x32x2_f32 v[4:19], v205, v213, v[4:19]
	s_waitcnt lgkmcnt(2)
	v_mfma_f32_32x32x2_f32 v[4:19], v206, v214, v[4:19]
	s_waitcnt lgkmcnt(0)
	v_mfma_f32_32x32x2_f32 v[4:19], v207, v215, v[4:19]
	s_barrier
	global_load_dwordx4 v[28:31], v[92:93], off offset:512
	global_load_dwordx4 v[24:27], v[58:59], off
	s_waitcnt vmcnt(3)
	v_cvt_f32_f16_sdwa v128, v36 dst_sel:DWORD dst_unused:UNUSED_PAD src0_sel:WORD_1
	v_cvt_f32_f16_e32 v36, v36
	v_cvt_f32_f16_e32 v129, v37
	v_cvt_f32_f16_sdwa v130, v38 dst_sel:DWORD dst_unused:UNUSED_PAD src0_sel:WORD_1
	v_cvt_f32_f16_e32 v133, v38
	ds_read_b128 v[32:35], v43 offset:13056
	ds_read_b128 v[116:119], v43 offset:13072
	ds_read_b128 v[120:123], v43 offset:17152
	ds_read_b128 v[124:127], v43 offset:17168
	v_cvt_f32_f16_sdwa v115, v37 dst_sel:DWORD dst_unused:UNUSED_PAD src0_sel:WORD_1
	v_cvt_f32_f16_sdwa v131, v39 dst_sel:DWORD dst_unused:UNUSED_PAD src0_sel:WORD_1
	v_cvt_f32_f16_e32 v132, v39
	v_sub_f32_e32 v36, v36, v0
	v_sub_f32_e32 v37, v128, v1
	v_sub_f32_e32 v38, v129, v2
	v_pk_mul_f32 v[36:37], v[88:89], v[36:37]
	v_sub_f32_e32 v128, v133, v0
	v_sub_f32_e32 v129, v130, v1
	v_sub_f32_e32 v39, v115, v3
	v_sub_f32_e32 v130, v132, v2
	v_sub_f32_e32 v131, v131, v3
	v_pk_mul_f32 v[128:129], v[88:89], v[128:129]
	s_waitcnt lgkmcnt(1)
	v_fma_f32 v32, v32, v36, v120
	v_fma_f32 v33, v33, v37, v121
	v_pk_mul_f32 v[38:39], v[90:91], v[38:39]
	v_pk_mul_f32 v[130:131], v[90:91], v[130:131]
	s_waitcnt lgkmcnt(0)
	v_fma_f32 v36, v116, v128, v124
	ds_write2_b32 v220, v32, v33 offset1:65
	v_fma_f32 v32, v117, v129, v125
	ds_write2_b32 v221, v36, v32 offset1:65
	v_fma_f32 v32, v34, v38, v122
	v_fma_f32 v33, v118, v130, v126
	v_fmac_f32_e32 v123, v35, v39
	v_fmac_f32_e32 v127, v119, v131
	ds_write2_b32 v220, v32, v123 offset0:130 offset1:195
	ds_write2_b32 v221, v33, v127 offset0:130 offset1:195
	s_waitcnt vmcnt(2)
	ds_write_b128 v96, v[20:23] offset:41984
	s_mov_b32 s16, 0
	v_mov_b32_e32 v20, v103
	s_waitcnt lgkmcnt(0)
	s_barrier
	ds_read_b32 v200, v218
	ds_read_b32 v208, v219
	ds_read_b32 v201, v218 offset:520
	ds_read_b32 v209, v219 offset:256
	ds_read_b32 v202, v218 offset:1040
	ds_read_b32 v210, v219 offset:512
	ds_read_b32 v203, v218 offset:1560
	ds_read_b32 v211, v219 offset:768
	ds_read_b32 v204, v218 offset:2080
	ds_read_b32 v212, v219 offset:1024
	ds_read_b32 v205, v218 offset:2600
	ds_read_b32 v213, v219 offset:1280
	ds_read_b32 v206, v218 offset:3120
	ds_read_b32 v214, v219 offset:1536
	s_waitcnt lgkmcnt(12)
	v_mfma_f32_32x32x2_f32 v[4:19], v200, v208, v[4:19]
	ds_read_b32 v207, v218 offset:3640
	ds_read_b32 v215, v219 offset:1792
	s_waitcnt lgkmcnt(12)
	v_mfma_f32_32x32x2_f32 v[4:19], v201, v209, v[4:19]
	s_waitcnt lgkmcnt(10)
	v_mfma_f32_32x32x2_f32 v[4:19], v202, v210, v[4:19]
	s_waitcnt lgkmcnt(8)
	v_mfma_f32_32x32x2_f32 v[4:19], v203, v211, v[4:19]
	s_waitcnt lgkmcnt(6)
	v_mfma_f32_32x32x2_f32 v[4:19], v204, v212, v[4:19]
	s_waitcnt lgkmcnt(4)
	v_mfma_f32_32x32x2_f32 v[4:19], v205, v213, v[4:19]
	s_waitcnt lgkmcnt(2)
	v_mfma_f32_32x32x2_f32 v[4:19], v206, v214, v[4:19]
	s_waitcnt lgkmcnt(0)
	v_mfma_f32_32x32x2_f32 v[4:19], v207, v215, v[4:19]
	s_barrier
	global_load_dwordx4 v[32:35], v[92:93], off offset:640
	global_load_dwordx4 v[20:23], v[60:61], off
	s_waitcnt vmcnt(3)
	v_cvt_f32_f16_sdwa v128, v28 dst_sel:DWORD dst_unused:UNUSED_PAD src0_sel:WORD_1
	v_cvt_f32_f16_e32 v28, v28
	v_cvt_f32_f16_e32 v129, v29
	v_cvt_f32_f16_sdwa v130, v30 dst_sel:DWORD dst_unused:UNUSED_PAD src0_sel:WORD_1
	v_cvt_f32_f16_e32 v133, v30
	ds_read_b128 v[36:39], v43 offset:13312
	ds_read_b128 v[116:119], v43 offset:13328
	ds_read_b128 v[120:123], v43 offset:17408
	ds_read_b128 v[124:127], v43 offset:17424
	v_cvt_f32_f16_sdwa v115, v29 dst_sel:DWORD dst_unused:UNUSED_PAD src0_sel:WORD_1
	v_cvt_f32_f16_sdwa v131, v31 dst_sel:DWORD dst_unused:UNUSED_PAD src0_sel:WORD_1
	v_cvt_f32_f16_e32 v132, v31
	v_sub_f32_e32 v28, v28, v0
	v_sub_f32_e32 v29, v128, v1
	v_sub_f32_e32 v30, v129, v2
	v_pk_mul_f32 v[28:29], v[88:89], v[28:29]
	v_sub_f32_e32 v128, v133, v0
	v_sub_f32_e32 v129, v130, v1
	v_sub_f32_e32 v31, v115, v3
	v_sub_f32_e32 v130, v132, v2
	v_sub_f32_e32 v131, v131, v3
	v_pk_mul_f32 v[128:129], v[88:89], v[128:129]
	s_waitcnt lgkmcnt(1)
	v_fma_f32 v28, v36, v28, v120
	v_fma_f32 v29, v37, v29, v121
	v_pk_mul_f32 v[30:31], v[90:91], v[30:31]
	v_pk_mul_f32 v[130:131], v[90:91], v[130:131]
	s_waitcnt lgkmcnt(0)
	v_fma_f32 v36, v116, v128, v124
	ds_write2_b32 v220, v28, v29 offset1:65
	v_fma_f32 v28, v117, v129, v125
	ds_write2_b32 v221, v36, v28 offset1:65
	v_fma_f32 v28, v38, v30, v122
	v_fma_f32 v29, v118, v130, v126
	v_fmac_f32_e32 v123, v39, v31
	v_fmac_f32_e32 v127, v119, v131
	ds_write2_b32 v220, v28, v123 offset0:130 offset1:195
	ds_write2_b32 v221, v29, v127 offset0:130 offset1:195
	s_waitcnt vmcnt(2)
	ds_write_b128 v96, v[24:27] offset:41984
	s_mov_b32 s16, 0
	v_mov_b32_e32 v24, v103
	s_waitcnt lgkmcnt(0)
	s_barrier
	ds_read_b32 v200, v218
	ds_read_b32 v208, v219
	ds_read_b32 v201, v218 offset:520
	ds_read_b32 v209, v219 offset:256
	ds_read_b32 v202, v218 offset:1040
	ds_read_b32 v210, v219 offset:512
	ds_read_b32 v203, v218 offset:1560
	ds_read_b32 v211, v219 offset:768
	ds_read_b32 v204, v218 offset:2080
	ds_read_b32 v212, v219 offset:1024
	ds_read_b32 v205, v218 offset:2600
	ds_read_b32 v213, v219 offset:1280
	ds_read_b32 v206, v218 offset:3120
	ds_read_b32 v214, v219 offset:1536
	s_waitcnt lgkmcnt(12)
	v_mfma_f32_32x32x2_f32 v[4:19], v200, v208, v[4:19]
	ds_read_b32 v207, v218 offset:3640
	ds_read_b32 v215, v219 offset:1792
	s_waitcnt lgkmcnt(12)
	v_mfma_f32_32x32x2_f32 v[4:19], v201, v209, v[4:19]
	s_waitcnt lgkmcnt(10)
	v_mfma_f32_32x32x2_f32 v[4:19], v202, v210, v[4:19]
	s_waitcnt lgkmcnt(8)
	v_mfma_f32_32x32x2_f32 v[4:19], v203, v211, v[4:19]
	s_waitcnt lgkmcnt(6)
	v_mfma_f32_32x32x2_f32 v[4:19], v204, v212, v[4:19]
	s_waitcnt lgkmcnt(4)
	v_mfma_f32_32x32x2_f32 v[4:19], v205, v213, v[4:19]
	s_waitcnt lgkmcnt(2)
	v_mfma_f32_32x32x2_f32 v[4:19], v206, v214, v[4:19]
	s_waitcnt lgkmcnt(0)
	v_mfma_f32_32x32x2_f32 v[4:19], v207, v215, v[4:19]
	s_barrier
	global_load_dwordx4 v[28:31], v[92:93], off offset:768
	global_load_dwordx4 v[24:27], v[62:63], off
	s_waitcnt vmcnt(3)
	v_cvt_f32_f16_sdwa v128, v32 dst_sel:DWORD dst_unused:UNUSED_PAD src0_sel:WORD_1
	v_cvt_f32_f16_e32 v32, v32
	v_cvt_f32_f16_e32 v129, v33
	v_cvt_f32_f16_sdwa v130, v34 dst_sel:DWORD dst_unused:UNUSED_PAD src0_sel:WORD_1
	v_cvt_f32_f16_e32 v133, v34
	ds_read_b128 v[36:39], v43 offset:13568
	ds_read_b128 v[116:119], v43 offset:13584
	ds_read_b128 v[120:123], v43 offset:17664
	ds_read_b128 v[124:127], v43 offset:17680
	v_cvt_f32_f16_sdwa v115, v33 dst_sel:DWORD dst_unused:UNUSED_PAD src0_sel:WORD_1
	v_cvt_f32_f16_sdwa v131, v35 dst_sel:DWORD dst_unused:UNUSED_PAD src0_sel:WORD_1
	v_cvt_f32_f16_e32 v132, v35
	v_sub_f32_e32 v32, v32, v0
	v_sub_f32_e32 v33, v128, v1
	v_sub_f32_e32 v34, v129, v2
	v_pk_mul_f32 v[32:33], v[88:89], v[32:33]
	v_sub_f32_e32 v128, v133, v0
	v_sub_f32_e32 v129, v130, v1
	v_sub_f32_e32 v35, v115, v3
	v_sub_f32_e32 v130, v132, v2
	v_sub_f32_e32 v131, v131, v3
	v_pk_mul_f32 v[128:129], v[88:89], v[128:129]
	s_waitcnt lgkmcnt(1)
	v_fma_f32 v32, v36, v32, v120
	v_fma_f32 v33, v37, v33, v121
	v_pk_mul_f32 v[34:35], v[90:91], v[34:35]
	v_pk_mul_f32 v[130:131], v[90:91], v[130:131]
	s_waitcnt lgkmcnt(0)
	v_fma_f32 v36, v116, v128, v124
	ds_write2_b32 v220, v32, v33 offset1:65
	v_fma_f32 v32, v117, v129, v125
	ds_write2_b32 v221, v36, v32 offset1:65
	v_fma_f32 v32, v38, v34, v122
	v_fma_f32 v33, v118, v130, v126
	v_fmac_f32_e32 v123, v39, v35
	v_fmac_f32_e32 v127, v119, v131
	ds_write2_b32 v220, v32, v123 offset0:130 offset1:195
	ds_write2_b32 v221, v33, v127 offset0:130 offset1:195
	s_waitcnt vmcnt(2)
	ds_write_b128 v96, v[20:23] offset:41984
	s_mov_b32 s16, 0
	v_mov_b32_e32 v20, v103
	s_waitcnt lgkmcnt(0)
	s_barrier
	ds_read_b32 v200, v218
	ds_read_b32 v208, v219
	ds_read_b32 v201, v218 offset:520
	ds_read_b32 v209, v219 offset:256
	ds_read_b32 v202, v218 offset:1040
	ds_read_b32 v210, v219 offset:512
	ds_read_b32 v203, v218 offset:1560
	ds_read_b32 v211, v219 offset:768
	ds_read_b32 v204, v218 offset:2080
	ds_read_b32 v212, v219 offset:1024
	ds_read_b32 v205, v218 offset:2600
	ds_read_b32 v213, v219 offset:1280
	ds_read_b32 v206, v218 offset:3120
	ds_read_b32 v214, v219 offset:1536
	s_waitcnt lgkmcnt(12)
	v_mfma_f32_32x32x2_f32 v[4:19], v200, v208, v[4:19]
	ds_read_b32 v207, v218 offset:3640
	ds_read_b32 v215, v219 offset:1792
	s_waitcnt lgkmcnt(12)
	v_mfma_f32_32x32x2_f32 v[4:19], v201, v209, v[4:19]
	s_waitcnt lgkmcnt(10)
	v_mfma_f32_32x32x2_f32 v[4:19], v202, v210, v[4:19]
	s_waitcnt lgkmcnt(8)
	v_mfma_f32_32x32x2_f32 v[4:19], v203, v211, v[4:19]
	s_waitcnt lgkmcnt(6)
	v_mfma_f32_32x32x2_f32 v[4:19], v204, v212, v[4:19]
	s_waitcnt lgkmcnt(4)
	v_mfma_f32_32x32x2_f32 v[4:19], v205, v213, v[4:19]
	s_waitcnt lgkmcnt(2)
	v_mfma_f32_32x32x2_f32 v[4:19], v206, v214, v[4:19]
	s_waitcnt lgkmcnt(0)
	v_mfma_f32_32x32x2_f32 v[4:19], v207, v215, v[4:19]
	s_barrier
	global_load_dwordx4 v[32:35], v[92:93], off offset:896
	global_load_dwordx4 v[20:23], v[64:65], off
	s_waitcnt vmcnt(3)
	v_cvt_f32_f16_sdwa v128, v28 dst_sel:DWORD dst_unused:UNUSED_PAD src0_sel:WORD_1
	v_cvt_f32_f16_e32 v28, v28
	v_cvt_f32_f16_e32 v129, v29
	v_cvt_f32_f16_sdwa v130, v30 dst_sel:DWORD dst_unused:UNUSED_PAD src0_sel:WORD_1
	v_cvt_f32_f16_e32 v133, v30
	ds_read_b128 v[36:39], v43 offset:13824
	ds_read_b128 v[116:119], v43 offset:13840
	ds_read_b128 v[120:123], v43 offset:17920
	ds_read_b128 v[124:127], v43 offset:17936
	v_cvt_f32_f16_sdwa v115, v29 dst_sel:DWORD dst_unused:UNUSED_PAD src0_sel:WORD_1
	v_cvt_f32_f16_sdwa v131, v31 dst_sel:DWORD dst_unused:UNUSED_PAD src0_sel:WORD_1
	v_cvt_f32_f16_e32 v132, v31
	v_sub_f32_e32 v28, v28, v0
	v_sub_f32_e32 v29, v128, v1
	v_sub_f32_e32 v30, v129, v2
	v_pk_mul_f32 v[28:29], v[88:89], v[28:29]
	v_sub_f32_e32 v128, v133, v0
	v_sub_f32_e32 v129, v130, v1
	v_sub_f32_e32 v31, v115, v3
	v_sub_f32_e32 v130, v132, v2
	v_sub_f32_e32 v131, v131, v3
	v_pk_mul_f32 v[128:129], v[88:89], v[128:129]
	s_waitcnt lgkmcnt(1)
	v_fma_f32 v28, v36, v28, v120
	v_fma_f32 v29, v37, v29, v121
	v_pk_mul_f32 v[30:31], v[90:91], v[30:31]
	v_pk_mul_f32 v[130:131], v[90:91], v[130:131]
	s_waitcnt lgkmcnt(0)
	v_fma_f32 v36, v116, v128, v124
	ds_write2_b32 v220, v28, v29 offset1:65
	v_fma_f32 v28, v117, v129, v125
	ds_write2_b32 v221, v36, v28 offset1:65
	v_fma_f32 v28, v38, v30, v122
	v_fma_f32 v29, v118, v130, v126
	v_fmac_f32_e32 v123, v39, v31
	v_fmac_f32_e32 v127, v119, v131
	ds_write2_b32 v220, v28, v123 offset0:130 offset1:195
	ds_write2_b32 v221, v29, v127 offset0:130 offset1:195
	s_waitcnt vmcnt(2)
	ds_write_b128 v96, v[24:27] offset:41984
	s_mov_b32 s16, 0
	v_mov_b32_e32 v24, v103
	s_waitcnt lgkmcnt(0)
	s_barrier
	ds_read_b32 v200, v218
	ds_read_b32 v208, v219
	ds_read_b32 v201, v218 offset:520
	ds_read_b32 v209, v219 offset:256
	ds_read_b32 v202, v218 offset:1040
	ds_read_b32 v210, v219 offset:512
	ds_read_b32 v203, v218 offset:1560
	ds_read_b32 v211, v219 offset:768
	ds_read_b32 v204, v218 offset:2080
	ds_read_b32 v212, v219 offset:1024
	ds_read_b32 v205, v218 offset:2600
	ds_read_b32 v213, v219 offset:1280
	ds_read_b32 v206, v218 offset:3120
	ds_read_b32 v214, v219 offset:1536
	s_waitcnt lgkmcnt(12)
	v_mfma_f32_32x32x2_f32 v[4:19], v200, v208, v[4:19]
	ds_read_b32 v207, v218 offset:3640
	ds_read_b32 v215, v219 offset:1792
	s_waitcnt lgkmcnt(12)
	v_mfma_f32_32x32x2_f32 v[4:19], v201, v209, v[4:19]
	s_waitcnt lgkmcnt(10)
	v_mfma_f32_32x32x2_f32 v[4:19], v202, v210, v[4:19]
	s_waitcnt lgkmcnt(8)
	v_mfma_f32_32x32x2_f32 v[4:19], v203, v211, v[4:19]
	s_waitcnt lgkmcnt(6)
	v_mfma_f32_32x32x2_f32 v[4:19], v204, v212, v[4:19]
	s_waitcnt lgkmcnt(4)
	v_mfma_f32_32x32x2_f32 v[4:19], v205, v213, v[4:19]
	s_waitcnt lgkmcnt(2)
	v_mfma_f32_32x32x2_f32 v[4:19], v206, v214, v[4:19]
	s_waitcnt lgkmcnt(0)
	v_mfma_f32_32x32x2_f32 v[4:19], v207, v215, v[4:19]
	s_barrier
	global_load_dwordx4 v[28:31], v[92:93], off offset:1024
	global_load_dwordx4 v[24:27], v[66:67], off
	s_waitcnt vmcnt(3)
	v_cvt_f32_f16_sdwa v128, v32 dst_sel:DWORD dst_unused:UNUSED_PAD src0_sel:WORD_1
	v_cvt_f32_f16_e32 v32, v32
	v_cvt_f32_f16_e32 v129, v33
	v_cvt_f32_f16_sdwa v130, v34 dst_sel:DWORD dst_unused:UNUSED_PAD src0_sel:WORD_1
	v_cvt_f32_f16_e32 v133, v34
	ds_read_b128 v[36:39], v43 offset:14080
	ds_read_b128 v[116:119], v43 offset:14096
	ds_read_b128 v[120:123], v43 offset:18176
	ds_read_b128 v[124:127], v43 offset:18192
	v_cvt_f32_f16_sdwa v115, v33 dst_sel:DWORD dst_unused:UNUSED_PAD src0_sel:WORD_1
	v_cvt_f32_f16_sdwa v131, v35 dst_sel:DWORD dst_unused:UNUSED_PAD src0_sel:WORD_1
	v_cvt_f32_f16_e32 v132, v35
	v_sub_f32_e32 v32, v32, v0
	v_sub_f32_e32 v33, v128, v1
	v_sub_f32_e32 v34, v129, v2
	v_pk_mul_f32 v[32:33], v[88:89], v[32:33]
	v_sub_f32_e32 v128, v133, v0
	v_sub_f32_e32 v129, v130, v1
	v_sub_f32_e32 v35, v115, v3
	v_sub_f32_e32 v130, v132, v2
	v_sub_f32_e32 v131, v131, v3
	v_pk_mul_f32 v[128:129], v[88:89], v[128:129]
	s_waitcnt lgkmcnt(1)
	v_fma_f32 v32, v36, v32, v120
	v_fma_f32 v33, v37, v33, v121
	v_pk_mul_f32 v[34:35], v[90:91], v[34:35]
	v_pk_mul_f32 v[130:131], v[90:91], v[130:131]
	s_waitcnt lgkmcnt(0)
	v_fma_f32 v36, v116, v128, v124
	ds_write2_b32 v220, v32, v33 offset1:65
	v_fma_f32 v32, v117, v129, v125
	ds_write2_b32 v221, v36, v32 offset1:65
	v_fma_f32 v32, v38, v34, v122
	v_fma_f32 v33, v118, v130, v126
	v_fmac_f32_e32 v123, v39, v35
	v_fmac_f32_e32 v127, v119, v131
	ds_write2_b32 v220, v32, v123 offset0:130 offset1:195
	ds_write2_b32 v221, v33, v127 offset0:130 offset1:195
	s_waitcnt vmcnt(2)
	ds_write_b128 v96, v[20:23] offset:41984
	s_mov_b32 s16, 0
	v_mov_b32_e32 v20, v103
	s_waitcnt lgkmcnt(0)
	s_barrier
	ds_read_b32 v200, v218
	ds_read_b32 v208, v219
	ds_read_b32 v201, v218 offset:520
	ds_read_b32 v209, v219 offset:256
	ds_read_b32 v202, v218 offset:1040
	ds_read_b32 v210, v219 offset:512
	ds_read_b32 v203, v218 offset:1560
	ds_read_b32 v211, v219 offset:768
	ds_read_b32 v204, v218 offset:2080
	ds_read_b32 v212, v219 offset:1024
	ds_read_b32 v205, v218 offset:2600
	ds_read_b32 v213, v219 offset:1280
	ds_read_b32 v206, v218 offset:3120
	ds_read_b32 v214, v219 offset:1536
	s_waitcnt lgkmcnt(12)
	v_mfma_f32_32x32x2_f32 v[4:19], v200, v208, v[4:19]
	ds_read_b32 v207, v218 offset:3640
	ds_read_b32 v215, v219 offset:1792
	s_waitcnt lgkmcnt(12)
	v_mfma_f32_32x32x2_f32 v[4:19], v201, v209, v[4:19]
	s_waitcnt lgkmcnt(10)
	v_mfma_f32_32x32x2_f32 v[4:19], v202, v210, v[4:19]
	s_waitcnt lgkmcnt(8)
	v_mfma_f32_32x32x2_f32 v[4:19], v203, v211, v[4:19]
	s_waitcnt lgkmcnt(6)
	v_mfma_f32_32x32x2_f32 v[4:19], v204, v212, v[4:19]
	s_waitcnt lgkmcnt(4)
	v_mfma_f32_32x32x2_f32 v[4:19], v205, v213, v[4:19]
	s_waitcnt lgkmcnt(2)
	v_mfma_f32_32x32x2_f32 v[4:19], v206, v214, v[4:19]
	s_waitcnt lgkmcnt(0)
	v_mfma_f32_32x32x2_f32 v[4:19], v207, v215, v[4:19]
	s_barrier
	global_load_dwordx4 v[32:35], v[92:93], off offset:1152
	global_load_dwordx4 v[20:23], v[68:69], off
	s_waitcnt vmcnt(3)
	v_cvt_f32_f16_sdwa v128, v28 dst_sel:DWORD dst_unused:UNUSED_PAD src0_sel:WORD_1
	v_cvt_f32_f16_e32 v28, v28
	v_cvt_f32_f16_e32 v129, v29
	v_cvt_f32_f16_sdwa v130, v30 dst_sel:DWORD dst_unused:UNUSED_PAD src0_sel:WORD_1
	v_cvt_f32_f16_e32 v133, v30
	ds_read_b128 v[36:39], v43 offset:14336
	ds_read_b128 v[116:119], v43 offset:14352
	ds_read_b128 v[120:123], v43 offset:18432
	ds_read_b128 v[124:127], v43 offset:18448
	v_cvt_f32_f16_sdwa v115, v29 dst_sel:DWORD dst_unused:UNUSED_PAD src0_sel:WORD_1
	v_cvt_f32_f16_sdwa v131, v31 dst_sel:DWORD dst_unused:UNUSED_PAD src0_sel:WORD_1
	v_cvt_f32_f16_e32 v132, v31
	v_sub_f32_e32 v28, v28, v0
	v_sub_f32_e32 v29, v128, v1
	v_sub_f32_e32 v30, v129, v2
	v_pk_mul_f32 v[28:29], v[88:89], v[28:29]
	v_sub_f32_e32 v128, v133, v0
	v_sub_f32_e32 v129, v130, v1
	v_sub_f32_e32 v31, v115, v3
	v_sub_f32_e32 v130, v132, v2
	v_sub_f32_e32 v131, v131, v3
	v_pk_mul_f32 v[128:129], v[88:89], v[128:129]
	s_waitcnt lgkmcnt(1)
	v_fma_f32 v28, v36, v28, v120
	v_fma_f32 v29, v37, v29, v121
	v_pk_mul_f32 v[30:31], v[90:91], v[30:31]
	v_pk_mul_f32 v[130:131], v[90:91], v[130:131]
	s_waitcnt lgkmcnt(0)
	v_fma_f32 v36, v116, v128, v124
	ds_write2_b32 v220, v28, v29 offset1:65
	v_fma_f32 v28, v117, v129, v125
	ds_write2_b32 v221, v36, v28 offset1:65
	v_fma_f32 v28, v38, v30, v122
	v_fma_f32 v29, v118, v130, v126
	v_fmac_f32_e32 v123, v39, v31
	v_fmac_f32_e32 v127, v119, v131
	ds_write2_b32 v220, v28, v123 offset0:130 offset1:195
	ds_write2_b32 v221, v29, v127 offset0:130 offset1:195
	s_waitcnt vmcnt(2)
	ds_write_b128 v96, v[24:27] offset:41984
	s_mov_b32 s16, 0
	v_mov_b32_e32 v24, v103
	s_waitcnt lgkmcnt(0)
	s_barrier
	ds_read_b32 v200, v218
	ds_read_b32 v208, v219
	ds_read_b32 v201, v218 offset:520
	ds_read_b32 v209, v219 offset:256
	ds_read_b32 v202, v218 offset:1040
	ds_read_b32 v210, v219 offset:512
	ds_read_b32 v203, v218 offset:1560
	ds_read_b32 v211, v219 offset:768
	ds_read_b32 v204, v218 offset:2080
	ds_read_b32 v212, v219 offset:1024
	ds_read_b32 v205, v218 offset:2600
	ds_read_b32 v213, v219 offset:1280
	ds_read_b32 v206, v218 offset:3120
	ds_read_b32 v214, v219 offset:1536
	s_waitcnt lgkmcnt(12)
	v_mfma_f32_32x32x2_f32 v[4:19], v200, v208, v[4:19]
	ds_read_b32 v207, v218 offset:3640
	ds_read_b32 v215, v219 offset:1792
	s_waitcnt lgkmcnt(12)
	v_mfma_f32_32x32x2_f32 v[4:19], v201, v209, v[4:19]
	s_waitcnt lgkmcnt(10)
	v_mfma_f32_32x32x2_f32 v[4:19], v202, v210, v[4:19]
	s_waitcnt lgkmcnt(8)
	v_mfma_f32_32x32x2_f32 v[4:19], v203, v211, v[4:19]
	s_waitcnt lgkmcnt(6)
	v_mfma_f32_32x32x2_f32 v[4:19], v204, v212, v[4:19]
	s_waitcnt lgkmcnt(4)
	v_mfma_f32_32x32x2_f32 v[4:19], v205, v213, v[4:19]
	s_waitcnt lgkmcnt(2)
	v_mfma_f32_32x32x2_f32 v[4:19], v206, v214, v[4:19]
	s_waitcnt lgkmcnt(0)
	v_mfma_f32_32x32x2_f32 v[4:19], v207, v215, v[4:19]
	s_barrier
	global_load_dwordx4 v[28:31], v[92:93], off offset:1280
	global_load_dwordx4 v[24:27], v[70:71], off
	s_waitcnt vmcnt(3)
	v_cvt_f32_f16_sdwa v128, v32 dst_sel:DWORD dst_unused:UNUSED_PAD src0_sel:WORD_1
	v_cvt_f32_f16_e32 v32, v32
	v_cvt_f32_f16_e32 v129, v33
	v_cvt_f32_f16_sdwa v130, v34 dst_sel:DWORD dst_unused:UNUSED_PAD src0_sel:WORD_1
	v_cvt_f32_f16_e32 v133, v34
	ds_read_b128 v[36:39], v43 offset:14592
	ds_read_b128 v[116:119], v43 offset:14608
	ds_read_b128 v[120:123], v43 offset:18688
	ds_read_b128 v[124:127], v43 offset:18704
	v_cvt_f32_f16_sdwa v115, v33 dst_sel:DWORD dst_unused:UNUSED_PAD src0_sel:WORD_1
	v_cvt_f32_f16_sdwa v131, v35 dst_sel:DWORD dst_unused:UNUSED_PAD src0_sel:WORD_1
	v_cvt_f32_f16_e32 v132, v35
	v_sub_f32_e32 v32, v32, v0
	v_sub_f32_e32 v33, v128, v1
	v_sub_f32_e32 v34, v129, v2
	v_pk_mul_f32 v[32:33], v[88:89], v[32:33]
	v_sub_f32_e32 v128, v133, v0
	v_sub_f32_e32 v129, v130, v1
	v_sub_f32_e32 v35, v115, v3
	v_sub_f32_e32 v130, v132, v2
	v_sub_f32_e32 v131, v131, v3
	v_pk_mul_f32 v[128:129], v[88:89], v[128:129]
	s_waitcnt lgkmcnt(1)
	v_fma_f32 v32, v36, v32, v120
	v_fma_f32 v33, v37, v33, v121
	v_pk_mul_f32 v[34:35], v[90:91], v[34:35]
	v_pk_mul_f32 v[130:131], v[90:91], v[130:131]
	s_waitcnt lgkmcnt(0)
	v_fma_f32 v36, v116, v128, v124
	ds_write2_b32 v220, v32, v33 offset1:65
	v_fma_f32 v32, v117, v129, v125
	ds_write2_b32 v221, v36, v32 offset1:65
	v_fma_f32 v32, v38, v34, v122
	v_fma_f32 v33, v118, v130, v126
	v_fmac_f32_e32 v123, v39, v35
	v_fmac_f32_e32 v127, v119, v131
	ds_write2_b32 v220, v32, v123 offset0:130 offset1:195
	ds_write2_b32 v221, v33, v127 offset0:130 offset1:195
	s_waitcnt vmcnt(2)
	ds_write_b128 v96, v[20:23] offset:41984
	s_mov_b32 s16, 0
	v_mov_b32_e32 v20, v103
	s_waitcnt lgkmcnt(0)
	s_barrier
	ds_read_b32 v200, v218
	ds_read_b32 v208, v219
	ds_read_b32 v201, v218 offset:520
	ds_read_b32 v209, v219 offset:256
	ds_read_b32 v202, v218 offset:1040
	ds_read_b32 v210, v219 offset:512
	ds_read_b32 v203, v218 offset:1560
	ds_read_b32 v211, v219 offset:768
	ds_read_b32 v204, v218 offset:2080
	ds_read_b32 v212, v219 offset:1024
	ds_read_b32 v205, v218 offset:2600
	ds_read_b32 v213, v219 offset:1280
	ds_read_b32 v206, v218 offset:3120
	ds_read_b32 v214, v219 offset:1536
	s_waitcnt lgkmcnt(12)
	v_mfma_f32_32x32x2_f32 v[4:19], v200, v208, v[4:19]
	ds_read_b32 v207, v218 offset:3640
	ds_read_b32 v215, v219 offset:1792
	s_waitcnt lgkmcnt(12)
	v_mfma_f32_32x32x2_f32 v[4:19], v201, v209, v[4:19]
	s_waitcnt lgkmcnt(10)
	v_mfma_f32_32x32x2_f32 v[4:19], v202, v210, v[4:19]
	s_waitcnt lgkmcnt(8)
	v_mfma_f32_32x32x2_f32 v[4:19], v203, v211, v[4:19]
	s_waitcnt lgkmcnt(6)
	v_mfma_f32_32x32x2_f32 v[4:19], v204, v212, v[4:19]
	s_waitcnt lgkmcnt(4)
	v_mfma_f32_32x32x2_f32 v[4:19], v205, v213, v[4:19]
	s_waitcnt lgkmcnt(2)
	v_mfma_f32_32x32x2_f32 v[4:19], v206, v214, v[4:19]
	s_waitcnt lgkmcnt(0)
	v_mfma_f32_32x32x2_f32 v[4:19], v207, v215, v[4:19]
	s_barrier
	global_load_dwordx4 v[32:35], v[92:93], off offset:1408
	global_load_dwordx4 v[20:23], v[72:73], off
	s_waitcnt vmcnt(3)
	v_cvt_f32_f16_sdwa v128, v28 dst_sel:DWORD dst_unused:UNUSED_PAD src0_sel:WORD_1
	v_cvt_f32_f16_e32 v28, v28
	v_cvt_f32_f16_e32 v129, v29
	v_cvt_f32_f16_sdwa v130, v30 dst_sel:DWORD dst_unused:UNUSED_PAD src0_sel:WORD_1
	v_cvt_f32_f16_e32 v133, v30
	ds_read_b128 v[36:39], v43 offset:14848
	ds_read_b128 v[116:119], v43 offset:14864
	ds_read_b128 v[120:123], v43 offset:18944
	ds_read_b128 v[124:127], v43 offset:18960
	v_cvt_f32_f16_sdwa v115, v29 dst_sel:DWORD dst_unused:UNUSED_PAD src0_sel:WORD_1
	v_cvt_f32_f16_sdwa v131, v31 dst_sel:DWORD dst_unused:UNUSED_PAD src0_sel:WORD_1
	v_cvt_f32_f16_e32 v132, v31
	v_sub_f32_e32 v28, v28, v0
	v_sub_f32_e32 v29, v128, v1
	v_sub_f32_e32 v30, v129, v2
	v_pk_mul_f32 v[28:29], v[88:89], v[28:29]
	v_sub_f32_e32 v128, v133, v0
	v_sub_f32_e32 v129, v130, v1
	v_sub_f32_e32 v31, v115, v3
	v_sub_f32_e32 v130, v132, v2
	v_sub_f32_e32 v131, v131, v3
	v_pk_mul_f32 v[128:129], v[88:89], v[128:129]
	s_waitcnt lgkmcnt(1)
	v_fma_f32 v28, v36, v28, v120
	v_fma_f32 v29, v37, v29, v121
	v_pk_mul_f32 v[30:31], v[90:91], v[30:31]
	v_pk_mul_f32 v[130:131], v[90:91], v[130:131]
	s_waitcnt lgkmcnt(0)
	v_fma_f32 v36, v116, v128, v124
	ds_write2_b32 v220, v28, v29 offset1:65
	v_fma_f32 v28, v117, v129, v125
	ds_write2_b32 v221, v36, v28 offset1:65
	v_fma_f32 v28, v38, v30, v122
	v_fma_f32 v29, v118, v130, v126
	v_fmac_f32_e32 v123, v39, v31
	v_fmac_f32_e32 v127, v119, v131
	ds_write2_b32 v220, v28, v123 offset0:130 offset1:195
	ds_write2_b32 v221, v29, v127 offset0:130 offset1:195
	s_waitcnt vmcnt(2)
	ds_write_b128 v96, v[24:27] offset:41984
	s_mov_b32 s16, 0
	v_mov_b32_e32 v24, v103
	s_waitcnt lgkmcnt(0)
	s_barrier
	ds_read_b32 v200, v218
	ds_read_b32 v208, v219
	ds_read_b32 v201, v218 offset:520
	ds_read_b32 v209, v219 offset:256
	ds_read_b32 v202, v218 offset:1040
	ds_read_b32 v210, v219 offset:512
	ds_read_b32 v203, v218 offset:1560
	ds_read_b32 v211, v219 offset:768
	ds_read_b32 v204, v218 offset:2080
	ds_read_b32 v212, v219 offset:1024
	ds_read_b32 v205, v218 offset:2600
	ds_read_b32 v213, v219 offset:1280
	ds_read_b32 v206, v218 offset:3120
	ds_read_b32 v214, v219 offset:1536
	s_waitcnt lgkmcnt(12)
	v_mfma_f32_32x32x2_f32 v[4:19], v200, v208, v[4:19]
	ds_read_b32 v207, v218 offset:3640
	ds_read_b32 v215, v219 offset:1792
	s_waitcnt lgkmcnt(12)
	v_mfma_f32_32x32x2_f32 v[4:19], v201, v209, v[4:19]
	s_waitcnt lgkmcnt(10)
	v_mfma_f32_32x32x2_f32 v[4:19], v202, v210, v[4:19]
	s_waitcnt lgkmcnt(8)
	v_mfma_f32_32x32x2_f32 v[4:19], v203, v211, v[4:19]
	s_waitcnt lgkmcnt(6)
	v_mfma_f32_32x32x2_f32 v[4:19], v204, v212, v[4:19]
	s_waitcnt lgkmcnt(4)
	v_mfma_f32_32x32x2_f32 v[4:19], v205, v213, v[4:19]
	s_waitcnt lgkmcnt(2)
	v_mfma_f32_32x32x2_f32 v[4:19], v206, v214, v[4:19]
	s_waitcnt lgkmcnt(0)
	v_mfma_f32_32x32x2_f32 v[4:19], v207, v215, v[4:19]
	s_barrier
	global_load_dwordx4 v[28:31], v[92:93], off offset:1536
	global_load_dwordx4 v[24:27], v[74:75], off
	s_waitcnt vmcnt(3)
	v_cvt_f32_f16_sdwa v128, v32 dst_sel:DWORD dst_unused:UNUSED_PAD src0_sel:WORD_1
	v_cvt_f32_f16_e32 v32, v32
	v_cvt_f32_f16_e32 v129, v33
	v_cvt_f32_f16_sdwa v130, v34 dst_sel:DWORD dst_unused:UNUSED_PAD src0_sel:WORD_1
	v_cvt_f32_f16_e32 v133, v34
	ds_read_b128 v[36:39], v43 offset:15104
	ds_read_b128 v[116:119], v43 offset:15120
	ds_read_b128 v[120:123], v43 offset:19200
	ds_read_b128 v[124:127], v43 offset:19216
	v_cvt_f32_f16_sdwa v115, v33 dst_sel:DWORD dst_unused:UNUSED_PAD src0_sel:WORD_1
	v_cvt_f32_f16_sdwa v131, v35 dst_sel:DWORD dst_unused:UNUSED_PAD src0_sel:WORD_1
	v_cvt_f32_f16_e32 v132, v35
	v_sub_f32_e32 v32, v32, v0
	v_sub_f32_e32 v33, v128, v1
	v_sub_f32_e32 v34, v129, v2
	v_pk_mul_f32 v[32:33], v[88:89], v[32:33]
	v_sub_f32_e32 v128, v133, v0
	v_sub_f32_e32 v129, v130, v1
	v_sub_f32_e32 v35, v115, v3
	v_sub_f32_e32 v130, v132, v2
	v_sub_f32_e32 v131, v131, v3
	v_pk_mul_f32 v[128:129], v[88:89], v[128:129]
	s_waitcnt lgkmcnt(1)
	v_fma_f32 v32, v36, v32, v120
	v_fma_f32 v33, v37, v33, v121
	v_pk_mul_f32 v[34:35], v[90:91], v[34:35]
	v_pk_mul_f32 v[130:131], v[90:91], v[130:131]
	s_waitcnt lgkmcnt(0)
	v_fma_f32 v36, v116, v128, v124
	ds_write2_b32 v220, v32, v33 offset1:65
	v_fma_f32 v32, v117, v129, v125
	ds_write2_b32 v221, v36, v32 offset1:65
	v_fma_f32 v32, v38, v34, v122
	v_fma_f32 v33, v118, v130, v126
	v_fmac_f32_e32 v123, v39, v35
	v_fmac_f32_e32 v127, v119, v131
	ds_write2_b32 v220, v32, v123 offset0:130 offset1:195
	ds_write2_b32 v221, v33, v127 offset0:130 offset1:195
	s_waitcnt vmcnt(2)
	ds_write_b128 v96, v[20:23] offset:41984
	s_mov_b32 s16, 0
	v_mov_b32_e32 v20, v103
	s_waitcnt lgkmcnt(0)
	s_barrier
	ds_read_b32 v200, v218
	ds_read_b32 v208, v219
	ds_read_b32 v201, v218 offset:520
	ds_read_b32 v209, v219 offset:256
	ds_read_b32 v202, v218 offset:1040
	ds_read_b32 v210, v219 offset:512
	ds_read_b32 v203, v218 offset:1560
	ds_read_b32 v211, v219 offset:768
	ds_read_b32 v204, v218 offset:2080
	ds_read_b32 v212, v219 offset:1024
	ds_read_b32 v205, v218 offset:2600
	ds_read_b32 v213, v219 offset:1280
	ds_read_b32 v206, v218 offset:3120
	ds_read_b32 v214, v219 offset:1536
	s_waitcnt lgkmcnt(12)
	v_mfma_f32_32x32x2_f32 v[4:19], v200, v208, v[4:19]
	ds_read_b32 v207, v218 offset:3640
	ds_read_b32 v215, v219 offset:1792
	s_waitcnt lgkmcnt(12)
	v_mfma_f32_32x32x2_f32 v[4:19], v201, v209, v[4:19]
	s_waitcnt lgkmcnt(10)
	v_mfma_f32_32x32x2_f32 v[4:19], v202, v210, v[4:19]
	s_waitcnt lgkmcnt(8)
	v_mfma_f32_32x32x2_f32 v[4:19], v203, v211, v[4:19]
	s_waitcnt lgkmcnt(6)
	v_mfma_f32_32x32x2_f32 v[4:19], v204, v212, v[4:19]
	s_waitcnt lgkmcnt(4)
	v_mfma_f32_32x32x2_f32 v[4:19], v205, v213, v[4:19]
	s_waitcnt lgkmcnt(2)
	v_mfma_f32_32x32x2_f32 v[4:19], v206, v214, v[4:19]
	s_waitcnt lgkmcnt(0)
	v_mfma_f32_32x32x2_f32 v[4:19], v207, v215, v[4:19]
	s_barrier
	global_load_dwordx4 v[32:35], v[92:93], off offset:1664
	global_load_dwordx4 v[20:23], v[76:77], off
	s_waitcnt vmcnt(3)
	v_cvt_f32_f16_sdwa v128, v28 dst_sel:DWORD dst_unused:UNUSED_PAD src0_sel:WORD_1
	v_cvt_f32_f16_e32 v28, v28
	v_cvt_f32_f16_e32 v129, v29
	v_cvt_f32_f16_sdwa v130, v30 dst_sel:DWORD dst_unused:UNUSED_PAD src0_sel:WORD_1
	v_cvt_f32_f16_e32 v133, v30
	ds_read_b128 v[36:39], v43 offset:15360
	ds_read_b128 v[116:119], v43 offset:15376
	ds_read_b128 v[120:123], v43 offset:19456
	ds_read_b128 v[124:127], v43 offset:19472
	v_cvt_f32_f16_sdwa v115, v29 dst_sel:DWORD dst_unused:UNUSED_PAD src0_sel:WORD_1
	v_cvt_f32_f16_sdwa v131, v31 dst_sel:DWORD dst_unused:UNUSED_PAD src0_sel:WORD_1
	v_cvt_f32_f16_e32 v132, v31
	v_sub_f32_e32 v28, v28, v0
	v_sub_f32_e32 v29, v128, v1
	v_sub_f32_e32 v30, v129, v2
	v_pk_mul_f32 v[28:29], v[88:89], v[28:29]
	v_sub_f32_e32 v128, v133, v0
	v_sub_f32_e32 v129, v130, v1
	v_sub_f32_e32 v31, v115, v3
	v_sub_f32_e32 v130, v132, v2
	v_sub_f32_e32 v131, v131, v3
	v_pk_mul_f32 v[128:129], v[88:89], v[128:129]
	s_waitcnt lgkmcnt(1)
	v_fma_f32 v28, v36, v28, v120
	v_fma_f32 v29, v37, v29, v121
	v_pk_mul_f32 v[30:31], v[90:91], v[30:31]
	v_pk_mul_f32 v[130:131], v[90:91], v[130:131]
	s_waitcnt lgkmcnt(0)
	v_fma_f32 v36, v116, v128, v124
	ds_write2_b32 v220, v28, v29 offset1:65
	v_fma_f32 v28, v117, v129, v125
	ds_write2_b32 v221, v36, v28 offset1:65
	v_fma_f32 v28, v38, v30, v122
	v_fma_f32 v29, v118, v130, v126
	v_fmac_f32_e32 v123, v39, v31
	v_fmac_f32_e32 v127, v119, v131
	ds_write2_b32 v220, v28, v123 offset0:130 offset1:195
	ds_write2_b32 v221, v29, v127 offset0:130 offset1:195
	s_waitcnt vmcnt(2)
	ds_write_b128 v96, v[24:27] offset:41984
	s_mov_b32 s16, 0
	v_mov_b32_e32 v24, v103
	s_waitcnt lgkmcnt(0)
	s_barrier
	ds_read_b32 v200, v218
	ds_read_b32 v208, v219
	ds_read_b32 v201, v218 offset:520
	ds_read_b32 v209, v219 offset:256
	ds_read_b32 v202, v218 offset:1040
	ds_read_b32 v210, v219 offset:512
	ds_read_b32 v203, v218 offset:1560
	ds_read_b32 v211, v219 offset:768
	ds_read_b32 v204, v218 offset:2080
	ds_read_b32 v212, v219 offset:1024
	ds_read_b32 v205, v218 offset:2600
	ds_read_b32 v213, v219 offset:1280
	ds_read_b32 v206, v218 offset:3120
	ds_read_b32 v214, v219 offset:1536
	s_waitcnt lgkmcnt(12)
	v_mfma_f32_32x32x2_f32 v[4:19], v200, v208, v[4:19]
	ds_read_b32 v207, v218 offset:3640
	ds_read_b32 v215, v219 offset:1792
	s_waitcnt lgkmcnt(12)
	v_mfma_f32_32x32x2_f32 v[4:19], v201, v209, v[4:19]
	s_waitcnt lgkmcnt(10)
	v_mfma_f32_32x32x2_f32 v[4:19], v202, v210, v[4:19]
	s_waitcnt lgkmcnt(8)
	v_mfma_f32_32x32x2_f32 v[4:19], v203, v211, v[4:19]
	s_waitcnt lgkmcnt(6)
	v_mfma_f32_32x32x2_f32 v[4:19], v204, v212, v[4:19]
	s_waitcnt lgkmcnt(4)
	v_mfma_f32_32x32x2_f32 v[4:19], v205, v213, v[4:19]
	s_waitcnt lgkmcnt(2)
	v_mfma_f32_32x32x2_f32 v[4:19], v206, v214, v[4:19]
	s_waitcnt lgkmcnt(0)
	v_mfma_f32_32x32x2_f32 v[4:19], v207, v215, v[4:19]
	s_barrier
	global_load_dwordx4 v[28:31], v[92:93], off offset:1792
	global_load_dwordx4 v[24:27], v[78:79], off
	s_waitcnt vmcnt(3)
	v_cvt_f32_f16_sdwa v128, v32 dst_sel:DWORD dst_unused:UNUSED_PAD src0_sel:WORD_1
	v_cvt_f32_f16_e32 v32, v32
	v_cvt_f32_f16_e32 v129, v33
	v_cvt_f32_f16_sdwa v130, v34 dst_sel:DWORD dst_unused:UNUSED_PAD src0_sel:WORD_1
	v_cvt_f32_f16_e32 v133, v34
	ds_read_b128 v[36:39], v43 offset:15616
	ds_read_b128 v[116:119], v43 offset:15632
	ds_read_b128 v[120:123], v43 offset:19712
	ds_read_b128 v[124:127], v43 offset:19728
	v_cvt_f32_f16_sdwa v115, v33 dst_sel:DWORD dst_unused:UNUSED_PAD src0_sel:WORD_1
	v_cvt_f32_f16_sdwa v131, v35 dst_sel:DWORD dst_unused:UNUSED_PAD src0_sel:WORD_1
	v_cvt_f32_f16_e32 v132, v35
	v_sub_f32_e32 v32, v32, v0
	v_sub_f32_e32 v33, v128, v1
	v_sub_f32_e32 v34, v129, v2
	v_pk_mul_f32 v[32:33], v[88:89], v[32:33]
	v_sub_f32_e32 v128, v133, v0
	v_sub_f32_e32 v129, v130, v1
	v_sub_f32_e32 v35, v115, v3
	v_sub_f32_e32 v130, v132, v2
	v_sub_f32_e32 v131, v131, v3
	v_pk_mul_f32 v[128:129], v[88:89], v[128:129]
	s_waitcnt lgkmcnt(1)
	v_fma_f32 v32, v36, v32, v120
	v_fma_f32 v33, v37, v33, v121
	v_pk_mul_f32 v[34:35], v[90:91], v[34:35]
	v_pk_mul_f32 v[130:131], v[90:91], v[130:131]
	s_waitcnt lgkmcnt(0)
	v_fma_f32 v36, v116, v128, v124
	ds_write2_b32 v220, v32, v33 offset1:65
	v_fma_f32 v32, v117, v129, v125
	ds_write2_b32 v221, v36, v32 offset1:65
	v_fma_f32 v32, v38, v34, v122
	v_fma_f32 v33, v118, v130, v126
	v_fmac_f32_e32 v123, v39, v35
	v_fmac_f32_e32 v127, v119, v131
	ds_write2_b32 v220, v32, v123 offset0:130 offset1:195
	ds_write2_b32 v221, v33, v127 offset0:130 offset1:195
	s_waitcnt vmcnt(2)
	ds_write_b128 v96, v[20:23] offset:41984
	s_mov_b32 s16, 0
	v_mov_b32_e32 v20, v103
	s_waitcnt lgkmcnt(0)
	s_barrier
	ds_read_b32 v200, v218
	ds_read_b32 v208, v219
	ds_read_b32 v201, v218 offset:520
	ds_read_b32 v209, v219 offset:256
	ds_read_b32 v202, v218 offset:1040
	ds_read_b32 v210, v219 offset:512
	ds_read_b32 v203, v218 offset:1560
	ds_read_b32 v211, v219 offset:768
	ds_read_b32 v204, v218 offset:2080
	ds_read_b32 v212, v219 offset:1024
	ds_read_b32 v205, v218 offset:2600
	ds_read_b32 v213, v219 offset:1280
	ds_read_b32 v206, v218 offset:3120
	ds_read_b32 v214, v219 offset:1536
	s_waitcnt lgkmcnt(12)
	v_mfma_f32_32x32x2_f32 v[4:19], v200, v208, v[4:19]
	ds_read_b32 v207, v218 offset:3640
	ds_read_b32 v215, v219 offset:1792
	s_waitcnt lgkmcnt(12)
	v_mfma_f32_32x32x2_f32 v[4:19], v201, v209, v[4:19]
	s_waitcnt lgkmcnt(10)
	v_mfma_f32_32x32x2_f32 v[4:19], v202, v210, v[4:19]
	s_waitcnt lgkmcnt(8)
	v_mfma_f32_32x32x2_f32 v[4:19], v203, v211, v[4:19]
	s_waitcnt lgkmcnt(6)
	v_mfma_f32_32x32x2_f32 v[4:19], v204, v212, v[4:19]
	s_waitcnt lgkmcnt(4)
	v_mfma_f32_32x32x2_f32 v[4:19], v205, v213, v[4:19]
	s_waitcnt lgkmcnt(2)
	v_mfma_f32_32x32x2_f32 v[4:19], v206, v214, v[4:19]
	s_waitcnt lgkmcnt(0)
	v_mfma_f32_32x32x2_f32 v[4:19], v207, v215, v[4:19]
	s_barrier
	global_load_dwordx4 v[32:35], v[92:93], off offset:1920
	global_load_dwordx4 v[20:23], v[80:81], off
	s_waitcnt vmcnt(3)
	v_cvt_f32_f16_sdwa v93, v28 dst_sel:DWORD dst_unused:UNUSED_PAD src0_sel:WORD_1
	v_cvt_f32_f16_e32 v28, v28
	v_cvt_f32_f16_sdwa v92, v29 dst_sel:DWORD dst_unused:UNUSED_PAD src0_sel:WORD_1
	v_cvt_f32_f16_sdwa v128, v30 dst_sel:DWORD dst_unused:UNUSED_PAD src0_sel:WORD_1
	v_cvt_f32_f16_e32 v131, v30
	ds_read_b128 v[36:39], v43 offset:15872
	ds_read_b128 v[116:119], v43 offset:15888
	ds_read_b128 v[120:123], v43 offset:19968
	ds_read_b128 v[124:127], v43 offset:19984
	v_cvt_f32_f16_e32 v115, v29
	v_cvt_f32_f16_sdwa v129, v31 dst_sel:DWORD dst_unused:UNUSED_PAD src0_sel:WORD_1
	v_cvt_f32_f16_e32 v130, v31
	v_sub_f32_e32 v28, v28, v0
	v_sub_f32_e32 v29, v93, v1
	v_sub_f32_e32 v31, v92, v3
	v_pk_mul_f32 v[28:29], v[88:89], v[28:29]
	v_sub_f32_e32 v92, v131, v0
	v_sub_f32_e32 v93, v128, v1
	v_sub_f32_e32 v30, v115, v2
	v_sub_f32_e32 v128, v130, v2
	v_sub_f32_e32 v129, v129, v3
	v_pk_mul_f32 v[92:93], v[88:89], v[92:93]
	s_waitcnt lgkmcnt(1)
	v_fma_f32 v28, v36, v28, v120
	v_fma_f32 v29, v37, v29, v121
	v_pk_mul_f32 v[30:31], v[90:91], v[30:31]
	v_pk_mul_f32 v[128:129], v[90:91], v[128:129]
	s_waitcnt lgkmcnt(0)
	v_fma_f32 v36, v116, v92, v124
	ds_write2_b32 v220, v28, v29 offset1:65
	v_fma_f32 v28, v117, v93, v125
	ds_write2_b32 v221, v36, v28 offset1:65
	v_fma_f32 v28, v38, v30, v122
	v_fma_f32 v29, v118, v128, v126
	v_fmac_f32_e32 v123, v39, v31
	v_fmac_f32_e32 v127, v119, v129
	ds_write2_b32 v220, v28, v123 offset0:130 offset1:195
	ds_write2_b32 v221, v29, v127 offset0:130 offset1:195
	s_waitcnt vmcnt(2)
	ds_write_b128 v96, v[24:27] offset:41984
	s_mov_b32 s16, 0
	v_mov_b32_e32 v24, v103
	s_waitcnt lgkmcnt(0)
	s_barrier
	ds_read_b32 v200, v218
	ds_read_b32 v208, v219
	ds_read_b32 v201, v218 offset:520
	ds_read_b32 v209, v219 offset:256
	ds_read_b32 v202, v218 offset:1040
	ds_read_b32 v210, v219 offset:512
	ds_read_b32 v203, v218 offset:1560
	ds_read_b32 v211, v219 offset:768
	ds_read_b32 v204, v218 offset:2080
	ds_read_b32 v212, v219 offset:1024
	ds_read_b32 v205, v218 offset:2600
	ds_read_b32 v213, v219 offset:1280
	ds_read_b32 v206, v218 offset:3120
	ds_read_b32 v214, v219 offset:1536
	s_waitcnt lgkmcnt(12)
	v_mfma_f32_32x32x2_f32 v[4:19], v200, v208, v[4:19]
	ds_read_b32 v207, v218 offset:3640
	ds_read_b32 v215, v219 offset:1792
	s_waitcnt lgkmcnt(12)
	v_mfma_f32_32x32x2_f32 v[4:19], v201, v209, v[4:19]
	s_waitcnt lgkmcnt(10)
	v_mfma_f32_32x32x2_f32 v[4:19], v202, v210, v[4:19]
	s_waitcnt lgkmcnt(8)
	v_mfma_f32_32x32x2_f32 v[4:19], v203, v211, v[4:19]
	s_waitcnt lgkmcnt(6)
	v_mfma_f32_32x32x2_f32 v[4:19], v204, v212, v[4:19]
	s_waitcnt lgkmcnt(4)
	v_mfma_f32_32x32x2_f32 v[4:19], v205, v213, v[4:19]
	s_waitcnt lgkmcnt(2)
	v_mfma_f32_32x32x2_f32 v[4:19], v206, v214, v[4:19]
	s_waitcnt lgkmcnt(0)
	v_mfma_f32_32x32x2_f32 v[4:19], v207, v215, v[4:19]
	s_waitcnt vmcnt(1)
	v_cvt_f32_f16_sdwa v93, v32 dst_sel:DWORD dst_unused:UNUSED_PAD src0_sel:WORD_1
	v_cvt_f32_f16_e32 v32, v32
	v_cvt_f32_f16_sdwa v121, v34 dst_sel:DWORD dst_unused:UNUSED_PAD src0_sel:WORD_1
	v_cvt_f32_f16_e32 v123, v34
	s_barrier
	ds_read_b128 v[24:27], v43 offset:16128
	ds_read_b128 v[28:31], v43 offset:16144
	ds_read_b128 v[36:39], v43 offset:20224
	ds_read_b128 v[116:119], v43 offset:20240
	v_cvt_f32_f16_sdwa v92, v33 dst_sel:DWORD dst_unused:UNUSED_PAD src0_sel:WORD_1
	v_cvt_f32_f16_e32 v115, v33
	v_cvt_f32_f16_sdwa v120, v35 dst_sel:DWORD dst_unused:UNUSED_PAD src0_sel:WORD_1
	v_cvt_f32_f16_e32 v122, v35
	v_sub_f32_e32 v32, v32, v0
	v_sub_f32_e32 v33, v93, v1
	v_sub_f32_e32 v0, v123, v0
	v_sub_f32_e32 v1, v121, v1
	v_sub_f32_e32 v34, v115, v2
	v_sub_f32_e32 v35, v92, v3
	v_pk_mul_f32 v[0:1], v[88:89], v[0:1]
	v_pk_mul_f32 v[34:35], v[90:91], v[34:35]
	v_sub_f32_e32 v2, v122, v2
	v_sub_f32_e32 v3, v120, v3
	s_waitcnt lgkmcnt(0)
	v_fma_f32 v0, v28, v0, v116
	v_fma_f32 v1, v29, v1, v117
	v_pk_mul_f32 v[32:33], v[88:89], v[32:33]
	v_pk_mul_f32 v[2:3], v[90:91], v[2:3]
	ds_write2_b32 v221, v0, v1 offset1:65
	v_fma_f32 v0, v26, v34, v38
	v_fmac_f32_e32 v39, v27, v35
	v_fma_f32 v24, v24, v32, v36
	v_fma_f32 v25, v25, v33, v37
	v_fma_f32 v1, v30, v2, v118
	ds_write2_b32 v220, v0, v39 offset0:130 offset1:195
	v_fmac_f32_e32 v119, v31, v3
	s_mov_b32 s16, 0
	v_mov_b32_e32 v0, v103
	ds_write2_b32 v220, v24, v25 offset1:65
	ds_write2_b32 v221, v1, v119 offset0:130 offset1:195
	s_waitcnt vmcnt(0)
	ds_write_b128 v96, v[20:23] offset:41984
	s_waitcnt lgkmcnt(0)
	s_barrier
	ds_read_b32 v200, v218
	ds_read_b32 v208, v219
	ds_read_b32 v201, v218 offset:520
	ds_read_b32 v209, v219 offset:256
	ds_read_b32 v202, v218 offset:1040
	ds_read_b32 v210, v219 offset:512
	ds_read_b32 v203, v218 offset:1560
	ds_read_b32 v211, v219 offset:768
	ds_read_b32 v204, v218 offset:2080
	ds_read_b32 v212, v219 offset:1024
	ds_read_b32 v205, v218 offset:2600
	ds_read_b32 v213, v219 offset:1280
	ds_read_b32 v206, v218 offset:3120
	ds_read_b32 v214, v219 offset:1536
	s_waitcnt lgkmcnt(12)
	v_mfma_f32_32x32x2_f32 v[4:19], v200, v208, v[4:19]
	ds_read_b32 v207, v218 offset:3640
	ds_read_b32 v215, v219 offset:1792
	s_waitcnt lgkmcnt(12)
	v_mfma_f32_32x32x2_f32 v[4:19], v201, v209, v[4:19]
	s_waitcnt lgkmcnt(10)
	v_mfma_f32_32x32x2_f32 v[4:19], v202, v210, v[4:19]
	s_waitcnt lgkmcnt(8)
	v_mfma_f32_32x32x2_f32 v[4:19], v203, v211, v[4:19]
	s_waitcnt lgkmcnt(6)
	v_mfma_f32_32x32x2_f32 v[4:19], v204, v212, v[4:19]
	s_waitcnt lgkmcnt(4)
	v_mfma_f32_32x32x2_f32 v[4:19], v205, v213, v[4:19]
	s_waitcnt lgkmcnt(2)
	v_mfma_f32_32x32x2_f32 v[4:19], v206, v214, v[4:19]
	s_waitcnt lgkmcnt(0)
	v_mfma_f32_32x32x2_f32 v[4:19], v207, v215, v[4:19]
	s_barrier
	s_nop 15
	s_nop 3
	ds_write_b32 v217, v4 offset:58752
	ds_write_b32 v217, v5 offset:58880
	ds_write_b32 v217, v6 offset:59008
	ds_write_b32 v217, v7 offset:59136
	ds_write_b32 v217, v8 offset:59776
	ds_write_b32 v217, v9 offset:59904
	ds_write_b32 v217, v10 offset:60032
	ds_write_b32 v217, v11 offset:60160
	ds_write_b32 v217, v12 offset:60800
	ds_write_b32 v217, v13 offset:60928
	ds_write_b32 v217, v14 offset:61056
	ds_write_b32 v217, v15 offset:61184
	ds_write_b32 v217, v16 offset:61824
	ds_write_b32 v217, v17 offset:61952
	ds_write_b32 v217, v18 offset:62080
	ds_write_b32 v217, v19 offset:62208
	s_waitcnt lgkmcnt(0)
	s_barrier
	global_load_dwordx4 v[0:3], v[50:51], off offset:384
	ds_read_b128 v[4:7], v98 offset:58752
	ds_read_b128 v[8:11], v99 offset:8192
	ds_read_b128 v[12:15], v99 offset:16384
	ds_read_b128 v[16:19], v99 offset:24576
	v_add_u32_e32 v20, 0xc400, v100
	v_add_u32_e32 v21, 0xc408, v100
	s_waitcnt lgkmcnt(2)
	v_pk_add_f32 v[4:5], v[4:5], v[8:9]
	v_pk_add_f32 v[6:7], v[6:7], v[10:11]
	s_waitcnt lgkmcnt(1)
	v_pk_add_f32 v[4:5], v[12:13], v[4:5]
	v_pk_add_f32 v[6:7], v[14:15], v[6:7]
	s_waitcnt lgkmcnt(0)
	v_pk_add_f32 v[4:5], v[16:17], v[4:5]
	v_pk_add_f32 v[6:7], v[18:19], v[6:7]
	s_waitcnt vmcnt(0)
	v_pk_add_f32 v[0:1], v[0:1], v[4:5]
	v_pk_add_f32 v[2:3], v[6:7], v[2:3]
	ds_write2_b32 v20, v0, v1 offset1:1
	ds_write2_b32 v21, v2, v3 offset1:1
	s_waitcnt lgkmcnt(0)
	s_barrier
	s_and_saveexec_b64 s[36:37], s[6:7]
	s_cbranch_execz .LBB0_3365
	v_add_u32_e32 v0, 0xc400, v108
	v_add_u32_e32 v1, 0xc408, v108
	v_add_u32_e32 v2, 0xc410, v108
	v_add_u32_e32 v3, 0xc418, v108
	ds_read2_b32 v[34:35], v0 offset1:1
	ds_read2_b32 v[28:29], v1 offset1:1
	ds_read2_b32 v[18:19], v2 offset1:1
	ds_read2_b32 v[8:9], v3 offset1:1
	s_mov_b32 s16, 0xff61b1e6
	s_waitcnt lgkmcnt(3)
	v_max_f32_e32 v0, v34, v34
	v_max_f32_e32 v0, 0xff61b1e6, v0
	v_cmp_lt_f32_e32 vcc, s16, v34
	v_cmp_gt_f32_e64 s[16:17], v35, v0
	v_add_u32_e32 v2, 0xc420, v108
	ds_read2_b32 v[20:21], v2 offset1:1
	v_cndmask_b32_e64 v0, v0, v35, s[16:17]
	v_cndmask_b32_e64 v1, 0, 1, s[16:17]
	s_waitcnt lgkmcnt(3)
	v_cmp_gt_f32_e64 s[16:17], v28, v0
	v_add_u32_e32 v2, 0xc428, v108
	v_add_u32_e32 v4, 0xc438, v108
	v_cndmask_b32_e64 v0, v0, v28, s[16:17]
	v_cndmask_b32_e64 v1, v1, 2, s[16:17]
	v_cmp_gt_f32_e64 s[16:17], v29, v0
	v_add_u32_e32 v3, 0xc430, v108
	ds_read2_b32 v[30:31], v2 offset1:1
	ds_read2_b32 v[16:17], v3 offset1:1
	ds_read2_b32 v[4:5], v4 offset1:1
	v_cndmask_b32_e64 v0, v0, v29, s[16:17]
	v_cndmask_b32_e64 v1, v1, 3, s[16:17]
	s_waitcnt lgkmcnt(5)
	v_cmp_gt_f32_e64 s[16:17], v18, v0
	v_add_u32_e32 v2, 0xc440, v108
	ds_read2_b32 v[12:13], v2 offset1:1
	v_cndmask_b32_e64 v0, v0, v18, s[16:17]
	v_cndmask_b32_e64 v1, v1, 4, s[16:17]
	v_cmp_gt_f32_e64 s[16:17], v19, v0
	v_add_u32_e32 v2, 0xc448, v108
	v_add_u32_e32 v6, 0xc458, v108
	v_cndmask_b32_e64 v0, v0, v19, s[16:17]
	v_cndmask_b32_e64 v1, v1, 5, s[16:17]
	s_waitcnt lgkmcnt(5)
	v_cmp_gt_f32_e64 s[16:17], v8, v0
	v_add_u32_e32 v3, 0xc450, v108
	ds_read2_b32 v[26:27], v2 offset1:1
	ds_read2_b32 v[14:15], v3 offset1:1
	ds_read2_b32 v[6:7], v6 offset1:1
	v_cndmask_b32_e64 v0, v0, v8, s[16:17]
	v_cndmask_b32_e64 v1, v1, 6, s[16:17]
	v_cmp_gt_f32_e64 s[16:17], v9, v0
	v_add_u32_e32 v2, 0xc460, v108
	ds_read2_b32 v[22:23], v2 offset1:1
	v_cndmask_b32_e64 v0, v0, v9, s[16:17]
	v_cndmask_b32_e64 v1, v1, 7, s[16:17]
	s_waitcnt lgkmcnt(8)
	v_cmp_gt_f32_e64 s[16:17], v20, v0
	v_add_u32_e32 v2, 0xc468, v108
	v_add_u32_e32 v10, 0xc478, v108
	v_cndmask_b32_e64 v0, v0, v20, s[16:17]
	v_cndmask_b32_e64 v1, v1, 8, s[16:17]
	v_cmp_gt_f32_e64 s[16:17], v21, v0
	v_add_u32_e32 v3, 0xc470, v108
	ds_read2_b32 v[32:33], v2 offset1:1
	ds_read2_b32 v[24:25], v3 offset1:1
	ds_read2_b32 v[10:11], v10 offset1:1
	v_cndmask_b32_e64 v0, v0, v21, s[16:17]
	v_cndmask_b32_e64 v1, v1, 9, s[16:17]
	s_waitcnt lgkmcnt(10)
	v_cmp_gt_f32_e64 s[16:17], v30, v0
	s_nop 1
	v_cndmask_b32_e64 v0, v0, v30, s[16:17]
	v_cndmask_b32_e64 v1, v1, 10, s[16:17]
	v_cmp_gt_f32_e64 s[16:17], v31, v0
	s_nop 1
	v_cndmask_b32_e64 v0, v0, v31, s[16:17]
	v_cndmask_b32_e64 v1, v1, 11, s[16:17]
	s_waitcnt lgkmcnt(9)
	v_cmp_gt_f32_e64 s[16:17], v16, v0
	s_nop 1
	v_cndmask_b32_e64 v0, v0, v16, s[16:17]
	v_cndmask_b32_e64 v1, v1, 12, s[16:17]
	v_cmp_gt_f32_e64 s[16:17], v17, v0
	s_nop 1
	v_cndmask_b32_e64 v0, v0, v17, s[16:17]
	v_cndmask_b32_e64 v1, v1, 13, s[16:17]
	s_waitcnt lgkmcnt(8)
	v_cmp_gt_f32_e64 s[16:17], v4, v0
	s_nop 1
	v_cndmask_b32_e64 v0, v0, v4, s[16:17]
	v_cndmask_b32_e64 v1, v1, 14, s[16:17]
	v_cmp_gt_f32_e64 s[16:17], v5, v0
	s_nop 1
	v_cndmask_b32_e64 v0, v0, v5, s[16:17]
	v_cndmask_b32_e64 v1, v1, 15, s[16:17]
	s_waitcnt lgkmcnt(7)
	v_cmp_gt_f32_e64 s[16:17], v12, v0
	s_nop 1
	v_cndmask_b32_e64 v0, v0, v12, s[16:17]
	v_cndmask_b32_e64 v1, v1, 16, s[16:17]
	v_cmp_gt_f32_e64 s[16:17], v13, v0
	s_nop 1
	v_cndmask_b32_e64 v0, v0, v13, s[16:17]
	v_cndmask_b32_e64 v1, v1, 17, s[16:17]
	s_waitcnt lgkmcnt(6)
	v_cmp_gt_f32_e64 s[16:17], v26, v0
	s_nop 1
	v_cndmask_b32_e64 v0, v0, v26, s[16:17]
	v_cndmask_b32_e64 v1, v1, 18, s[16:17]
	v_cmp_gt_f32_e64 s[16:17], v27, v0
	s_nop 1
	v_cndmask_b32_e64 v0, v0, v27, s[16:17]
	v_cndmask_b32_e64 v1, v1, 19, s[16:17]
	s_waitcnt lgkmcnt(5)
	v_cmp_gt_f32_e64 s[16:17], v14, v0
	s_nop 1
	v_cndmask_b32_e64 v0, v0, v14, s[16:17]
	v_cndmask_b32_e64 v1, v1, 20, s[16:17]
	v_cmp_gt_f32_e64 s[16:17], v15, v0
	s_nop 1
	v_cndmask_b32_e64 v0, v0, v15, s[16:17]
	v_cndmask_b32_e64 v1, v1, 21, s[16:17]
	s_waitcnt lgkmcnt(4)
	v_cmp_gt_f32_e64 s[16:17], v6, v0
	s_nop 1
	v_cndmask_b32_e64 v0, v0, v6, s[16:17]
	v_cndmask_b32_e64 v1, v1, 22, s[16:17]
	v_cmp_gt_f32_e64 s[16:17], v7, v0
	s_nop 1
	v_cndmask_b32_e64 v0, v0, v7, s[16:17]
	v_cndmask_b32_e64 v1, v1, 23, s[16:17]
	s_waitcnt lgkmcnt(3)
	v_cmp_gt_f32_e64 s[16:17], v22, v0
	s_nop 1
	v_cndmask_b32_e64 v0, v0, v22, s[16:17]
	v_cndmask_b32_e64 v1, v1, 24, s[16:17]
	v_cmp_gt_f32_e64 s[16:17], v23, v0
	s_nop 1
	v_cndmask_b32_e64 v0, v0, v23, s[16:17]
	v_cndmask_b32_e64 v1, v1, 25, s[16:17]
	s_waitcnt lgkmcnt(2)
	v_cmp_gt_f32_e64 s[16:17], v32, v0
	s_nop 1
	v_cndmask_b32_e64 v0, v0, v32, s[16:17]
	v_cndmask_b32_e64 v1, v1, 26, s[16:17]
	v_cmp_gt_f32_e64 s[16:17], v33, v0
	s_nop 1
	v_cndmask_b32_e64 v0, v0, v33, s[16:17]
	v_cndmask_b32_e64 v1, v1, 27, s[16:17]
	s_waitcnt lgkmcnt(1)
	v_cmp_gt_f32_e64 s[16:17], v24, v0
	s_nop 1
	v_cndmask_b32_e64 v0, v0, v24, s[16:17]
	v_cndmask_b32_e64 v1, v1, 28, s[16:17]
	v_cmp_gt_f32_e64 s[16:17], v25, v0
	s_nop 1
	v_cndmask_b32_e64 v0, v0, v25, s[16:17]
	v_cndmask_b32_e64 v1, v1, 29, s[16:17]
	s_waitcnt lgkmcnt(0)
	v_cmp_gt_f32_e64 s[16:17], v10, v0
	s_nop 1
	v_cndmask_b32_e64 v0, v0, v10, s[16:17]
	v_cndmask_b32_e64 v1, v1, 30, s[16:17]
	v_cmp_gt_f32_e64 s[16:17], v11, v0
	s_nop 1
	v_cndmask_b32_e64 v36, v0, v11, s[16:17]
	v_cndmask_b32_e64 v0, v1, 31, s[16:17]
	v_cmp_ne_u32_e64 s[16:17], 0, v0
	v_lshlrev_b32_e64 v2, v0, 1
	s_and_b64 s[16:17], s[16:17], vcc
	v_cndmask_b32_e64 v1, v112, v34, s[16:17]
	v_and_b32_e32 v3, 2, v2
	v_cmp_eq_u32_e64 s[16:17], 0, v3
	v_cmp_gt_f32_e64 s[18:19], v35, v1
	s_and_b64 s[16:17], s[16:17], s[18:19]
	v_cndmask_b32_e64 v1, v1, v35, s[16:17]
	v_and_b32_e32 v37, 4, v2
	v_cndmask_b32_e64 v3, 0, 1, s[16:17]
	v_cmp_eq_u32_e64 s[16:17], 0, v37
	v_cmp_gt_f32_e64 s[18:19], v28, v1
	s_and_b64 s[16:17], s[16:17], s[18:19]
	v_cndmask_b32_e64 v1, v1, v28, s[16:17]
	v_and_b32_e32 v37, 8, v2
	v_cndmask_b32_e64 v3, v3, 2, s[16:17]
	v_cmp_eq_u32_e64 s[16:17], 0, v37
	v_cmp_gt_f32_e64 s[18:19], v29, v1
	s_and_b64 s[16:17], s[16:17], s[18:19]
	v_cndmask_b32_e64 v1, v1, v29, s[16:17]
	v_and_b32_e32 v37, 16, v2
	v_cndmask_b32_e64 v3, v3, 3, s[16:17]
	v_cmp_eq_u32_e64 s[16:17], 0, v37
	v_cmp_gt_f32_e64 s[18:19], v18, v1
	s_and_b64 s[16:17], s[16:17], s[18:19]
	v_cndmask_b32_e64 v1, v1, v18, s[16:17]
	v_and_b32_e32 v37, 32, v2
	v_cndmask_b32_e64 v3, v3, 4, s[16:17]
	v_cmp_eq_u32_e64 s[16:17], 0, v37
	v_cmp_gt_f32_e64 s[18:19], v19, v1
	s_and_b64 s[16:17], s[16:17], s[18:19]
	v_cndmask_b32_e64 v1, v1, v19, s[16:17]
	v_and_b32_e32 v37, 64, v2
	v_cndmask_b32_e64 v3, v3, 5, s[16:17]
	v_cmp_eq_u32_e64 s[16:17], 0, v37
	v_cmp_gt_f32_e64 s[18:19], v8, v1
	s_and_b64 s[16:17], s[16:17], s[18:19]
	v_cndmask_b32_e64 v1, v1, v8, s[16:17]
	v_and_b32_e32 v37, 0x80, v2
	v_cndmask_b32_e64 v3, v3, 6, s[16:17]
	v_cmp_eq_u32_e64 s[16:17], 0, v37
	v_cmp_gt_f32_e64 s[18:19], v9, v1
	s_and_b64 s[16:17], s[16:17], s[18:19]
	v_cndmask_b32_e64 v1, v1, v9, s[16:17]
	v_and_b32_e32 v37, 0x100, v2
	v_cndmask_b32_e64 v3, v3, 7, s[16:17]
	v_cmp_eq_u32_e64 s[16:17], 0, v37
	v_cmp_gt_f32_e64 s[18:19], v20, v1
	s_and_b64 s[16:17], s[16:17], s[18:19]
	v_cndmask_b32_e64 v1, v1, v20, s[16:17]
	v_and_b32_e32 v37, 0x200, v2
	v_cndmask_b32_e64 v3, v3, 8, s[16:17]
	v_cmp_eq_u32_e64 s[16:17], 0, v37
	v_cmp_gt_f32_e64 s[18:19], v21, v1
	s_and_b64 s[16:17], s[16:17], s[18:19]
	v_cndmask_b32_e64 v1, v1, v21, s[16:17]
	v_and_b32_e32 v37, 0x400, v2
	v_cndmask_b32_e64 v3, v3, 9, s[16:17]
	v_cmp_eq_u32_e64 s[16:17], 0, v37
	v_cmp_gt_f32_e64 s[18:19], v30, v1
	s_and_b64 s[16:17], s[16:17], s[18:19]
	v_cndmask_b32_e64 v1, v1, v30, s[16:17]
	v_and_b32_e32 v37, 0x800, v2
	v_cndmask_b32_e64 v3, v3, 10, s[16:17]
	v_cmp_eq_u32_e64 s[16:17], 0, v37
	v_cmp_gt_f32_e64 s[18:19], v31, v1
	s_and_b64 s[16:17], s[16:17], s[18:19]
	v_cndmask_b32_e64 v1, v1, v31, s[16:17]
	v_and_b32_e32 v37, 0x1000, v2
	v_cndmask_b32_e64 v3, v3, 11, s[16:17]
	v_cmp_eq_u32_e64 s[16:17], 0, v37
	v_cmp_gt_f32_e64 s[18:19], v16, v1
	s_and_b64 s[16:17], s[16:17], s[18:19]
	v_cndmask_b32_e64 v1, v1, v16, s[16:17]
	v_and_b32_e32 v37, 0x2000, v2
	v_cndmask_b32_e64 v3, v3, 12, s[16:17]
	v_cmp_eq_u32_e64 s[16:17], 0, v37
	v_cmp_gt_f32_e64 s[18:19], v17, v1
	s_and_b64 s[16:17], s[16:17], s[18:19]
	v_cndmask_b32_e64 v1, v1, v17, s[16:17]
	v_and_b32_e32 v37, 0x4000, v2
	v_cndmask_b32_e64 v3, v3, 13, s[16:17]
	v_cmp_eq_u32_e64 s[16:17], 0, v37
	v_cmp_gt_f32_e64 s[18:19], v4, v1
	s_and_b64 s[16:17], s[16:17], s[18:19]
	v_cndmask_b32_e64 v1, v1, v4, s[16:17]
	v_and_b32_e32 v37, 0x8000, v2
	v_cndmask_b32_e64 v3, v3, 14, s[16:17]
	v_cmp_eq_u32_e64 s[16:17], 0, v37
	v_cmp_gt_f32_e64 s[18:19], v5, v1
	s_and_b64 s[16:17], s[16:17], s[18:19]
	v_cndmask_b32_e64 v1, v1, v5, s[16:17]
	v_and_b32_e32 v37, 0x10000, v2
	v_cndmask_b32_e64 v3, v3, 15, s[16:17]
	v_cmp_eq_u32_e64 s[16:17], 0, v37
	v_cmp_gt_f32_e64 s[18:19], v12, v1
	s_and_b64 s[16:17], s[16:17], s[18:19]
	v_cndmask_b32_e64 v1, v1, v12, s[16:17]
	v_and_b32_e32 v37, 0x20000, v2
	v_cndmask_b32_e64 v3, v3, 16, s[16:17]
	v_cmp_eq_u32_e64 s[16:17], 0, v37
	v_cmp_gt_f32_e64 s[18:19], v13, v1
	s_and_b64 s[16:17], s[16:17], s[18:19]
	v_cndmask_b32_e64 v1, v1, v13, s[16:17]
	v_and_b32_e32 v37, 0x40000, v2
	v_cndmask_b32_e64 v3, v3, 17, s[16:17]
	v_cmp_eq_u32_e64 s[16:17], 0, v37
	v_cmp_gt_f32_e64 s[18:19], v26, v1
	s_and_b64 s[16:17], s[16:17], s[18:19]
	v_cndmask_b32_e64 v1, v1, v26, s[16:17]
	v_and_b32_e32 v37, 0x80000, v2
	v_cndmask_b32_e64 v3, v3, 18, s[16:17]
	v_cmp_eq_u32_e64 s[16:17], 0, v37
	v_cmp_gt_f32_e64 s[18:19], v27, v1
	s_and_b64 s[16:17], s[16:17], s[18:19]
	v_cndmask_b32_e64 v1, v1, v27, s[16:17]
	v_and_b32_e32 v37, 0x100000, v2
	v_cndmask_b32_e64 v3, v3, 19, s[16:17]
	v_cmp_eq_u32_e64 s[16:17], 0, v37
	v_cmp_gt_f32_e64 s[18:19], v14, v1
	s_and_b64 s[16:17], s[16:17], s[18:19]
	v_cndmask_b32_e64 v1, v1, v14, s[16:17]
	v_and_b32_e32 v37, 0x200000, v2
	v_cndmask_b32_e64 v3, v3, 20, s[16:17]
	v_cmp_eq_u32_e64 s[16:17], 0, v37
	v_cmp_gt_f32_e64 s[18:19], v15, v1
	s_and_b64 s[16:17], s[16:17], s[18:19]
	v_cndmask_b32_e64 v1, v1, v15, s[16:17]
	v_and_b32_e32 v37, 0x400000, v2
	v_cndmask_b32_e64 v3, v3, 21, s[16:17]
	v_cmp_eq_u32_e64 s[16:17], 0, v37
	v_cmp_gt_f32_e64 s[18:19], v6, v1
	s_and_b64 s[16:17], s[16:17], s[18:19]
	v_cndmask_b32_e64 v1, v1, v6, s[16:17]
	v_and_b32_e32 v37, 0x800000, v2
	v_cndmask_b32_e64 v3, v3, 22, s[16:17]
	v_cmp_eq_u32_e64 s[16:17], 0, v37
	v_cmp_gt_f32_e64 s[18:19], v7, v1
	s_and_b64 s[16:17], s[16:17], s[18:19]
	v_cndmask_b32_e64 v1, v1, v7, s[16:17]
	v_and_b32_e32 v37, 0x1000000, v2
	v_cndmask_b32_e64 v3, v3, 23, s[16:17]
	v_cmp_eq_u32_e64 s[16:17], 0, v37
	v_cmp_gt_f32_e64 s[18:19], v22, v1
	s_and_b64 s[16:17], s[16:17], s[18:19]
	v_cndmask_b32_e64 v1, v1, v22, s[16:17]
	v_and_b32_e32 v37, 0x2000000, v2
	v_cndmask_b32_e64 v3, v3, 24, s[16:17]
	v_cmp_eq_u32_e64 s[16:17], 0, v37
	v_cmp_gt_f32_e64 s[18:19], v23, v1
	s_and_b64 s[16:17], s[16:17], s[18:19]
	v_cndmask_b32_e64 v1, v1, v23, s[16:17]
	v_and_b32_e32 v37, 0x4000000, v2
	v_cndmask_b32_e64 v3, v3, 25, s[16:17]
	v_cmp_eq_u32_e64 s[16:17], 0, v37
	v_cmp_gt_f32_e64 s[18:19], v32, v1
	s_and_b64 s[16:17], s[16:17], s[18:19]
	v_cndmask_b32_e64 v1, v1, v32, s[16:17]
	v_and_b32_e32 v37, 0x8000000, v2
	v_cndmask_b32_e64 v3, v3, 26, s[16:17]
	v_cmp_eq_u32_e64 s[16:17], 0, v37
	v_cmp_gt_f32_e64 s[18:19], v33, v1
	s_and_b64 s[16:17], s[16:17], s[18:19]
	v_cndmask_b32_e64 v1, v1, v33, s[16:17]
	v_and_b32_e32 v37, 0x10000000, v2
	v_cndmask_b32_e64 v3, v3, 27, s[16:17]
	v_cmp_eq_u32_e64 s[16:17], 0, v37
	v_cmp_gt_f32_e64 s[18:19], v24, v1
	s_and_b64 s[16:17], s[16:17], s[18:19]
	v_cndmask_b32_e64 v1, v1, v24, s[16:17]
	v_and_b32_e32 v37, 0x20000000, v2
	v_cndmask_b32_e64 v3, v3, 28, s[16:17]
	v_cmp_eq_u32_e64 s[16:17], 0, v37
	v_cmp_gt_f32_e64 s[18:19], v25, v1
	s_and_b64 s[16:17], s[16:17], s[18:19]
	v_cndmask_b32_e64 v1, v1, v25, s[16:17]
	v_and_b32_e32 v37, 2.0, v2
	v_cndmask_b32_e64 v3, v3, 29, s[16:17]
	v_cmp_eq_u32_e64 s[16:17], 0, v37
	v_cmp_gt_f32_e64 s[18:19], v10, v1
	s_and_b64 s[16:17], s[16:17], s[18:19]
	v_cndmask_b32_e64 v1, v1, v10, s[16:17]
	v_cndmask_b32_e64 v3, v3, 30, s[16:17]
	v_cmp_ne_u32_e64 s[16:17], 31, v0
	v_cmp_gt_f32_e64 s[18:19], v11, v1
	s_and_b64 s[16:17], s[16:17], s[18:19]
	v_cndmask_b32_e64 v37, v1, v11, s[16:17]
	v_cndmask_b32_e64 v1, v3, 31, s[16:17]
	v_lshl_or_b32 v3, 1, v1, v2
	v_and_b32_e32 v2, 1, v3
	v_cmp_eq_u32_e64 s[16:17], 0, v2
	s_and_b64 s[16:17], s[16:17], vcc
	v_and_b32_e32 v38, 2, v3
	v_cndmask_b32_e64 v2, v112, v34, s[16:17]
	v_cmp_eq_u32_e64 s[16:17], 0, v38
	v_cmp_gt_f32_e64 s[18:19], v35, v2
	s_and_b64 s[16:17], s[16:17], s[18:19]
	v_cndmask_b32_e64 v2, v2, v35, s[16:17]
	v_and_b32_e32 v39, 4, v3
	v_cndmask_b32_e64 v38, 0, 1, s[16:17]
	v_cmp_eq_u32_e64 s[16:17], 0, v39
	v_cmp_gt_f32_e64 s[18:19], v28, v2
	s_and_b64 s[16:17], s[16:17], s[18:19]
	v_cndmask_b32_e64 v2, v2, v28, s[16:17]
	v_and_b32_e32 v39, 8, v3
	v_cndmask_b32_e64 v38, v38, 2, s[16:17]
	v_cmp_eq_u32_e64 s[16:17], 0, v39
	v_cmp_gt_f32_e64 s[18:19], v29, v2
	s_and_b64 s[16:17], s[16:17], s[18:19]
	v_cndmask_b32_e64 v2, v2, v29, s[16:17]
	v_and_b32_e32 v39, 16, v3
	v_cndmask_b32_e64 v38, v38, 3, s[16:17]
	v_cmp_eq_u32_e64 s[16:17], 0, v39
	v_cmp_gt_f32_e64 s[18:19], v18, v2
	s_and_b64 s[16:17], s[16:17], s[18:19]
	v_cndmask_b32_e64 v2, v2, v18, s[16:17]
	v_and_b32_e32 v39, 32, v3
	v_cndmask_b32_e64 v38, v38, 4, s[16:17]
	v_cmp_eq_u32_e64 s[16:17], 0, v39
	v_cmp_gt_f32_e64 s[18:19], v19, v2
	s_and_b64 s[16:17], s[16:17], s[18:19]
	v_cndmask_b32_e64 v2, v2, v19, s[16:17]
	v_and_b32_e32 v39, 64, v3
	v_cndmask_b32_e64 v38, v38, 5, s[16:17]
	v_cmp_eq_u32_e64 s[16:17], 0, v39
	v_cmp_gt_f32_e64 s[18:19], v8, v2
	s_and_b64 s[16:17], s[16:17], s[18:19]
	v_cndmask_b32_e64 v2, v2, v8, s[16:17]
	v_and_b32_e32 v39, 0x80, v3
	v_cndmask_b32_e64 v38, v38, 6, s[16:17]
	v_cmp_eq_u32_e64 s[16:17], 0, v39
	v_cmp_gt_f32_e64 s[18:19], v9, v2
	s_and_b64 s[16:17], s[16:17], s[18:19]
	v_cndmask_b32_e64 v2, v2, v9, s[16:17]
	v_and_b32_e32 v39, 0x100, v3
	v_cndmask_b32_e64 v38, v38, 7, s[16:17]
	v_cmp_eq_u32_e64 s[16:17], 0, v39
	v_cmp_gt_f32_e64 s[18:19], v20, v2
	s_and_b64 s[16:17], s[16:17], s[18:19]
	v_cndmask_b32_e64 v2, v2, v20, s[16:17]
	v_and_b32_e32 v39, 0x200, v3
	v_cndmask_b32_e64 v38, v38, 8, s[16:17]
	v_cmp_eq_u32_e64 s[16:17], 0, v39
	v_cmp_gt_f32_e64 s[18:19], v21, v2
	s_and_b64 s[16:17], s[16:17], s[18:19]
	v_cndmask_b32_e64 v2, v2, v21, s[16:17]
	v_and_b32_e32 v39, 0x400, v3
	v_cndmask_b32_e64 v38, v38, 9, s[16:17]
	v_cmp_eq_u32_e64 s[16:17], 0, v39
	v_cmp_gt_f32_e64 s[18:19], v30, v2
	s_and_b64 s[16:17], s[16:17], s[18:19]
	v_cndmask_b32_e64 v2, v2, v30, s[16:17]
	v_and_b32_e32 v39, 0x800, v3
	v_cndmask_b32_e64 v38, v38, 10, s[16:17]
	v_cmp_eq_u32_e64 s[16:17], 0, v39
	v_cmp_gt_f32_e64 s[18:19], v31, v2
	s_and_b64 s[16:17], s[16:17], s[18:19]
	v_cndmask_b32_e64 v2, v2, v31, s[16:17]
	v_and_b32_e32 v39, 0x1000, v3
	v_cndmask_b32_e64 v38, v38, 11, s[16:17]
	v_cmp_eq_u32_e64 s[16:17], 0, v39
	v_cmp_gt_f32_e64 s[18:19], v16, v2
	s_and_b64 s[16:17], s[16:17], s[18:19]
	v_cndmask_b32_e64 v2, v2, v16, s[16:17]
	v_and_b32_e32 v39, 0x2000, v3
	v_cndmask_b32_e64 v38, v38, 12, s[16:17]
	v_cmp_eq_u32_e64 s[16:17], 0, v39
	v_cmp_gt_f32_e64 s[18:19], v17, v2
	s_and_b64 s[16:17], s[16:17], s[18:19]
	v_cndmask_b32_e64 v2, v2, v17, s[16:17]
	v_and_b32_e32 v39, 0x4000, v3
	v_cndmask_b32_e64 v38, v38, 13, s[16:17]
	v_cmp_eq_u32_e64 s[16:17], 0, v39
	v_cmp_gt_f32_e64 s[18:19], v4, v2
	s_and_b64 s[16:17], s[16:17], s[18:19]
	v_cndmask_b32_e64 v2, v2, v4, s[16:17]
	v_and_b32_e32 v39, 0x8000, v3
	v_cndmask_b32_e64 v38, v38, 14, s[16:17]
	v_cmp_eq_u32_e64 s[16:17], 0, v39
	v_cmp_gt_f32_e64 s[18:19], v5, v2
	s_and_b64 s[16:17], s[16:17], s[18:19]
	v_cndmask_b32_e64 v2, v2, v5, s[16:17]
	v_and_b32_e32 v39, 0x10000, v3
	v_cndmask_b32_e64 v38, v38, 15, s[16:17]
	v_cmp_eq_u32_e64 s[16:17], 0, v39
	v_cmp_gt_f32_e64 s[18:19], v12, v2
	s_and_b64 s[16:17], s[16:17], s[18:19]
	v_cndmask_b32_e64 v2, v2, v12, s[16:17]
	v_and_b32_e32 v39, 0x20000, v3
	v_cndmask_b32_e64 v38, v38, 16, s[16:17]
	v_cmp_eq_u32_e64 s[16:17], 0, v39
	v_cmp_gt_f32_e64 s[18:19], v13, v2
	s_and_b64 s[16:17], s[16:17], s[18:19]
	v_cndmask_b32_e64 v2, v2, v13, s[16:17]
	v_and_b32_e32 v39, 0x40000, v3
	v_cndmask_b32_e64 v38, v38, 17, s[16:17]
	v_cmp_eq_u32_e64 s[16:17], 0, v39
	v_cmp_gt_f32_e64 s[18:19], v26, v2
	s_and_b64 s[16:17], s[16:17], s[18:19]
	v_cndmask_b32_e64 v2, v2, v26, s[16:17]
	v_and_b32_e32 v39, 0x80000, v3
	v_cndmask_b32_e64 v38, v38, 18, s[16:17]
	v_cmp_eq_u32_e64 s[16:17], 0, v39
	v_cmp_gt_f32_e64 s[18:19], v27, v2
	s_and_b64 s[16:17], s[16:17], s[18:19]
	v_cndmask_b32_e64 v2, v2, v27, s[16:17]
	v_and_b32_e32 v39, 0x100000, v3
	v_cndmask_b32_e64 v38, v38, 19, s[16:17]
	v_cmp_eq_u32_e64 s[16:17], 0, v39
	v_cmp_gt_f32_e64 s[18:19], v14, v2
	s_and_b64 s[16:17], s[16:17], s[18:19]
	v_cndmask_b32_e64 v2, v2, v14, s[16:17]
	v_and_b32_e32 v39, 0x200000, v3
	v_cndmask_b32_e64 v38, v38, 20, s[16:17]
	v_cmp_eq_u32_e64 s[16:17], 0, v39
	v_cmp_gt_f32_e64 s[18:19], v15, v2
	s_and_b64 s[16:17], s[16:17], s[18:19]
	v_cndmask_b32_e64 v2, v2, v15, s[16:17]
	v_and_b32_e32 v39, 0x400000, v3
	v_cndmask_b32_e64 v38, v38, 21, s[16:17]
	v_cmp_eq_u32_e64 s[16:17], 0, v39
	v_cmp_gt_f32_e64 s[18:19], v6, v2
	s_and_b64 s[16:17], s[16:17], s[18:19]
	v_cndmask_b32_e64 v2, v2, v6, s[16:17]
	v_and_b32_e32 v39, 0x800000, v3
	v_cndmask_b32_e64 v38, v38, 22, s[16:17]
	v_cmp_eq_u32_e64 s[16:17], 0, v39
	v_cmp_gt_f32_e64 s[18:19], v7, v2
	s_and_b64 s[16:17], s[16:17], s[18:19]
	v_cndmask_b32_e64 v2, v2, v7, s[16:17]
	v_and_b32_e32 v39, 0x1000000, v3
	v_cndmask_b32_e64 v38, v38, 23, s[16:17]
	v_cmp_eq_u32_e64 s[16:17], 0, v39
	v_cmp_gt_f32_e64 s[18:19], v22, v2
	s_and_b64 s[16:17], s[16:17], s[18:19]
	v_cndmask_b32_e64 v2, v2, v22, s[16:17]
	v_and_b32_e32 v39, 0x2000000, v3
	v_cndmask_b32_e64 v38, v38, 24, s[16:17]
	v_cmp_eq_u32_e64 s[16:17], 0, v39
	v_cmp_gt_f32_e64 s[18:19], v23, v2
	s_and_b64 s[16:17], s[16:17], s[18:19]
	v_cndmask_b32_e64 v2, v2, v23, s[16:17]
	v_and_b32_e32 v39, 0x4000000, v3
	v_cndmask_b32_e64 v38, v38, 25, s[16:17]
	v_cmp_eq_u32_e64 s[16:17], 0, v39
	v_cmp_gt_f32_e64 s[18:19], v32, v2
	s_and_b64 s[16:17], s[16:17], s[18:19]
	v_cndmask_b32_e64 v2, v2, v32, s[16:17]
	v_and_b32_e32 v39, 0x8000000, v3
	v_cndmask_b32_e64 v38, v38, 26, s[16:17]
	v_cmp_eq_u32_e64 s[16:17], 0, v39
	v_cmp_gt_f32_e64 s[18:19], v33, v2
	s_and_b64 s[16:17], s[16:17], s[18:19]
	v_cndmask_b32_e64 v2, v2, v33, s[16:17]
	v_and_b32_e32 v39, 0x10000000, v3
	v_cndmask_b32_e64 v38, v38, 27, s[16:17]
	v_cmp_eq_u32_e64 s[16:17], 0, v39
	v_cmp_gt_f32_e64 s[18:19], v24, v2
	s_and_b64 s[16:17], s[16:17], s[18:19]
	v_cndmask_b32_e64 v2, v2, v24, s[16:17]
	v_and_b32_e32 v39, 0x20000000, v3
	v_cndmask_b32_e64 v38, v38, 28, s[16:17]
	v_cmp_eq_u32_e64 s[16:17], 0, v39
	v_cmp_gt_f32_e64 s[18:19], v25, v2
	s_and_b64 s[16:17], s[16:17], s[18:19]
	v_cndmask_b32_e64 v2, v2, v25, s[16:17]
	v_and_b32_e32 v39, 2.0, v3
	v_cndmask_b32_e64 v38, v38, 29, s[16:17]
	v_cmp_eq_u32_e64 s[16:17], 0, v39
	v_cmp_gt_f32_e64 s[18:19], v10, v2
	s_and_b64 s[16:17], s[16:17], s[18:19]
	v_cndmask_b32_e64 v2, v2, v10, s[16:17]
	v_cndmask_b32_e64 v38, v38, 30, s[16:17]
	v_cmp_lt_i32_e64 s[16:17], -1, v3
	v_cmp_gt_f32_e64 s[18:19], v11, v2
	s_and_b64 s[16:17], s[16:17], s[18:19]
	v_cndmask_b32_e64 v39, v2, v11, s[16:17]
	v_cndmask_b32_e64 v2, v38, 31, s[16:17]
	v_lshlrev_b32_e64 v38, v2, 1
	v_bitop3_b32 v89, v38, 1, v3 bitop3:0xc8
	v_cmp_eq_u32_e64 s[16:17], 0, v89
	s_and_b64 vcc, s[16:17], vcc
	v_cndmask_b32_e32 v34, v112, v34, vcc
	v_bitop3_b32 v89, v38, 2, v3 bitop3:0xc8
	v_cmp_eq_u32_e32 vcc, 0, v89
	v_cmp_gt_f32_e64 s[16:17], v35, v34
	s_and_b64 vcc, vcc, s[16:17]
	v_cndmask_b32_e32 v34, v34, v35, vcc
	v_bitop3_b32 v89, v38, 4, v3 bitop3:0xc8
	v_cndmask_b32_e64 v35, 0, 1, vcc
	v_cmp_eq_u32_e32 vcc, 0, v89
	v_cmp_gt_f32_e64 s[16:17], v28, v34
	s_and_b64 vcc, vcc, s[16:17]
	v_cndmask_b32_e32 v28, v34, v28, vcc
	v_cndmask_b32_e64 v34, v35, 2, vcc
	v_bitop3_b32 v35, v38, 8, v3 bitop3:0xc8
	v_cmp_eq_u32_e32 vcc, 0, v35
	v_cmp_gt_f32_e64 s[16:17], v29, v28
	s_and_b64 vcc, vcc, s[16:17]
	v_cndmask_b32_e32 v28, v28, v29, vcc
	v_cndmask_b32_e64 v29, v34, 3, vcc
	v_bitop3_b32 v34, v38, 16, v3 bitop3:0xc8
	v_cmp_eq_u32_e32 vcc, 0, v34
	v_cmp_gt_f32_e64 s[16:17], v18, v28
	s_and_b64 vcc, vcc, s[16:17]
	v_cndmask_b32_e32 v18, v28, v18, vcc
	v_cndmask_b32_e64 v28, v29, 4, vcc
	v_bitop3_b32 v29, v38, 32, v3 bitop3:0xc8
	v_cmp_eq_u32_e32 vcc, 0, v29
	v_cmp_gt_f32_e64 s[16:17], v19, v18
	s_and_b64 vcc, vcc, s[16:17]
	v_cndmask_b32_e32 v18, v18, v19, vcc
	v_cndmask_b32_e64 v19, v28, 5, vcc
	v_bitop3_b32 v28, v38, 64, v3 bitop3:0xc8
	v_cmp_eq_u32_e32 vcc, 0, v28
	v_cmp_gt_f32_e64 s[16:17], v8, v18
	s_and_b64 vcc, vcc, s[16:17]
	s_movk_i32 s16, 0x80
	v_cndmask_b32_e32 v8, v18, v8, vcc
	v_cndmask_b32_e64 v18, v19, 6, vcc
	v_bitop3_b32 v19, v38, s16, v3 bitop3:0xc8
	v_cmp_eq_u32_e32 vcc, 0, v19
	v_cmp_gt_f32_e64 s[16:17], v9, v8
	s_and_b64 vcc, vcc, s[16:17]
	s_movk_i32 s16, 0x100
	v_cndmask_b32_e32 v8, v8, v9, vcc
	v_cndmask_b32_e64 v9, v18, 7, vcc
	v_bitop3_b32 v18, v38, s16, v3 bitop3:0xc8
	v_cmp_eq_u32_e32 vcc, 0, v18
	v_cmp_gt_f32_e64 s[16:17], v20, v8
	s_and_b64 vcc, vcc, s[16:17]
	s_movk_i32 s16, 0x200
	v_cndmask_b32_e32 v8, v8, v20, vcc
	v_bitop3_b32 v18, v38, s16, v3 bitop3:0xc8
	v_cndmask_b32_e64 v9, v9, 8, vcc
	v_cmp_eq_u32_e32 vcc, 0, v18
	v_cmp_gt_f32_e64 s[16:17], v21, v8
	s_and_b64 vcc, vcc, s[16:17]
	v_cndmask_b32_e32 v8, v8, v21, vcc
	v_bitop3_b32 v18, v38, s52, v3 bitop3:0xc8
	v_cndmask_b32_e64 v9, v9, 9, vcc
	v_cmp_eq_u32_e32 vcc, 0, v18
	v_cmp_gt_f32_e64 s[16:17], v30, v8
	s_and_b64 vcc, vcc, s[16:17]
	s_movk_i32 s16, 0x800
	v_cndmask_b32_e32 v8, v8, v30, vcc
	v_bitop3_b32 v18, v38, s16, v3 bitop3:0xc8
	v_cndmask_b32_e64 v9, v9, 10, vcc
	v_cmp_eq_u32_e32 vcc, 0, v18
	v_cmp_gt_f32_e64 s[16:17], v31, v8
	s_and_b64 vcc, vcc, s[16:17]
	s_movk_i32 s16, 0x1000
	v_cndmask_b32_e32 v8, v8, v31, vcc
	v_bitop3_b32 v18, v38, s16, v3 bitop3:0xc8
	v_cndmask_b32_e64 v9, v9, 11, vcc
	v_cmp_eq_u32_e32 vcc, 0, v18
	v_cmp_gt_f32_e64 s[16:17], v16, v8
	s_and_b64 vcc, vcc, s[16:17]
	s_movk_i32 s16, 0x2000
	v_cndmask_b32_e32 v8, v8, v16, vcc
	v_bitop3_b32 v16, v38, s16, v3 bitop3:0xc8
	v_cndmask_b32_e64 v9, v9, 12, vcc
	v_cmp_eq_u32_e32 vcc, 0, v16
	v_cmp_gt_f32_e64 s[16:17], v17, v8
	s_and_b64 vcc, vcc, s[16:17]
	s_movk_i32 s16, 0x4000
	v_cndmask_b32_e32 v8, v8, v17, vcc
	v_bitop3_b32 v16, v38, s16, v3 bitop3:0xc8
	v_cndmask_b32_e64 v9, v9, 13, vcc
	v_cmp_eq_u32_e32 vcc, 0, v16
	v_cmp_gt_f32_e64 s[16:17], v4, v8
	s_and_b64 vcc, vcc, s[16:17]
	s_mov_b32 s16, 0x8000
	v_cndmask_b32_e32 v4, v8, v4, vcc
	v_cndmask_b32_e64 v8, v9, 14, vcc
	v_bitop3_b32 v9, v38, s16, v3 bitop3:0xc8
	v_cmp_eq_u32_e32 vcc, 0, v9
	v_cmp_gt_f32_e64 s[16:17], v5, v4
	s_and_b64 vcc, vcc, s[16:17]
	s_mov_b32 s16, 0x10000
	v_cndmask_b32_e32 v4, v4, v5, vcc
	v_cndmask_b32_e64 v5, v8, 15, vcc
	v_bitop3_b32 v8, v38, s16, v3 bitop3:0xc8
	v_cmp_eq_u32_e32 vcc, 0, v8
	v_cmp_gt_f32_e64 s[16:17], v12, v4
	s_and_b64 vcc, vcc, s[16:17]
	s_mov_b32 s16, 0x20000
	v_cndmask_b32_e32 v4, v4, v12, vcc
	v_bitop3_b32 v8, v38, s16, v3 bitop3:0xc8
	v_cndmask_b32_e64 v5, v5, 16, vcc
	v_cmp_eq_u32_e32 vcc, 0, v8
	v_cmp_gt_f32_e64 s[16:17], v13, v4
	s_and_b64 vcc, vcc, s[16:17]
	s_mov_b32 s16, 0x40000
	v_cndmask_b32_e32 v4, v4, v13, vcc
	v_bitop3_b32 v8, v38, s16, v3 bitop3:0xc8
	v_cndmask_b32_e64 v5, v5, 17, vcc
	v_cmp_eq_u32_e32 vcc, 0, v8
	v_cmp_gt_f32_e64 s[16:17], v26, v4
	s_and_b64 vcc, vcc, s[16:17]
	v_cndmask_b32_e32 v4, v4, v26, vcc
	v_bitop3_b32 v8, v38, s61, v3 bitop3:0xc8
	v_cndmask_b32_e64 v5, v5, 18, vcc
	v_cmp_eq_u32_e32 vcc, 0, v8
	v_cmp_gt_f32_e64 s[16:17], v27, v4
	s_and_b64 vcc, vcc, s[16:17]
	v_cndmask_b32_e32 v4, v4, v27, vcc
	v_bitop3_b32 v8, v38, s62, v3 bitop3:0xc8
	v_cndmask_b32_e64 v5, v5, 19, vcc
	v_cmp_eq_u32_e32 vcc, 0, v8
	v_cmp_gt_f32_e64 s[16:17], v14, v4
	s_and_b64 vcc, vcc, s[16:17]
	v_cndmask_b32_e32 v4, v4, v14, vcc
	v_bitop3_b32 v8, v38, s63, v3 bitop3:0xc8
	v_cndmask_b32_e64 v5, v5, 20, vcc
	v_cmp_eq_u32_e32 vcc, 0, v8
	v_cmp_gt_f32_e64 s[16:17], v15, v4
	s_and_b64 vcc, vcc, s[16:17]
	v_cndmask_b32_e32 v4, v4, v15, vcc
	v_bitop3_b32 v8, v38, s64, v3 bitop3:0xc8
	v_cndmask_b32_e64 v5, v5, 21, vcc
	v_cmp_eq_u32_e32 vcc, 0, v8
	v_cmp_gt_f32_e64 s[16:17], v6, v4
	s_and_b64 vcc, vcc, s[16:17]
	v_cndmask_b32_e32 v4, v4, v6, vcc
	v_bitop3_b32 v6, v38, s65, v3 bitop3:0xc8
	v_cndmask_b32_e64 v5, v5, 22, vcc
	v_cmp_eq_u32_e32 vcc, 0, v6
	v_cmp_gt_f32_e64 s[16:17], v7, v4
	s_and_b64 vcc, vcc, s[16:17]
	v_cndmask_b32_e32 v4, v4, v7, vcc
	v_bitop3_b32 v6, v38, s66, v3 bitop3:0xc8
	v_cndmask_b32_e64 v5, v5, 23, vcc
	v_cmp_eq_u32_e32 vcc, 0, v6
	v_cmp_gt_f32_e64 s[16:17], v22, v4
	s_and_b64 vcc, vcc, s[16:17]
	v_cndmask_b32_e32 v4, v4, v22, vcc
	v_bitop3_b32 v6, v38, s67, v3 bitop3:0xc8
	v_cndmask_b32_e64 v5, v5, 24, vcc
	v_cmp_eq_u32_e32 vcc, 0, v6
	v_cmp_gt_f32_e64 s[16:17], v23, v4
	s_and_b64 vcc, vcc, s[16:17]
	v_cndmask_b32_e32 v4, v4, v23, vcc
	v_bitop3_b32 v6, v38, s84, v3 bitop3:0xc8
	v_cndmask_b32_e64 v5, v5, 25, vcc
	v_cmp_eq_u32_e32 vcc, 0, v6
	v_cmp_gt_f32_e64 s[16:17], v32, v4
	s_and_b64 vcc, vcc, s[16:17]
	v_cndmask_b32_e32 v4, v4, v32, vcc
	v_bitop3_b32 v6, v38, s85, v3 bitop3:0xc8
	v_cndmask_b32_e64 v5, v5, 26, vcc
	v_cmp_eq_u32_e32 vcc, 0, v6
	v_cmp_gt_f32_e64 s[16:17], v33, v4
	s_and_b64 vcc, vcc, s[16:17]
	v_cndmask_b32_e32 v4, v4, v33, vcc
	v_bitop3_b32 v6, v38, s86, v3 bitop3:0xc8
	v_cndmask_b32_e64 v5, v5, 27, vcc
	v_cmp_eq_u32_e32 vcc, 0, v6
	v_cmp_gt_f32_e64 s[16:17], v24, v4
	s_and_b64 vcc, vcc, s[16:17]
	v_cndmask_b32_e32 v4, v4, v24, vcc
	v_bitop3_b32 v6, v38, s87, v3 bitop3:0xc8
	v_cndmask_b32_e64 v5, v5, 28, vcc
	v_cmp_eq_u32_e32 vcc, 0, v6
	v_cmp_gt_f32_e64 s[16:17], v25, v4
	s_and_b64 vcc, vcc, s[16:17]
	v_or_b32_e32 v88, v38, v3
	v_cndmask_b32_e32 v4, v4, v25, vcc
	v_bitop3_b32 v3, v38, 2.0, v3 bitop3:0xc8
	v_cndmask_b32_e64 v5, v5, 29, vcc
	v_cmp_eq_u32_e32 vcc, 0, v3
	v_cmp_gt_f32_e64 s[16:17], v10, v4
	s_and_b64 vcc, vcc, s[16:17]
	v_cndmask_b32_e32 v3, v4, v10, vcc
	v_cndmask_b32_e64 v4, v5, 30, vcc
	v_cmp_lt_i32_e32 vcc, -1, v88
	v_cmp_gt_f32_e64 s[16:17], v11, v3
	s_and_b64 vcc, vcc, s[16:17]
	v_cndmask_b32_e32 v5, v3, v11, vcc
	v_cndmask_b32_e64 v3, v4, 31, vcc
	v_sub_f32_e32 v4, v36, v36
	v_mul_f32_e32 v4, 0x3fb8aa3b, v4
	v_exp_f32_e32 v10, v4
	v_sub_f32_e32 v4, v37, v36
	v_mul_f32_e32 v4, 0x3fb8aa3b, v4
	v_exp_f32_e32 v11, v4
	v_sub_f32_e32 v4, v39, v36
	v_mul_f32_e32 v4, 0x3fb8aa3b, v4
	v_exp_f32_e32 v12, v4
	v_sub_f32_e32 v4, v5, v36
	v_mul_f32_e32 v4, 0x3fb8aa3b, v4
	v_exp_f32_e32 v13, v4
	v_add_f32_e32 v4, 0, v10
	v_add_f32_e32 v4, v4, v11
	v_add_f32_e32 v4, v4, v12
	v_add_f32_e32 v14, v4, v13
	v_div_scale_f32 v15, s[16:17], v14, v14, v10
	v_rcp_f32_e32 v16, v15
	v_lshl_add_u32 v4, s91, 8, v94
	v_ashrrev_i32_e32 v5, 31, v4
	v_lshlrev_b64 v[6:7], 2, v[4:5]
	v_fma_f32 v5, -v15, v16, 1.0
	v_fmac_f32_e32 v16, v5, v16
	v_div_scale_f32 v5, vcc, v10, v14, v10
	v_mul_f32_e32 v17, v5, v16
	v_fma_f32 v18, -v15, v17, v5
	v_fmac_f32_e32 v17, v18, v16
	v_fma_f32 v5, -v15, v17, v5
	v_div_fmas_f32 v5, v5, v16, v17
	v_div_fixup_f32 v5, v5, v14, v10
	v_div_scale_f32 v10, s[16:17], v14, v14, v11
	v_rcp_f32_e32 v15, v10
	v_lshl_add_u64 v[8:9], s[20:21], 0, v[6:7]
	v_lshl_add_u64 v[6:7], s[22:23], 0, v[6:7]
	global_store_dword v[6:7], v5, off
	v_or_b32_e32 v6, 1, v4
	v_fma_f32 v4, -v10, v15, 1.0
	v_lshl_add_u32 v5, v0, 2, 0
	v_fmac_f32_e32 v15, v4, v15
	v_div_scale_f32 v4, vcc, v11, v14, v11
	ds_add_u32 v5, v109 offset:58624
	v_mul_f32_e32 v5, v4, v15
	v_fma_f32 v16, -v10, v5, v4
	v_fmac_f32_e32 v5, v16, v15
	v_fma_f32 v4, -v10, v5, v4
	v_div_fmas_f32 v4, v4, v15, v5
	v_div_scale_f32 v5, s[16:17], v14, v14, v12
	v_rcp_f32_e32 v15, v5
	v_ashrrev_i32_e32 v7, 31, v6
	v_div_fixup_f32 v4, v4, v14, v11
	v_lshl_add_u64 v[10:11], v[6:7], 2, s[22:23]
	v_lshl_add_u32 v6, v1, 2, 0
	ds_add_u32 v6, v109 offset:58624
	v_fma_f32 v6, -v5, v15, 1.0
	v_fmac_f32_e32 v15, v6, v15
	v_div_scale_f32 v6, vcc, v12, v14, v12
	v_mul_f32_e32 v7, v6, v15
	v_fma_f32 v16, -v5, v7, v6
	v_fmac_f32_e32 v7, v16, v15
	v_fma_f32 v5, -v5, v7, v6
	v_div_scale_f32 v6, s[16:17], v14, v14, v13
	v_div_fmas_f32 v5, v5, v15, v7
	v_rcp_f32_e32 v7, v6
	v_div_fixup_f32 v5, v5, v14, v12
	v_lshl_add_u32 v12, v2, 2, 0
	ds_add_u32 v12, v109 offset:58624
	global_store_dwordx4 v[8:9], v[0:3], off
	s_nop 1
	v_fma_f32 v0, -v6, v7, 1.0
	v_fmac_f32_e32 v7, v0, v7
	v_div_scale_f32 v0, vcc, v13, v14, v13
	v_mul_f32_e32 v1, v0, v7
	v_fma_f32 v2, -v6, v1, v0
	v_fmac_f32_e32 v1, v2, v7
	v_fma_f32 v0, -v6, v1, v0
	v_div_fmas_f32 v0, v0, v7, v1
	v_div_fixup_f32 v6, v0, v14, v13
	global_store_dwordx3 v[10:11], v[4:6], off
	v_lshl_add_u32 v0, v3, 2, 0
	ds_add_u32 v0, v109 offset:58624
